# fused fp8 GEMM schedule + H1 prio2 + epilogue flat->global + saddr-form LDS-DMA loads
# baseline (speedup 1.0000x reference)
; #define PG8_STAGE(bufoff, gbase, voff) do { _Pragma("unroll") for (int _i = 0; _i < 2; ++_i) \
;         __builtin_amdgcn_global_load_lds((const unsigned*)((const char*)(gbase) + (voff)[_i]), (PG8_LAS unsigned*)(lds + (bufoff) + ldsw + _i * 8192), 16, 0, 0); } while (0)
; #define PG8_WAIT_V(n) asm volatile("s_waitcnt vmcnt(" #n ")" ::: "memory")
; #define PG8_WAIT_L(n) asm volatile("s_waitcnt lgkmcnt(" #n ")" ::: "memory")
; #define PG8_BAR __builtin_amdgcn_s_barrier()
; #define PG8_SCHED __builtin_amdgcn_sched_barrier(0)
; template <class Epi, class Sched, bool ALIGN_EPI = true, bool F8 = false>
; __device__ __forceinline__ void gemm_phase(PG8_LAS unsigned char* lds, const Sched& S, const Epi& E) {
;     ...
;             PG8_LDB(B0, 0, 0); PG8_LDB(B1, 0, 1); PG8_SCHED; PG8_LDA(At, 0, 0); PG8_STAGE(PG8_SA(1, 1), a1, voffA[1]);
;             PG8_WAIT_V(8); PG8_WAIT_L(0); PG8_BAR; PG8_MMA(0, 0, At, B0); PG8_MMA(0, 1, At, B1); PG8_BAR; PG8_SCHED;
;             PG8_LDA(At, 0, 1); PG8_STAGE(PG8_SB(0, 0), b2, voffB[0]); PG8_STAGE(PG8_SB(0, 1), b2, voffB[1]); PG8_STAGE(PG8_SA(0, 0), a2, vA2[0]);
;             PG8_WAIT_V(8); PG8_WAIT_L(0); PG8_BAR; PG8_MMA(1, 0, At, B0); PG8_MMA(1, 1, At, B1); PG8_BAR; PG8_SCHED;
.LBB0_372:
	ds_read_b128 v[18:21], v207
	ds_read_b128 v[22:25], v207 offset:1024
	ds_read_b128 v[26:29], v207 offset:2048
	ds_read_b128 v[30:33], v207 offset:3072
	ds_read_b128 v[2:5], v208
	ds_read_b128 v[6:9], v208 offset:1024
	ds_read_b128 v[10:13], v208 offset:2048
	ds_read_b128 v[14:17], v208 offset:3072
	s_add_u32 s28, s26, 0x8000
	s_addc_u32 s29, s27, 0
	s_cmp_eq_u32 s21, 12
	s_cselect_b32 s40, s22, s28
	s_cselect_b32 s41, s23, s29
	s_cselect_b32 s30, s24, s5
	s_cselect_b32 s31, s25, s19
	s_add_u32 s28, s40, 0x8000
	s_addc_u32 s29, s41, 0
	s_add_i32 m0, s46, 0xc000
	ds_read_b128 v[212:215], v209
	ds_read_b128 v[216:219], v209 offset:1024
	ds_read_b128 v[220:223], v209 offset:2048
	ds_read_b128 v[224:227], v209 offset:3072
	ds_read_b128 v[228:231], v209 offset:4096
	ds_read_b128 v[232:235], v209 offset:5120
	ds_read_b128 v[236:239], v209 offset:6144
	ds_read_b128 v[240:243], v209 offset:7168
	global_load_lds_dwordx4 v190, s[26:27]
	s_add_i32 m0, s46, 0xe000
	s_nop 0
	global_load_lds_dwordx4 v188, s[26:27]
	s_waitcnt vmcnt(8)
	s_waitcnt lgkmcnt(0)
	s_setprio 1
	s_waitcnt lgkmcnt(0)
	v_mfma_scale_f32_16x16x128_f8f6f4 v[158:161], v[18:25], v[212:219], v[158:161], v210, v210 op_sel_hi:[0,0,0]
	v_mfma_scale_f32_16x16x128_f8f6f4 v[154:157], v[26:33], v[212:219], v[154:157], v210, v210 op_sel_hi:[0,0,0]
	v_mfma_scale_f32_16x16x128_f8f6f4 v[142:145], v[18:25], v[220:227], v[142:145], v210, v210 op_sel_hi:[0,0,0]
	v_mfma_scale_f32_16x16x128_f8f6f4 v[138:141], v[26:33], v[220:227], v[138:141], v210, v210 op_sel_hi:[0,0,0]
	v_mfma_scale_f32_16x16x128_f8f6f4 v[126:129], v[18:25], v[228:235], v[126:129], v210, v210 op_sel_hi:[0,0,0]
	v_mfma_scale_f32_16x16x128_f8f6f4 v[122:125], v[26:33], v[228:235], v[122:125], v210, v210 op_sel_hi:[0,0,0]
	v_mfma_scale_f32_16x16x128_f8f6f4 v[110:113], v[18:25], v[236:243], v[110:113], v210, v210 op_sel_hi:[0,0,0]
	v_mfma_scale_f32_16x16x128_f8f6f4 v[106:109], v[26:33], v[236:243], v[106:109], v210, v210 op_sel_hi:[0,0,0]
	s_nop 3
	s_setprio 0
	s_setprio 1
	v_mfma_scale_f32_16x16x128_f8f6f4 v[150:153], v[2:9], v[212:219], v[150:153], v210, v210 op_sel_hi:[0,0,0]
	v_mfma_scale_f32_16x16x128_f8f6f4 v[146:149], v[10:17], v[212:219], v[146:149], v210, v210 op_sel_hi:[0,0,0]
	v_mfma_scale_f32_16x16x128_f8f6f4 v[134:137], v[2:9], v[220:227], v[134:137], v210, v210 op_sel_hi:[0,0,0]
	v_mfma_scale_f32_16x16x128_f8f6f4 v[130:133], v[10:17], v[220:227], v[130:133], v210, v210 op_sel_hi:[0,0,0]
	v_mfma_scale_f32_16x16x128_f8f6f4 v[118:121], v[2:9], v[228:235], v[118:121], v210, v210 op_sel_hi:[0,0,0]
	v_mfma_scale_f32_16x16x128_f8f6f4 v[114:117], v[10:17], v[228:235], v[114:117], v210, v210 op_sel_hi:[0,0,0]
	v_mfma_scale_f32_16x16x128_f8f6f4 v[102:105], v[2:9], v[236:243], v[102:105], v210, v210 op_sel_hi:[0,0,0]
	v_mfma_scale_f32_16x16x128_f8f6f4 v[98:101], v[10:17], v[236:243], v[98:101], v210, v210 op_sel_hi:[0,0,0]
	s_nop 3
	s_setprio 0
	s_barrier
	s_add_i32 s67, s62, s45
	s_mov_b32 m0, s67
	ds_read_b128 v[212:215], v209 offset:16384
	ds_read_b128 v[216:219], v209 offset:17408
	ds_read_b128 v[220:223], v209 offset:18432
	ds_read_b128 v[224:227], v209 offset:19456
	ds_read_b128 v[228:231], v209 offset:20480
	ds_read_b128 v[232:235], v209 offset:21504
	ds_read_b128 v[236:239], v209 offset:22528
	ds_read_b128 v[240:243], v209 offset:23552
	global_load_lds_dwordx4 v164, s[30:31]
	s_add_i32 m0, s67, 0x2000
	s_add_i32 s67, s63, s45
	global_load_lds_dwordx4 v166, s[30:31]
	s_add_u32 s98, s30, s8
	s_addc_u32 s99, s31, s9
	s_mov_b32 m0, s67
	s_nop 0
	global_load_lds_dwordx4 v164, s[98:99]
	s_add_u32 s100, s30, s8
	s_addc_u32 s101, s31, s9
	s_add_i32 m0, s67, 0x2000
	s_nop 0
	global_load_lds_dwordx4 v166, s[100:101]
	s_mov_b32 m0, s46
	s_nop 0
	global_load_lds_dwordx4 v174, s[40:41]
	s_mov_b32 m0, s47
	s_nop 0
	global_load_lds_dwordx4 v176, s[40:41]
	s_waitcnt vmcnt(8)
	s_waitcnt lgkmcnt(0)
	s_setprio 1
	s_waitcnt lgkmcnt(0)
	v_mfma_scale_f32_16x16x128_f8f6f4 v[94:97], v[18:25], v[212:219], v[94:97], v210, v210 op_sel_hi:[0,0,0]
	v_mfma_scale_f32_16x16x128_f8f6f4 v[90:93], v[26:33], v[212:219], v[90:93], v210, v210 op_sel_hi:[0,0,0]
	v_mfma_scale_f32_16x16x128_f8f6f4 v[78:81], v[18:25], v[220:227], v[78:81], v210, v210 op_sel_hi:[0,0,0]
	v_mfma_scale_f32_16x16x128_f8f6f4 v[74:77], v[26:33], v[220:227], v[74:77], v210, v210 op_sel_hi:[0,0,0]
	v_mfma_scale_f32_16x16x128_f8f6f4 v[62:65], v[18:25], v[228:235], v[62:65], v210, v210 op_sel_hi:[0,0,0]
	v_mfma_scale_f32_16x16x128_f8f6f4 v[58:61], v[26:33], v[228:235], v[58:61], v210, v210 op_sel_hi:[0,0,0]
	v_mfma_scale_f32_16x16x128_f8f6f4 v[46:49], v[18:25], v[236:243], v[46:49], v210, v210 op_sel_hi:[0,0,0]
	v_mfma_scale_f32_16x16x128_f8f6f4 v[42:45], v[26:33], v[236:243], v[42:45], v210, v210 op_sel_hi:[0,0,0]
	s_nop 3
	s_setprio 0
	s_setprio 1
	v_mfma_scale_f32_16x16x128_f8f6f4 v[86:89], v[2:9], v[212:219], v[86:89], v210, v210 op_sel_hi:[0,0,0]
	v_mfma_scale_f32_16x16x128_f8f6f4 v[82:85], v[10:17], v[212:219], v[82:85], v210, v210 op_sel_hi:[0,0,0]
	v_mfma_scale_f32_16x16x128_f8f6f4 v[70:73], v[2:9], v[220:227], v[70:73], v210, v210 op_sel_hi:[0,0,0]
	v_mfma_scale_f32_16x16x128_f8f6f4 v[66:69], v[10:17], v[220:227], v[66:69], v210, v210 op_sel_hi:[0,0,0]
	v_mfma_scale_f32_16x16x128_f8f6f4 v[54:57], v[2:9], v[228:235], v[54:57], v210, v210 op_sel_hi:[0,0,0]
	v_mfma_scale_f32_16x16x128_f8f6f4 v[50:53], v[10:17], v[228:235], v[50:53], v210, v210 op_sel_hi:[0,0,0]
	v_mfma_scale_f32_16x16x128_f8f6f4 v[38:41], v[2:9], v[236:243], v[38:41], v210, v210 op_sel_hi:[0,0,0]
	v_mfma_scale_f32_16x16x128_f8f6f4 v[34:37], v[10:17], v[236:243], v[34:37], v210, v210 op_sel_hi:[0,0,0]
	s_nop 3
	s_setprio 0
	s_barrier
; #define PG8_STAGE(bufoff, gbase, voff) do { _Pragma("unroll") for (int _i = 0; _i < 2; ++_i) \
;         __builtin_amdgcn_global_load_lds((const unsigned*)((const char*)(gbase) + (voff)[_i]), (PG8_LAS unsigned*)(lds + (bufoff) + ldsw + _i * 8192), 16, 0, 0); } while (0)
; #define PG8_WAIT_V(n) asm volatile("s_waitcnt vmcnt(" #n ")" ::: "memory")
; #define PG8_WAIT_L(n) asm volatile("s_waitcnt lgkmcnt(" #n ")" ::: "memory")
; #define PG8_BAR __builtin_amdgcn_s_barrier()
; #define PG8_SCHED __builtin_amdgcn_sched_barrier(0)
; template <class Epi, class Sched, bool ALIGN_EPI = true, bool F8 = false>
; __device__ __forceinline__ void gemm_phase(PG8_LAS unsigned char* lds, const Sched& S, const Epi& E) {
;     ...
;         for (int t = 0; t < nt; t += 2) {
;             const bool last = (t == nt - 2);
;             if constexpr (Sched::GATHER) { if (last && has_next) S.a_off(nxt, Rs, Cs, voffAn); }
;             const char* a1 = cA + (size_t)(t + 1) * kstep;
;             const char* a2 = last ? nA : cA + (size_t)(t + 2) * kstep; const char* b2 = last ? nB : cB + (size_t)(t + 2) * kstepB;
;             const char* a3 = a2 + kstep; const char* b3 = b2 + kstepB;
;     ...
;             PG8_LDB(B0, 1, 0); PG8_LDB(B1, 1, 1); PG8_SCHED; PG8_LDA(At, 1, 0); PG8_STAGE(PG8_SA(0, 1), a2, vA2[1]);
;             PG8_WAIT_V(8); PG8_WAIT_L(0); PG8_BAR; PG8_MMA(0, 0, At, B0); PG8_MMA(0, 1, At, B1); PG8_BAR; PG8_SCHED;
;             PG8_LDA(At, 1, 1); PG8_STAGE(PG8_SB(1, 0), b3, voffB[0]); PG8_STAGE(PG8_SB(1, 1), b3, voffB[1]); PG8_STAGE(PG8_SA(1, 0), a3, vA2[0]);
;             PG8_WAIT_V(8); PG8_WAIT_L(0); PG8_BAR; PG8_MMA(1, 0, At, B0); PG8_MMA(1, 1, At, B1); PG8_BAR; PG8_SCHED;
;         }
	s_add_i32 s67, 0, 0x18000
	s_add_i32 s68, 0, 0x1c000
	v_add_u32_e32 v14, s67, v202
	v_add_u32_e32 v30, s68, v202
	ds_read_b128 v[2:5], v14
	ds_read_b128 v[6:9], v14 offset:1024
	ds_read_b128 v[10:13], v14 offset:2048
	ds_read_b128 v[14:17], v14 offset:3072
	ds_read_b128 v[18:21], v30
	ds_read_b128 v[22:25], v30 offset:1024
	ds_read_b128 v[26:29], v30 offset:2048
	ds_read_b128 v[30:33], v30 offset:3072
	s_mov_b32 m0, s48
	ds_read_b128 v[212:215], v209 offset:32768
	ds_read_b128 v[216:219], v209 offset:33792
	ds_read_b128 v[220:223], v209 offset:34816
	ds_read_b128 v[224:227], v209 offset:35840
	ds_read_b128 v[228:231], v209 offset:36864
	ds_read_b128 v[232:235], v209 offset:37888
	ds_read_b128 v[236:239], v209 offset:38912
	ds_read_b128 v[240:243], v209 offset:39936
	global_load_lds_dwordx4 v178, s[40:41]
	s_mov_b32 m0, s49
	s_nop 0
	global_load_lds_dwordx4 v180, s[40:41]
	s_waitcnt vmcnt(8)
	s_waitcnt lgkmcnt(0)
	s_setprio 1
	s_waitcnt lgkmcnt(0)
	v_mfma_scale_f32_16x16x128_f8f6f4 v[158:161], v[2:9], v[212:219], v[158:161], v210, v210 op_sel_hi:[0,0,0]
	v_mfma_scale_f32_16x16x128_f8f6f4 v[154:157], v[10:17], v[212:219], v[154:157], v210, v210 op_sel_hi:[0,0,0]
	v_mfma_scale_f32_16x16x128_f8f6f4 v[142:145], v[2:9], v[220:227], v[142:145], v210, v210 op_sel_hi:[0,0,0]
	v_mfma_scale_f32_16x16x128_f8f6f4 v[138:141], v[10:17], v[220:227], v[138:141], v210, v210 op_sel_hi:[0,0,0]
	v_mfma_scale_f32_16x16x128_f8f6f4 v[126:129], v[2:9], v[228:235], v[126:129], v210, v210 op_sel_hi:[0,0,0]
	v_mfma_scale_f32_16x16x128_f8f6f4 v[122:125], v[10:17], v[228:235], v[122:125], v210, v210 op_sel_hi:[0,0,0]
	v_mfma_scale_f32_16x16x128_f8f6f4 v[110:113], v[2:9], v[236:243], v[110:113], v210, v210 op_sel_hi:[0,0,0]
	v_mfma_scale_f32_16x16x128_f8f6f4 v[106:109], v[10:17], v[236:243], v[106:109], v210, v210 op_sel_hi:[0,0,0]
	s_nop 3
	s_setprio 0
	s_setprio 1
	v_mfma_scale_f32_16x16x128_f8f6f4 v[150:153], v[18:25], v[212:219], v[150:153], v210, v210 op_sel_hi:[0,0,0]
	v_mfma_scale_f32_16x16x128_f8f6f4 v[146:149], v[26:33], v[212:219], v[146:149], v210, v210 op_sel_hi:[0,0,0]
	v_mfma_scale_f32_16x16x128_f8f6f4 v[134:137], v[18:25], v[220:227], v[134:137], v210, v210 op_sel_hi:[0,0,0]
	v_mfma_scale_f32_16x16x128_f8f6f4 v[130:133], v[26:33], v[220:227], v[130:133], v210, v210 op_sel_hi:[0,0,0]
	v_mfma_scale_f32_16x16x128_f8f6f4 v[118:121], v[18:25], v[228:235], v[118:121], v210, v210 op_sel_hi:[0,0,0]
	v_mfma_scale_f32_16x16x128_f8f6f4 v[114:117], v[26:33], v[228:235], v[114:117], v210, v210 op_sel_hi:[0,0,0]
	v_mfma_scale_f32_16x16x128_f8f6f4 v[102:105], v[18:25], v[236:243], v[102:105], v210, v210 op_sel_hi:[0,0,0]
	v_mfma_scale_f32_16x16x128_f8f6f4 v[98:101], v[26:33], v[236:243], v[98:101], v210, v210 op_sel_hi:[0,0,0]
	s_nop 3
	s_setprio 0
	s_barrier
	s_add_u32 s30, s30, 0x8000
	s_addc_u32 s31, s31, 0
	s_add_i32 s40, s67, s45
	s_mov_b32 m0, s40
	ds_read_b128 v[212:215], v209 offset:49152
	ds_read_b128 v[216:219], v209 offset:50176
	ds_read_b128 v[220:223], v209 offset:51200
	ds_read_b128 v[224:227], v209 offset:52224
	ds_read_b128 v[228:231], v209 offset:53248
	ds_read_b128 v[232:235], v209 offset:54272
	ds_read_b128 v[236:239], v209 offset:55296
	ds_read_b128 v[240:243], v209 offset:56320
	global_load_lds_dwordx4 v164, s[30:31]
	s_add_i32 m0, s40, 0x2000
	s_add_i32 s40, s68, s45
	global_load_lds_dwordx4 v166, s[30:31]
	s_mov_b32 m0, s40
	s_nop 0
	global_load_lds_dwordx4 v168, s[30:31]
	s_add_i32 m0, s40, 0x2000
	s_nop 0
	global_load_lds_dwordx4 v172, s[30:31]
	s_mov_b32 m0, s52
	s_nop 0
	global_load_lds_dwordx4 v174, s[28:29]
	s_mov_b32 m0, s53
	s_nop 0
	global_load_lds_dwordx4 v176, s[28:29]
	s_waitcnt vmcnt(8)
	s_waitcnt lgkmcnt(0)
	s_setprio 1
	s_waitcnt lgkmcnt(0)
	v_mfma_scale_f32_16x16x128_f8f6f4 v[94:97], v[2:9], v[212:219], v[94:97], v210, v210 op_sel_hi:[0,0,0]
	v_mfma_scale_f32_16x16x128_f8f6f4 v[90:93], v[10:17], v[212:219], v[90:93], v210, v210 op_sel_hi:[0,0,0]
	v_mfma_scale_f32_16x16x128_f8f6f4 v[78:81], v[2:9], v[220:227], v[78:81], v210, v210 op_sel_hi:[0,0,0]
	v_mfma_scale_f32_16x16x128_f8f6f4 v[74:77], v[10:17], v[220:227], v[74:77], v210, v210 op_sel_hi:[0,0,0]
	v_mfma_scale_f32_16x16x128_f8f6f4 v[62:65], v[2:9], v[228:235], v[62:65], v210, v210 op_sel_hi:[0,0,0]
	v_mfma_scale_f32_16x16x128_f8f6f4 v[58:61], v[10:17], v[228:235], v[58:61], v210, v210 op_sel_hi:[0,0,0]
	v_mfma_scale_f32_16x16x128_f8f6f4 v[46:49], v[2:9], v[236:243], v[46:49], v210, v210 op_sel_hi:[0,0,0]
	v_mfma_scale_f32_16x16x128_f8f6f4 v[42:45], v[10:17], v[236:243], v[42:45], v210, v210 op_sel_hi:[0,0,0]
	s_nop 3
	s_setprio 0
	s_setprio 1
	v_mfma_scale_f32_16x16x128_f8f6f4 v[86:89], v[18:25], v[212:219], v[86:89], v210, v210 op_sel_hi:[0,0,0]
	v_mfma_scale_f32_16x16x128_f8f6f4 v[82:85], v[26:33], v[212:219], v[82:85], v210, v210 op_sel_hi:[0,0,0]
	v_mfma_scale_f32_16x16x128_f8f6f4 v[70:73], v[18:25], v[220:227], v[70:73], v210, v210 op_sel_hi:[0,0,0]
	v_mfma_scale_f32_16x16x128_f8f6f4 v[66:69], v[26:33], v[220:227], v[66:69], v210, v210 op_sel_hi:[0,0,0]
	v_mfma_scale_f32_16x16x128_f8f6f4 v[54:57], v[18:25], v[228:235], v[54:57], v210, v210 op_sel_hi:[0,0,0]
	v_mfma_scale_f32_16x16x128_f8f6f4 v[50:53], v[26:33], v[228:235], v[50:53], v210, v210 op_sel_hi:[0,0,0]
	v_mfma_scale_f32_16x16x128_f8f6f4 v[38:41], v[18:25], v[236:243], v[38:41], v210, v210 op_sel_hi:[0,0,0]
	v_mfma_scale_f32_16x16x128_f8f6f4 v[34:37], v[26:33], v[236:243], v[34:37], v210, v210 op_sel_hi:[0,0,0]
	s_nop 3
	s_setprio 0
	s_barrier
	s_add_i32 s21, s21, 2
	s_add_u32 s5, s5, 0x10000
	s_addc_u32 s19, s19, 0
	s_add_u32 s26, s26, 0x10000
	s_addc_u32 s27, s27, 0
	s_cmp_gt_u32 s21, 13
	s_cbranch_scc0 .LBB0_372
	s_branch .Lfx_9967
; #define PG8_STAGE(bufoff, gbase, voff) do { _Pragma("unroll") for (int _i = 0; _i < 2; ++_i) \
;         __builtin_amdgcn_global_load_lds((const unsigned*)((const char*)(gbase) + (voff)[_i]), (PG8_LAS unsigned*)(lds + (bufoff) + ldsw + _i * 8192), 16, 0, 0); } while (0)
; #define PG8_WAIT_V(n) asm volatile("s_waitcnt vmcnt(" #n ")" ::: "memory")
; #define PG8_WAIT_L(n) asm volatile("s_waitcnt lgkmcnt(" #n ")" ::: "memory")
; #define PG8_BAR __builtin_amdgcn_s_barrier()
; #define PG8_SCHED __builtin_amdgcn_sched_barrier(0)
; template <class Epi, class Sched, bool ALIGN_EPI = true, bool F8 = false>
; __device__ __forceinline__ void gemm_phase(PG8_LAS unsigned char* lds, const Sched& S, const Epi& E) {
;     ...
;             PG8_LDB(B0, 0, 0); PG8_LDB(B1, 0, 1); PG8_SCHED; PG8_LDA(At, 0, 0); PG8_STAGE(PG8_SA(1, 1), a1, voffA[1]);
;             PG8_WAIT_V(8); PG8_WAIT_L(0); PG8_BAR; PG8_MMA(0, 0, At, B0); PG8_MMA(0, 1, At, B1); PG8_BAR; PG8_SCHED;
;             PG8_LDA(At, 0, 1); PG8_STAGE(PG8_SB(0, 0), b2, voffB[0]); PG8_STAGE(PG8_SB(0, 1), b2, voffB[1]); PG8_STAGE(PG8_SA(0, 0), a2, vA2[0]);
;             PG8_WAIT_V(8); PG8_WAIT_L(0); PG8_BAR; PG8_MMA(1, 0, At, B0); PG8_MMA(1, 1, At, B1); PG8_BAR; PG8_SCHED;
;             PG8_LDB(B0, 1, 0); PG8_LDB(B1, 1, 1); PG8_SCHED; PG8_LDA(At, 1, 0); PG8_STAGE(PG8_SA(0, 1), a2, vA2[1]);
;             PG8_WAIT_V(8); PG8_WAIT_L(0); PG8_BAR; PG8_MMA(0, 0, At, B0); PG8_MMA(0, 1, At, B1); PG8_BAR; PG8_SCHED;
.Lh1e_9967:
.Lh1_372:
	ds_read_b128 v[18:21], v207
	ds_read_b128 v[22:25], v207 offset:1024
	ds_read_b128 v[26:29], v207 offset:2048
	ds_read_b128 v[30:33], v207 offset:3072
	ds_read_b128 v[2:5], v208
	ds_read_b128 v[6:9], v208 offset:1024
	ds_read_b128 v[10:13], v208 offset:2048
	ds_read_b128 v[14:17], v208 offset:3072
	s_add_u32 s28, s26, 0x8000
	s_addc_u32 s29, s27, 0
	s_cmp_eq_u32 s21, 12
	s_cselect_b32 s40, s22, s28
	s_cselect_b32 s41, s23, s29
	s_cselect_b32 s30, s24, s5
	s_cselect_b32 s31, s25, s19
	s_add_u32 s28, s40, 0x8000
	s_addc_u32 s29, s41, 0
	s_add_i32 m0, s46, 0xc000
	ds_read_b128 v[212:215], v209
	ds_read_b128 v[216:219], v209 offset:1024
	ds_read_b128 v[220:223], v209 offset:2048
	ds_read_b128 v[224:227], v209 offset:3072
	ds_read_b128 v[228:231], v209 offset:4096
	ds_read_b128 v[232:235], v209 offset:5120
	ds_read_b128 v[236:239], v209 offset:6144
	ds_read_b128 v[240:243], v209 offset:7168
	global_load_lds_dwordx4 v190, s[26:27]
	s_add_i32 m0, s46, 0xe000
	s_nop 0
	global_load_lds_dwordx4 v188, s[26:27]
	s_waitcnt vmcnt(8)
	s_waitcnt lgkmcnt(0)
	s_barrier
	s_setprio 2
	s_waitcnt lgkmcnt(0)
	v_mfma_scale_f32_16x16x128_f8f6f4 v[158:161], v[18:25], v[212:219], v[158:161], v210, v210 op_sel_hi:[0,0,0]
	v_mfma_scale_f32_16x16x128_f8f6f4 v[154:157], v[26:33], v[212:219], v[154:157], v210, v210 op_sel_hi:[0,0,0]
	v_mfma_scale_f32_16x16x128_f8f6f4 v[142:145], v[18:25], v[220:227], v[142:145], v210, v210 op_sel_hi:[0,0,0]
	v_mfma_scale_f32_16x16x128_f8f6f4 v[138:141], v[26:33], v[220:227], v[138:141], v210, v210 op_sel_hi:[0,0,0]
	v_mfma_scale_f32_16x16x128_f8f6f4 v[126:129], v[18:25], v[228:235], v[126:129], v210, v210 op_sel_hi:[0,0,0]
	v_mfma_scale_f32_16x16x128_f8f6f4 v[122:125], v[26:33], v[228:235], v[122:125], v210, v210 op_sel_hi:[0,0,0]
	v_mfma_scale_f32_16x16x128_f8f6f4 v[110:113], v[18:25], v[236:243], v[110:113], v210, v210 op_sel_hi:[0,0,0]
	v_mfma_scale_f32_16x16x128_f8f6f4 v[106:109], v[26:33], v[236:243], v[106:109], v210, v210 op_sel_hi:[0,0,0]
	s_nop 3
	s_setprio 0
	s_setprio 2
	v_mfma_scale_f32_16x16x128_f8f6f4 v[150:153], v[2:9], v[212:219], v[150:153], v210, v210 op_sel_hi:[0,0,0]
	v_mfma_scale_f32_16x16x128_f8f6f4 v[146:149], v[10:17], v[212:219], v[146:149], v210, v210 op_sel_hi:[0,0,0]
	v_mfma_scale_f32_16x16x128_f8f6f4 v[134:137], v[2:9], v[220:227], v[134:137], v210, v210 op_sel_hi:[0,0,0]
	v_mfma_scale_f32_16x16x128_f8f6f4 v[130:133], v[10:17], v[220:227], v[130:133], v210, v210 op_sel_hi:[0,0,0]
	v_mfma_scale_f32_16x16x128_f8f6f4 v[118:121], v[2:9], v[228:235], v[118:121], v210, v210 op_sel_hi:[0,0,0]
	v_mfma_scale_f32_16x16x128_f8f6f4 v[114:117], v[10:17], v[228:235], v[114:117], v210, v210 op_sel_hi:[0,0,0]
	v_mfma_scale_f32_16x16x128_f8f6f4 v[102:105], v[2:9], v[236:243], v[102:105], v210, v210 op_sel_hi:[0,0,0]
	v_mfma_scale_f32_16x16x128_f8f6f4 v[98:101], v[10:17], v[236:243], v[98:101], v210, v210 op_sel_hi:[0,0,0]
	s_nop 3
	s_setprio 0
	s_add_i32 s67, s62, s45
	s_mov_b32 m0, s67
	ds_read_b128 v[212:215], v209 offset:16384
	ds_read_b128 v[216:219], v209 offset:17408
	ds_read_b128 v[220:223], v209 offset:18432
	ds_read_b128 v[224:227], v209 offset:19456
	ds_read_b128 v[228:231], v209 offset:20480
	ds_read_b128 v[232:235], v209 offset:21504
	ds_read_b128 v[236:239], v209 offset:22528
	ds_read_b128 v[240:243], v209 offset:23552
	global_load_lds_dwordx4 v164, s[30:31]
	s_add_i32 m0, s67, 0x2000
	s_add_i32 s67, s63, s45
	global_load_lds_dwordx4 v166, s[30:31]
	s_add_u32 s98, s30, s8
	s_addc_u32 s99, s31, s9
	s_mov_b32 m0, s67
	s_nop 0
	global_load_lds_dwordx4 v164, s[98:99]
	s_add_u32 s100, s30, s8
	s_addc_u32 s101, s31, s9
	s_add_i32 m0, s67, 0x2000
	s_nop 0
	global_load_lds_dwordx4 v166, s[100:101]
	s_mov_b32 m0, s46
	s_nop 0
	global_load_lds_dwordx4 v174, s[40:41]
	s_mov_b32 m0, s47
	s_nop 0
	global_load_lds_dwordx4 v176, s[40:41]
	s_waitcnt vmcnt(8)
	s_waitcnt lgkmcnt(0)
	s_barrier
	s_setprio 2
	s_waitcnt lgkmcnt(0)
	v_mfma_scale_f32_16x16x128_f8f6f4 v[94:97], v[18:25], v[212:219], v[94:97], v210, v210 op_sel_hi:[0,0,0]
	v_mfma_scale_f32_16x16x128_f8f6f4 v[90:93], v[26:33], v[212:219], v[90:93], v210, v210 op_sel_hi:[0,0,0]
	v_mfma_scale_f32_16x16x128_f8f6f4 v[78:81], v[18:25], v[220:227], v[78:81], v210, v210 op_sel_hi:[0,0,0]
	v_mfma_scale_f32_16x16x128_f8f6f4 v[74:77], v[26:33], v[220:227], v[74:77], v210, v210 op_sel_hi:[0,0,0]
	v_mfma_scale_f32_16x16x128_f8f6f4 v[62:65], v[18:25], v[228:235], v[62:65], v210, v210 op_sel_hi:[0,0,0]
	v_mfma_scale_f32_16x16x128_f8f6f4 v[58:61], v[26:33], v[228:235], v[58:61], v210, v210 op_sel_hi:[0,0,0]
	v_mfma_scale_f32_16x16x128_f8f6f4 v[46:49], v[18:25], v[236:243], v[46:49], v210, v210 op_sel_hi:[0,0,0]
	v_mfma_scale_f32_16x16x128_f8f6f4 v[42:45], v[26:33], v[236:243], v[42:45], v210, v210 op_sel_hi:[0,0,0]
	s_nop 3
	s_setprio 0
	s_setprio 2
	v_mfma_scale_f32_16x16x128_f8f6f4 v[86:89], v[2:9], v[212:219], v[86:89], v210, v210 op_sel_hi:[0,0,0]
	v_mfma_scale_f32_16x16x128_f8f6f4 v[82:85], v[10:17], v[212:219], v[82:85], v210, v210 op_sel_hi:[0,0,0]
	v_mfma_scale_f32_16x16x128_f8f6f4 v[70:73], v[2:9], v[220:227], v[70:73], v210, v210 op_sel_hi:[0,0,0]
	v_mfma_scale_f32_16x16x128_f8f6f4 v[66:69], v[10:17], v[220:227], v[66:69], v210, v210 op_sel_hi:[0,0,0]
	v_mfma_scale_f32_16x16x128_f8f6f4 v[54:57], v[2:9], v[228:235], v[54:57], v210, v210 op_sel_hi:[0,0,0]
	v_mfma_scale_f32_16x16x128_f8f6f4 v[50:53], v[10:17], v[228:235], v[50:53], v210, v210 op_sel_hi:[0,0,0]
	v_mfma_scale_f32_16x16x128_f8f6f4 v[38:41], v[2:9], v[236:243], v[38:41], v210, v210 op_sel_hi:[0,0,0]
	v_mfma_scale_f32_16x16x128_f8f6f4 v[34:37], v[10:17], v[236:243], v[34:37], v210, v210 op_sel_hi:[0,0,0]
	s_nop 3
	s_setprio 0
	s_add_i32 s67, 0, 0x18000
	s_add_i32 s68, 0, 0x1c000
	v_add_u32_e32 v14, s67, v202
	v_add_u32_e32 v30, s68, v202
	ds_read_b128 v[2:5], v14
	ds_read_b128 v[6:9], v14 offset:1024
	ds_read_b128 v[10:13], v14 offset:2048
	ds_read_b128 v[14:17], v14 offset:3072
	ds_read_b128 v[18:21], v30
	ds_read_b128 v[22:25], v30 offset:1024
	ds_read_b128 v[26:29], v30 offset:2048
	ds_read_b128 v[30:33], v30 offset:3072
	s_mov_b32 m0, s48
	ds_read_b128 v[212:215], v209 offset:32768
	ds_read_b128 v[216:219], v209 offset:33792
	ds_read_b128 v[220:223], v209 offset:34816
	ds_read_b128 v[224:227], v209 offset:35840
	ds_read_b128 v[228:231], v209 offset:36864
	ds_read_b128 v[232:235], v209 offset:37888
	ds_read_b128 v[236:239], v209 offset:38912
	ds_read_b128 v[240:243], v209 offset:39936
	global_load_lds_dwordx4 v178, s[40:41]
	s_mov_b32 m0, s49
	s_nop 0
	global_load_lds_dwordx4 v180, s[40:41]
	s_waitcnt vmcnt(8)
	s_waitcnt lgkmcnt(0)
	s_barrier
; #define PG8_STAGE(bufoff, gbase, voff) do { _Pragma("unroll") for (int _i = 0; _i < 2; ++_i) \
;         __builtin_amdgcn_global_load_lds((const unsigned*)((const char*)(gbase) + (voff)[_i]), (PG8_LAS unsigned*)(lds + (bufoff) + ldsw + _i * 8192), 16, 0, 0); } while (0)
; #define PG8_WAIT_V(n) asm volatile("s_waitcnt vmcnt(" #n ")" ::: "memory")
; #define PG8_WAIT_L(n) asm volatile("s_waitcnt lgkmcnt(" #n ")" ::: "memory")
; #define PG8_BAR __builtin_amdgcn_s_barrier()
; #define PG8_SCHED __builtin_amdgcn_sched_barrier(0)
; template <class Epi, class Sched, bool ALIGN_EPI = true, bool F8 = false>
; __device__ __forceinline__ void gemm_phase(PG8_LAS unsigned char* lds, const Sched& S, const Epi& E) {
;     ...
;         for (int t = 0; t < nt; t += 2) {
;             const bool last = (t == nt - 2);
;             if constexpr (Sched::GATHER) { if (last && has_next) S.a_off(nxt, Rs, Cs, voffAn); }
;             const char* a1 = cA + (size_t)(t + 1) * kstep;
;             const char* a2 = last ? nA : cA + (size_t)(t + 2) * kstep; const char* b2 = last ? nB : cB + (size_t)(t + 2) * kstepB;
;             const char* a3 = a2 + kstep; const char* b3 = b2 + kstepB;
;     ...
;             PG8_WAIT_V(8); PG8_WAIT_L(0); PG8_BAR; PG8_MMA(0, 0, At, B0); PG8_MMA(0, 1, At, B1); PG8_BAR; PG8_SCHED;
;             PG8_LDA(At, 1, 1); PG8_STAGE(PG8_SB(1, 0), b3, voffB[0]); PG8_STAGE(PG8_SB(1, 1), b3, voffB[1]); PG8_STAGE(PG8_SA(1, 0), a3, vA2[0]);
;             PG8_WAIT_V(8); PG8_WAIT_L(0); PG8_BAR; PG8_MMA(1, 0, At, B0); PG8_MMA(1, 1, At, B1); PG8_BAR; PG8_SCHED;
;         }
	s_setprio 2
	s_waitcnt lgkmcnt(0)
	v_mfma_scale_f32_16x16x128_f8f6f4 v[158:161], v[2:9], v[212:219], v[158:161], v210, v210 op_sel_hi:[0,0,0]
	v_mfma_scale_f32_16x16x128_f8f6f4 v[154:157], v[10:17], v[212:219], v[154:157], v210, v210 op_sel_hi:[0,0,0]
	v_mfma_scale_f32_16x16x128_f8f6f4 v[142:145], v[2:9], v[220:227], v[142:145], v210, v210 op_sel_hi:[0,0,0]
	v_mfma_scale_f32_16x16x128_f8f6f4 v[138:141], v[10:17], v[220:227], v[138:141], v210, v210 op_sel_hi:[0,0,0]
	v_mfma_scale_f32_16x16x128_f8f6f4 v[126:129], v[2:9], v[228:235], v[126:129], v210, v210 op_sel_hi:[0,0,0]
	v_mfma_scale_f32_16x16x128_f8f6f4 v[122:125], v[10:17], v[228:235], v[122:125], v210, v210 op_sel_hi:[0,0,0]
	v_mfma_scale_f32_16x16x128_f8f6f4 v[110:113], v[2:9], v[236:243], v[110:113], v210, v210 op_sel_hi:[0,0,0]
	v_mfma_scale_f32_16x16x128_f8f6f4 v[106:109], v[10:17], v[236:243], v[106:109], v210, v210 op_sel_hi:[0,0,0]
	s_nop 3
	s_setprio 0
	s_setprio 2
	v_mfma_scale_f32_16x16x128_f8f6f4 v[150:153], v[18:25], v[212:219], v[150:153], v210, v210 op_sel_hi:[0,0,0]
	v_mfma_scale_f32_16x16x128_f8f6f4 v[146:149], v[26:33], v[212:219], v[146:149], v210, v210 op_sel_hi:[0,0,0]
	v_mfma_scale_f32_16x16x128_f8f6f4 v[134:137], v[18:25], v[220:227], v[134:137], v210, v210 op_sel_hi:[0,0,0]
	v_mfma_scale_f32_16x16x128_f8f6f4 v[130:133], v[26:33], v[220:227], v[130:133], v210, v210 op_sel_hi:[0,0,0]
	v_mfma_scale_f32_16x16x128_f8f6f4 v[118:121], v[18:25], v[228:235], v[118:121], v210, v210 op_sel_hi:[0,0,0]
	v_mfma_scale_f32_16x16x128_f8f6f4 v[114:117], v[26:33], v[228:235], v[114:117], v210, v210 op_sel_hi:[0,0,0]
	v_mfma_scale_f32_16x16x128_f8f6f4 v[102:105], v[18:25], v[236:243], v[102:105], v210, v210 op_sel_hi:[0,0,0]
	v_mfma_scale_f32_16x16x128_f8f6f4 v[98:101], v[26:33], v[236:243], v[98:101], v210, v210 op_sel_hi:[0,0,0]
	s_nop 3
	s_setprio 0
	s_add_u32 s30, s30, 0x8000
	s_addc_u32 s31, s31, 0
	s_add_i32 s40, s67, s45
	s_mov_b32 m0, s40
	ds_read_b128 v[212:215], v209 offset:49152
	ds_read_b128 v[216:219], v209 offset:50176
	ds_read_b128 v[220:223], v209 offset:51200
	ds_read_b128 v[224:227], v209 offset:52224
	ds_read_b128 v[228:231], v209 offset:53248
	ds_read_b128 v[232:235], v209 offset:54272
	ds_read_b128 v[236:239], v209 offset:55296
	ds_read_b128 v[240:243], v209 offset:56320
	global_load_lds_dwordx4 v164, s[30:31]
	s_add_i32 m0, s40, 0x2000
	s_add_i32 s40, s68, s45
	global_load_lds_dwordx4 v166, s[30:31]
	s_mov_b32 m0, s40
	s_nop 0
	global_load_lds_dwordx4 v168, s[30:31]
	s_add_i32 m0, s40, 0x2000
	s_nop 0
	global_load_lds_dwordx4 v172, s[30:31]
	s_mov_b32 m0, s52
	s_nop 0
	global_load_lds_dwordx4 v174, s[28:29]
	s_mov_b32 m0, s53
	s_nop 0
	global_load_lds_dwordx4 v176, s[28:29]
	s_waitcnt vmcnt(8)
	s_waitcnt lgkmcnt(0)
	s_barrier
	s_setprio 2
	s_waitcnt lgkmcnt(0)
	v_mfma_scale_f32_16x16x128_f8f6f4 v[94:97], v[2:9], v[212:219], v[94:97], v210, v210 op_sel_hi:[0,0,0]
	v_mfma_scale_f32_16x16x128_f8f6f4 v[90:93], v[10:17], v[212:219], v[90:93], v210, v210 op_sel_hi:[0,0,0]
	v_mfma_scale_f32_16x16x128_f8f6f4 v[78:81], v[2:9], v[220:227], v[78:81], v210, v210 op_sel_hi:[0,0,0]
	v_mfma_scale_f32_16x16x128_f8f6f4 v[74:77], v[10:17], v[220:227], v[74:77], v210, v210 op_sel_hi:[0,0,0]
	v_mfma_scale_f32_16x16x128_f8f6f4 v[62:65], v[2:9], v[228:235], v[62:65], v210, v210 op_sel_hi:[0,0,0]
	v_mfma_scale_f32_16x16x128_f8f6f4 v[58:61], v[10:17], v[228:235], v[58:61], v210, v210 op_sel_hi:[0,0,0]
	v_mfma_scale_f32_16x16x128_f8f6f4 v[46:49], v[2:9], v[236:243], v[46:49], v210, v210 op_sel_hi:[0,0,0]
	v_mfma_scale_f32_16x16x128_f8f6f4 v[42:45], v[10:17], v[236:243], v[42:45], v210, v210 op_sel_hi:[0,0,0]
	s_nop 3
	s_setprio 0
	s_setprio 2
	v_mfma_scale_f32_16x16x128_f8f6f4 v[86:89], v[18:25], v[212:219], v[86:89], v210, v210 op_sel_hi:[0,0,0]
	v_mfma_scale_f32_16x16x128_f8f6f4 v[82:85], v[26:33], v[212:219], v[82:85], v210, v210 op_sel_hi:[0,0,0]
	v_mfma_scale_f32_16x16x128_f8f6f4 v[70:73], v[18:25], v[220:227], v[70:73], v210, v210 op_sel_hi:[0,0,0]
	v_mfma_scale_f32_16x16x128_f8f6f4 v[66:69], v[26:33], v[220:227], v[66:69], v210, v210 op_sel_hi:[0,0,0]
	v_mfma_scale_f32_16x16x128_f8f6f4 v[54:57], v[18:25], v[228:235], v[54:57], v210, v210 op_sel_hi:[0,0,0]
	v_mfma_scale_f32_16x16x128_f8f6f4 v[50:53], v[26:33], v[228:235], v[50:53], v210, v210 op_sel_hi:[0,0,0]
	v_mfma_scale_f32_16x16x128_f8f6f4 v[38:41], v[18:25], v[236:243], v[38:41], v210, v210 op_sel_hi:[0,0,0]
	v_mfma_scale_f32_16x16x128_f8f6f4 v[34:37], v[26:33], v[236:243], v[34:37], v210, v210 op_sel_hi:[0,0,0]
	s_nop 3
	s_setprio 0
	s_add_i32 s21, s21, 2
	s_add_u32 s5, s5, 0x10000
	s_addc_u32 s19, s19, 0
	s_add_u32 s26, s26, 0x10000
	s_addc_u32 s27, s27, 0
	s_cmp_gt_u32 s21, 13
	s_cbranch_scc0 .Lh1_372

; __device__ __forceinline__ unsigned pk_bf16(float lo, float hi) { const bf16x2_t r = __builtin_convertvector((f32x2){lo, hi}, bf16x2_t); return __builtin_bit_cast(unsigned, r); }
; __device__ __forceinline__ void st16_bf16(bf16* dst, f32x4 a, f32x4 b, f32x4 c, f32x4 d) {
;     u32x4 w0, w1; w0.x = pk_bf16(a[0], a[1]); w0.y = pk_bf16(a[2], a[3]); w0.z = pk_bf16(b[0], b[1]); w0.w = pk_bf16(b[2], b[3]);
;     w1.x = pk_bf16(c[0], c[1]); w1.y = pk_bf16(c[2], c[3]); w1.z = pk_bf16(d[0], d[1]); w1.w = pk_bf16(d[2], d[3]);
;     *(u32x4*)dst = w0; *(u32x4*)(dst + 8) = w1; }
;     __device__ __forceinline__ void operator()(AccRef acc, const GUnit& u, int wr, int wc, int fr, int fq) const {
;     ...
; #pragma unroll
;         for (int ai = 0; ai < 2; ++ai)
; #pragma unroll
;             for (int m = 0; m < 4; ++m) { const int row = pm * 256 + ai * 128 + wr * 64 + m * 16 + fr; bf16* dst;
;                 if (pn < 4) dst = UF + (size_t)row * FW + col;
;                 else { const int g = (col - FW) >> 4, b = row >> 13, t = row & (SEQ - 1); dst = A2 + ((size_t)((g * 4 + b) * NCH + NCTXCH + (t >> 5)) * A2LD + (t & 31) * 16); }
;                 constexpr float SC = S8 ? W8_INV : 1.0f; st16_bf16(dst, acc[ai][0][m][0] * SC, acc[ai][0][m][1] * SC, acc[ai][1][m][0] * SC, acc[ai][1][m][1] * SC); }
.LBB0_379:
	v_pk_mul_f32 v[8:9], v[160:161], s[16:17] op_sel_hi:[1,0]
	v_pk_mul_f32 v[12:13], v[158:159], s[16:17] op_sel_hi:[1,0]
	v_pk_mul_f32 v[16:17], v[156:157], s[16:17] op_sel_hi:[1,0]
	v_pk_mul_f32 v[14:15], v[154:155], s[16:17] op_sel_hi:[1,0]
	v_cndmask_b32_e64 v5, 0, 1, s[26:27]
	v_pk_mul_f32 v[18:19], v[152:153], s[16:17] op_sel_hi:[1,0]
	v_pk_mul_f32 v[20:21], v[150:151], s[16:17] op_sel_hi:[1,0]
	v_pk_mul_f32 v[22:23], v[148:149], s[16:17] op_sel_hi:[1,0]
	v_pk_mul_f32 v[24:25], v[146:147], s[16:17] op_sel_hi:[1,0]
	v_cvt_pk_bf16_f32 v12, v12, v13
	v_cvt_pk_bf16_f32 v13, v8, v9
	v_cvt_pk_bf16_f32 v14, v14, v15
	v_cvt_pk_bf16_f32 v15, v16, v17
	v_cmp_ne_u32_e64 s[4:5], 1, v5
	s_andn2_b64 vcc, exec, s[26:27]
	s_mov_b64 s[26:27], -1
	v_cvt_pk_bf16_f32 v16, v20, v21
	v_cvt_pk_bf16_f32 v17, v18, v19
	v_cvt_pk_bf16_f32 v18, v24, v25
	v_cvt_pk_bf16_f32 v19, v22, v23
	global_store_dwordx4 v[6:7], v[12:15], off
	global_store_dwordx4 v[6:7], v[16:19], off offset:16
	s_cbranch_vccnz .LBB0_381
	s_lshr_b32 s21, s19, 5
	s_and_b32 s21, s21, 0xfe
	v_add_u32_e32 v5, s21, v4
	v_mad_i64_i32 v[6:7], s[26:27], v5, s65, v[184:185]
	s_mov_b64 s[26:27], 0

; __device__ __forceinline__ unsigned pk_bf16(float lo, float hi) { const bf16x2_t r = __builtin_convertvector((f32x2){lo, hi}, bf16x2_t); return __builtin_bit_cast(unsigned, r); }
; __device__ __forceinline__ void st16_bf16(bf16* dst, f32x4 a, f32x4 b, f32x4 c, f32x4 d) {
;     u32x4 w0, w1; w0.x = pk_bf16(a[0], a[1]); w0.y = pk_bf16(a[2], a[3]); w0.z = pk_bf16(b[0], b[1]); w0.w = pk_bf16(b[2], b[3]);
;     w1.x = pk_bf16(c[0], c[1]); w1.y = pk_bf16(c[2], c[3]); w1.z = pk_bf16(d[0], d[1]); w1.w = pk_bf16(d[2], d[3]);
;     *(u32x4*)dst = w0; *(u32x4*)(dst + 8) = w1; }
;     __device__ __forceinline__ void operator()(AccRef acc, const GUnit& u, int wr, int wc, int fr, int fq) const {
;     ...
; #pragma unroll
;         for (int ai = 0; ai < 2; ++ai)
; #pragma unroll
;             for (int m = 0; m < 4; ++m) { const int row = pm * 256 + ai * 128 + wr * 64 + m * 16 + fr; bf16* dst;
;                 if (pn < 4) dst = UF + (size_t)row * FW + col;
;                 else { const int g = (col - FW) >> 4, b = row >> 13, t = row & (SEQ - 1); dst = A2 + ((size_t)((g * 4 + b) * NCH + NCTXCH + (t >> 5)) * A2LD + (t & 31) * 16); }
;                 constexpr float SC = S8 ? W8_INV : 1.0f; st16_bf16(dst, acc[ai][0][m][0] * SC, acc[ai][0][m][1] * SC, acc[ai][1][m][0] * SC, acc[ai][1][m][1] * SC); }
.LBB0_383:
	v_pk_mul_f32 v[8:9], v[144:145], s[16:17] op_sel_hi:[1,0]
	v_pk_mul_f32 v[12:13], v[142:143], s[16:17] op_sel_hi:[1,0]
	v_pk_mul_f32 v[16:17], v[140:141], s[16:17] op_sel_hi:[1,0]
	v_pk_mul_f32 v[14:15], v[138:139], s[16:17] op_sel_hi:[1,0]
	v_pk_mul_f32 v[18:19], v[136:137], s[16:17] op_sel_hi:[1,0]
	v_pk_mul_f32 v[20:21], v[134:135], s[16:17] op_sel_hi:[1,0]
	v_pk_mul_f32 v[22:23], v[132:133], s[16:17] op_sel_hi:[1,0]
	v_pk_mul_f32 v[24:25], v[130:131], s[16:17] op_sel_hi:[1,0]
	v_cvt_pk_bf16_f32 v12, v12, v13
	v_cvt_pk_bf16_f32 v13, v8, v9
	v_cvt_pk_bf16_f32 v14, v14, v15
	v_cvt_pk_bf16_f32 v15, v16, v17
	v_or_b32_e32 v8, s19, v204
	s_and_b64 vcc, exec, s[4:5]
	s_mov_b64 s[26:27], -1
	v_cvt_pk_bf16_f32 v16, v20, v21
	v_cvt_pk_bf16_f32 v17, v18, v19
	v_cvt_pk_bf16_f32 v18, v24, v25
	v_cvt_pk_bf16_f32 v19, v22, v23
	global_store_dwordx4 v[6:7], v[12:15], off
	global_store_dwordx4 v[6:7], v[16:19], off offset:16
	s_cbranch_vccnz .LBB0_385
	v_bfe_u32 v5, v8, 5, 8
	v_add_u32_e32 v5, v4, v5
	v_mad_i64_i32 v[6:7], s[26:27], v5, s65, v[182:183]
	s_mov_b64 s[26:27], 0

; __device__ __forceinline__ unsigned pk_bf16(float lo, float hi) { const bf16x2_t r = __builtin_convertvector((f32x2){lo, hi}, bf16x2_t); return __builtin_bit_cast(unsigned, r); }
; __device__ __forceinline__ void st16_bf16(bf16* dst, f32x4 a, f32x4 b, f32x4 c, f32x4 d) {
;     u32x4 w0, w1; w0.x = pk_bf16(a[0], a[1]); w0.y = pk_bf16(a[2], a[3]); w0.z = pk_bf16(b[0], b[1]); w0.w = pk_bf16(b[2], b[3]);
;     w1.x = pk_bf16(c[0], c[1]); w1.y = pk_bf16(c[2], c[3]); w1.z = pk_bf16(d[0], d[1]); w1.w = pk_bf16(d[2], d[3]);
;     *(u32x4*)dst = w0; *(u32x4*)(dst + 8) = w1; }
;     __device__ __forceinline__ void operator()(AccRef acc, const GUnit& u, int wr, int wc, int fr, int fq) const {
;     ...
; #pragma unroll
;         for (int ai = 0; ai < 2; ++ai)
; #pragma unroll
;             for (int m = 0; m < 4; ++m) { const int row = pm * 256 + ai * 128 + wr * 64 + m * 16 + fr; bf16* dst;
;                 if (pn < 4) dst = UF + (size_t)row * FW + col;
;                 else { const int g = (col - FW) >> 4, b = row >> 13, t = row & (SEQ - 1); dst = A2 + ((size_t)((g * 4 + b) * NCH + NCTXCH + (t >> 5)) * A2LD + (t & 31) * 16); }
;                 constexpr float SC = S8 ? W8_INV : 1.0f; st16_bf16(dst, acc[ai][0][m][0] * SC, acc[ai][0][m][1] * SC, acc[ai][1][m][0] * SC, acc[ai][1][m][1] * SC); }
.LBB0_387:
	v_pk_mul_f32 v[8:9], v[128:129], s[16:17] op_sel_hi:[1,0]
	v_pk_mul_f32 v[12:13], v[126:127], s[16:17] op_sel_hi:[1,0]
	v_pk_mul_f32 v[16:17], v[124:125], s[16:17] op_sel_hi:[1,0]
	v_pk_mul_f32 v[14:15], v[122:123], s[16:17] op_sel_hi:[1,0]
	v_pk_mul_f32 v[18:19], v[120:121], s[16:17] op_sel_hi:[1,0]
	v_pk_mul_f32 v[20:21], v[118:119], s[16:17] op_sel_hi:[1,0]
	v_pk_mul_f32 v[22:23], v[116:117], s[16:17] op_sel_hi:[1,0]
	v_pk_mul_f32 v[24:25], v[114:115], s[16:17] op_sel_hi:[1,0]
	v_cvt_pk_bf16_f32 v12, v12, v13
	v_cvt_pk_bf16_f32 v13, v8, v9
	v_cvt_pk_bf16_f32 v14, v14, v15
	v_cvt_pk_bf16_f32 v15, v16, v17
	v_or_b32_e32 v8, s19, v205
	s_and_b64 vcc, exec, s[4:5]
	s_mov_b64 s[26:27], -1
	v_cvt_pk_bf16_f32 v16, v20, v21
	v_cvt_pk_bf16_f32 v17, v18, v19
	v_cvt_pk_bf16_f32 v18, v24, v25
	v_cvt_pk_bf16_f32 v19, v22, v23
	global_store_dwordx4 v[6:7], v[12:15], off
	global_store_dwordx4 v[6:7], v[16:19], off offset:16
	s_cbranch_vccnz .LBB0_389
	v_bfe_u32 v5, v8, 5, 8
	v_add_u32_e32 v4, v4, v5
	v_mad_i64_i32 v[6:7], s[26:27], v4, s65, v[186:187]
	s_mov_b64 s[26:27], 0

; __device__ __forceinline__ unsigned pk_bf16(float lo, float hi) { const bf16x2_t r = __builtin_convertvector((f32x2){lo, hi}, bf16x2_t); return __builtin_bit_cast(unsigned, r); }
; __device__ __forceinline__ void st16_bf16(bf16* dst, f32x4 a, f32x4 b, f32x4 c, f32x4 d) {
;     u32x4 w0, w1; w0.x = pk_bf16(a[0], a[1]); w0.y = pk_bf16(a[2], a[3]); w0.z = pk_bf16(b[0], b[1]); w0.w = pk_bf16(b[2], b[3]);
;     w1.x = pk_bf16(c[0], c[1]); w1.y = pk_bf16(c[2], c[3]); w1.z = pk_bf16(d[0], d[1]); w1.w = pk_bf16(d[2], d[3]);
;     *(u32x4*)dst = w0; *(u32x4*)(dst + 8) = w1; }
;     __device__ __forceinline__ void operator()(AccRef acc, const GUnit& u, int wr, int wc, int fr, int fq) const {
;     ...
; #pragma unroll
;         for (int ai = 0; ai < 2; ++ai)
; #pragma unroll
;             for (int m = 0; m < 4; ++m) { const int row = pm * 256 + ai * 128 + wr * 64 + m * 16 + fr; bf16* dst;
;                 if (pn < 4) dst = UF + (size_t)row * FW + col;
;                 else { const int g = (col - FW) >> 4, b = row >> 13, t = row & (SEQ - 1); dst = A2 + ((size_t)((g * 4 + b) * NCH + NCTXCH + (t >> 5)) * A2LD + (t & 31) * 16); }
;                 constexpr float SC = S8 ? W8_INV : 1.0f; st16_bf16(dst, acc[ai][0][m][0] * SC, acc[ai][0][m][1] * SC, acc[ai][1][m][0] * SC, acc[ai][1][m][1] * SC); }
.LBB0_391:
	s_addk_i32 s19, 0x80
	v_pk_mul_f32 v[4:5], v[112:113], s[16:17] op_sel_hi:[1,0]
	s_ashr_i32 s21, s19, 13
	v_cvt_pk_bf16_f32 v13, v4, v5
	v_add_u32_e32 v4, s21, v10
	v_pk_mul_f32 v[8:9], v[110:111], s[16:17] op_sel_hi:[1,0]
	v_pk_mul_f32 v[16:17], v[108:109], s[16:17] op_sel_hi:[1,0]
	v_pk_mul_f32 v[14:15], v[106:107], s[16:17] op_sel_hi:[1,0]
	v_mad_u64_u32 v[4:5], s[26:27], v4, s64, 8
	v_pk_mul_f32 v[18:19], v[104:105], s[16:17] op_sel_hi:[1,0]
	v_pk_mul_f32 v[20:21], v[102:103], s[16:17] op_sel_hi:[1,0]
	v_pk_mul_f32 v[22:23], v[100:101], s[16:17] op_sel_hi:[1,0]
	v_pk_mul_f32 v[24:25], v[98:99], s[16:17] op_sel_hi:[1,0]
	v_cvt_pk_bf16_f32 v12, v8, v9
	v_cvt_pk_bf16_f32 v14, v14, v15
	v_cvt_pk_bf16_f32 v15, v16, v17
	s_and_b64 vcc, exec, s[4:5]
	s_mov_b64 s[26:27], -1
	v_cvt_pk_bf16_f32 v16, v20, v21
	v_cvt_pk_bf16_f32 v17, v18, v19
	v_cvt_pk_bf16_f32 v18, v24, v25
	v_cvt_pk_bf16_f32 v19, v22, v23
	global_store_dwordx4 v[6:7], v[12:15], off
	global_store_dwordx4 v[6:7], v[16:19], off offset:16
	s_cbranch_vccnz .LBB0_393
	s_lshr_b32 s21, s19, 5
	s_and_b32 s21, s21, 0xfe
	v_add_u32_e32 v5, s21, v4
	v_mad_i64_i32 v[6:7], s[26:27], v5, s65, v[182:183]
	s_mov_b64 s[26:27], 0

; __device__ __forceinline__ unsigned pk_bf16(float lo, float hi) { const bf16x2_t r = __builtin_convertvector((f32x2){lo, hi}, bf16x2_t); return __builtin_bit_cast(unsigned, r); }
; __device__ __forceinline__ void st16_bf16(bf16* dst, f32x4 a, f32x4 b, f32x4 c, f32x4 d) {
;     u32x4 w0, w1; w0.x = pk_bf16(a[0], a[1]); w0.y = pk_bf16(a[2], a[3]); w0.z = pk_bf16(b[0], b[1]); w0.w = pk_bf16(b[2], b[3]);
;     w1.x = pk_bf16(c[0], c[1]); w1.y = pk_bf16(c[2], c[3]); w1.z = pk_bf16(d[0], d[1]); w1.w = pk_bf16(d[2], d[3]);
;     *(u32x4*)dst = w0; *(u32x4*)(dst + 8) = w1; }
;     __device__ __forceinline__ void operator()(AccRef acc, const GUnit& u, int wr, int wc, int fr, int fq) const {
;     ...
; #pragma unroll
;         for (int ai = 0; ai < 2; ++ai)
; #pragma unroll
;             for (int m = 0; m < 4; ++m) { const int row = pm * 256 + ai * 128 + wr * 64 + m * 16 + fr; bf16* dst;
;                 if (pn < 4) dst = UF + (size_t)row * FW + col;
;                 else { const int g = (col - FW) >> 4, b = row >> 13, t = row & (SEQ - 1); dst = A2 + ((size_t)((g * 4 + b) * NCH + NCTXCH + (t >> 5)) * A2LD + (t & 31) * 16); }
;                 constexpr float SC = S8 ? W8_INV : 1.0f; st16_bf16(dst, acc[ai][0][m][0] * SC, acc[ai][0][m][1] * SC, acc[ai][1][m][0] * SC, acc[ai][1][m][1] * SC); }
.LBB0_395:
	v_pk_mul_f32 v[10:11], v[96:97], s[16:17] op_sel_hi:[1,0]
	v_pk_mul_f32 v[8:9], v[94:95], s[16:17] op_sel_hi:[1,0]
	v_pk_mul_f32 v[12:13], v[92:93], s[16:17] op_sel_hi:[1,0]
	v_pk_mul_f32 v[14:15], v[90:91], s[16:17] op_sel_hi:[1,0]
	v_pk_mul_f32 v[16:17], v[88:89], s[16:17] op_sel_hi:[1,0]
	v_pk_mul_f32 v[18:19], v[86:87], s[16:17] op_sel_hi:[1,0]
	v_pk_mul_f32 v[20:21], v[84:85], s[16:17] op_sel_hi:[1,0]
	v_pk_mul_f32 v[22:23], v[82:83], s[16:17] op_sel_hi:[1,0]
	v_cvt_pk_bf16_f32 v8, v8, v9
	v_cvt_pk_bf16_f32 v9, v10, v11
	v_cvt_pk_bf16_f32 v10, v14, v15
	v_cvt_pk_bf16_f32 v11, v12, v13
	s_and_b64 vcc, exec, s[4:5]
	s_mov_b64 s[26:27], -1
	v_cvt_pk_bf16_f32 v12, v18, v19
	v_cvt_pk_bf16_f32 v13, v16, v17
	v_cvt_pk_bf16_f32 v14, v22, v23
	v_cvt_pk_bf16_f32 v15, v20, v21
	global_store_dwordx4 v[6:7], v[8:11], off
	global_store_dwordx4 v[6:7], v[12:15], off offset:16
	s_cbranch_vccnz .LBB0_397
	s_lshr_b32 s21, s19, 5
	s_and_b32 s21, s21, 0xfe
	v_add_u32_e32 v5, s21, v4
	v_mad_i64_i32 v[6:7], s[26:27], v5, s65, v[184:185]
	s_mov_b64 s[26:27], 0

; __device__ __forceinline__ unsigned pk_bf16(float lo, float hi) { const bf16x2_t r = __builtin_convertvector((f32x2){lo, hi}, bf16x2_t); return __builtin_bit_cast(unsigned, r); }
; __device__ __forceinline__ void st16_bf16(bf16* dst, f32x4 a, f32x4 b, f32x4 c, f32x4 d) {
;     u32x4 w0, w1; w0.x = pk_bf16(a[0], a[1]); w0.y = pk_bf16(a[2], a[3]); w0.z = pk_bf16(b[0], b[1]); w0.w = pk_bf16(b[2], b[3]);
;     w1.x = pk_bf16(c[0], c[1]); w1.y = pk_bf16(c[2], c[3]); w1.z = pk_bf16(d[0], d[1]); w1.w = pk_bf16(d[2], d[3]);
;     *(u32x4*)dst = w0; *(u32x4*)(dst + 8) = w1; }
;     __device__ __forceinline__ void operator()(AccRef acc, const GUnit& u, int wr, int wc, int fr, int fq) const {
;     ...
; #pragma unroll
;         for (int ai = 0; ai < 2; ++ai)
; #pragma unroll
;             for (int m = 0; m < 4; ++m) { const int row = pm * 256 + ai * 128 + wr * 64 + m * 16 + fr; bf16* dst;
;                 if (pn < 4) dst = UF + (size_t)row * FW + col;
;                 else { const int g = (col - FW) >> 4, b = row >> 13, t = row & (SEQ - 1); dst = A2 + ((size_t)((g * 4 + b) * NCH + NCTXCH + (t >> 5)) * A2LD + (t & 31) * 16); }
;                 constexpr float SC = S8 ? W8_INV : 1.0f; st16_bf16(dst, acc[ai][0][m][0] * SC, acc[ai][0][m][1] * SC, acc[ai][1][m][0] * SC, acc[ai][1][m][1] * SC); }
.LBB0_399:
	v_pk_mul_f32 v[10:11], v[80:81], s[16:17] op_sel_hi:[1,0]
	v_pk_mul_f32 v[8:9], v[78:79], s[16:17] op_sel_hi:[1,0]
	v_pk_mul_f32 v[12:13], v[76:77], s[16:17] op_sel_hi:[1,0]
	v_pk_mul_f32 v[14:15], v[74:75], s[16:17] op_sel_hi:[1,0]
	v_pk_mul_f32 v[16:17], v[72:73], s[16:17] op_sel_hi:[1,0]
	v_pk_mul_f32 v[18:19], v[70:71], s[16:17] op_sel_hi:[1,0]
	v_pk_mul_f32 v[20:21], v[68:69], s[16:17] op_sel_hi:[1,0]
	v_pk_mul_f32 v[22:23], v[66:67], s[16:17] op_sel_hi:[1,0]
	v_cvt_pk_bf16_f32 v8, v8, v9
	v_cvt_pk_bf16_f32 v9, v10, v11
	v_cvt_pk_bf16_f32 v10, v14, v15
	v_cvt_pk_bf16_f32 v11, v12, v13
	v_cvt_pk_bf16_f32 v12, v18, v19
	v_cvt_pk_bf16_f32 v13, v16, v17
	v_cvt_pk_bf16_f32 v14, v22, v23
	v_cvt_pk_bf16_f32 v15, v20, v21
	global_store_dwordx4 v[6:7], v[8:11], off
	global_store_dwordx4 v[6:7], v[12:15], off offset:16
	s_and_b64 vcc, exec, s[4:5]
	v_or_b32_e32 v8, s19, v204
	s_mov_b64 s[26:27], -1
	s_cbranch_vccnz .LBB0_401
	v_bfe_u32 v5, v8, 5, 8
	v_add_u32_e32 v5, v4, v5
	v_mad_i64_i32 v[6:7], s[26:27], v5, s65, v[182:183]
	s_mov_b64 s[26:27], 0

; __device__ __forceinline__ unsigned pk_bf16(float lo, float hi) { const bf16x2_t r = __builtin_convertvector((f32x2){lo, hi}, bf16x2_t); return __builtin_bit_cast(unsigned, r); }
; __device__ __forceinline__ void st16_bf16(bf16* dst, f32x4 a, f32x4 b, f32x4 c, f32x4 d) {
;     u32x4 w0, w1; w0.x = pk_bf16(a[0], a[1]); w0.y = pk_bf16(a[2], a[3]); w0.z = pk_bf16(b[0], b[1]); w0.w = pk_bf16(b[2], b[3]);
;     w1.x = pk_bf16(c[0], c[1]); w1.y = pk_bf16(c[2], c[3]); w1.z = pk_bf16(d[0], d[1]); w1.w = pk_bf16(d[2], d[3]);
;     *(u32x4*)dst = w0; *(u32x4*)(dst + 8) = w1; }
;     __device__ __forceinline__ void operator()(AccRef acc, const GUnit& u, int wr, int wc, int fr, int fq) const {
;     ...
; #pragma unroll
;         for (int ai = 0; ai < 2; ++ai)
; #pragma unroll
;             for (int m = 0; m < 4; ++m) { const int row = pm * 256 + ai * 128 + wr * 64 + m * 16 + fr; bf16* dst;
;                 if (pn < 4) dst = UF + (size_t)row * FW + col;
;                 else { const int g = (col - FW) >> 4, b = row >> 13, t = row & (SEQ - 1); dst = A2 + ((size_t)((g * 4 + b) * NCH + NCTXCH + (t >> 5)) * A2LD + (t & 31) * 16); }
;                 constexpr float SC = S8 ? W8_INV : 1.0f; st16_bf16(dst, acc[ai][0][m][0] * SC, acc[ai][0][m][1] * SC, acc[ai][1][m][0] * SC, acc[ai][1][m][1] * SC); }
.LBB0_403:
	v_pk_mul_f32 v[10:11], v[64:65], s[16:17] op_sel_hi:[1,0]
	v_pk_mul_f32 v[8:9], v[62:63], s[16:17] op_sel_hi:[1,0]
	v_pk_mul_f32 v[12:13], v[60:61], s[16:17] op_sel_hi:[1,0]
	v_pk_mul_f32 v[14:15], v[58:59], s[16:17] op_sel_hi:[1,0]
	v_pk_mul_f32 v[16:17], v[56:57], s[16:17] op_sel_hi:[1,0]
	v_pk_mul_f32 v[18:19], v[54:55], s[16:17] op_sel_hi:[1,0]
	v_pk_mul_f32 v[20:21], v[52:53], s[16:17] op_sel_hi:[1,0]
	v_pk_mul_f32 v[22:23], v[50:51], s[16:17] op_sel_hi:[1,0]
	v_cvt_pk_bf16_f32 v8, v8, v9
	v_cvt_pk_bf16_f32 v9, v10, v11
	v_cvt_pk_bf16_f32 v10, v14, v15
	v_cvt_pk_bf16_f32 v11, v12, v13
	v_cvt_pk_bf16_f32 v12, v18, v19
	v_cvt_pk_bf16_f32 v13, v16, v17
	v_cvt_pk_bf16_f32 v14, v22, v23
	v_cvt_pk_bf16_f32 v15, v20, v21
	global_store_dwordx4 v[6:7], v[8:11], off
	global_store_dwordx4 v[6:7], v[12:15], off offset:16
	s_and_b64 vcc, exec, s[4:5]
	v_or_b32_e32 v8, s19, v205
	s_mov_b64 s[4:5], -1
	s_cbranch_vccnz .LBB0_405
	v_bfe_u32 v5, v8, 5, 8
	v_add_u32_e32 v4, v4, v5
	v_mad_i64_i32 v[6:7], s[4:5], v4, s65, v[186:187]
	s_mov_b64 s[4:5], 0

; __device__ __forceinline__ unsigned pk_bf16(float lo, float hi) { const bf16x2_t r = __builtin_convertvector((f32x2){lo, hi}, bf16x2_t); return __builtin_bit_cast(unsigned, r); }
; __device__ __forceinline__ void st16_bf16(bf16* dst, f32x4 a, f32x4 b, f32x4 c, f32x4 d) {
;     u32x4 w0, w1; w0.x = pk_bf16(a[0], a[1]); w0.y = pk_bf16(a[2], a[3]); w0.z = pk_bf16(b[0], b[1]); w0.w = pk_bf16(b[2], b[3]);
;     w1.x = pk_bf16(c[0], c[1]); w1.y = pk_bf16(c[2], c[3]); w1.z = pk_bf16(d[0], d[1]); w1.w = pk_bf16(d[2], d[3]);
;     *(u32x4*)dst = w0; *(u32x4*)(dst + 8) = w1; }
;     __device__ __forceinline__ void operator()(AccRef acc, const GUnit& u, int wr, int wc, int fr, int fq) const {
;     ...
; #pragma unroll
;         for (int ai = 0; ai < 2; ++ai)
; #pragma unroll
;             for (int m = 0; m < 4; ++m) { const int row = pm * 256 + ai * 128 + wr * 64 + m * 16 + fr; bf16* dst;
;                 if (pn < 4) dst = UF + (size_t)row * FW + col;
;                 else { const int g = (col - FW) >> 4, b = row >> 13, t = row & (SEQ - 1); dst = A2 + ((size_t)((g * 4 + b) * NCH + NCTXCH + (t >> 5)) * A2LD + (t & 31) * 16); }
;                 constexpr float SC = S8 ? W8_INV : 1.0f; st16_bf16(dst, acc[ai][0][m][0] * SC, acc[ai][0][m][1] * SC, acc[ai][1][m][0] * SC, acc[ai][1][m][1] * SC); }
.LBB0_407:
	v_pk_mul_f32 v[4:5], v[48:49], s[16:17] op_sel_hi:[1,0]
	v_pk_mul_f32 v[2:3], v[46:47], s[16:17] op_sel_hi:[1,0]
	v_pk_mul_f32 v[8:9], v[44:45], s[16:17] op_sel_hi:[1,0]
	v_pk_mul_f32 v[10:11], v[42:43], s[16:17] op_sel_hi:[1,0]
	v_pk_mul_f32 v[12:13], v[40:41], s[16:17] op_sel_hi:[1,0]
	v_pk_mul_f32 v[14:15], v[38:39], s[16:17] op_sel_hi:[1,0]
	v_pk_mul_f32 v[16:17], v[36:37], s[16:17] op_sel_hi:[1,0]
	v_pk_mul_f32 v[18:19], v[34:35], s[16:17] op_sel_hi:[1,0]
	v_cvt_pk_bf16_f32 v2, v2, v3
	v_cvt_pk_bf16_f32 v3, v4, v5
	v_cvt_pk_bf16_f32 v4, v10, v11
	v_cvt_pk_bf16_f32 v5, v8, v9
	s_andn2_b64 vcc, exec, s[0:1]
	s_mov_b64 s[0:1], -1
	v_cvt_pk_bf16_f32 v8, v14, v15
	v_cvt_pk_bf16_f32 v9, v12, v13
	v_cvt_pk_bf16_f32 v10, v18, v19
	v_cvt_pk_bf16_f32 v11, v16, v17
	global_store_dwordx4 v[6:7], v[2:5], off
	global_store_dwordx4 v[6:7], v[8:11], off offset:16
	s_cbranch_vccnz .LBB0_368
	s_andn2_b64 vcc, exec, s[10:11]
	s_cbranch_vccnz .LBB0_367
	s_branch .LBB0_367

; #define PG8_STAGE(bufoff, gbase, voff) do { _Pragma("unroll") for (int _i = 0; _i < 2; ++_i) \
;         __builtin_amdgcn_global_load_lds((const unsigned*)((const char*)(gbase) + (voff)[_i]), (PG8_LAS unsigned*)(lds + (bufoff) + ldsw + _i * 8192), 16, 0, 0); } while (0)
; #define PG8_WAIT_V(n) asm volatile("s_waitcnt vmcnt(" #n ")" ::: "memory")
; #define PG8_WAIT_L(n) asm volatile("s_waitcnt lgkmcnt(" #n ")" ::: "memory")
; #define PG8_BAR __builtin_amdgcn_s_barrier()
; #define PG8_SCHED __builtin_amdgcn_sched_barrier(0)
; template <class Epi, class Sched, bool ALIGN_EPI = true, bool F8 = false>
; __device__ __forceinline__ void gemm_phase(PG8_LAS unsigned char* lds, const Sched& S, const Epi& E) {
;     ...
;             PG8_LDB(B0, 0, 0); PG8_LDB(B1, 0, 1); PG8_SCHED; PG8_LDA(At, 0, 0); PG8_STAGE(PG8_SA(1, 1), a1, voffA[1]);
;             PG8_WAIT_V(8); PG8_WAIT_L(0); PG8_BAR; PG8_MMA(0, 0, At, B0); PG8_MMA(0, 1, At, B1); PG8_BAR; PG8_SCHED;
;             PG8_LDA(At, 0, 1); PG8_STAGE(PG8_SB(0, 0), b2, voffB[0]); PG8_STAGE(PG8_SB(0, 1), b2, voffB[1]); PG8_STAGE(PG8_SA(0, 0), a2, vA2[0]);
;             PG8_WAIT_V(8); PG8_WAIT_L(0); PG8_BAR; PG8_MMA(1, 0, At, B0); PG8_MMA(1, 1, At, B1); PG8_BAR; PG8_SCHED;
;             PG8_LDB(B0, 1, 0); PG8_LDB(B1, 1, 1); PG8_SCHED; PG8_LDA(At, 1, 0); PG8_STAGE(PG8_SA(0, 1), a2, vA2[1]);
;             PG8_WAIT_V(8); PG8_WAIT_L(0); PG8_BAR; PG8_MMA(0, 0, At, B0); PG8_MMA(0, 1, At, B1); PG8_BAR; PG8_SCHED;
.LBB0_428:
	ds_read_b128 v[18:21], v192
	ds_read_b128 v[22:25], v192 offset:1024
	ds_read_b128 v[26:29], v192 offset:2048
	ds_read_b128 v[30:33], v192 offset:3072
	ds_read_b128 v[2:5], v193
	ds_read_b128 v[6:9], v193 offset:1024
	ds_read_b128 v[10:13], v193 offset:2048
	ds_read_b128 v[14:17], v193 offset:3072
	s_add_u32 s26, s24, 0x8000
	s_addc_u32 s27, s25, 0
	s_cmp_eq_u32 s74, 12
	s_cselect_b32 s30, s20, s26
	s_cselect_b32 s31, s21, s27
	s_cselect_b32 s28, s22, s17
	s_cselect_b32 s29, s23, s19
	s_add_u32 s26, s30, 0x8000
	s_addc_u32 s27, s31, 0
	s_add_i32 m0, s48, 0xc000
	ds_read_b128 v[198:201], v194
	ds_read_b128 v[202:205], v194 offset:1024
	ds_read_b128 v[206:209], v194 offset:2048
	ds_read_b128 v[210:213], v194 offset:3072
	ds_read_b128 v[214:217], v194 offset:4096
	ds_read_b128 v[218:221], v194 offset:5120
	ds_read_b128 v[222:225], v194 offset:6144
	ds_read_b128 v[226:229], v194 offset:7168
	global_load_lds_dwordx4 v184, s[24:25]
	s_add_i32 m0, s48, 0xe000
	s_nop 0
	global_load_lds_dwordx4 v182, s[24:25]
	s_waitcnt vmcnt(8)
	s_waitcnt lgkmcnt(0)
	s_setprio 1
	s_waitcnt lgkmcnt(0)
	v_mfma_scale_f32_16x16x128_f8f6f4 v[158:161], v[18:25], v[198:205], v[158:161], v195, v195 op_sel_hi:[0,0,0]
	v_mfma_scale_f32_16x16x128_f8f6f4 v[154:157], v[26:33], v[198:205], v[154:157], v195, v195 op_sel_hi:[0,0,0]
	v_mfma_scale_f32_16x16x128_f8f6f4 v[142:145], v[18:25], v[206:213], v[142:145], v195, v195 op_sel_hi:[0,0,0]
	v_mfma_scale_f32_16x16x128_f8f6f4 v[138:141], v[26:33], v[206:213], v[138:141], v195, v195 op_sel_hi:[0,0,0]
	v_mfma_scale_f32_16x16x128_f8f6f4 v[126:129], v[18:25], v[214:221], v[126:129], v195, v195 op_sel_hi:[0,0,0]
	v_mfma_scale_f32_16x16x128_f8f6f4 v[122:125], v[26:33], v[214:221], v[122:125], v195, v195 op_sel_hi:[0,0,0]
	v_mfma_scale_f32_16x16x128_f8f6f4 v[110:113], v[18:25], v[222:229], v[110:113], v195, v195 op_sel_hi:[0,0,0]
	v_mfma_scale_f32_16x16x128_f8f6f4 v[106:109], v[26:33], v[222:229], v[106:109], v195, v195 op_sel_hi:[0,0,0]
	s_nop 3
	s_setprio 0
	s_setprio 1
	v_mfma_scale_f32_16x16x128_f8f6f4 v[150:153], v[2:9], v[198:205], v[150:153], v195, v195 op_sel_hi:[0,0,0]
	v_mfma_scale_f32_16x16x128_f8f6f4 v[146:149], v[10:17], v[198:205], v[146:149], v195, v195 op_sel_hi:[0,0,0]
	v_mfma_scale_f32_16x16x128_f8f6f4 v[134:137], v[2:9], v[206:213], v[134:137], v195, v195 op_sel_hi:[0,0,0]
	v_mfma_scale_f32_16x16x128_f8f6f4 v[130:133], v[10:17], v[206:213], v[130:133], v195, v195 op_sel_hi:[0,0,0]
	v_mfma_scale_f32_16x16x128_f8f6f4 v[118:121], v[2:9], v[214:221], v[118:121], v195, v195 op_sel_hi:[0,0,0]
	v_mfma_scale_f32_16x16x128_f8f6f4 v[114:117], v[10:17], v[214:221], v[114:117], v195, v195 op_sel_hi:[0,0,0]
	v_mfma_scale_f32_16x16x128_f8f6f4 v[102:105], v[2:9], v[222:229], v[102:105], v195, v195 op_sel_hi:[0,0,0]
	v_mfma_scale_f32_16x16x128_f8f6f4 v[98:101], v[10:17], v[222:229], v[98:101], v195, v195 op_sel_hi:[0,0,0]
	s_nop 3
	s_setprio 0
	s_barrier
	s_add_i32 s75, s65, s47
	s_mov_b32 m0, s75
	ds_read_b128 v[198:201], v194 offset:16384
	ds_read_b128 v[202:205], v194 offset:17408
	ds_read_b128 v[206:209], v194 offset:18432
	ds_read_b128 v[210:213], v194 offset:19456
	ds_read_b128 v[214:217], v194 offset:20480
	ds_read_b128 v[218:221], v194 offset:21504
	ds_read_b128 v[222:225], v194 offset:22528
	ds_read_b128 v[226:229], v194 offset:23552
	global_load_lds_dwordx4 v164, s[28:29]
	s_add_i32 m0, s75, 0x2000
	s_add_i32 s75, s66, s47
	global_load_lds_dwordx4 v166, s[28:29]
	s_add_u32 s98, s28, s4
	s_addc_u32 s99, s29, s5
	s_mov_b32 m0, s75
	s_nop 0
	global_load_lds_dwordx4 v164, s[98:99]
	s_add_u32 s100, s28, s4
	s_addc_u32 s101, s29, s5
	s_add_i32 m0, s75, 0x2000
	s_nop 0
	global_load_lds_dwordx4 v166, s[100:101]
	s_mov_b32 m0, s48
	s_nop 0
	global_load_lds_dwordx4 v174, s[30:31]
	s_mov_b32 m0, s49
	s_nop 0
	global_load_lds_dwordx4 v176, s[30:31]
	s_waitcnt vmcnt(8)
	s_waitcnt lgkmcnt(0)
	s_setprio 1
	s_waitcnt lgkmcnt(0)
	v_mfma_scale_f32_16x16x128_f8f6f4 v[94:97], v[18:25], v[198:205], v[94:97], v195, v195 op_sel_hi:[0,0,0]
	v_mfma_scale_f32_16x16x128_f8f6f4 v[90:93], v[26:33], v[198:205], v[90:93], v195, v195 op_sel_hi:[0,0,0]
	v_mfma_scale_f32_16x16x128_f8f6f4 v[78:81], v[18:25], v[206:213], v[78:81], v195, v195 op_sel_hi:[0,0,0]
	v_mfma_scale_f32_16x16x128_f8f6f4 v[74:77], v[26:33], v[206:213], v[74:77], v195, v195 op_sel_hi:[0,0,0]
	v_mfma_scale_f32_16x16x128_f8f6f4 v[62:65], v[18:25], v[214:221], v[62:65], v195, v195 op_sel_hi:[0,0,0]
	v_mfma_scale_f32_16x16x128_f8f6f4 v[58:61], v[26:33], v[214:221], v[58:61], v195, v195 op_sel_hi:[0,0,0]
	v_mfma_scale_f32_16x16x128_f8f6f4 v[46:49], v[18:25], v[222:229], v[46:49], v195, v195 op_sel_hi:[0,0,0]
	v_mfma_scale_f32_16x16x128_f8f6f4 v[42:45], v[26:33], v[222:229], v[42:45], v195, v195 op_sel_hi:[0,0,0]
	s_nop 3
	s_setprio 0
	s_setprio 1
	v_mfma_scale_f32_16x16x128_f8f6f4 v[86:89], v[2:9], v[198:205], v[86:89], v195, v195 op_sel_hi:[0,0,0]
	v_mfma_scale_f32_16x16x128_f8f6f4 v[82:85], v[10:17], v[198:205], v[82:85], v195, v195 op_sel_hi:[0,0,0]
	v_mfma_scale_f32_16x16x128_f8f6f4 v[70:73], v[2:9], v[206:213], v[70:73], v195, v195 op_sel_hi:[0,0,0]
	v_mfma_scale_f32_16x16x128_f8f6f4 v[66:69], v[10:17], v[206:213], v[66:69], v195, v195 op_sel_hi:[0,0,0]
	v_mfma_scale_f32_16x16x128_f8f6f4 v[54:57], v[2:9], v[214:221], v[54:57], v195, v195 op_sel_hi:[0,0,0]
	v_mfma_scale_f32_16x16x128_f8f6f4 v[50:53], v[10:17], v[214:221], v[50:53], v195, v195 op_sel_hi:[0,0,0]
	v_mfma_scale_f32_16x16x128_f8f6f4 v[38:41], v[2:9], v[222:229], v[38:41], v195, v195 op_sel_hi:[0,0,0]
	v_mfma_scale_f32_16x16x128_f8f6f4 v[34:37], v[10:17], v[222:229], v[34:37], v195, v195 op_sel_hi:[0,0,0]
	s_nop 3
	s_setprio 0
	s_barrier
; #define PG8_STAGE(bufoff, gbase, voff) do { _Pragma("unroll") for (int _i = 0; _i < 2; ++_i) \
;         __builtin_amdgcn_global_load_lds((const unsigned*)((const char*)(gbase) + (voff)[_i]), (PG8_LAS unsigned*)(lds + (bufoff) + ldsw + _i * 8192), 16, 0, 0); } while (0)
; #define PG8_WAIT_V(n) asm volatile("s_waitcnt vmcnt(" #n ")" ::: "memory")
; #define PG8_WAIT_L(n) asm volatile("s_waitcnt lgkmcnt(" #n ")" ::: "memory")
; #define PG8_BAR __builtin_amdgcn_s_barrier()
; #define PG8_SCHED __builtin_amdgcn_sched_barrier(0)
; template <class Epi, class Sched, bool ALIGN_EPI = true, bool F8 = false>
; __device__ __forceinline__ void gemm_phase(PG8_LAS unsigned char* lds, const Sched& S, const Epi& E) {
;     ...
;         for (int t = 0; t < nt; t += 2) {
;             const bool last = (t == nt - 2);
;             if constexpr (Sched::GATHER) { if (last && has_next) S.a_off(nxt, Rs, Cs, voffAn); }
;             const char* a1 = cA + (size_t)(t + 1) * kstep;
;             const char* a2 = last ? nA : cA + (size_t)(t + 2) * kstep; const char* b2 = last ? nB : cB + (size_t)(t + 2) * kstepB;
;             const char* a3 = a2 + kstep; const char* b3 = b2 + kstepB;
;     ...
;             PG8_LDB(B0, 1, 0); PG8_LDB(B1, 1, 1); PG8_SCHED; PG8_LDA(At, 1, 0); PG8_STAGE(PG8_SA(0, 1), a2, vA2[1]);
;             PG8_WAIT_V(8); PG8_WAIT_L(0); PG8_BAR; PG8_MMA(0, 0, At, B0); PG8_MMA(0, 1, At, B1); PG8_BAR; PG8_SCHED;
;             PG8_LDA(At, 1, 1); PG8_STAGE(PG8_SB(1, 0), b3, voffB[0]); PG8_STAGE(PG8_SB(1, 1), b3, voffB[1]); PG8_STAGE(PG8_SA(1, 0), a3, vA2[0]);
;             PG8_WAIT_V(8); PG8_WAIT_L(0); PG8_BAR; PG8_MMA(1, 0, At, B0); PG8_MMA(1, 1, At, B1); PG8_BAR; PG8_SCHED;
;         }
	s_add_i32 s75, 0, 0x18000
	s_add_i32 s76, 0, 0x1c000
	v_add_u32_e32 v14, s75, v191
	v_add_u32_e32 v30, s76, v191
	ds_read_b128 v[2:5], v14
	ds_read_b128 v[6:9], v14 offset:1024
	ds_read_b128 v[10:13], v14 offset:2048
	ds_read_b128 v[14:17], v14 offset:3072
	ds_read_b128 v[18:21], v30
	ds_read_b128 v[22:25], v30 offset:1024
	ds_read_b128 v[26:29], v30 offset:2048
	ds_read_b128 v[30:33], v30 offset:3072
	s_mov_b32 m0, s50
	ds_read_b128 v[198:201], v194 offset:32768
	ds_read_b128 v[202:205], v194 offset:33792
	ds_read_b128 v[206:209], v194 offset:34816
	ds_read_b128 v[210:213], v194 offset:35840
	ds_read_b128 v[214:217], v194 offset:36864
	ds_read_b128 v[218:221], v194 offset:37888
	ds_read_b128 v[222:225], v194 offset:38912
	ds_read_b128 v[226:229], v194 offset:39936
	global_load_lds_dwordx4 v178, s[30:31]
	s_mov_b32 m0, s51
	s_nop 0
	global_load_lds_dwordx4 v180, s[30:31]
	s_waitcnt vmcnt(8)
	s_waitcnt lgkmcnt(0)
	s_setprio 1
	s_waitcnt lgkmcnt(0)
	v_mfma_scale_f32_16x16x128_f8f6f4 v[158:161], v[2:9], v[198:205], v[158:161], v195, v195 op_sel_hi:[0,0,0]
	v_mfma_scale_f32_16x16x128_f8f6f4 v[154:157], v[10:17], v[198:205], v[154:157], v195, v195 op_sel_hi:[0,0,0]
	v_mfma_scale_f32_16x16x128_f8f6f4 v[142:145], v[2:9], v[206:213], v[142:145], v195, v195 op_sel_hi:[0,0,0]
	v_mfma_scale_f32_16x16x128_f8f6f4 v[138:141], v[10:17], v[206:213], v[138:141], v195, v195 op_sel_hi:[0,0,0]
	v_mfma_scale_f32_16x16x128_f8f6f4 v[126:129], v[2:9], v[214:221], v[126:129], v195, v195 op_sel_hi:[0,0,0]
	v_mfma_scale_f32_16x16x128_f8f6f4 v[122:125], v[10:17], v[214:221], v[122:125], v195, v195 op_sel_hi:[0,0,0]
	v_mfma_scale_f32_16x16x128_f8f6f4 v[110:113], v[2:9], v[222:229], v[110:113], v195, v195 op_sel_hi:[0,0,0]
	v_mfma_scale_f32_16x16x128_f8f6f4 v[106:109], v[10:17], v[222:229], v[106:109], v195, v195 op_sel_hi:[0,0,0]
	s_nop 3
	s_setprio 0
	s_setprio 1
	v_mfma_scale_f32_16x16x128_f8f6f4 v[150:153], v[18:25], v[198:205], v[150:153], v195, v195 op_sel_hi:[0,0,0]
	v_mfma_scale_f32_16x16x128_f8f6f4 v[146:149], v[26:33], v[198:205], v[146:149], v195, v195 op_sel_hi:[0,0,0]
	v_mfma_scale_f32_16x16x128_f8f6f4 v[134:137], v[18:25], v[206:213], v[134:137], v195, v195 op_sel_hi:[0,0,0]
	v_mfma_scale_f32_16x16x128_f8f6f4 v[130:133], v[26:33], v[206:213], v[130:133], v195, v195 op_sel_hi:[0,0,0]
	v_mfma_scale_f32_16x16x128_f8f6f4 v[118:121], v[18:25], v[214:221], v[118:121], v195, v195 op_sel_hi:[0,0,0]
	v_mfma_scale_f32_16x16x128_f8f6f4 v[114:117], v[26:33], v[214:221], v[114:117], v195, v195 op_sel_hi:[0,0,0]
	v_mfma_scale_f32_16x16x128_f8f6f4 v[102:105], v[18:25], v[222:229], v[102:105], v195, v195 op_sel_hi:[0,0,0]
	v_mfma_scale_f32_16x16x128_f8f6f4 v[98:101], v[26:33], v[222:229], v[98:101], v195, v195 op_sel_hi:[0,0,0]
	s_nop 3
	s_setprio 0
	s_barrier
	s_add_u32 s28, s28, 0x8000
	s_addc_u32 s29, s29, 0
	s_add_i32 s30, s75, s47
	s_mov_b32 m0, s30
	ds_read_b128 v[198:201], v194 offset:49152
	ds_read_b128 v[202:205], v194 offset:50176
	ds_read_b128 v[206:209], v194 offset:51200
	ds_read_b128 v[210:213], v194 offset:52224
	ds_read_b128 v[214:217], v194 offset:53248
	ds_read_b128 v[218:221], v194 offset:54272
	ds_read_b128 v[222:225], v194 offset:55296
	ds_read_b128 v[226:229], v194 offset:56320
	global_load_lds_dwordx4 v164, s[28:29]
	s_add_i32 m0, s30, 0x2000
	s_add_i32 s30, s76, s47
	global_load_lds_dwordx4 v166, s[28:29]
	s_mov_b32 m0, s30
	s_nop 0
	global_load_lds_dwordx4 v168, s[28:29]
	s_add_i32 m0, s30, 0x2000
	s_nop 0
	global_load_lds_dwordx4 v172, s[28:29]
	s_mov_b32 m0, s60
	s_nop 0
	global_load_lds_dwordx4 v174, s[26:27]
	s_mov_b32 m0, s61
	s_nop 0
	global_load_lds_dwordx4 v176, s[26:27]
	s_waitcnt vmcnt(8)
	s_waitcnt lgkmcnt(0)
	s_setprio 1
	s_waitcnt lgkmcnt(0)
	v_mfma_scale_f32_16x16x128_f8f6f4 v[94:97], v[2:9], v[198:205], v[94:97], v195, v195 op_sel_hi:[0,0,0]
	v_mfma_scale_f32_16x16x128_f8f6f4 v[90:93], v[10:17], v[198:205], v[90:93], v195, v195 op_sel_hi:[0,0,0]
	v_mfma_scale_f32_16x16x128_f8f6f4 v[78:81], v[2:9], v[206:213], v[78:81], v195, v195 op_sel_hi:[0,0,0]
	v_mfma_scale_f32_16x16x128_f8f6f4 v[74:77], v[10:17], v[206:213], v[74:77], v195, v195 op_sel_hi:[0,0,0]
	v_mfma_scale_f32_16x16x128_f8f6f4 v[62:65], v[2:9], v[214:221], v[62:65], v195, v195 op_sel_hi:[0,0,0]
	v_mfma_scale_f32_16x16x128_f8f6f4 v[58:61], v[10:17], v[214:221], v[58:61], v195, v195 op_sel_hi:[0,0,0]
	v_mfma_scale_f32_16x16x128_f8f6f4 v[46:49], v[2:9], v[222:229], v[46:49], v195, v195 op_sel_hi:[0,0,0]
	v_mfma_scale_f32_16x16x128_f8f6f4 v[42:45], v[10:17], v[222:229], v[42:45], v195, v195 op_sel_hi:[0,0,0]
	s_nop 3
	s_setprio 0
	s_setprio 1
	v_mfma_scale_f32_16x16x128_f8f6f4 v[86:89], v[18:25], v[198:205], v[86:89], v195, v195 op_sel_hi:[0,0,0]
	v_mfma_scale_f32_16x16x128_f8f6f4 v[82:85], v[26:33], v[198:205], v[82:85], v195, v195 op_sel_hi:[0,0,0]
	v_mfma_scale_f32_16x16x128_f8f6f4 v[70:73], v[18:25], v[206:213], v[70:73], v195, v195 op_sel_hi:[0,0,0]
	v_mfma_scale_f32_16x16x128_f8f6f4 v[66:69], v[26:33], v[206:213], v[66:69], v195, v195 op_sel_hi:[0,0,0]
	v_mfma_scale_f32_16x16x128_f8f6f4 v[54:57], v[18:25], v[214:221], v[54:57], v195, v195 op_sel_hi:[0,0,0]
	v_mfma_scale_f32_16x16x128_f8f6f4 v[50:53], v[26:33], v[214:221], v[50:53], v195, v195 op_sel_hi:[0,0,0]
	v_mfma_scale_f32_16x16x128_f8f6f4 v[38:41], v[18:25], v[222:229], v[38:41], v195, v195 op_sel_hi:[0,0,0]
	v_mfma_scale_f32_16x16x128_f8f6f4 v[34:37], v[26:33], v[222:229], v[34:37], v195, v195 op_sel_hi:[0,0,0]
	s_nop 3
	s_setprio 0
	s_barrier
	s_add_i32 s74, s74, 2
	s_add_u32 s17, s17, 0x10000
	s_addc_u32 s19, s19, 0
	s_add_u32 s24, s24, 0x10000
	s_addc_u32 s25, s25, 0
	s_cmp_gt_u32 s74, 13
	s_cbranch_scc0 .LBB0_428
	s_branch .Lfx_11141
; #define PG8_STAGE(bufoff, gbase, voff) do { _Pragma("unroll") for (int _i = 0; _i < 2; ++_i) \
;         __builtin_amdgcn_global_load_lds((const unsigned*)((const char*)(gbase) + (voff)[_i]), (PG8_LAS unsigned*)(lds + (bufoff) + ldsw + _i * 8192), 16, 0, 0); } while (0)
; #define PG8_WAIT_V(n) asm volatile("s_waitcnt vmcnt(" #n ")" ::: "memory")
; #define PG8_WAIT_L(n) asm volatile("s_waitcnt lgkmcnt(" #n ")" ::: "memory")
; #define PG8_BAR __builtin_amdgcn_s_barrier()
; #define PG8_SCHED __builtin_amdgcn_sched_barrier(0)
; template <class Epi, class Sched, bool ALIGN_EPI = true, bool F8 = false>
; __device__ __forceinline__ void gemm_phase(PG8_LAS unsigned char* lds, const Sched& S, const Epi& E) {
;     ...
;             PG8_LDB(B0, 0, 0); PG8_LDB(B1, 0, 1); PG8_SCHED; PG8_LDA(At, 0, 0); PG8_STAGE(PG8_SA(1, 1), a1, voffA[1]);
;             PG8_WAIT_V(8); PG8_WAIT_L(0); PG8_BAR; PG8_MMA(0, 0, At, B0); PG8_MMA(0, 1, At, B1); PG8_BAR; PG8_SCHED;
;             PG8_LDA(At, 0, 1); PG8_STAGE(PG8_SB(0, 0), b2, voffB[0]); PG8_STAGE(PG8_SB(0, 1), b2, voffB[1]); PG8_STAGE(PG8_SA(0, 0), a2, vA2[0]);
;             PG8_WAIT_V(8); PG8_WAIT_L(0); PG8_BAR; PG8_MMA(1, 0, At, B0); PG8_MMA(1, 1, At, B1); PG8_BAR; PG8_SCHED;
;             PG8_LDB(B0, 1, 0); PG8_LDB(B1, 1, 1); PG8_SCHED; PG8_LDA(At, 1, 0); PG8_STAGE(PG8_SA(0, 1), a2, vA2[1]);
;             PG8_WAIT_V(8); PG8_WAIT_L(0); PG8_BAR; PG8_MMA(0, 0, At, B0); PG8_MMA(0, 1, At, B1); PG8_BAR; PG8_SCHED;
.Lh1e_11141:
.Lh1_428:
	ds_read_b128 v[18:21], v192
	ds_read_b128 v[22:25], v192 offset:1024
	ds_read_b128 v[26:29], v192 offset:2048
	ds_read_b128 v[30:33], v192 offset:3072
	ds_read_b128 v[2:5], v193
	ds_read_b128 v[6:9], v193 offset:1024
	ds_read_b128 v[10:13], v193 offset:2048
	ds_read_b128 v[14:17], v193 offset:3072
	s_add_u32 s26, s24, 0x8000
	s_addc_u32 s27, s25, 0
	s_cmp_eq_u32 s74, 12
	s_cselect_b32 s30, s20, s26
	s_cselect_b32 s31, s21, s27
	s_cselect_b32 s28, s22, s17
	s_cselect_b32 s29, s23, s19
	s_add_u32 s26, s30, 0x8000
	s_addc_u32 s27, s31, 0
	s_add_i32 m0, s48, 0xc000
	ds_read_b128 v[198:201], v194
	ds_read_b128 v[202:205], v194 offset:1024
	ds_read_b128 v[206:209], v194 offset:2048
	ds_read_b128 v[210:213], v194 offset:3072
	ds_read_b128 v[214:217], v194 offset:4096
	ds_read_b128 v[218:221], v194 offset:5120
	ds_read_b128 v[222:225], v194 offset:6144
	ds_read_b128 v[226:229], v194 offset:7168
	global_load_lds_dwordx4 v184, s[24:25]
	s_add_i32 m0, s48, 0xe000
	s_nop 0
	global_load_lds_dwordx4 v182, s[24:25]
	s_waitcnt vmcnt(8)
	s_waitcnt lgkmcnt(0)
	s_barrier
	s_setprio 2
	s_waitcnt lgkmcnt(0)
	v_mfma_scale_f32_16x16x128_f8f6f4 v[158:161], v[18:25], v[198:205], v[158:161], v195, v195 op_sel_hi:[0,0,0]
	v_mfma_scale_f32_16x16x128_f8f6f4 v[154:157], v[26:33], v[198:205], v[154:157], v195, v195 op_sel_hi:[0,0,0]
	v_mfma_scale_f32_16x16x128_f8f6f4 v[142:145], v[18:25], v[206:213], v[142:145], v195, v195 op_sel_hi:[0,0,0]
	v_mfma_scale_f32_16x16x128_f8f6f4 v[138:141], v[26:33], v[206:213], v[138:141], v195, v195 op_sel_hi:[0,0,0]
	v_mfma_scale_f32_16x16x128_f8f6f4 v[126:129], v[18:25], v[214:221], v[126:129], v195, v195 op_sel_hi:[0,0,0]
	v_mfma_scale_f32_16x16x128_f8f6f4 v[122:125], v[26:33], v[214:221], v[122:125], v195, v195 op_sel_hi:[0,0,0]
	v_mfma_scale_f32_16x16x128_f8f6f4 v[110:113], v[18:25], v[222:229], v[110:113], v195, v195 op_sel_hi:[0,0,0]
	v_mfma_scale_f32_16x16x128_f8f6f4 v[106:109], v[26:33], v[222:229], v[106:109], v195, v195 op_sel_hi:[0,0,0]
	s_nop 3
	s_setprio 0
	s_setprio 2
	v_mfma_scale_f32_16x16x128_f8f6f4 v[150:153], v[2:9], v[198:205], v[150:153], v195, v195 op_sel_hi:[0,0,0]
	v_mfma_scale_f32_16x16x128_f8f6f4 v[146:149], v[10:17], v[198:205], v[146:149], v195, v195 op_sel_hi:[0,0,0]
	v_mfma_scale_f32_16x16x128_f8f6f4 v[134:137], v[2:9], v[206:213], v[134:137], v195, v195 op_sel_hi:[0,0,0]
	v_mfma_scale_f32_16x16x128_f8f6f4 v[130:133], v[10:17], v[206:213], v[130:133], v195, v195 op_sel_hi:[0,0,0]
	v_mfma_scale_f32_16x16x128_f8f6f4 v[118:121], v[2:9], v[214:221], v[118:121], v195, v195 op_sel_hi:[0,0,0]
	v_mfma_scale_f32_16x16x128_f8f6f4 v[114:117], v[10:17], v[214:221], v[114:117], v195, v195 op_sel_hi:[0,0,0]
	v_mfma_scale_f32_16x16x128_f8f6f4 v[102:105], v[2:9], v[222:229], v[102:105], v195, v195 op_sel_hi:[0,0,0]
	v_mfma_scale_f32_16x16x128_f8f6f4 v[98:101], v[10:17], v[222:229], v[98:101], v195, v195 op_sel_hi:[0,0,0]
	s_nop 3
	s_setprio 0
	s_add_i32 s75, s65, s47
	s_mov_b32 m0, s75
	ds_read_b128 v[198:201], v194 offset:16384
	ds_read_b128 v[202:205], v194 offset:17408
	ds_read_b128 v[206:209], v194 offset:18432
	ds_read_b128 v[210:213], v194 offset:19456
	ds_read_b128 v[214:217], v194 offset:20480
	ds_read_b128 v[218:221], v194 offset:21504
	ds_read_b128 v[222:225], v194 offset:22528
	ds_read_b128 v[226:229], v194 offset:23552
	global_load_lds_dwordx4 v164, s[28:29]
	s_add_i32 m0, s75, 0x2000
	s_add_i32 s75, s66, s47
	global_load_lds_dwordx4 v166, s[28:29]
	s_add_u32 s98, s28, s4
	s_addc_u32 s99, s29, s5
	s_mov_b32 m0, s75
	s_nop 0
	global_load_lds_dwordx4 v164, s[98:99]
	s_add_u32 s100, s28, s4
	s_addc_u32 s101, s29, s5
	s_add_i32 m0, s75, 0x2000
	s_nop 0
	global_load_lds_dwordx4 v166, s[100:101]
	s_mov_b32 m0, s48
	s_nop 0
	global_load_lds_dwordx4 v174, s[30:31]
	s_mov_b32 m0, s49
	s_nop 0
	global_load_lds_dwordx4 v176, s[30:31]
	s_waitcnt vmcnt(8)
	s_waitcnt lgkmcnt(0)
	s_barrier
	s_setprio 2
	s_waitcnt lgkmcnt(0)
	v_mfma_scale_f32_16x16x128_f8f6f4 v[94:97], v[18:25], v[198:205], v[94:97], v195, v195 op_sel_hi:[0,0,0]
	v_mfma_scale_f32_16x16x128_f8f6f4 v[90:93], v[26:33], v[198:205], v[90:93], v195, v195 op_sel_hi:[0,0,0]
	v_mfma_scale_f32_16x16x128_f8f6f4 v[78:81], v[18:25], v[206:213], v[78:81], v195, v195 op_sel_hi:[0,0,0]
	v_mfma_scale_f32_16x16x128_f8f6f4 v[74:77], v[26:33], v[206:213], v[74:77], v195, v195 op_sel_hi:[0,0,0]
	v_mfma_scale_f32_16x16x128_f8f6f4 v[62:65], v[18:25], v[214:221], v[62:65], v195, v195 op_sel_hi:[0,0,0]
	v_mfma_scale_f32_16x16x128_f8f6f4 v[58:61], v[26:33], v[214:221], v[58:61], v195, v195 op_sel_hi:[0,0,0]
	v_mfma_scale_f32_16x16x128_f8f6f4 v[46:49], v[18:25], v[222:229], v[46:49], v195, v195 op_sel_hi:[0,0,0]
	v_mfma_scale_f32_16x16x128_f8f6f4 v[42:45], v[26:33], v[222:229], v[42:45], v195, v195 op_sel_hi:[0,0,0]
	s_nop 3
	s_setprio 0
	s_setprio 2
	v_mfma_scale_f32_16x16x128_f8f6f4 v[86:89], v[2:9], v[198:205], v[86:89], v195, v195 op_sel_hi:[0,0,0]
	v_mfma_scale_f32_16x16x128_f8f6f4 v[82:85], v[10:17], v[198:205], v[82:85], v195, v195 op_sel_hi:[0,0,0]
	v_mfma_scale_f32_16x16x128_f8f6f4 v[70:73], v[2:9], v[206:213], v[70:73], v195, v195 op_sel_hi:[0,0,0]
	v_mfma_scale_f32_16x16x128_f8f6f4 v[66:69], v[10:17], v[206:213], v[66:69], v195, v195 op_sel_hi:[0,0,0]
	v_mfma_scale_f32_16x16x128_f8f6f4 v[54:57], v[2:9], v[214:221], v[54:57], v195, v195 op_sel_hi:[0,0,0]
	v_mfma_scale_f32_16x16x128_f8f6f4 v[50:53], v[10:17], v[214:221], v[50:53], v195, v195 op_sel_hi:[0,0,0]
	v_mfma_scale_f32_16x16x128_f8f6f4 v[38:41], v[2:9], v[222:229], v[38:41], v195, v195 op_sel_hi:[0,0,0]
	v_mfma_scale_f32_16x16x128_f8f6f4 v[34:37], v[10:17], v[222:229], v[34:37], v195, v195 op_sel_hi:[0,0,0]
	s_nop 3
	s_setprio 0
	s_add_i32 s75, 0, 0x18000
	s_add_i32 s76, 0, 0x1c000
	v_add_u32_e32 v14, s75, v191
	v_add_u32_e32 v30, s76, v191
	ds_read_b128 v[2:5], v14
	ds_read_b128 v[6:9], v14 offset:1024
	ds_read_b128 v[10:13], v14 offset:2048
	ds_read_b128 v[14:17], v14 offset:3072
	ds_read_b128 v[18:21], v30
	ds_read_b128 v[22:25], v30 offset:1024
	ds_read_b128 v[26:29], v30 offset:2048
	ds_read_b128 v[30:33], v30 offset:3072
	s_mov_b32 m0, s50
	ds_read_b128 v[198:201], v194 offset:32768
	ds_read_b128 v[202:205], v194 offset:33792
	ds_read_b128 v[206:209], v194 offset:34816
	ds_read_b128 v[210:213], v194 offset:35840
	ds_read_b128 v[214:217], v194 offset:36864
	ds_read_b128 v[218:221], v194 offset:37888
	ds_read_b128 v[222:225], v194 offset:38912
	ds_read_b128 v[226:229], v194 offset:39936
	global_load_lds_dwordx4 v178, s[30:31]
	s_mov_b32 m0, s51
	s_nop 0
	global_load_lds_dwordx4 v180, s[30:31]
	s_waitcnt vmcnt(8)
	s_waitcnt lgkmcnt(0)
	s_barrier
; #define PG8_STAGE(bufoff, gbase, voff) do { _Pragma("unroll") for (int _i = 0; _i < 2; ++_i) \
;         __builtin_amdgcn_global_load_lds((const unsigned*)((const char*)(gbase) + (voff)[_i]), (PG8_LAS unsigned*)(lds + (bufoff) + ldsw + _i * 8192), 16, 0, 0); } while (0)
; #define PG8_WAIT_V(n) asm volatile("s_waitcnt vmcnt(" #n ")" ::: "memory")
; #define PG8_WAIT_L(n) asm volatile("s_waitcnt lgkmcnt(" #n ")" ::: "memory")
; #define PG8_BAR __builtin_amdgcn_s_barrier()
; #define PG8_SCHED __builtin_amdgcn_sched_barrier(0)
; template <class Epi, class Sched, bool ALIGN_EPI = true, bool F8 = false>
; __device__ __forceinline__ void gemm_phase(PG8_LAS unsigned char* lds, const Sched& S, const Epi& E) {
;     ...
;         for (int t = 0; t < nt; t += 2) {
;             const bool last = (t == nt - 2);
;             if constexpr (Sched::GATHER) { if (last && has_next) S.a_off(nxt, Rs, Cs, voffAn); }
;             const char* a1 = cA + (size_t)(t + 1) * kstep;
;             const char* a2 = last ? nA : cA + (size_t)(t + 2) * kstep; const char* b2 = last ? nB : cB + (size_t)(t + 2) * kstepB;
;             const char* a3 = a2 + kstep; const char* b3 = b2 + kstepB;
;     ...
;             PG8_WAIT_V(8); PG8_WAIT_L(0); PG8_BAR; PG8_MMA(0, 0, At, B0); PG8_MMA(0, 1, At, B1); PG8_BAR; PG8_SCHED;
;             PG8_LDA(At, 1, 1); PG8_STAGE(PG8_SB(1, 0), b3, voffB[0]); PG8_STAGE(PG8_SB(1, 1), b3, voffB[1]); PG8_STAGE(PG8_SA(1, 0), a3, vA2[0]);
;             PG8_WAIT_V(8); PG8_WAIT_L(0); PG8_BAR; PG8_MMA(1, 0, At, B0); PG8_MMA(1, 1, At, B1); PG8_BAR; PG8_SCHED;
;         }
	s_setprio 2
	s_waitcnt lgkmcnt(0)
	v_mfma_scale_f32_16x16x128_f8f6f4 v[158:161], v[2:9], v[198:205], v[158:161], v195, v195 op_sel_hi:[0,0,0]
	v_mfma_scale_f32_16x16x128_f8f6f4 v[154:157], v[10:17], v[198:205], v[154:157], v195, v195 op_sel_hi:[0,0,0]
	v_mfma_scale_f32_16x16x128_f8f6f4 v[142:145], v[2:9], v[206:213], v[142:145], v195, v195 op_sel_hi:[0,0,0]
	v_mfma_scale_f32_16x16x128_f8f6f4 v[138:141], v[10:17], v[206:213], v[138:141], v195, v195 op_sel_hi:[0,0,0]
	v_mfma_scale_f32_16x16x128_f8f6f4 v[126:129], v[2:9], v[214:221], v[126:129], v195, v195 op_sel_hi:[0,0,0]
	v_mfma_scale_f32_16x16x128_f8f6f4 v[122:125], v[10:17], v[214:221], v[122:125], v195, v195 op_sel_hi:[0,0,0]
	v_mfma_scale_f32_16x16x128_f8f6f4 v[110:113], v[2:9], v[222:229], v[110:113], v195, v195 op_sel_hi:[0,0,0]
	v_mfma_scale_f32_16x16x128_f8f6f4 v[106:109], v[10:17], v[222:229], v[106:109], v195, v195 op_sel_hi:[0,0,0]
	s_nop 3
	s_setprio 0
	s_setprio 2
	v_mfma_scale_f32_16x16x128_f8f6f4 v[150:153], v[18:25], v[198:205], v[150:153], v195, v195 op_sel_hi:[0,0,0]
	v_mfma_scale_f32_16x16x128_f8f6f4 v[146:149], v[26:33], v[198:205], v[146:149], v195, v195 op_sel_hi:[0,0,0]
	v_mfma_scale_f32_16x16x128_f8f6f4 v[134:137], v[18:25], v[206:213], v[134:137], v195, v195 op_sel_hi:[0,0,0]
	v_mfma_scale_f32_16x16x128_f8f6f4 v[130:133], v[26:33], v[206:213], v[130:133], v195, v195 op_sel_hi:[0,0,0]
	v_mfma_scale_f32_16x16x128_f8f6f4 v[118:121], v[18:25], v[214:221], v[118:121], v195, v195 op_sel_hi:[0,0,0]
	v_mfma_scale_f32_16x16x128_f8f6f4 v[114:117], v[26:33], v[214:221], v[114:117], v195, v195 op_sel_hi:[0,0,0]
	v_mfma_scale_f32_16x16x128_f8f6f4 v[102:105], v[18:25], v[222:229], v[102:105], v195, v195 op_sel_hi:[0,0,0]
	v_mfma_scale_f32_16x16x128_f8f6f4 v[98:101], v[26:33], v[222:229], v[98:101], v195, v195 op_sel_hi:[0,0,0]
	s_nop 3
	s_setprio 0
	s_add_u32 s28, s28, 0x8000
	s_addc_u32 s29, s29, 0
	s_add_i32 s30, s75, s47
	s_mov_b32 m0, s30
	ds_read_b128 v[198:201], v194 offset:49152
	ds_read_b128 v[202:205], v194 offset:50176
	ds_read_b128 v[206:209], v194 offset:51200
	ds_read_b128 v[210:213], v194 offset:52224
	ds_read_b128 v[214:217], v194 offset:53248
	ds_read_b128 v[218:221], v194 offset:54272
	ds_read_b128 v[222:225], v194 offset:55296
	ds_read_b128 v[226:229], v194 offset:56320
	global_load_lds_dwordx4 v164, s[28:29]
	s_add_i32 m0, s30, 0x2000
	s_add_i32 s30, s76, s47
	global_load_lds_dwordx4 v166, s[28:29]
	s_mov_b32 m0, s30
	s_nop 0
	global_load_lds_dwordx4 v168, s[28:29]
	s_add_i32 m0, s30, 0x2000
	s_nop 0
	global_load_lds_dwordx4 v172, s[28:29]
	s_mov_b32 m0, s60
	s_nop 0
	global_load_lds_dwordx4 v174, s[26:27]
	s_mov_b32 m0, s61
	s_nop 0
	global_load_lds_dwordx4 v176, s[26:27]
	s_waitcnt vmcnt(8)
	s_waitcnt lgkmcnt(0)
	s_barrier
	s_setprio 2
	s_waitcnt lgkmcnt(0)
	v_mfma_scale_f32_16x16x128_f8f6f4 v[94:97], v[2:9], v[198:205], v[94:97], v195, v195 op_sel_hi:[0,0,0]
	v_mfma_scale_f32_16x16x128_f8f6f4 v[90:93], v[10:17], v[198:205], v[90:93], v195, v195 op_sel_hi:[0,0,0]
	v_mfma_scale_f32_16x16x128_f8f6f4 v[78:81], v[2:9], v[206:213], v[78:81], v195, v195 op_sel_hi:[0,0,0]
	v_mfma_scale_f32_16x16x128_f8f6f4 v[74:77], v[10:17], v[206:213], v[74:77], v195, v195 op_sel_hi:[0,0,0]
	v_mfma_scale_f32_16x16x128_f8f6f4 v[62:65], v[2:9], v[214:221], v[62:65], v195, v195 op_sel_hi:[0,0,0]
	v_mfma_scale_f32_16x16x128_f8f6f4 v[58:61], v[10:17], v[214:221], v[58:61], v195, v195 op_sel_hi:[0,0,0]
	v_mfma_scale_f32_16x16x128_f8f6f4 v[46:49], v[2:9], v[222:229], v[46:49], v195, v195 op_sel_hi:[0,0,0]
	v_mfma_scale_f32_16x16x128_f8f6f4 v[42:45], v[10:17], v[222:229], v[42:45], v195, v195 op_sel_hi:[0,0,0]
	s_nop 3
	s_setprio 0
	s_setprio 2
	v_mfma_scale_f32_16x16x128_f8f6f4 v[86:89], v[18:25], v[198:205], v[86:89], v195, v195 op_sel_hi:[0,0,0]
	v_mfma_scale_f32_16x16x128_f8f6f4 v[82:85], v[26:33], v[198:205], v[82:85], v195, v195 op_sel_hi:[0,0,0]
	v_mfma_scale_f32_16x16x128_f8f6f4 v[70:73], v[18:25], v[206:213], v[70:73], v195, v195 op_sel_hi:[0,0,0]
	v_mfma_scale_f32_16x16x128_f8f6f4 v[66:69], v[26:33], v[206:213], v[66:69], v195, v195 op_sel_hi:[0,0,0]
	v_mfma_scale_f32_16x16x128_f8f6f4 v[54:57], v[18:25], v[214:221], v[54:57], v195, v195 op_sel_hi:[0,0,0]
	v_mfma_scale_f32_16x16x128_f8f6f4 v[50:53], v[26:33], v[214:221], v[50:53], v195, v195 op_sel_hi:[0,0,0]
	v_mfma_scale_f32_16x16x128_f8f6f4 v[38:41], v[18:25], v[222:229], v[38:41], v195, v195 op_sel_hi:[0,0,0]
	v_mfma_scale_f32_16x16x128_f8f6f4 v[34:37], v[26:33], v[222:229], v[34:37], v195, v195 op_sel_hi:[0,0,0]
	s_nop 3
	s_setprio 0
	s_add_i32 s74, s74, 2
	s_add_u32 s17, s17, 0x10000
	s_addc_u32 s19, s19, 0
	s_add_u32 s24, s24, 0x10000
	s_addc_u32 s25, s25, 0
	s_cmp_gt_u32 s74, 13
	s_cbranch_scc0 .Lh1_428

; __device__ __forceinline__ float fsigmoid(float x) { return __builtin_amdgcn_rcpf(1.0f + __builtin_amdgcn_exp2f(-1.44269504f * x)); }
; __device__ __forceinline__ unsigned pk4_u8(float a, float b, float c, float d) {
;     const unsigned ya = __builtin_bit_cast(unsigned, a * 255.0f + 8388608.0f), yb = __builtin_bit_cast(unsigned, b * 255.0f + 8388608.0f), yc = __builtin_bit_cast(unsigned, c * 255.0f + 8388608.0f), yd = __builtin_bit_cast(unsigned, d * 255.0f + 8388608.0f);
;     const unsigned w01 = __builtin_amdgcn_perm(yb, ya, 0x0c0c0400u), w23 = __builtin_amdgcn_perm(yd, yc, 0x0c0c0400u);
;     return __builtin_amdgcn_perm(w23, w01, 0x05040100u); }
;     __device__ __forceinline__ void operator()(AccRef acc, const GUnit& u, int wr, int wc, int fr, int fq) const {
;         const int pm = u.x0, pn = u.x1; unsigned char* base = (pn < 8 ? GZF : GZS) + (size_t)(pm * 256 + wr * 64 + fr) * D + (pn & 7) * 256 + wc * 64 + 16 * fq;
; #pragma unroll
;         for (int ai = 0; ai < 2; ++ai)
; #pragma unroll
;             for (int m = 0; m < 4; ++m) { u32x4 w;
; #pragma unroll
;                 for (int bj = 0; bj < 2; ++bj)
; #pragma unroll
;                     for (int n = 0; n < 2; ++n) { const f32x4 v = acc[ai][bj][m][n]; w[bj * 2 + n] = pk4_u8(fsigmoid(v[0] * W8_INV), fsigmoid(v[1] * W8_INV), fsigmoid(v[2] * W8_INV), fsigmoid(v[3] * W8_INV)); }
;                 *(u32x4*)(base + (size_t)(ai * 128 + m * 16) * D) = w; }
.LBB0_431:
	s_nop 15
	s_nop 7
	s_nop 15
	s_nop 7
	v_lshl_add_u32 v2, s8, 8, v190
	v_mul_f32_e32 v4, 0x3c800000, v158
	v_mul_f32_e32 v5, 0x3c800000, v159
	v_mul_f32_e32 v6, 0x3c800000, v160
	v_mul_f32_e32 v7, 0x3c800000, v161
	v_mul_f32_e32 v4, 0xbfb8aa3b, v4
	v_mul_f32_e32 v5, 0xbfb8aa3b, v5
	v_mul_f32_e32 v6, 0xbfb8aa3b, v6
	v_mul_f32_e32 v7, 0xbfb8aa3b, v7
	v_exp_f32_e32 v4, v4
	v_exp_f32_e32 v5, v5
	v_exp_f32_e32 v6, v6
	v_exp_f32_e32 v7, v7
	v_add_f32_e32 v4, 1.0, v4
	v_add_f32_e32 v5, 1.0, v5
	v_add_f32_e32 v6, 1.0, v6
	v_add_f32_e32 v7, 1.0, v7
	v_rcp_f32_e32 v4, v4
	v_rcp_f32_e32 v5, v5
	v_rcp_f32_e32 v6, v6
	v_rcp_f32_e32 v7, v7
	v_fmamk_f32 v4, v4, 0x437f0000, v196
	v_fmamk_f32 v5, v5, 0x437f0000, v196
	v_fmamk_f32 v6, v6, 0x437f0000, v196
	v_fmamk_f32 v7, v7, 0x437f0000, v196
	v_perm_b32 v4, v5, v4, s67
	v_perm_b32 v5, v7, v6, s67
	v_mul_f32_e32 v6, 0x3c800000, v154
	v_mul_f32_e32 v7, 0x3c800000, v155
	v_mul_f32_e32 v6, 0xbfb8aa3b, v6
	v_mul_f32_e32 v7, 0xbfb8aa3b, v7
	v_exp_f32_e32 v6, v6
	v_exp_f32_e32 v7, v7
	v_perm_b32 v4, v5, v4, s68
	v_mul_f32_e32 v8, 0x3c800000, v157
	v_add_f32_e32 v5, 1.0, v6
	v_add_f32_e32 v6, 1.0, v7
	v_mul_f32_e32 v7, 0x3c800000, v156
	v_mul_f32_e32 v7, 0xbfb8aa3b, v7
	v_mul_f32_e32 v8, 0xbfb8aa3b, v8
	v_exp_f32_e32 v7, v7
	v_exp_f32_e32 v8, v8
	v_rcp_f32_e32 v5, v5
	v_rcp_f32_e32 v6, v6
	v_add_f32_e32 v7, 1.0, v7
	v_add_f32_e32 v8, 1.0, v8
	v_rcp_f32_e32 v7, v7
	v_rcp_f32_e32 v8, v8
	v_fmamk_f32 v5, v5, 0x437f0000, v196
	v_fmamk_f32 v6, v6, 0x437f0000, v196
	v_fmamk_f32 v7, v7, 0x437f0000, v196
	v_fmamk_f32 v8, v8, 0x437f0000, v196
	v_perm_b32 v5, v6, v5, s67
	v_perm_b32 v6, v8, v7, s67
	v_mul_f32_e32 v7, 0x3c800000, v150
	v_mul_f32_e32 v8, 0x3c800000, v151
	v_mul_f32_e32 v7, 0xbfb8aa3b, v7
	v_mul_f32_e32 v8, 0xbfb8aa3b, v8
	v_exp_f32_e32 v7, v7
	v_exp_f32_e32 v8, v8
	v_perm_b32 v5, v6, v5, s68
	v_mul_f32_e32 v9, 0x3c800000, v153
	v_add_f32_e32 v6, 1.0, v7
	v_add_f32_e32 v7, 1.0, v8
	v_mul_f32_e32 v8, 0x3c800000, v152
	v_mul_f32_e32 v8, 0xbfb8aa3b, v8
	v_mul_f32_e32 v9, 0xbfb8aa3b, v9
	v_exp_f32_e32 v8, v8
	v_exp_f32_e32 v9, v9
	v_rcp_f32_e32 v6, v6
	v_rcp_f32_e32 v7, v7
	v_add_f32_e32 v8, 1.0, v8
	v_add_f32_e32 v9, 1.0, v9
	v_rcp_f32_e32 v8, v8
	v_rcp_f32_e32 v9, v9
	v_fmamk_f32 v6, v6, 0x437f0000, v196
	v_fmamk_f32 v7, v7, 0x437f0000, v196
	v_fmamk_f32 v8, v8, 0x437f0000, v196
	v_fmamk_f32 v9, v9, 0x437f0000, v196
	v_perm_b32 v6, v7, v6, s67
	v_perm_b32 v7, v9, v8, s67
	v_mul_f32_e32 v8, 0x3c800000, v146
	v_mul_f32_e32 v9, 0x3c800000, v147
	v_mul_f32_e32 v8, 0xbfb8aa3b, v8
	v_mul_f32_e32 v9, 0xbfb8aa3b, v9
	v_exp_f32_e32 v8, v8
	v_exp_f32_e32 v9, v9
	v_perm_b32 v6, v7, v6, s68
	v_mul_f32_e32 v10, 0x3c800000, v149
	v_add_f32_e32 v7, 1.0, v8
	v_add_f32_e32 v8, 1.0, v9
	v_mul_f32_e32 v9, 0x3c800000, v148
	v_mul_f32_e32 v9, 0xbfb8aa3b, v9
	v_mul_f32_e32 v10, 0xbfb8aa3b, v10
	v_exp_f32_e32 v9, v9
	v_exp_f32_e32 v10, v10
	v_rcp_f32_e32 v7, v7
	v_rcp_f32_e32 v8, v8
	v_add_f32_e32 v9, 1.0, v9
	v_add_f32_e32 v10, 1.0, v10
	v_rcp_f32_e32 v9, v9
	v_rcp_f32_e32 v10, v10
	s_cmp_lt_i32 s73, 8
	v_ashrrev_i32_e32 v3, 31, v2
	s_cselect_b32 s25, s41, s59
	s_cselect_b32 s24, s40, s53
	v_lshlrev_b64 v[2:3], 11, v[2:3]
	s_lshl_b32 s8, s73, 8
	v_lshl_add_u64 v[2:3], s[24:25], 0, v[2:3]
	s_and_b32 s8, s8, 0x700
	v_lshl_add_u64 v[2:3], v[2:3], 0, s[8:9]
	v_fmamk_f32 v7, v7, 0x437f0000, v196
	v_fmamk_f32 v8, v8, 0x437f0000, v196
	v_fmamk_f32 v9, v9, 0x437f0000, v196
	v_fmamk_f32 v10, v10, 0x437f0000, v196
	v_lshl_add_u64 v[2:3], v[2:3], 0, s[14:15]
	v_perm_b32 v7, v8, v7, s67
	v_perm_b32 v8, v10, v9, s67
	v_lshl_add_u64 v[2:3], v[2:3], 0, v[162:163]
	v_perm_b32 v7, v8, v7, s68
	s_nop 15
	s_nop 7
	s_nop 15
	s_nop 7
	v_mul_f32_e32 v8, 0x3c800000, v142
	v_mul_f32_e32 v9, 0x3c800000, v143
	global_store_dwordx4 v[2:3], v[4:7], off
	v_mul_f32_e32 v8, 0xbfb8aa3b, v8
	v_mul_f32_e32 v9, 0xbfb8aa3b, v9
	v_mul_f32_e32 v6, 0x3c800000, v144
	v_mul_f32_e32 v7, 0x3c800000, v145
	v_mul_f32_e32 v6, 0xbfb8aa3b, v6
	v_mul_f32_e32 v7, 0xbfb8aa3b, v7
	v_exp_f32_e32 v8, v8
	v_exp_f32_e32 v9, v9
	v_exp_f32_e32 v6, v6
	v_exp_f32_e32 v7, v7
	v_add_f32_e32 v4, 1.0, v8
	v_add_f32_e32 v5, 1.0, v9
	v_add_f32_e32 v6, 1.0, v6
	v_add_f32_e32 v7, 1.0, v7
	v_rcp_f32_e32 v4, v4
	v_rcp_f32_e32 v5, v5
	v_rcp_f32_e32 v6, v6
	v_rcp_f32_e32 v7, v7
	v_fmamk_f32 v4, v4, 0x437f0000, v196
	v_fmamk_f32 v5, v5, 0x437f0000, v196
	v_fmamk_f32 v6, v6, 0x437f0000, v196
	v_fmamk_f32 v7, v7, 0x437f0000, v196
	v_perm_b32 v4, v5, v4, s67
	v_perm_b32 v5, v7, v6, s67
	v_mul_f32_e32 v6, 0x3c800000, v138
	v_mul_f32_e32 v7, 0x3c800000, v139
	v_mul_f32_e32 v6, 0xbfb8aa3b, v6
	v_mul_f32_e32 v7, 0xbfb8aa3b, v7
	v_exp_f32_e32 v6, v6
	v_exp_f32_e32 v7, v7
	v_perm_b32 v4, v5, v4, s68
	v_mul_f32_e32 v8, 0x3c800000, v141
	v_add_f32_e32 v5, 1.0, v6
	v_add_f32_e32 v6, 1.0, v7
	v_mul_f32_e32 v7, 0x3c800000, v140
	v_mul_f32_e32 v7, 0xbfb8aa3b, v7
	v_mul_f32_e32 v8, 0xbfb8aa3b, v8
	v_exp_f32_e32 v7, v7
	v_exp_f32_e32 v8, v8
	v_rcp_f32_e32 v5, v5
	v_rcp_f32_e32 v6, v6
	v_add_f32_e32 v7, 1.0, v7
	v_add_f32_e32 v8, 1.0, v8
	v_rcp_f32_e32 v7, v7
	v_rcp_f32_e32 v8, v8
	v_fmamk_f32 v5, v5, 0x437f0000, v196
	v_fmamk_f32 v6, v6, 0x437f0000, v196
	v_fmamk_f32 v7, v7, 0x437f0000, v196
	v_fmamk_f32 v8, v8, 0x437f0000, v196
	v_perm_b32 v5, v6, v5, s67
	v_perm_b32 v6, v8, v7, s67
	v_mul_f32_e32 v7, 0x3c800000, v134
	v_mul_f32_e32 v8, 0x3c800000, v135
	v_mul_f32_e32 v7, 0xbfb8aa3b, v7
	v_mul_f32_e32 v8, 0xbfb8aa3b, v8
	v_exp_f32_e32 v7, v7
	v_exp_f32_e32 v8, v8
	v_perm_b32 v5, v6, v5, s68
	v_mul_f32_e32 v9, 0x3c800000, v137
	v_add_f32_e32 v6, 1.0, v7
	v_add_f32_e32 v7, 1.0, v8
	v_mul_f32_e32 v8, 0x3c800000, v136
; __device__ __forceinline__ float fsigmoid(float x) { return __builtin_amdgcn_rcpf(1.0f + __builtin_amdgcn_exp2f(-1.44269504f * x)); }
; __device__ __forceinline__ unsigned pk4_u8(float a, float b, float c, float d) {
;     const unsigned ya = __builtin_bit_cast(unsigned, a * 255.0f + 8388608.0f), yb = __builtin_bit_cast(unsigned, b * 255.0f + 8388608.0f), yc = __builtin_bit_cast(unsigned, c * 255.0f + 8388608.0f), yd = __builtin_bit_cast(unsigned, d * 255.0f + 8388608.0f);
;     const unsigned w01 = __builtin_amdgcn_perm(yb, ya, 0x0c0c0400u), w23 = __builtin_amdgcn_perm(yd, yc, 0x0c0c0400u);
;     return __builtin_amdgcn_perm(w23, w01, 0x05040100u); }
;     __device__ __forceinline__ void operator()(AccRef acc, const GUnit& u, int wr, int wc, int fr, int fq) const {
;         const int pm = u.x0, pn = u.x1; unsigned char* base = (pn < 8 ? GZF : GZS) + (size_t)(pm * 256 + wr * 64 + fr) * D + (pn & 7) * 256 + wc * 64 + 16 * fq;
; #pragma unroll
;         for (int ai = 0; ai < 2; ++ai)
; #pragma unroll
;             for (int m = 0; m < 4; ++m) { u32x4 w;
; #pragma unroll
;                 for (int bj = 0; bj < 2; ++bj)
; #pragma unroll
;                     for (int n = 0; n < 2; ++n) { const f32x4 v = acc[ai][bj][m][n]; w[bj * 2 + n] = pk4_u8(fsigmoid(v[0] * W8_INV), fsigmoid(v[1] * W8_INV), fsigmoid(v[2] * W8_INV), fsigmoid(v[3] * W8_INV)); }
;                 *(u32x4*)(base + (size_t)(ai * 128 + m * 16) * D) = w; }
	v_mul_f32_e32 v8, 0xbfb8aa3b, v8
	v_mul_f32_e32 v9, 0xbfb8aa3b, v9
	v_exp_f32_e32 v8, v8
	v_exp_f32_e32 v9, v9
	v_rcp_f32_e32 v6, v6
	v_rcp_f32_e32 v7, v7
	v_add_f32_e32 v8, 1.0, v8
	v_add_f32_e32 v9, 1.0, v9
	v_rcp_f32_e32 v8, v8
	v_rcp_f32_e32 v9, v9
	v_fmamk_f32 v6, v6, 0x437f0000, v196
	v_fmamk_f32 v7, v7, 0x437f0000, v196
	v_fmamk_f32 v8, v8, 0x437f0000, v196
	v_fmamk_f32 v9, v9, 0x437f0000, v196
	v_perm_b32 v6, v7, v6, s67
	v_perm_b32 v7, v9, v8, s67
	v_mul_f32_e32 v8, 0x3c800000, v130
	v_mul_f32_e32 v9, 0x3c800000, v131
	v_mul_f32_e32 v8, 0xbfb8aa3b, v8
	v_mul_f32_e32 v9, 0xbfb8aa3b, v9
	v_exp_f32_e32 v8, v8
	v_exp_f32_e32 v9, v9
	v_perm_b32 v6, v7, v6, s68
	v_mul_f32_e32 v10, 0x3c800000, v133
	v_add_f32_e32 v7, 1.0, v8
	v_add_f32_e32 v8, 1.0, v9
	v_mul_f32_e32 v9, 0x3c800000, v132
	v_mul_f32_e32 v9, 0xbfb8aa3b, v9
	v_mul_f32_e32 v10, 0xbfb8aa3b, v10
	v_exp_f32_e32 v9, v9
	v_exp_f32_e32 v10, v10
	v_rcp_f32_e32 v7, v7
	v_rcp_f32_e32 v8, v8
	v_add_f32_e32 v9, 1.0, v9
	v_add_f32_e32 v10, 1.0, v10
	v_rcp_f32_e32 v9, v9
	v_rcp_f32_e32 v10, v10
	v_fmamk_f32 v7, v7, 0x437f0000, v196
	v_fmamk_f32 v8, v8, 0x437f0000, v196
	v_fmamk_f32 v9, v9, 0x437f0000, v196
	v_fmamk_f32 v10, v10, 0x437f0000, v196
	v_perm_b32 v7, v8, v7, s67
	v_perm_b32 v8, v10, v9, s67
	v_perm_b32 v7, v8, v7, s68
	v_add_co_u32_e32 v8, vcc, s63, v2
	v_mul_f32_e32 v10, 0x3c800000, v126
	s_nop 0
	v_addc_co_u32_e32 v9, vcc, 0, v3, vcc
	v_mul_f32_e32 v11, 0x3c800000, v127
	global_store_dwordx4 v[8:9], v[4:7], off
	v_mul_f32_e32 v10, 0xbfb8aa3b, v10
	v_mul_f32_e32 v11, 0xbfb8aa3b, v11
	v_mul_f32_e32 v6, 0x3c800000, v128
	v_mul_f32_e32 v7, 0x3c800000, v129
	v_mul_f32_e32 v6, 0xbfb8aa3b, v6
	v_mul_f32_e32 v7, 0xbfb8aa3b, v7
	v_exp_f32_e32 v10, v10
	v_exp_f32_e32 v11, v11
	v_exp_f32_e32 v6, v6
	v_exp_f32_e32 v7, v7
	v_add_f32_e32 v4, 1.0, v10
	v_add_f32_e32 v5, 1.0, v11
	v_add_f32_e32 v6, 1.0, v6
	v_add_f32_e32 v7, 1.0, v7
	v_rcp_f32_e32 v4, v4
	v_rcp_f32_e32 v5, v5
	v_rcp_f32_e32 v6, v6
	v_rcp_f32_e32 v7, v7
	v_fmamk_f32 v4, v4, 0x437f0000, v196
	v_fmamk_f32 v5, v5, 0x437f0000, v196
	v_fmamk_f32 v6, v6, 0x437f0000, v196
	v_fmamk_f32 v7, v7, 0x437f0000, v196
	v_perm_b32 v4, v5, v4, s67
	v_perm_b32 v5, v7, v6, s67
	v_mul_f32_e32 v6, 0x3c800000, v122
	v_mul_f32_e32 v7, 0x3c800000, v123
	v_mul_f32_e32 v6, 0xbfb8aa3b, v6
	v_mul_f32_e32 v7, 0xbfb8aa3b, v7
	v_exp_f32_e32 v6, v6
	v_exp_f32_e32 v7, v7
	v_perm_b32 v4, v5, v4, s68
	v_mul_f32_e32 v8, 0x3c800000, v125
	v_add_f32_e32 v5, 1.0, v6
	v_add_f32_e32 v6, 1.0, v7
	v_mul_f32_e32 v7, 0x3c800000, v124
	v_mul_f32_e32 v7, 0xbfb8aa3b, v7
	v_mul_f32_e32 v8, 0xbfb8aa3b, v8
	v_exp_f32_e32 v7, v7
	v_exp_f32_e32 v8, v8
	v_rcp_f32_e32 v5, v5
	v_rcp_f32_e32 v6, v6
	v_add_f32_e32 v7, 1.0, v7
	v_add_f32_e32 v8, 1.0, v8
	v_rcp_f32_e32 v7, v7
	v_rcp_f32_e32 v8, v8
	v_fmamk_f32 v5, v5, 0x437f0000, v196
	v_fmamk_f32 v6, v6, 0x437f0000, v196
	v_fmamk_f32 v7, v7, 0x437f0000, v196
	v_fmamk_f32 v8, v8, 0x437f0000, v196
	v_perm_b32 v5, v6, v5, s67
	v_perm_b32 v6, v8, v7, s67
	v_mul_f32_e32 v7, 0x3c800000, v118
	v_mul_f32_e32 v8, 0x3c800000, v119
	v_mul_f32_e32 v7, 0xbfb8aa3b, v7
	v_mul_f32_e32 v8, 0xbfb8aa3b, v8
	v_exp_f32_e32 v7, v7
	v_exp_f32_e32 v8, v8
	v_perm_b32 v5, v6, v5, s68
	v_mul_f32_e32 v9, 0x3c800000, v121
	v_add_f32_e32 v6, 1.0, v7
	v_add_f32_e32 v7, 1.0, v8
	v_mul_f32_e32 v8, 0x3c800000, v120
	v_mul_f32_e32 v8, 0xbfb8aa3b, v8
	v_mul_f32_e32 v9, 0xbfb8aa3b, v9
	v_exp_f32_e32 v8, v8
	v_exp_f32_e32 v9, v9
	v_rcp_f32_e32 v6, v6
	v_rcp_f32_e32 v7, v7
	v_add_f32_e32 v8, 1.0, v8
	v_add_f32_e32 v9, 1.0, v9
	v_rcp_f32_e32 v8, v8
	v_rcp_f32_e32 v9, v9
	v_fmamk_f32 v6, v6, 0x437f0000, v196
	v_fmamk_f32 v7, v7, 0x437f0000, v196
	v_fmamk_f32 v8, v8, 0x437f0000, v196
	v_fmamk_f32 v9, v9, 0x437f0000, v196
	v_perm_b32 v6, v7, v6, s67
	v_perm_b32 v7, v9, v8, s67
	v_mul_f32_e32 v8, 0x3c800000, v114
	v_mul_f32_e32 v9, 0x3c800000, v115
	v_mul_f32_e32 v8, 0xbfb8aa3b, v8
	v_mul_f32_e32 v9, 0xbfb8aa3b, v9
	v_exp_f32_e32 v8, v8
	v_exp_f32_e32 v9, v9
	v_perm_b32 v6, v7, v6, s68
	v_mul_f32_e32 v10, 0x3c800000, v117
	v_add_f32_e32 v7, 1.0, v8
	v_add_f32_e32 v8, 1.0, v9
	v_mul_f32_e32 v9, 0x3c800000, v116
	v_mul_f32_e32 v9, 0xbfb8aa3b, v9
	v_mul_f32_e32 v10, 0xbfb8aa3b, v10
	v_exp_f32_e32 v9, v9
	v_exp_f32_e32 v10, v10
	v_rcp_f32_e32 v7, v7
	v_rcp_f32_e32 v8, v8
	v_add_f32_e32 v9, 1.0, v9
	v_add_f32_e32 v10, 1.0, v10
	v_rcp_f32_e32 v9, v9
	v_rcp_f32_e32 v10, v10
	v_fmamk_f32 v7, v7, 0x437f0000, v196
	v_fmamk_f32 v8, v8, 0x437f0000, v196
	v_fmamk_f32 v9, v9, 0x437f0000, v196
	v_fmamk_f32 v10, v10, 0x437f0000, v196
	v_perm_b32 v7, v8, v7, s67
	v_perm_b32 v8, v10, v9, s67
	v_perm_b32 v7, v8, v7, s68
	v_add_co_u32_e32 v8, vcc, s52, v2
	v_mul_f32_e32 v10, 0x3c800000, v110
	s_nop 0
	v_addc_co_u32_e32 v9, vcc, 0, v3, vcc
	v_mul_f32_e32 v11, 0x3c800000, v111
	global_store_dwordx4 v[8:9], v[4:7], off
	v_mul_f32_e32 v10, 0xbfb8aa3b, v10
	v_mul_f32_e32 v11, 0xbfb8aa3b, v11
	v_mul_f32_e32 v6, 0x3c800000, v112
	v_mul_f32_e32 v7, 0x3c800000, v113
	v_mul_f32_e32 v6, 0xbfb8aa3b, v6
	v_mul_f32_e32 v7, 0xbfb8aa3b, v7
	v_exp_f32_e32 v10, v10
	v_exp_f32_e32 v11, v11
	v_exp_f32_e32 v6, v6
	v_exp_f32_e32 v7, v7
	v_add_f32_e32 v4, 1.0, v10
	v_add_f32_e32 v5, 1.0, v11
	v_add_f32_e32 v6, 1.0, v6
	v_add_f32_e32 v7, 1.0, v7
	v_rcp_f32_e32 v4, v4
	v_rcp_f32_e32 v5, v5
	v_rcp_f32_e32 v6, v6
	v_rcp_f32_e32 v7, v7
	v_fmamk_f32 v4, v4, 0x437f0000, v196
	v_fmamk_f32 v5, v5, 0x437f0000, v196
	v_fmamk_f32 v6, v6, 0x437f0000, v196
	v_fmamk_f32 v7, v7, 0x437f0000, v196
	v_perm_b32 v4, v5, v4, s67
	v_perm_b32 v5, v7, v6, s67
	v_mul_f32_e32 v6, 0x3c800000, v106
	v_mul_f32_e32 v7, 0x3c800000, v107
; __device__ __forceinline__ float fsigmoid(float x) { return __builtin_amdgcn_rcpf(1.0f + __builtin_amdgcn_exp2f(-1.44269504f * x)); }
; __device__ __forceinline__ unsigned pk4_u8(float a, float b, float c, float d) {
;     const unsigned ya = __builtin_bit_cast(unsigned, a * 255.0f + 8388608.0f), yb = __builtin_bit_cast(unsigned, b * 255.0f + 8388608.0f), yc = __builtin_bit_cast(unsigned, c * 255.0f + 8388608.0f), yd = __builtin_bit_cast(unsigned, d * 255.0f + 8388608.0f);
;     const unsigned w01 = __builtin_amdgcn_perm(yb, ya, 0x0c0c0400u), w23 = __builtin_amdgcn_perm(yd, yc, 0x0c0c0400u);
;     return __builtin_amdgcn_perm(w23, w01, 0x05040100u); }
;     __device__ __forceinline__ void operator()(AccRef acc, const GUnit& u, int wr, int wc, int fr, int fq) const {
;         const int pm = u.x0, pn = u.x1; unsigned char* base = (pn < 8 ? GZF : GZS) + (size_t)(pm * 256 + wr * 64 + fr) * D + (pn & 7) * 256 + wc * 64 + 16 * fq;
; #pragma unroll
;         for (int ai = 0; ai < 2; ++ai)
; #pragma unroll
;             for (int m = 0; m < 4; ++m) { u32x4 w;
; #pragma unroll
;                 for (int bj = 0; bj < 2; ++bj)
; #pragma unroll
;                     for (int n = 0; n < 2; ++n) { const f32x4 v = acc[ai][bj][m][n]; w[bj * 2 + n] = pk4_u8(fsigmoid(v[0] * W8_INV), fsigmoid(v[1] * W8_INV), fsigmoid(v[2] * W8_INV), fsigmoid(v[3] * W8_INV)); }
;                 *(u32x4*)(base + (size_t)(ai * 128 + m * 16) * D) = w; }
	v_mul_f32_e32 v6, 0xbfb8aa3b, v6
	v_mul_f32_e32 v7, 0xbfb8aa3b, v7
	v_exp_f32_e32 v6, v6
	v_exp_f32_e32 v7, v7
	v_perm_b32 v4, v5, v4, s68
	v_mul_f32_e32 v8, 0x3c800000, v109
	v_add_f32_e32 v5, 1.0, v6
	v_add_f32_e32 v6, 1.0, v7
	v_mul_f32_e32 v7, 0x3c800000, v108
	v_mul_f32_e32 v7, 0xbfb8aa3b, v7
	v_mul_f32_e32 v8, 0xbfb8aa3b, v8
	v_exp_f32_e32 v7, v7
	v_exp_f32_e32 v8, v8
	v_rcp_f32_e32 v5, v5
	v_rcp_f32_e32 v6, v6
	v_add_f32_e32 v7, 1.0, v7
	v_add_f32_e32 v8, 1.0, v8
	v_rcp_f32_e32 v7, v7
	v_rcp_f32_e32 v8, v8
	v_fmamk_f32 v5, v5, 0x437f0000, v196
	v_fmamk_f32 v6, v6, 0x437f0000, v196
	v_fmamk_f32 v7, v7, 0x437f0000, v196
	v_fmamk_f32 v8, v8, 0x437f0000, v196
	v_perm_b32 v5, v6, v5, s67
	v_perm_b32 v6, v8, v7, s67
	v_mul_f32_e32 v7, 0x3c800000, v102
	v_mul_f32_e32 v8, 0x3c800000, v103
	v_mul_f32_e32 v7, 0xbfb8aa3b, v7
	v_mul_f32_e32 v8, 0xbfb8aa3b, v8
	v_exp_f32_e32 v7, v7
	v_exp_f32_e32 v8, v8
	v_perm_b32 v5, v6, v5, s68
	v_mul_f32_e32 v9, 0x3c800000, v105
	v_add_f32_e32 v6, 1.0, v7
	v_add_f32_e32 v7, 1.0, v8
	v_mul_f32_e32 v8, 0x3c800000, v104
	v_mul_f32_e32 v8, 0xbfb8aa3b, v8
	v_mul_f32_e32 v9, 0xbfb8aa3b, v9
	v_exp_f32_e32 v8, v8
	v_exp_f32_e32 v9, v9
	v_rcp_f32_e32 v6, v6
	v_rcp_f32_e32 v7, v7
	v_add_f32_e32 v8, 1.0, v8
	v_add_f32_e32 v9, 1.0, v9
	v_rcp_f32_e32 v8, v8
	v_rcp_f32_e32 v9, v9
	v_fmamk_f32 v6, v6, 0x437f0000, v196
	v_fmamk_f32 v7, v7, 0x437f0000, v196
	v_fmamk_f32 v8, v8, 0x437f0000, v196
	v_fmamk_f32 v9, v9, 0x437f0000, v196
	v_perm_b32 v6, v7, v6, s67
	v_perm_b32 v7, v9, v8, s67
	v_mul_f32_e32 v8, 0x3c800000, v98
	v_mul_f32_e32 v9, 0x3c800000, v99
	v_mul_f32_e32 v8, 0xbfb8aa3b, v8
	v_mul_f32_e32 v9, 0xbfb8aa3b, v9
	v_exp_f32_e32 v8, v8
	v_exp_f32_e32 v9, v9
	v_perm_b32 v6, v7, v6, s68
	v_mul_f32_e32 v10, 0x3c800000, v101
	v_add_f32_e32 v7, 1.0, v8
	v_add_f32_e32 v8, 1.0, v9
	v_mul_f32_e32 v9, 0x3c800000, v100
	v_mul_f32_e32 v9, 0xbfb8aa3b, v9
	v_mul_f32_e32 v10, 0xbfb8aa3b, v10
	v_exp_f32_e32 v9, v9
	v_exp_f32_e32 v10, v10
	v_rcp_f32_e32 v7, v7
	v_rcp_f32_e32 v8, v8
	v_add_f32_e32 v9, 1.0, v9
	v_add_f32_e32 v10, 1.0, v10
	v_rcp_f32_e32 v9, v9
	v_rcp_f32_e32 v10, v10
	v_fmamk_f32 v7, v7, 0x437f0000, v196
	v_fmamk_f32 v8, v8, 0x437f0000, v196
	v_fmamk_f32 v9, v9, 0x437f0000, v196
	v_fmamk_f32 v10, v10, 0x437f0000, v196
	v_perm_b32 v7, v8, v7, s67
	v_perm_b32 v8, v10, v9, s67
	v_perm_b32 v7, v8, v7, s68
	v_add_co_u32_e32 v8, vcc, s62, v2
	v_mul_f32_e32 v10, 0x3c800000, v94
	s_nop 0
	v_addc_co_u32_e32 v9, vcc, 0, v3, vcc
	v_mul_f32_e32 v11, 0x3c800000, v95
	global_store_dwordx4 v[8:9], v[4:7], off
	v_mul_f32_e32 v10, 0xbfb8aa3b, v10
	v_mul_f32_e32 v11, 0xbfb8aa3b, v11
	v_mul_f32_e32 v6, 0x3c800000, v96
	v_mul_f32_e32 v7, 0x3c800000, v97
	v_mul_f32_e32 v6, 0xbfb8aa3b, v6
	v_mul_f32_e32 v7, 0xbfb8aa3b, v7
	v_exp_f32_e32 v10, v10
	v_exp_f32_e32 v11, v11
	v_exp_f32_e32 v6, v6
	v_exp_f32_e32 v7, v7
	v_add_f32_e32 v4, 1.0, v10
	v_add_f32_e32 v5, 1.0, v11
	v_add_f32_e32 v6, 1.0, v6
	v_add_f32_e32 v7, 1.0, v7
	v_rcp_f32_e32 v4, v4
	v_rcp_f32_e32 v5, v5
	v_rcp_f32_e32 v6, v6
	v_rcp_f32_e32 v7, v7
	v_fmamk_f32 v4, v4, 0x437f0000, v196
	v_fmamk_f32 v5, v5, 0x437f0000, v196
	v_fmamk_f32 v6, v6, 0x437f0000, v196
	v_fmamk_f32 v7, v7, 0x437f0000, v196
	v_perm_b32 v4, v5, v4, s67
	v_perm_b32 v5, v7, v6, s67
	v_mul_f32_e32 v6, 0x3c800000, v90
	v_mul_f32_e32 v7, 0x3c800000, v91
	v_mul_f32_e32 v6, 0xbfb8aa3b, v6
	v_mul_f32_e32 v7, 0xbfb8aa3b, v7
	v_exp_f32_e32 v6, v6
	v_exp_f32_e32 v7, v7
	v_perm_b32 v4, v5, v4, s68
	v_mul_f32_e32 v8, 0x3c800000, v93
	v_add_f32_e32 v5, 1.0, v6
	v_add_f32_e32 v6, 1.0, v7
	v_mul_f32_e32 v7, 0x3c800000, v92
	v_mul_f32_e32 v7, 0xbfb8aa3b, v7
	v_mul_f32_e32 v8, 0xbfb8aa3b, v8
	v_exp_f32_e32 v7, v7
	v_exp_f32_e32 v8, v8
	v_rcp_f32_e32 v5, v5
	v_rcp_f32_e32 v6, v6
	v_add_f32_e32 v7, 1.0, v7
	v_add_f32_e32 v8, 1.0, v8
	v_rcp_f32_e32 v7, v7
	v_rcp_f32_e32 v8, v8
	v_fmamk_f32 v5, v5, 0x437f0000, v196
	v_fmamk_f32 v6, v6, 0x437f0000, v196
	v_fmamk_f32 v7, v7, 0x437f0000, v196
	v_fmamk_f32 v8, v8, 0x437f0000, v196
	v_perm_b32 v5, v6, v5, s67
	v_perm_b32 v6, v8, v7, s67
	v_mul_f32_e32 v7, 0x3c800000, v86
	v_mul_f32_e32 v8, 0x3c800000, v87
	v_mul_f32_e32 v7, 0xbfb8aa3b, v7
	v_mul_f32_e32 v8, 0xbfb8aa3b, v8
	v_exp_f32_e32 v7, v7
	v_exp_f32_e32 v8, v8
	v_perm_b32 v5, v6, v5, s68
	v_mul_f32_e32 v9, 0x3c800000, v89
	v_add_f32_e32 v6, 1.0, v7
	v_add_f32_e32 v7, 1.0, v8
	v_mul_f32_e32 v8, 0x3c800000, v88
	v_mul_f32_e32 v8, 0xbfb8aa3b, v8
	v_mul_f32_e32 v9, 0xbfb8aa3b, v9
	v_exp_f32_e32 v8, v8
	v_exp_f32_e32 v9, v9
	v_rcp_f32_e32 v6, v6
	v_rcp_f32_e32 v7, v7
	v_add_f32_e32 v8, 1.0, v8
	v_add_f32_e32 v9, 1.0, v9
	v_rcp_f32_e32 v8, v8
	v_rcp_f32_e32 v9, v9
	v_fmamk_f32 v6, v6, 0x437f0000, v196
	v_fmamk_f32 v7, v7, 0x437f0000, v196
	v_fmamk_f32 v8, v8, 0x437f0000, v196
	v_fmamk_f32 v9, v9, 0x437f0000, v196
	v_perm_b32 v6, v7, v6, s67
	v_perm_b32 v7, v9, v8, s67
	v_mul_f32_e32 v8, 0x3c800000, v82
	v_mul_f32_e32 v9, 0x3c800000, v83
	v_mul_f32_e32 v8, 0xbfb8aa3b, v8
	v_mul_f32_e32 v9, 0xbfb8aa3b, v9
	v_exp_f32_e32 v8, v8
	v_exp_f32_e32 v9, v9
	v_perm_b32 v6, v7, v6, s68
	v_mul_f32_e32 v10, 0x3c800000, v85
	v_add_f32_e32 v7, 1.0, v8
	v_add_f32_e32 v8, 1.0, v9
	v_mul_f32_e32 v9, 0x3c800000, v84
	v_mul_f32_e32 v9, 0xbfb8aa3b, v9
	v_mul_f32_e32 v10, 0xbfb8aa3b, v10
	v_exp_f32_e32 v9, v9
	v_exp_f32_e32 v10, v10
	v_rcp_f32_e32 v7, v7
	v_rcp_f32_e32 v8, v8
	v_add_f32_e32 v9, 1.0, v9
	v_add_f32_e32 v10, 1.0, v10
	v_rcp_f32_e32 v9, v9
	v_rcp_f32_e32 v10, v10
	v_fmamk_f32 v7, v7, 0x437f0000, v196
	v_fmamk_f32 v8, v8, 0x437f0000, v196
	v_fmamk_f32 v9, v9, 0x437f0000, v196
	v_fmamk_f32 v10, v10, 0x437f0000, v196
	v_perm_b32 v7, v8, v7, s67
; __device__ __forceinline__ float fsigmoid(float x) { return __builtin_amdgcn_rcpf(1.0f + __builtin_amdgcn_exp2f(-1.44269504f * x)); }
; __device__ __forceinline__ unsigned pk4_u8(float a, float b, float c, float d) {
;     const unsigned ya = __builtin_bit_cast(unsigned, a * 255.0f + 8388608.0f), yb = __builtin_bit_cast(unsigned, b * 255.0f + 8388608.0f), yc = __builtin_bit_cast(unsigned, c * 255.0f + 8388608.0f), yd = __builtin_bit_cast(unsigned, d * 255.0f + 8388608.0f);
;     const unsigned w01 = __builtin_amdgcn_perm(yb, ya, 0x0c0c0400u), w23 = __builtin_amdgcn_perm(yd, yc, 0x0c0c0400u);
;     return __builtin_amdgcn_perm(w23, w01, 0x05040100u); }
;     __device__ __forceinline__ void operator()(AccRef acc, const GUnit& u, int wr, int wc, int fr, int fq) const {
;         const int pm = u.x0, pn = u.x1; unsigned char* base = (pn < 8 ? GZF : GZS) + (size_t)(pm * 256 + wr * 64 + fr) * D + (pn & 7) * 256 + wc * 64 + 16 * fq;
; #pragma unroll
;         for (int ai = 0; ai < 2; ++ai)
; #pragma unroll
;             for (int m = 0; m < 4; ++m) { u32x4 w;
; #pragma unroll
;                 for (int bj = 0; bj < 2; ++bj)
; #pragma unroll
;                     for (int n = 0; n < 2; ++n) { const f32x4 v = acc[ai][bj][m][n]; w[bj * 2 + n] = pk4_u8(fsigmoid(v[0] * W8_INV), fsigmoid(v[1] * W8_INV), fsigmoid(v[2] * W8_INV), fsigmoid(v[3] * W8_INV)); }
;                 *(u32x4*)(base + (size_t)(ai * 128 + m * 16) * D) = w; }
	v_perm_b32 v8, v10, v9, s67
	v_perm_b32 v7, v8, v7, s68
	v_add_co_u32_e32 v8, vcc, s69, v2
	v_mul_f32_e32 v10, 0x3c800000, v78
	s_nop 0
	v_addc_co_u32_e32 v9, vcc, 0, v3, vcc
	v_mul_f32_e32 v11, 0x3c800000, v79
	global_store_dwordx4 v[8:9], v[4:7], off
	v_mul_f32_e32 v10, 0xbfb8aa3b, v10
	v_mul_f32_e32 v11, 0xbfb8aa3b, v11
	v_mul_f32_e32 v6, 0x3c800000, v80
	v_mul_f32_e32 v7, 0x3c800000, v81
	v_mul_f32_e32 v6, 0xbfb8aa3b, v6
	v_mul_f32_e32 v7, 0xbfb8aa3b, v7
	v_exp_f32_e32 v10, v10
	v_exp_f32_e32 v11, v11
	v_exp_f32_e32 v6, v6
	v_exp_f32_e32 v7, v7
	v_add_f32_e32 v4, 1.0, v10
	v_add_f32_e32 v5, 1.0, v11
	v_add_f32_e32 v6, 1.0, v6
	v_add_f32_e32 v7, 1.0, v7
	v_rcp_f32_e32 v4, v4
	v_rcp_f32_e32 v5, v5
	v_rcp_f32_e32 v6, v6
	v_rcp_f32_e32 v7, v7
	v_fmamk_f32 v4, v4, 0x437f0000, v196
	v_fmamk_f32 v5, v5, 0x437f0000, v196
	v_fmamk_f32 v6, v6, 0x437f0000, v196
	v_fmamk_f32 v7, v7, 0x437f0000, v196
	v_perm_b32 v4, v5, v4, s67
	v_perm_b32 v5, v7, v6, s67
	v_mul_f32_e32 v6, 0x3c800000, v74
	v_mul_f32_e32 v7, 0x3c800000, v75
	v_mul_f32_e32 v6, 0xbfb8aa3b, v6
	v_mul_f32_e32 v7, 0xbfb8aa3b, v7
	v_exp_f32_e32 v6, v6
	v_exp_f32_e32 v7, v7
	v_perm_b32 v4, v5, v4, s68
	v_mul_f32_e32 v8, 0x3c800000, v77
	v_add_f32_e32 v5, 1.0, v6
	v_add_f32_e32 v6, 1.0, v7
	v_mul_f32_e32 v7, 0x3c800000, v76
	v_mul_f32_e32 v7, 0xbfb8aa3b, v7
	v_mul_f32_e32 v8, 0xbfb8aa3b, v8
	v_exp_f32_e32 v7, v7
	v_exp_f32_e32 v8, v8
	v_rcp_f32_e32 v5, v5
	v_rcp_f32_e32 v6, v6
	v_add_f32_e32 v7, 1.0, v7
	v_add_f32_e32 v8, 1.0, v8
	v_rcp_f32_e32 v7, v7
	v_rcp_f32_e32 v8, v8
	v_fmamk_f32 v5, v5, 0x437f0000, v196
	v_fmamk_f32 v6, v6, 0x437f0000, v196
	v_fmamk_f32 v7, v7, 0x437f0000, v196
	v_fmamk_f32 v8, v8, 0x437f0000, v196
	v_perm_b32 v5, v6, v5, s67
	v_perm_b32 v6, v8, v7, s67
	v_mul_f32_e32 v7, 0x3c800000, v70
	v_mul_f32_e32 v8, 0x3c800000, v71
	v_mul_f32_e32 v7, 0xbfb8aa3b, v7
	v_mul_f32_e32 v8, 0xbfb8aa3b, v8
	v_exp_f32_e32 v7, v7
	v_exp_f32_e32 v8, v8
	v_perm_b32 v5, v6, v5, s68
	v_mul_f32_e32 v9, 0x3c800000, v73
	v_add_f32_e32 v6, 1.0, v7
	v_add_f32_e32 v7, 1.0, v8
	v_mul_f32_e32 v8, 0x3c800000, v72
	v_mul_f32_e32 v8, 0xbfb8aa3b, v8
	v_mul_f32_e32 v9, 0xbfb8aa3b, v9
	v_exp_f32_e32 v8, v8
	v_exp_f32_e32 v9, v9
	v_rcp_f32_e32 v6, v6
	v_rcp_f32_e32 v7, v7
	v_add_f32_e32 v8, 1.0, v8
	v_add_f32_e32 v9, 1.0, v9
	v_rcp_f32_e32 v8, v8
	v_rcp_f32_e32 v9, v9
	v_fmamk_f32 v6, v6, 0x437f0000, v196
	v_fmamk_f32 v7, v7, 0x437f0000, v196
	v_fmamk_f32 v8, v8, 0x437f0000, v196
	v_fmamk_f32 v9, v9, 0x437f0000, v196
	v_perm_b32 v6, v7, v6, s67
	v_perm_b32 v7, v9, v8, s67
	v_mul_f32_e32 v8, 0x3c800000, v66
	v_mul_f32_e32 v9, 0x3c800000, v67
	v_mul_f32_e32 v8, 0xbfb8aa3b, v8
	v_mul_f32_e32 v9, 0xbfb8aa3b, v9
	v_exp_f32_e32 v8, v8
	v_exp_f32_e32 v9, v9
	v_perm_b32 v6, v7, v6, s68
	v_mul_f32_e32 v10, 0x3c800000, v69
	v_add_f32_e32 v7, 1.0, v8
	v_add_f32_e32 v8, 1.0, v9
	v_mul_f32_e32 v9, 0x3c800000, v68
	v_mul_f32_e32 v9, 0xbfb8aa3b, v9
	v_mul_f32_e32 v10, 0xbfb8aa3b, v10
	v_exp_f32_e32 v9, v9
	v_exp_f32_e32 v10, v10
	v_rcp_f32_e32 v7, v7
	v_rcp_f32_e32 v8, v8
	v_add_f32_e32 v9, 1.0, v9
	v_add_f32_e32 v10, 1.0, v10
	v_rcp_f32_e32 v9, v9
	v_rcp_f32_e32 v10, v10
	v_fmamk_f32 v7, v7, 0x437f0000, v196
	v_fmamk_f32 v8, v8, 0x437f0000, v196
	v_fmamk_f32 v9, v9, 0x437f0000, v196
	v_fmamk_f32 v10, v10, 0x437f0000, v196
	v_perm_b32 v7, v8, v7, s67
	v_perm_b32 v8, v10, v9, s67
	v_perm_b32 v7, v8, v7, s68
	v_add_co_u32_e32 v8, vcc, s70, v2
	v_mul_f32_e32 v10, 0x3c800000, v62
	s_nop 0
	v_addc_co_u32_e32 v9, vcc, 0, v3, vcc
	v_mul_f32_e32 v11, 0x3c800000, v63
	global_store_dwordx4 v[8:9], v[4:7], off
	v_mul_f32_e32 v10, 0xbfb8aa3b, v10
	v_mul_f32_e32 v11, 0xbfb8aa3b, v11
	v_mul_f32_e32 v6, 0x3c800000, v64
	v_mul_f32_e32 v7, 0x3c800000, v65
	v_mul_f32_e32 v6, 0xbfb8aa3b, v6
	v_mul_f32_e32 v7, 0xbfb8aa3b, v7
	v_exp_f32_e32 v10, v10
	v_exp_f32_e32 v11, v11
	v_exp_f32_e32 v6, v6
	v_exp_f32_e32 v7, v7
	v_add_f32_e32 v4, 1.0, v10
	v_add_f32_e32 v5, 1.0, v11
	v_add_f32_e32 v6, 1.0, v6
	v_add_f32_e32 v7, 1.0, v7
	v_rcp_f32_e32 v4, v4
	v_rcp_f32_e32 v5, v5
	v_rcp_f32_e32 v6, v6
	v_rcp_f32_e32 v7, v7
	v_fmamk_f32 v4, v4, 0x437f0000, v196
	v_fmamk_f32 v5, v5, 0x437f0000, v196
	v_fmamk_f32 v6, v6, 0x437f0000, v196
	v_fmamk_f32 v7, v7, 0x437f0000, v196
	v_perm_b32 v4, v5, v4, s67
	v_perm_b32 v5, v7, v6, s67
	v_mul_f32_e32 v6, 0x3c800000, v58
	v_mul_f32_e32 v7, 0x3c800000, v59
	v_mul_f32_e32 v6, 0xbfb8aa3b, v6
	v_mul_f32_e32 v7, 0xbfb8aa3b, v7
	v_exp_f32_e32 v6, v6
	v_exp_f32_e32 v7, v7
	v_perm_b32 v4, v5, v4, s68
	v_mul_f32_e32 v8, 0x3c800000, v61
	v_add_f32_e32 v5, 1.0, v6
	v_add_f32_e32 v6, 1.0, v7
	v_mul_f32_e32 v7, 0x3c800000, v60
	v_mul_f32_e32 v7, 0xbfb8aa3b, v7
	v_mul_f32_e32 v8, 0xbfb8aa3b, v8
	v_exp_f32_e32 v7, v7
	v_exp_f32_e32 v8, v8
	v_rcp_f32_e32 v5, v5
	v_rcp_f32_e32 v6, v6
	v_add_f32_e32 v7, 1.0, v7
	v_add_f32_e32 v8, 1.0, v8
	v_rcp_f32_e32 v7, v7
	v_rcp_f32_e32 v8, v8
	v_fmamk_f32 v5, v5, 0x437f0000, v196
	v_fmamk_f32 v6, v6, 0x437f0000, v196
	v_fmamk_f32 v7, v7, 0x437f0000, v196
	v_fmamk_f32 v8, v8, 0x437f0000, v196
	v_perm_b32 v5, v6, v5, s67
	v_perm_b32 v6, v8, v7, s67
	v_mul_f32_e32 v7, 0x3c800000, v54
	v_mul_f32_e32 v8, 0x3c800000, v55
; __device__ __forceinline__ float fsigmoid(float x) { return __builtin_amdgcn_rcpf(1.0f + __builtin_amdgcn_exp2f(-1.44269504f * x)); }
; __device__ __forceinline__ unsigned pk4_u8(float a, float b, float c, float d) {
;     const unsigned ya = __builtin_bit_cast(unsigned, a * 255.0f + 8388608.0f), yb = __builtin_bit_cast(unsigned, b * 255.0f + 8388608.0f), yc = __builtin_bit_cast(unsigned, c * 255.0f + 8388608.0f), yd = __builtin_bit_cast(unsigned, d * 255.0f + 8388608.0f);
;     const unsigned w01 = __builtin_amdgcn_perm(yb, ya, 0x0c0c0400u), w23 = __builtin_amdgcn_perm(yd, yc, 0x0c0c0400u);
;     return __builtin_amdgcn_perm(w23, w01, 0x05040100u); }
;     __device__ __forceinline__ void operator()(AccRef acc, const GUnit& u, int wr, int wc, int fr, int fq) const {
;         const int pm = u.x0, pn = u.x1; unsigned char* base = (pn < 8 ? GZF : GZS) + (size_t)(pm * 256 + wr * 64 + fr) * D + (pn & 7) * 256 + wc * 64 + 16 * fq;
; #pragma unroll
;         for (int ai = 0; ai < 2; ++ai)
; #pragma unroll
;             for (int m = 0; m < 4; ++m) { u32x4 w;
; #pragma unroll
;                 for (int bj = 0; bj < 2; ++bj)
; #pragma unroll
;                     for (int n = 0; n < 2; ++n) { const f32x4 v = acc[ai][bj][m][n]; w[bj * 2 + n] = pk4_u8(fsigmoid(v[0] * W8_INV), fsigmoid(v[1] * W8_INV), fsigmoid(v[2] * W8_INV), fsigmoid(v[3] * W8_INV)); }
;                 *(u32x4*)(base + (size_t)(ai * 128 + m * 16) * D) = w; }
	v_mul_f32_e32 v7, 0xbfb8aa3b, v7
	v_mul_f32_e32 v8, 0xbfb8aa3b, v8
	v_exp_f32_e32 v7, v7
	v_exp_f32_e32 v8, v8
	v_perm_b32 v5, v6, v5, s68
	v_mul_f32_e32 v9, 0x3c800000, v57
	v_add_f32_e32 v6, 1.0, v7
	v_add_f32_e32 v7, 1.0, v8
	v_mul_f32_e32 v8, 0x3c800000, v56
	v_mul_f32_e32 v8, 0xbfb8aa3b, v8
	v_mul_f32_e32 v9, 0xbfb8aa3b, v9
	v_exp_f32_e32 v8, v8
	v_exp_f32_e32 v9, v9
	v_rcp_f32_e32 v6, v6
	v_rcp_f32_e32 v7, v7
	v_add_f32_e32 v8, 1.0, v8
	v_add_f32_e32 v9, 1.0, v9
	v_rcp_f32_e32 v8, v8
	v_rcp_f32_e32 v9, v9
	v_fmamk_f32 v6, v6, 0x437f0000, v196
	v_fmamk_f32 v7, v7, 0x437f0000, v196
	v_fmamk_f32 v8, v8, 0x437f0000, v196
	v_fmamk_f32 v9, v9, 0x437f0000, v196
	v_perm_b32 v6, v7, v6, s67
	v_perm_b32 v7, v9, v8, s67
	v_mul_f32_e32 v8, 0x3c800000, v50
	v_mul_f32_e32 v9, 0x3c800000, v51
	v_mul_f32_e32 v8, 0xbfb8aa3b, v8
	v_mul_f32_e32 v9, 0xbfb8aa3b, v9
	v_exp_f32_e32 v8, v8
	v_exp_f32_e32 v9, v9
	v_perm_b32 v6, v7, v6, s68
	v_mul_f32_e32 v10, 0x3c800000, v53
	v_add_f32_e32 v7, 1.0, v8
	v_add_f32_e32 v8, 1.0, v9
	v_mul_f32_e32 v9, 0x3c800000, v52
	v_mul_f32_e32 v9, 0xbfb8aa3b, v9
	v_mul_f32_e32 v10, 0xbfb8aa3b, v10
	v_exp_f32_e32 v9, v9
	v_exp_f32_e32 v10, v10
	v_rcp_f32_e32 v7, v7
	v_rcp_f32_e32 v8, v8
	v_add_f32_e32 v9, 1.0, v9
	v_add_f32_e32 v10, 1.0, v10
	v_rcp_f32_e32 v9, v9
	v_rcp_f32_e32 v10, v10
	v_fmamk_f32 v7, v7, 0x437f0000, v196
	v_fmamk_f32 v8, v8, 0x437f0000, v196
	v_fmamk_f32 v9, v9, 0x437f0000, v196
	v_fmamk_f32 v10, v10, 0x437f0000, v196
	v_perm_b32 v7, v8, v7, s67
	v_perm_b32 v8, v10, v9, s67
	v_perm_b32 v7, v8, v7, s68
	v_add_co_u32_e32 v8, vcc, s71, v2
	v_mul_f32_e32 v10, 0x3c800000, v46
	s_nop 0
	v_addc_co_u32_e32 v9, vcc, 0, v3, vcc
	v_mul_f32_e32 v11, 0x3c800000, v47
	global_store_dwordx4 v[8:9], v[4:7], off
	v_mul_f32_e32 v10, 0xbfb8aa3b, v10
	v_mul_f32_e32 v11, 0xbfb8aa3b, v11
	v_mul_f32_e32 v6, 0x3c800000, v48
	v_mul_f32_e32 v7, 0x3c800000, v49
	v_mul_f32_e32 v6, 0xbfb8aa3b, v6
	v_mul_f32_e32 v7, 0xbfb8aa3b, v7
	v_exp_f32_e32 v10, v10
	v_exp_f32_e32 v11, v11
	v_exp_f32_e32 v6, v6
	v_exp_f32_e32 v7, v7
	v_add_f32_e32 v4, 1.0, v10
	v_add_f32_e32 v5, 1.0, v11
	v_add_f32_e32 v6, 1.0, v6
	v_add_f32_e32 v7, 1.0, v7
	v_rcp_f32_e32 v4, v4
	v_rcp_f32_e32 v5, v5
	v_rcp_f32_e32 v6, v6
	v_rcp_f32_e32 v7, v7
	v_fmamk_f32 v4, v4, 0x437f0000, v196
	v_fmamk_f32 v5, v5, 0x437f0000, v196
	v_fmamk_f32 v6, v6, 0x437f0000, v196
	v_fmamk_f32 v7, v7, 0x437f0000, v196
	v_perm_b32 v4, v5, v4, s67
	v_perm_b32 v5, v7, v6, s67
	v_mul_f32_e32 v6, 0x3c800000, v42
	v_mul_f32_e32 v7, 0x3c800000, v43
	v_mul_f32_e32 v6, 0xbfb8aa3b, v6
	v_mul_f32_e32 v7, 0xbfb8aa3b, v7
	v_exp_f32_e32 v6, v6
	v_exp_f32_e32 v7, v7
	v_perm_b32 v4, v5, v4, s68
	v_mul_f32_e32 v8, 0x3c800000, v45
	v_add_f32_e32 v5, 1.0, v6
	v_add_f32_e32 v6, 1.0, v7
	v_mul_f32_e32 v7, 0x3c800000, v44
	v_mul_f32_e32 v7, 0xbfb8aa3b, v7
	v_mul_f32_e32 v8, 0xbfb8aa3b, v8
	v_exp_f32_e32 v7, v7
	v_exp_f32_e32 v8, v8
	v_rcp_f32_e32 v5, v5
	v_rcp_f32_e32 v6, v6
	v_add_f32_e32 v7, 1.0, v7
	v_add_f32_e32 v8, 1.0, v8
	v_rcp_f32_e32 v7, v7
	v_rcp_f32_e32 v8, v8
	v_fmamk_f32 v5, v5, 0x437f0000, v196
	v_fmamk_f32 v6, v6, 0x437f0000, v196
	v_fmamk_f32 v7, v7, 0x437f0000, v196
	v_fmamk_f32 v8, v8, 0x437f0000, v196
	v_perm_b32 v5, v6, v5, s67
	v_perm_b32 v6, v8, v7, s67
	v_mul_f32_e32 v7, 0x3c800000, v38
	v_mul_f32_e32 v8, 0x3c800000, v39
	v_mul_f32_e32 v7, 0xbfb8aa3b, v7
	v_mul_f32_e32 v8, 0xbfb8aa3b, v8
	v_exp_f32_e32 v7, v7
	v_exp_f32_e32 v8, v8
	v_perm_b32 v5, v6, v5, s68
	v_mul_f32_e32 v9, 0x3c800000, v41
	v_add_f32_e32 v6, 1.0, v7
	v_add_f32_e32 v7, 1.0, v8
	v_mul_f32_e32 v8, 0x3c800000, v40
	v_mul_f32_e32 v8, 0xbfb8aa3b, v8
	v_mul_f32_e32 v9, 0xbfb8aa3b, v9
	v_exp_f32_e32 v8, v8
	v_exp_f32_e32 v9, v9
	v_rcp_f32_e32 v6, v6
	v_rcp_f32_e32 v7, v7
	v_add_f32_e32 v8, 1.0, v8
	v_add_f32_e32 v9, 1.0, v9
	v_rcp_f32_e32 v8, v8
	v_rcp_f32_e32 v9, v9
	v_fmamk_f32 v6, v6, 0x437f0000, v196
	v_fmamk_f32 v7, v7, 0x437f0000, v196
	v_fmamk_f32 v8, v8, 0x437f0000, v196
	v_fmamk_f32 v9, v9, 0x437f0000, v196
	v_perm_b32 v6, v7, v6, s67
	v_perm_b32 v7, v9, v8, s67
	v_mul_f32_e32 v8, 0x3c800000, v34
	v_mul_f32_e32 v9, 0x3c800000, v35
	v_mul_f32_e32 v8, 0xbfb8aa3b, v8
	v_mul_f32_e32 v9, 0xbfb8aa3b, v9
	v_exp_f32_e32 v8, v8
	v_exp_f32_e32 v9, v9
	v_perm_b32 v6, v7, v6, s68
	v_mul_f32_e32 v10, 0x3c800000, v37
	v_add_f32_e32 v7, 1.0, v8
	v_add_f32_e32 v8, 1.0, v9
	v_mul_f32_e32 v9, 0x3c800000, v36
	v_mul_f32_e32 v9, 0xbfb8aa3b, v9
	v_mul_f32_e32 v10, 0xbfb8aa3b, v10
	v_exp_f32_e32 v9, v9
	v_exp_f32_e32 v10, v10
	v_rcp_f32_e32 v7, v7
	v_rcp_f32_e32 v8, v8
	v_add_f32_e32 v9, 1.0, v9
	v_add_f32_e32 v10, 1.0, v10
	v_rcp_f32_e32 v9, v9
	v_rcp_f32_e32 v10, v10
	v_fmamk_f32 v7, v7, 0x437f0000, v196
	v_fmamk_f32 v8, v8, 0x437f0000, v196
	v_fmamk_f32 v9, v9, 0x437f0000, v196
	v_fmamk_f32 v10, v10, 0x437f0000, v196
	v_add_co_u32_e32 v2, vcc, 0x58000, v2
	v_perm_b32 v7, v8, v7, s67
	v_perm_b32 v8, v10, v9, s67
	v_addc_co_u32_e32 v3, vcc, 0, v3, vcc
	v_perm_b32 v7, v8, v7, s68
	s_andn2_b64 vcc, exec, s[0:1]
	s_mov_b64 s[0:1], -1
	global_store_dwordx4 v[2:3], v[4:7], off
	s_cbranch_vccnz .LBB0_420
	s_andn2_b64 vcc, exec, s[10:11]
	s_cbranch_vccnz .LBB0_419
	s_branch .LBB0_419

; #define PG8_STAGE(bufoff, gbase, voff) do { _Pragma("unroll") for (int _i = 0; _i < 2; ++_i) \
;         __builtin_amdgcn_global_load_lds((const unsigned*)((const char*)(gbase) + (voff)[_i]), (PG8_LAS unsigned*)(lds + (bufoff) + ldsw + _i * 8192), 16, 0, 0); } while (0)
; #define PG8_WAIT_V(n) asm volatile("s_waitcnt vmcnt(" #n ")" ::: "memory")
; #define PG8_WAIT_L(n) asm volatile("s_waitcnt lgkmcnt(" #n ")" ::: "memory")
; #define PG8_BAR __builtin_amdgcn_s_barrier()
; #define PG8_SCHED __builtin_amdgcn_sched_barrier(0)
; template <class Epi, class Sched, bool ALIGN_EPI = true, bool F8 = false>
; __device__ __forceinline__ void gemm_phase(PG8_LAS unsigned char* lds, const Sched& S, const Epi& E) {
;     ...
;             PG8_LDB(B0, 0, 0); PG8_LDB(B1, 0, 1); PG8_SCHED; PG8_LDA(At, 0, 0); PG8_STAGE(PG8_SA(1, 1), a1, voffA[1]);
;             PG8_WAIT_V(8); PG8_WAIT_L(0); PG8_BAR; PG8_MMA(0, 0, At, B0); PG8_MMA(0, 1, At, B1); PG8_BAR; PG8_SCHED;
;             PG8_LDA(At, 0, 1); PG8_STAGE(PG8_SB(0, 0), b2, voffB[0]); PG8_STAGE(PG8_SB(0, 1), b2, voffB[1]); PG8_STAGE(PG8_SA(0, 0), a2, vA2[0]);
;             PG8_WAIT_V(8); PG8_WAIT_L(0); PG8_BAR; PG8_MMA(1, 0, At, B0); PG8_MMA(1, 1, At, B1); PG8_BAR; PG8_SCHED;
;             PG8_LDB(B0, 1, 0); PG8_LDB(B1, 1, 1); PG8_SCHED; PG8_LDA(At, 1, 0); PG8_STAGE(PG8_SA(0, 1), a2, vA2[1]);
;             PG8_WAIT_V(8); PG8_WAIT_L(0); PG8_BAR; PG8_MMA(0, 0, At, B0); PG8_MMA(0, 1, At, B1); PG8_BAR; PG8_SCHED;
.LBB0_834:
	v_add_u32_e32 v10, s58, v190
	ds_read_b128 v[2:5], v10
	ds_read_b128 v[6:9], v10 offset:1024
	ds_read_b128 v[142:145], v10 offset:2048
	ds_read_b128 v[146:149], v10 offset:3072
	v_add_u32_e32 v10, s59, v190
	ds_read_b128 v[150:153], v10
	ds_read_b128 v[154:157], v10 offset:1024
	ds_read_b128 v[202:205], v10 offset:2048
	ds_read_b128 v[206:209], v10 offset:3072
	s_add_i32 s77, s26, 2
	s_add_u32 s27, s24, 0x8000
	s_addc_u32 s28, s25, 0
	s_cmp_eq_u32 s74, s26
	s_cselect_b32 s30, s20, s27
	s_cselect_b32 s31, s21, s28
	s_cselect_b32 s28, s22, s75
	s_cselect_b32 s29, s23, s76
	s_add_u32 s26, s30, 0x8000
	s_addc_u32 s27, s31, 0
	s_add_i32 m0, s45, 0xc000
	ds_read_b128 v[210:213], v198
	ds_read_b128 v[214:217], v198 offset:1024
	ds_read_b128 v[218:221], v198 offset:2048
	ds_read_b128 v[222:225], v198 offset:3072
	ds_read_b128 v[226:229], v198 offset:4096
	ds_read_b128 v[230:233], v198 offset:5120
	ds_read_b128 v[234:237], v198 offset:6144
	ds_read_b128 v[238:241], v198 offset:7168
	global_load_lds_dwordx4 v182, s[24:25]
	s_add_i32 m0, s45, 0xe000
	s_nop 0
	global_load_lds_dwordx4 v180, s[24:25]
	s_waitcnt vmcnt(8)
	s_waitcnt lgkmcnt(0)
	s_setprio 1
	s_waitcnt lgkmcnt(0)
	v_mfma_scale_f32_16x16x128_f8f6f4 v[138:141], v[2:9], v[210:217], v[138:141], v199, v199 op_sel_hi:[0,0,0]
	v_mfma_scale_f32_16x16x128_f8f6f4 v[134:137], v[142:149], v[210:217], v[134:137], v199, v199 op_sel_hi:[0,0,0]
	v_mfma_scale_f32_16x16x128_f8f6f4 v[130:133], v[2:9], v[218:225], v[130:133], v199, v199 op_sel_hi:[0,0,0]
	v_mfma_scale_f32_16x16x128_f8f6f4 v[126:129], v[142:149], v[218:225], v[126:129], v199, v199 op_sel_hi:[0,0,0]
	v_mfma_scale_f32_16x16x128_f8f6f4 v[122:125], v[2:9], v[226:233], v[122:125], v199, v199 op_sel_hi:[0,0,0]
	v_mfma_scale_f32_16x16x128_f8f6f4 v[118:121], v[142:149], v[226:233], v[118:121], v199, v199 op_sel_hi:[0,0,0]
	v_mfma_scale_f32_16x16x128_f8f6f4 v[114:117], v[2:9], v[234:241], v[114:117], v199, v199 op_sel_hi:[0,0,0]
	v_mfma_scale_f32_16x16x128_f8f6f4 v[110:113], v[142:149], v[234:241], v[110:113], v199, v199 op_sel_hi:[0,0,0]
	s_nop 3
	s_setprio 0
	s_setprio 1
	v_mfma_scale_f32_16x16x128_f8f6f4 v[106:109], v[150:157], v[210:217], v[106:109], v199, v199 op_sel_hi:[0,0,0]
	v_mfma_scale_f32_16x16x128_f8f6f4 v[102:105], v[202:209], v[210:217], v[102:105], v199, v199 op_sel_hi:[0,0,0]
	v_mfma_scale_f32_16x16x128_f8f6f4 v[98:101], v[150:157], v[218:225], v[98:101], v199, v199 op_sel_hi:[0,0,0]
	v_mfma_scale_f32_16x16x128_f8f6f4 v[94:97], v[202:209], v[218:225], v[94:97], v199, v199 op_sel_hi:[0,0,0]
	v_mfma_scale_f32_16x16x128_f8f6f4 v[90:93], v[150:157], v[226:233], v[90:93], v199, v199 op_sel_hi:[0,0,0]
	v_mfma_scale_f32_16x16x128_f8f6f4 v[86:89], v[202:209], v[226:233], v[86:89], v199, v199 op_sel_hi:[0,0,0]
	v_mfma_scale_f32_16x16x128_f8f6f4 v[82:85], v[150:157], v[234:241], v[82:85], v199, v199 op_sel_hi:[0,0,0]
	v_mfma_scale_f32_16x16x128_f8f6f4 v[78:81], v[202:209], v[234:241], v[78:81], v199, v199 op_sel_hi:[0,0,0]
	s_nop 3
	s_setprio 0
	s_barrier
	s_add_i32 s78, s58, s44
	s_mov_b32 m0, s78
	ds_read_b128 v[210:213], v198 offset:16384
	ds_read_b128 v[214:217], v198 offset:17408
	ds_read_b128 v[218:221], v198 offset:18432
	ds_read_b128 v[222:225], v198 offset:19456
	ds_read_b128 v[226:229], v198 offset:20480
	ds_read_b128 v[230:233], v198 offset:21504
	ds_read_b128 v[234:237], v198 offset:22528
	ds_read_b128 v[238:241], v198 offset:23552
	global_load_lds_dwordx4 v158, s[28:29]
	s_add_i32 m0, s78, 0x2000
	s_add_i32 s78, s59, s44
	global_load_lds_dwordx4 v160, s[28:29]
	s_add_u32 s98, s28, s8
	s_addc_u32 s99, s29, s9
	s_mov_b32 m0, s78
	s_nop 0
	global_load_lds_dwordx4 v158, s[98:99]
	s_add_u32 s100, s28, s8
	s_addc_u32 s101, s29, s9
	s_add_i32 m0, s78, 0x2000
	s_nop 0
	global_load_lds_dwordx4 v160, s[100:101]
	s_mov_b32 m0, s45
	s_nop 0
	global_load_lds_dwordx4 v162, s[30:31]
	s_mov_b32 m0, s46
	s_nop 0
	global_load_lds_dwordx4 v164, s[30:31]
	s_waitcnt vmcnt(8)
	s_waitcnt lgkmcnt(0)
	s_setprio 1
	s_waitcnt lgkmcnt(0)
	v_mfma_scale_f32_16x16x128_f8f6f4 v[74:77], v[2:9], v[210:217], v[74:77], v199, v199 op_sel_hi:[0,0,0]
	v_mfma_scale_f32_16x16x128_f8f6f4 v[70:73], v[142:149], v[210:217], v[70:73], v199, v199 op_sel_hi:[0,0,0]
	v_mfma_scale_f32_16x16x128_f8f6f4 v[66:69], v[2:9], v[218:225], v[66:69], v199, v199 op_sel_hi:[0,0,0]
	v_mfma_scale_f32_16x16x128_f8f6f4 v[62:65], v[142:149], v[218:225], v[62:65], v199, v199 op_sel_hi:[0,0,0]
	v_mfma_scale_f32_16x16x128_f8f6f4 v[58:61], v[2:9], v[226:233], v[58:61], v199, v199 op_sel_hi:[0,0,0]
	v_mfma_scale_f32_16x16x128_f8f6f4 v[54:57], v[142:149], v[226:233], v[54:57], v199, v199 op_sel_hi:[0,0,0]
	v_mfma_scale_f32_16x16x128_f8f6f4 v[50:53], v[2:9], v[234:241], v[50:53], v199, v199 op_sel_hi:[0,0,0]
	v_mfma_scale_f32_16x16x128_f8f6f4 v[46:49], v[142:149], v[234:241], v[46:49], v199, v199 op_sel_hi:[0,0,0]
	s_nop 3
	s_setprio 0
	s_setprio 1
	v_mfma_scale_f32_16x16x128_f8f6f4 v[42:45], v[150:157], v[210:217], v[42:45], v199, v199 op_sel_hi:[0,0,0]
	v_mfma_scale_f32_16x16x128_f8f6f4 v[38:41], v[202:209], v[210:217], v[38:41], v199, v199 op_sel_hi:[0,0,0]
	v_mfma_scale_f32_16x16x128_f8f6f4 v[34:37], v[150:157], v[218:225], v[34:37], v199, v199 op_sel_hi:[0,0,0]
	v_mfma_scale_f32_16x16x128_f8f6f4 v[30:33], v[202:209], v[218:225], v[30:33], v199, v199 op_sel_hi:[0,0,0]
	v_mfma_scale_f32_16x16x128_f8f6f4 v[26:29], v[150:157], v[226:233], v[26:29], v199, v199 op_sel_hi:[0,0,0]
	v_mfma_scale_f32_16x16x128_f8f6f4 v[22:25], v[202:209], v[226:233], v[22:25], v199, v199 op_sel_hi:[0,0,0]
	v_mfma_scale_f32_16x16x128_f8f6f4 v[18:21], v[150:157], v[234:241], v[18:21], v199, v199 op_sel_hi:[0,0,0]
	v_mfma_scale_f32_16x16x128_f8f6f4 v[14:17], v[202:209], v[234:241], v[14:17], v199, v199 op_sel_hi:[0,0,0]
	s_nop 3
	s_setprio 0
	s_barrier
; #define PG8_STAGE(bufoff, gbase, voff) do { _Pragma("unroll") for (int _i = 0; _i < 2; ++_i) \
;         __builtin_amdgcn_global_load_lds((const unsigned*)((const char*)(gbase) + (voff)[_i]), (PG8_LAS unsigned*)(lds + (bufoff) + ldsw + _i * 8192), 16, 0, 0); } while (0)
; #define PG8_WAIT_V(n) asm volatile("s_waitcnt vmcnt(" #n ")" ::: "memory")
; #define PG8_WAIT_L(n) asm volatile("s_waitcnt lgkmcnt(" #n ")" ::: "memory")
; #define PG8_BAR __builtin_amdgcn_s_barrier()
; #define PG8_SCHED __builtin_amdgcn_sched_barrier(0)
; template <class Epi, class Sched, bool ALIGN_EPI = true, bool F8 = false>
; __device__ __forceinline__ void gemm_phase(PG8_LAS unsigned char* lds, const Sched& S, const Epi& E) {
;     ...
;         for (int t = 0; t < nt; t += 2) {
;             const bool last = (t == nt - 2);
;             if constexpr (Sched::GATHER) { if (last && has_next) S.a_off(nxt, Rs, Cs, voffAn); }
;             const char* a1 = cA + (size_t)(t + 1) * kstep;
;             const char* a2 = last ? nA : cA + (size_t)(t + 2) * kstep; const char* b2 = last ? nB : cB + (size_t)(t + 2) * kstepB;
;             const char* a3 = a2 + kstep; const char* b3 = b2 + kstepB;
;     ...
;             PG8_LDB(B0, 1, 0); PG8_LDB(B1, 1, 1); PG8_SCHED; PG8_LDA(At, 1, 0); PG8_STAGE(PG8_SA(0, 1), a2, vA2[1]);
;             PG8_WAIT_V(8); PG8_WAIT_L(0); PG8_BAR; PG8_MMA(0, 0, At, B0); PG8_MMA(0, 1, At, B1); PG8_BAR; PG8_SCHED;
;             PG8_LDA(At, 1, 1); PG8_STAGE(PG8_SB(1, 0), b3, voffB[0]); PG8_STAGE(PG8_SB(1, 1), b3, voffB[1]); PG8_STAGE(PG8_SA(1, 0), a3, vA2[0]);
;             PG8_WAIT_V(8); PG8_WAIT_L(0); PG8_BAR; PG8_MMA(1, 0, At, B0); PG8_MMA(1, 1, At, B1); PG8_BAR; PG8_SCHED;
;         }
	s_add_i32 s78, 0, 0x18000
	s_add_i32 s79, 0, 0x1c000
	v_add_u32_e32 v2, s78, v190
	v_add_u32_e32 v10, s79, v190
	ds_read_b128 v[142:145], v2
	ds_read_b128 v[146:149], v2 offset:1024
	ds_read_b128 v[150:153], v2 offset:2048
	ds_read_b128 v[154:157], v2 offset:3072
	ds_read_b128 v[2:5], v10
	ds_read_b128 v[6:9], v10 offset:1024
	ds_read_b128 v[202:205], v10 offset:2048
	ds_read_b128 v[206:209], v10 offset:3072
	s_mov_b32 m0, s47
	ds_read_b128 v[210:213], v198 offset:32768
	ds_read_b128 v[214:217], v198 offset:33792
	ds_read_b128 v[218:221], v198 offset:34816
	ds_read_b128 v[222:225], v198 offset:35840
	ds_read_b128 v[226:229], v198 offset:36864
	ds_read_b128 v[230:233], v198 offset:37888
	ds_read_b128 v[234:237], v198 offset:38912
	ds_read_b128 v[238:241], v198 offset:39936
	global_load_lds_dwordx4 v166, s[30:31]
	s_mov_b32 m0, s48
	s_nop 0
	global_load_lds_dwordx4 v168, s[30:31]
	s_waitcnt vmcnt(8)
	s_waitcnt lgkmcnt(0)
	s_setprio 1
	s_waitcnt lgkmcnt(0)
	v_mfma_scale_f32_16x16x128_f8f6f4 v[138:141], v[142:149], v[210:217], v[138:141], v199, v199 op_sel_hi:[0,0,0]
	v_mfma_scale_f32_16x16x128_f8f6f4 v[134:137], v[150:157], v[210:217], v[134:137], v199, v199 op_sel_hi:[0,0,0]
	v_mfma_scale_f32_16x16x128_f8f6f4 v[130:133], v[142:149], v[218:225], v[130:133], v199, v199 op_sel_hi:[0,0,0]
	v_mfma_scale_f32_16x16x128_f8f6f4 v[126:129], v[150:157], v[218:225], v[126:129], v199, v199 op_sel_hi:[0,0,0]
	v_mfma_scale_f32_16x16x128_f8f6f4 v[122:125], v[142:149], v[226:233], v[122:125], v199, v199 op_sel_hi:[0,0,0]
	v_mfma_scale_f32_16x16x128_f8f6f4 v[118:121], v[150:157], v[226:233], v[118:121], v199, v199 op_sel_hi:[0,0,0]
	v_mfma_scale_f32_16x16x128_f8f6f4 v[114:117], v[142:149], v[234:241], v[114:117], v199, v199 op_sel_hi:[0,0,0]
	v_mfma_scale_f32_16x16x128_f8f6f4 v[110:113], v[150:157], v[234:241], v[110:113], v199, v199 op_sel_hi:[0,0,0]
	s_nop 3
	s_setprio 0
	s_setprio 1
	v_mfma_scale_f32_16x16x128_f8f6f4 v[106:109], v[2:9], v[210:217], v[106:109], v199, v199 op_sel_hi:[0,0,0]
	v_mfma_scale_f32_16x16x128_f8f6f4 v[102:105], v[202:209], v[210:217], v[102:105], v199, v199 op_sel_hi:[0,0,0]
	v_mfma_scale_f32_16x16x128_f8f6f4 v[98:101], v[2:9], v[218:225], v[98:101], v199, v199 op_sel_hi:[0,0,0]
	v_mfma_scale_f32_16x16x128_f8f6f4 v[94:97], v[202:209], v[218:225], v[94:97], v199, v199 op_sel_hi:[0,0,0]
	v_mfma_scale_f32_16x16x128_f8f6f4 v[90:93], v[2:9], v[226:233], v[90:93], v199, v199 op_sel_hi:[0,0,0]
	v_mfma_scale_f32_16x16x128_f8f6f4 v[86:89], v[202:209], v[226:233], v[86:89], v199, v199 op_sel_hi:[0,0,0]
	v_mfma_scale_f32_16x16x128_f8f6f4 v[82:85], v[2:9], v[234:241], v[82:85], v199, v199 op_sel_hi:[0,0,0]
	v_mfma_scale_f32_16x16x128_f8f6f4 v[78:81], v[202:209], v[234:241], v[78:81], v199, v199 op_sel_hi:[0,0,0]
	s_nop 3
	s_setprio 0
	s_barrier
	s_add_u32 s28, s28, 0x8000
	s_addc_u32 s29, s29, 0
	s_add_i32 s30, s78, s44
	s_mov_b32 m0, s30
	ds_read_b128 v[210:213], v198 offset:49152
	ds_read_b128 v[214:217], v198 offset:50176
	ds_read_b128 v[218:221], v198 offset:51200
	ds_read_b128 v[222:225], v198 offset:52224
	ds_read_b128 v[226:229], v198 offset:53248
	ds_read_b128 v[230:233], v198 offset:54272
	ds_read_b128 v[234:237], v198 offset:55296
	ds_read_b128 v[238:241], v198 offset:56320
	global_load_lds_dwordx4 v158, s[28:29]
	s_add_i32 m0, s30, 0x2000
	s_add_i32 s30, s79, s44
	global_load_lds_dwordx4 v160, s[28:29]
	s_mov_b32 m0, s30
	s_nop 0
	global_load_lds_dwordx4 v172, s[28:29]
	s_add_i32 m0, s30, 0x2000
	s_nop 0
	global_load_lds_dwordx4 v174, s[28:29]
	s_mov_b32 m0, s50
	s_nop 0
	global_load_lds_dwordx4 v162, s[26:27]
	s_mov_b32 m0, s51
	s_nop 0
	global_load_lds_dwordx4 v164, s[26:27]
	s_waitcnt vmcnt(8)
	s_waitcnt lgkmcnt(0)
	s_setprio 1
	s_waitcnt lgkmcnt(0)
	v_mfma_scale_f32_16x16x128_f8f6f4 v[74:77], v[142:149], v[210:217], v[74:77], v199, v199 op_sel_hi:[0,0,0]
	v_mfma_scale_f32_16x16x128_f8f6f4 v[70:73], v[150:157], v[210:217], v[70:73], v199, v199 op_sel_hi:[0,0,0]
	v_mfma_scale_f32_16x16x128_f8f6f4 v[66:69], v[142:149], v[218:225], v[66:69], v199, v199 op_sel_hi:[0,0,0]
	v_mfma_scale_f32_16x16x128_f8f6f4 v[62:65], v[150:157], v[218:225], v[62:65], v199, v199 op_sel_hi:[0,0,0]
	v_mfma_scale_f32_16x16x128_f8f6f4 v[58:61], v[142:149], v[226:233], v[58:61], v199, v199 op_sel_hi:[0,0,0]
	v_mfma_scale_f32_16x16x128_f8f6f4 v[54:57], v[150:157], v[226:233], v[54:57], v199, v199 op_sel_hi:[0,0,0]
	v_mfma_scale_f32_16x16x128_f8f6f4 v[50:53], v[142:149], v[234:241], v[50:53], v199, v199 op_sel_hi:[0,0,0]
	v_mfma_scale_f32_16x16x128_f8f6f4 v[46:49], v[150:157], v[234:241], v[46:49], v199, v199 op_sel_hi:[0,0,0]
	s_nop 3
	s_setprio 0
	s_setprio 1
	v_mfma_scale_f32_16x16x128_f8f6f4 v[42:45], v[2:9], v[210:217], v[42:45], v199, v199 op_sel_hi:[0,0,0]
	v_mfma_scale_f32_16x16x128_f8f6f4 v[38:41], v[202:209], v[210:217], v[38:41], v199, v199 op_sel_hi:[0,0,0]
	v_mfma_scale_f32_16x16x128_f8f6f4 v[34:37], v[2:9], v[218:225], v[34:37], v199, v199 op_sel_hi:[0,0,0]
	v_mfma_scale_f32_16x16x128_f8f6f4 v[30:33], v[202:209], v[218:225], v[30:33], v199, v199 op_sel_hi:[0,0,0]
	v_mfma_scale_f32_16x16x128_f8f6f4 v[26:29], v[2:9], v[226:233], v[26:29], v199, v199 op_sel_hi:[0,0,0]
	v_mfma_scale_f32_16x16x128_f8f6f4 v[22:25], v[202:209], v[226:233], v[22:25], v199, v199 op_sel_hi:[0,0,0]
	v_mfma_scale_f32_16x16x128_f8f6f4 v[18:21], v[2:9], v[234:241], v[18:21], v199, v199 op_sel_hi:[0,0,0]
	v_mfma_scale_f32_16x16x128_f8f6f4 v[14:17], v[202:209], v[234:241], v[14:17], v199, v199 op_sel_hi:[0,0,0]
	s_nop 3
	s_setprio 0
	s_barrier
	s_add_u32 s75, s75, 0x10000
	s_addc_u32 s76, s76, 0
	s_add_u32 s24, s24, 0x10000
	s_addc_u32 s25, s25, 0
	s_cmp_ge_i32 s77, s72
	s_mov_b32 s26, s77
	s_cbranch_scc0 .LBB0_834
	s_branch .Lfx_23459
; #define PG8_STAGE(bufoff, gbase, voff) do { _Pragma("unroll") for (int _i = 0; _i < 2; ++_i) \
;         __builtin_amdgcn_global_load_lds((const unsigned*)((const char*)(gbase) + (voff)[_i]), (PG8_LAS unsigned*)(lds + (bufoff) + ldsw + _i * 8192), 16, 0, 0); } while (0)
; #define PG8_WAIT_V(n) asm volatile("s_waitcnt vmcnt(" #n ")" ::: "memory")
; #define PG8_WAIT_L(n) asm volatile("s_waitcnt lgkmcnt(" #n ")" ::: "memory")
; template <class Epi, class Sched, bool ALIGN_EPI = true, bool F8 = false>
; __device__ __forceinline__ void gemm_phase(PG8_LAS unsigned char* lds, const Sched& S, const Epi& E) {
;     ...
;         for (int t = 0; t < nt; t += 2) {
;             const bool last = (t == nt - 2);
;             if constexpr (Sched::GATHER) { if (last && has_next) S.a_off(nxt, Rs, Cs, voffAn); }
;             const char* a1 = cA + (size_t)(t + 1) * kstep;
;             const char* a2 = last ? nA : cA + (size_t)(t + 2) * kstep; const char* b2 = last ? nB : cB + (size_t)(t + 2) * kstepB;
;             const char* a3 = a2 + kstep; const char* b3 = b2 + kstepB;
;             unsigned vA2[2][2];
; #pragma unroll
;             for (int h = 0; h < 2; ++h)
; #pragma unroll
;                 for (int i = 0; i < 2; ++i) { if constexpr (Sched::GATHER) vA2[h][i] = (last && has_next) ? voffAn[h][i] : voffA[h][i]; else vA2[h][i] = voffA[h][i]; }
;             PG8_LDB(B0, 0, 0); PG8_LDB(B1, 0, 1); PG8_SCHED; PG8_LDA(At, 0, 0); PG8_STAGE(PG8_SA(1, 1), a1, voffA[1]);
;             PG8_WAIT_V(8); PG8_WAIT_L(0); PG8_BAR; PG8_MMA(0, 0, At, B0); PG8_MMA(0, 1, At, B1); PG8_BAR; PG8_SCHED;
;             PG8_LDA(At, 0, 1); PG8_STAGE(PG8_SB(0, 0), b2, voffB[0]); PG8_STAGE(PG8_SB(0, 1), b2, voffB[1]); PG8_STAGE(PG8_SA(0, 0), a2, vA2[0]);
;             PG8_WAIT_V(8); PG8_WAIT_L(0); PG8_BAR; PG8_MMA(1, 0, At, B0); PG8_MMA(1, 1, At, B1); PG8_BAR; PG8_SCHED;
;             PG8_LDB(B0, 1, 0); PG8_LDB(B1, 1, 1); PG8_SCHED; PG8_LDA(At, 1, 0); PG8_STAGE(PG8_SA(0, 1), a2, vA2[1]);
;             PG8_WAIT_V(8); PG8_WAIT_L(0); PG8_BAR; PG8_MMA(0, 0, At, B0); PG8_MMA(0, 1, At, B1); PG8_BAR; PG8_SCHED;
;             PG8_LDA(At, 1, 1); PG8_STAGE(PG8_SB(1, 0), b3, voffB[0]); PG8_STAGE(PG8_SB(1, 1), b3, voffB[1]); PG8_STAGE(PG8_SA(1, 0), a3, vA2[0]);
;             PG8_WAIT_V(8); PG8_WAIT_L(0); PG8_BAR; PG8_MMA(1, 0, At, B0); PG8_MMA(1, 1, At, B1); PG8_BAR; PG8_SCHED;
.Lh1e_23459:
.Lh1_834:
	v_add_u32_e32 v10, s58, v190
	ds_read_b128 v[2:5], v10
	ds_read_b128 v[6:9], v10 offset:1024
	ds_read_b128 v[142:145], v10 offset:2048
	ds_read_b128 v[146:149], v10 offset:3072
	v_add_u32_e32 v10, s59, v190
	ds_read_b128 v[150:153], v10
	ds_read_b128 v[154:157], v10 offset:1024
	ds_read_b128 v[202:205], v10 offset:2048
	ds_read_b128 v[206:209], v10 offset:3072
	s_add_i32 s77, s26, 2
	s_add_u32 s27, s24, 0x8000
	s_addc_u32 s28, s25, 0
	s_cmp_eq_u32 s74, s26
	s_cselect_b32 s30, s20, s27
	s_cselect_b32 s31, s21, s28
	s_cselect_b32 s28, s22, s75
	s_cselect_b32 s29, s23, s76
	s_add_u32 s26, s30, 0x8000
	s_addc_u32 s27, s31, 0
	s_add_i32 m0, s45, 0xc000
	ds_read_b128 v[210:213], v198
	ds_read_b128 v[214:217], v198 offset:1024
	ds_read_b128 v[218:221], v198 offset:2048
	ds_read_b128 v[222:225], v198 offset:3072
	ds_read_b128 v[226:229], v198 offset:4096
	ds_read_b128 v[230:233], v198 offset:5120
	ds_read_b128 v[234:237], v198 offset:6144
	ds_read_b128 v[238:241], v198 offset:7168
	global_load_lds_dwordx4 v182, s[24:25]
	s_add_i32 m0, s45, 0xe000
	s_nop 0
	global_load_lds_dwordx4 v180, s[24:25]
	s_waitcnt vmcnt(8)
	s_waitcnt lgkmcnt(0)
	s_barrier
	s_setprio 2
	s_waitcnt lgkmcnt(0)
	v_mfma_scale_f32_16x16x128_f8f6f4 v[138:141], v[2:9], v[210:217], v[138:141], v199, v199 op_sel_hi:[0,0,0]
	v_mfma_scale_f32_16x16x128_f8f6f4 v[134:137], v[142:149], v[210:217], v[134:137], v199, v199 op_sel_hi:[0,0,0]
	v_mfma_scale_f32_16x16x128_f8f6f4 v[130:133], v[2:9], v[218:225], v[130:133], v199, v199 op_sel_hi:[0,0,0]
	v_mfma_scale_f32_16x16x128_f8f6f4 v[126:129], v[142:149], v[218:225], v[126:129], v199, v199 op_sel_hi:[0,0,0]
	v_mfma_scale_f32_16x16x128_f8f6f4 v[122:125], v[2:9], v[226:233], v[122:125], v199, v199 op_sel_hi:[0,0,0]
	v_mfma_scale_f32_16x16x128_f8f6f4 v[118:121], v[142:149], v[226:233], v[118:121], v199, v199 op_sel_hi:[0,0,0]
	v_mfma_scale_f32_16x16x128_f8f6f4 v[114:117], v[2:9], v[234:241], v[114:117], v199, v199 op_sel_hi:[0,0,0]
	v_mfma_scale_f32_16x16x128_f8f6f4 v[110:113], v[142:149], v[234:241], v[110:113], v199, v199 op_sel_hi:[0,0,0]
	s_nop 3
	s_setprio 0
	s_setprio 2
	v_mfma_scale_f32_16x16x128_f8f6f4 v[106:109], v[150:157], v[210:217], v[106:109], v199, v199 op_sel_hi:[0,0,0]
	v_mfma_scale_f32_16x16x128_f8f6f4 v[102:105], v[202:209], v[210:217], v[102:105], v199, v199 op_sel_hi:[0,0,0]
	v_mfma_scale_f32_16x16x128_f8f6f4 v[98:101], v[150:157], v[218:225], v[98:101], v199, v199 op_sel_hi:[0,0,0]
	v_mfma_scale_f32_16x16x128_f8f6f4 v[94:97], v[202:209], v[218:225], v[94:97], v199, v199 op_sel_hi:[0,0,0]
	v_mfma_scale_f32_16x16x128_f8f6f4 v[90:93], v[150:157], v[226:233], v[90:93], v199, v199 op_sel_hi:[0,0,0]
	v_mfma_scale_f32_16x16x128_f8f6f4 v[86:89], v[202:209], v[226:233], v[86:89], v199, v199 op_sel_hi:[0,0,0]
	v_mfma_scale_f32_16x16x128_f8f6f4 v[82:85], v[150:157], v[234:241], v[82:85], v199, v199 op_sel_hi:[0,0,0]
	v_mfma_scale_f32_16x16x128_f8f6f4 v[78:81], v[202:209], v[234:241], v[78:81], v199, v199 op_sel_hi:[0,0,0]
	s_nop 3
	s_setprio 0
	s_add_i32 s78, s58, s44
	s_mov_b32 m0, s78
	ds_read_b128 v[210:213], v198 offset:16384
	ds_read_b128 v[214:217], v198 offset:17408
	ds_read_b128 v[218:221], v198 offset:18432
	ds_read_b128 v[222:225], v198 offset:19456
	ds_read_b128 v[226:229], v198 offset:20480
	ds_read_b128 v[230:233], v198 offset:21504
	ds_read_b128 v[234:237], v198 offset:22528
	ds_read_b128 v[238:241], v198 offset:23552
	global_load_lds_dwordx4 v158, s[28:29]
	s_add_i32 m0, s78, 0x2000
	s_add_i32 s78, s59, s44
	global_load_lds_dwordx4 v160, s[28:29]
	s_add_u32 s98, s28, s8
	s_addc_u32 s99, s29, s9
	s_mov_b32 m0, s78
	s_nop 0
	global_load_lds_dwordx4 v158, s[98:99]
	s_add_u32 s100, s28, s8
	s_addc_u32 s101, s29, s9
	s_add_i32 m0, s78, 0x2000
	s_nop 0
	global_load_lds_dwordx4 v160, s[100:101]
	s_mov_b32 m0, s45
	s_nop 0
	global_load_lds_dwordx4 v162, s[30:31]
	s_mov_b32 m0, s46
	s_nop 0
	global_load_lds_dwordx4 v164, s[30:31]
	s_waitcnt vmcnt(8)
	s_waitcnt lgkmcnt(0)
	s_barrier
	s_setprio 2
	s_waitcnt lgkmcnt(0)
	v_mfma_scale_f32_16x16x128_f8f6f4 v[74:77], v[2:9], v[210:217], v[74:77], v199, v199 op_sel_hi:[0,0,0]
	v_mfma_scale_f32_16x16x128_f8f6f4 v[70:73], v[142:149], v[210:217], v[70:73], v199, v199 op_sel_hi:[0,0,0]
	v_mfma_scale_f32_16x16x128_f8f6f4 v[66:69], v[2:9], v[218:225], v[66:69], v199, v199 op_sel_hi:[0,0,0]
	v_mfma_scale_f32_16x16x128_f8f6f4 v[62:65], v[142:149], v[218:225], v[62:65], v199, v199 op_sel_hi:[0,0,0]
	v_mfma_scale_f32_16x16x128_f8f6f4 v[58:61], v[2:9], v[226:233], v[58:61], v199, v199 op_sel_hi:[0,0,0]
	v_mfma_scale_f32_16x16x128_f8f6f4 v[54:57], v[142:149], v[226:233], v[54:57], v199, v199 op_sel_hi:[0,0,0]
	v_mfma_scale_f32_16x16x128_f8f6f4 v[50:53], v[2:9], v[234:241], v[50:53], v199, v199 op_sel_hi:[0,0,0]
	v_mfma_scale_f32_16x16x128_f8f6f4 v[46:49], v[142:149], v[234:241], v[46:49], v199, v199 op_sel_hi:[0,0,0]
	s_nop 3
	s_setprio 0
	s_setprio 2
	v_mfma_scale_f32_16x16x128_f8f6f4 v[42:45], v[150:157], v[210:217], v[42:45], v199, v199 op_sel_hi:[0,0,0]
	v_mfma_scale_f32_16x16x128_f8f6f4 v[38:41], v[202:209], v[210:217], v[38:41], v199, v199 op_sel_hi:[0,0,0]
	v_mfma_scale_f32_16x16x128_f8f6f4 v[34:37], v[150:157], v[218:225], v[34:37], v199, v199 op_sel_hi:[0,0,0]
	v_mfma_scale_f32_16x16x128_f8f6f4 v[30:33], v[202:209], v[218:225], v[30:33], v199, v199 op_sel_hi:[0,0,0]
	v_mfma_scale_f32_16x16x128_f8f6f4 v[26:29], v[150:157], v[226:233], v[26:29], v199, v199 op_sel_hi:[0,0,0]
	v_mfma_scale_f32_16x16x128_f8f6f4 v[22:25], v[202:209], v[226:233], v[22:25], v199, v199 op_sel_hi:[0,0,0]
	v_mfma_scale_f32_16x16x128_f8f6f4 v[18:21], v[150:157], v[234:241], v[18:21], v199, v199 op_sel_hi:[0,0,0]
	v_mfma_scale_f32_16x16x128_f8f6f4 v[14:17], v[202:209], v[234:241], v[14:17], v199, v199 op_sel_hi:[0,0,0]
	s_nop 3
	s_setprio 0
	s_add_i32 s78, 0, 0x18000
	s_add_i32 s79, 0, 0x1c000
	v_add_u32_e32 v2, s78, v190
	v_add_u32_e32 v10, s79, v190
	ds_read_b128 v[142:145], v2
	ds_read_b128 v[146:149], v2 offset:1024
	ds_read_b128 v[150:153], v2 offset:2048
	ds_read_b128 v[154:157], v2 offset:3072
	ds_read_b128 v[2:5], v10
	ds_read_b128 v[6:9], v10 offset:1024
	ds_read_b128 v[202:205], v10 offset:2048
	ds_read_b128 v[206:209], v10 offset:3072
	s_mov_b32 m0, s47
	ds_read_b128 v[210:213], v198 offset:32768
	ds_read_b128 v[214:217], v198 offset:33792
	ds_read_b128 v[218:221], v198 offset:34816
	ds_read_b128 v[222:225], v198 offset:35840
	ds_read_b128 v[226:229], v198 offset:36864
	ds_read_b128 v[230:233], v198 offset:37888
	ds_read_b128 v[234:237], v198 offset:38912
	ds_read_b128 v[238:241], v198 offset:39936
	global_load_lds_dwordx4 v166, s[30:31]
	s_mov_b32 m0, s48
	s_nop 0
	global_load_lds_dwordx4 v168, s[30:31]
	s_waitcnt vmcnt(8)
	s_waitcnt lgkmcnt(0)
	s_barrier
; #define PG8_STAGE(bufoff, gbase, voff) do { _Pragma("unroll") for (int _i = 0; _i < 2; ++_i) \
;         __builtin_amdgcn_global_load_lds((const unsigned*)((const char*)(gbase) + (voff)[_i]), (PG8_LAS unsigned*)(lds + (bufoff) + ldsw + _i * 8192), 16, 0, 0); } while (0)
; #define PG8_WAIT_V(n) asm volatile("s_waitcnt vmcnt(" #n ")" ::: "memory")
; #define PG8_WAIT_L(n) asm volatile("s_waitcnt lgkmcnt(" #n ")" ::: "memory")
; template <class Epi, class Sched, bool ALIGN_EPI = true, bool F8 = false>
; __device__ __forceinline__ void gemm_phase(PG8_LAS unsigned char* lds, const Sched& S, const Epi& E) {
;     ...
;         for (int t = 0; t < nt; t += 2) {
;             const bool last = (t == nt - 2);
;             if constexpr (Sched::GATHER) { if (last && has_next) S.a_off(nxt, Rs, Cs, voffAn); }
;             const char* a1 = cA + (size_t)(t + 1) * kstep;
;             const char* a2 = last ? nA : cA + (size_t)(t + 2) * kstep; const char* b2 = last ? nB : cB + (size_t)(t + 2) * kstepB;
;             const char* a3 = a2 + kstep; const char* b3 = b2 + kstepB;
;             unsigned vA2[2][2];
; #pragma unroll
;             for (int h = 0; h < 2; ++h)
; #pragma unroll
;                 for (int i = 0; i < 2; ++i) { if constexpr (Sched::GATHER) vA2[h][i] = (last && has_next) ? voffAn[h][i] : voffA[h][i]; else vA2[h][i] = voffA[h][i]; }
;             PG8_LDB(B0, 0, 0); PG8_LDB(B1, 0, 1); PG8_SCHED; PG8_LDA(At, 0, 0); PG8_STAGE(PG8_SA(1, 1), a1, voffA[1]);
;             PG8_WAIT_V(8); PG8_WAIT_L(0); PG8_BAR; PG8_MMA(0, 0, At, B0); PG8_MMA(0, 1, At, B1); PG8_BAR; PG8_SCHED;
;             PG8_LDA(At, 0, 1); PG8_STAGE(PG8_SB(0, 0), b2, voffB[0]); PG8_STAGE(PG8_SB(0, 1), b2, voffB[1]); PG8_STAGE(PG8_SA(0, 0), a2, vA2[0]);
;             PG8_WAIT_V(8); PG8_WAIT_L(0); PG8_BAR; PG8_MMA(1, 0, At, B0); PG8_MMA(1, 1, At, B1); PG8_BAR; PG8_SCHED;
;             PG8_LDB(B0, 1, 0); PG8_LDB(B1, 1, 1); PG8_SCHED; PG8_LDA(At, 1, 0); PG8_STAGE(PG8_SA(0, 1), a2, vA2[1]);
;             PG8_WAIT_V(8); PG8_WAIT_L(0); PG8_BAR; PG8_MMA(0, 0, At, B0); PG8_MMA(0, 1, At, B1); PG8_BAR; PG8_SCHED;
;             PG8_LDA(At, 1, 1); PG8_STAGE(PG8_SB(1, 0), b3, voffB[0]); PG8_STAGE(PG8_SB(1, 1), b3, voffB[1]); PG8_STAGE(PG8_SA(1, 0), a3, vA2[0]);
;             PG8_WAIT_V(8); PG8_WAIT_L(0); PG8_BAR; PG8_MMA(1, 0, At, B0); PG8_MMA(1, 1, At, B1); PG8_BAR; PG8_SCHED;
	s_setprio 2
	s_waitcnt lgkmcnt(0)
	v_mfma_scale_f32_16x16x128_f8f6f4 v[138:141], v[142:149], v[210:217], v[138:141], v199, v199 op_sel_hi:[0,0,0]
	v_mfma_scale_f32_16x16x128_f8f6f4 v[134:137], v[150:157], v[210:217], v[134:137], v199, v199 op_sel_hi:[0,0,0]
	v_mfma_scale_f32_16x16x128_f8f6f4 v[130:133], v[142:149], v[218:225], v[130:133], v199, v199 op_sel_hi:[0,0,0]
	v_mfma_scale_f32_16x16x128_f8f6f4 v[126:129], v[150:157], v[218:225], v[126:129], v199, v199 op_sel_hi:[0,0,0]
	v_mfma_scale_f32_16x16x128_f8f6f4 v[122:125], v[142:149], v[226:233], v[122:125], v199, v199 op_sel_hi:[0,0,0]
	v_mfma_scale_f32_16x16x128_f8f6f4 v[118:121], v[150:157], v[226:233], v[118:121], v199, v199 op_sel_hi:[0,0,0]
	v_mfma_scale_f32_16x16x128_f8f6f4 v[114:117], v[142:149], v[234:241], v[114:117], v199, v199 op_sel_hi:[0,0,0]
	v_mfma_scale_f32_16x16x128_f8f6f4 v[110:113], v[150:157], v[234:241], v[110:113], v199, v199 op_sel_hi:[0,0,0]
	s_nop 3
	s_setprio 0
	s_setprio 2
	v_mfma_scale_f32_16x16x128_f8f6f4 v[106:109], v[2:9], v[210:217], v[106:109], v199, v199 op_sel_hi:[0,0,0]
	v_mfma_scale_f32_16x16x128_f8f6f4 v[102:105], v[202:209], v[210:217], v[102:105], v199, v199 op_sel_hi:[0,0,0]
	v_mfma_scale_f32_16x16x128_f8f6f4 v[98:101], v[2:9], v[218:225], v[98:101], v199, v199 op_sel_hi:[0,0,0]
	v_mfma_scale_f32_16x16x128_f8f6f4 v[94:97], v[202:209], v[218:225], v[94:97], v199, v199 op_sel_hi:[0,0,0]
	v_mfma_scale_f32_16x16x128_f8f6f4 v[90:93], v[2:9], v[226:233], v[90:93], v199, v199 op_sel_hi:[0,0,0]
	v_mfma_scale_f32_16x16x128_f8f6f4 v[86:89], v[202:209], v[226:233], v[86:89], v199, v199 op_sel_hi:[0,0,0]
	v_mfma_scale_f32_16x16x128_f8f6f4 v[82:85], v[2:9], v[234:241], v[82:85], v199, v199 op_sel_hi:[0,0,0]
	v_mfma_scale_f32_16x16x128_f8f6f4 v[78:81], v[202:209], v[234:241], v[78:81], v199, v199 op_sel_hi:[0,0,0]
	s_nop 3
	s_setprio 0
	s_add_u32 s28, s28, 0x8000
	s_addc_u32 s29, s29, 0
	s_add_i32 s30, s78, s44
	s_mov_b32 m0, s30
	ds_read_b128 v[210:213], v198 offset:49152
	ds_read_b128 v[214:217], v198 offset:50176
	ds_read_b128 v[218:221], v198 offset:51200
	ds_read_b128 v[222:225], v198 offset:52224
	ds_read_b128 v[226:229], v198 offset:53248
	ds_read_b128 v[230:233], v198 offset:54272
	ds_read_b128 v[234:237], v198 offset:55296
	ds_read_b128 v[238:241], v198 offset:56320
	global_load_lds_dwordx4 v158, s[28:29]
	s_add_i32 m0, s30, 0x2000
	s_add_i32 s30, s79, s44
	global_load_lds_dwordx4 v160, s[28:29]
	s_mov_b32 m0, s30
	s_nop 0
	global_load_lds_dwordx4 v172, s[28:29]
	s_add_i32 m0, s30, 0x2000
	s_nop 0
	global_load_lds_dwordx4 v174, s[28:29]
	s_mov_b32 m0, s50
	s_nop 0
	global_load_lds_dwordx4 v162, s[26:27]
	s_mov_b32 m0, s51
	s_nop 0
	global_load_lds_dwordx4 v164, s[26:27]
	s_waitcnt vmcnt(8)
	s_waitcnt lgkmcnt(0)
	s_barrier
	s_setprio 2
	s_waitcnt lgkmcnt(0)
	v_mfma_scale_f32_16x16x128_f8f6f4 v[74:77], v[142:149], v[210:217], v[74:77], v199, v199 op_sel_hi:[0,0,0]
	v_mfma_scale_f32_16x16x128_f8f6f4 v[70:73], v[150:157], v[210:217], v[70:73], v199, v199 op_sel_hi:[0,0,0]
	v_mfma_scale_f32_16x16x128_f8f6f4 v[66:69], v[142:149], v[218:225], v[66:69], v199, v199 op_sel_hi:[0,0,0]
	v_mfma_scale_f32_16x16x128_f8f6f4 v[62:65], v[150:157], v[218:225], v[62:65], v199, v199 op_sel_hi:[0,0,0]
	v_mfma_scale_f32_16x16x128_f8f6f4 v[58:61], v[142:149], v[226:233], v[58:61], v199, v199 op_sel_hi:[0,0,0]
	v_mfma_scale_f32_16x16x128_f8f6f4 v[54:57], v[150:157], v[226:233], v[54:57], v199, v199 op_sel_hi:[0,0,0]
	v_mfma_scale_f32_16x16x128_f8f6f4 v[50:53], v[142:149], v[234:241], v[50:53], v199, v199 op_sel_hi:[0,0,0]
	v_mfma_scale_f32_16x16x128_f8f6f4 v[46:49], v[150:157], v[234:241], v[46:49], v199, v199 op_sel_hi:[0,0,0]
	s_nop 3
	s_setprio 0
	s_setprio 2
	v_mfma_scale_f32_16x16x128_f8f6f4 v[42:45], v[2:9], v[210:217], v[42:45], v199, v199 op_sel_hi:[0,0,0]
	v_mfma_scale_f32_16x16x128_f8f6f4 v[38:41], v[202:209], v[210:217], v[38:41], v199, v199 op_sel_hi:[0,0,0]
	v_mfma_scale_f32_16x16x128_f8f6f4 v[34:37], v[2:9], v[218:225], v[34:37], v199, v199 op_sel_hi:[0,0,0]
	v_mfma_scale_f32_16x16x128_f8f6f4 v[30:33], v[202:209], v[218:225], v[30:33], v199, v199 op_sel_hi:[0,0,0]
	v_mfma_scale_f32_16x16x128_f8f6f4 v[26:29], v[2:9], v[226:233], v[26:29], v199, v199 op_sel_hi:[0,0,0]
	v_mfma_scale_f32_16x16x128_f8f6f4 v[22:25], v[202:209], v[226:233], v[22:25], v199, v199 op_sel_hi:[0,0,0]
	v_mfma_scale_f32_16x16x128_f8f6f4 v[18:21], v[2:9], v[234:241], v[18:21], v199, v199 op_sel_hi:[0,0,0]
	v_mfma_scale_f32_16x16x128_f8f6f4 v[14:17], v[202:209], v[234:241], v[14:17], v199, v199 op_sel_hi:[0,0,0]
	s_nop 3
	s_setprio 0
	s_add_u32 s75, s75, 0x10000
	s_addc_u32 s76, s76, 0
	s_add_u32 s24, s24, 0x10000
	s_addc_u32 s25, s25, 0
	s_cmp_ge_i32 s77, s72
	s_mov_b32 s26, s77
	s_cbranch_scc0 .Lh1_834

; __device__ __forceinline__ f32x4 u8x4_f32(unsigned w) { return (f32x4){(float)(w & 0xffu), (float)((w >> 8) & 0xffu), (float)((w >> 16) & 0xffu), (float)(w >> 24)}; }
; __device__ __forceinline__ unsigned pk4_fp8(float a, float b, float c, float d) { int w = 0; w = __builtin_amdgcn_cvt_pk_fp8_f32(clamp8(a), clamp8(b), w, false); w = __builtin_amdgcn_cvt_pk_fp8_f32(clamp8(c), clamp8(d), w, true); return (unsigned)w; }
; __host__ __device__ __forceinline__ size_t tiled_off(size_t r, int kb, int ktiles) { return (((r >> 8) * ktiles + (kb >> 7)) << 15) + ((r & 255) << 7) + (kb & 127); }
; template <class Epi, class Sched, bool ALIGN_EPI = true, bool F8 = false>
; __device__ __forceinline__ void gemm_phase(PG8_LAS unsigned char* lds, const Sched& S, const Epi& E) {
;     ...
;         if constexpr (F8) {
; #pragma unroll
;             for (int a = 0; a < 2; ++a)
; #pragma unroll
;                 for (int b = 0; b < 2; ++b)
;                     asm volatile("s_nop 15\n\ts_nop 7" : "+v"(acc[a][b][0][0]), "+v"(acc[a][b][0][1]), "+v"(acc[a][b][1][0]), "+v"(acc[a][b][1][1]), "+v"(acc[a][b][2][0]), "+v"(acc[a][b][2][1]), "+v"(acc[a][b][3][0]), "+v"(acc[a][b][3][1]));
;         }
;         E(acc, cur, wr, wc, fr, fq);
;     __device__ __forceinline__ void operator()(f32x4 (&acc)[2][2][4][2], const GUnit& u, int wr, int wc, int fr, int fq) const {
;     ...
; #pragma unroll
;         for (int ai = 0; ai < 2; ++ai) {
;             u32x4 qf[4];
; #pragma unroll
;             for (int m = 0; m < 4; ++m) qf[m] = __builtin_nontemporal_load((const u32x4*)(GZF + off0 + (size_t)(ai * 128 + m * 16) * D));
; #pragma unroll
;             for (int m = 0; m < 4; ++m) { u32x4 w;
; #pragma unroll
;                 for (int q = 0; q < 4; ++q) { const f32x4 f = u8x4_f32(qf[m][q]); const f32x4 a = acc[ai][q >> 1][m][q & 1]; f32x4 v;
; #pragma unroll
;                     for (int j = 0; j < 4; ++j) v[j] = a[j] * (fmaxf(f[j], 0.5f) * (W8_INV / 255.0f));
;                     w[q] = pk4_fp8(v[0], v[1], v[2], v[3]); }
;                 *(u32x4*)(M8 + tiled_off((size_t)(u.x0 * 256 + wr * 64 + fr + ai * 128 + m * 16), u.x1 * 256 + wc * 64 + 16 * fq, D / 128)) = w; }
;             asm volatile("" ::: "memory");
;         }
.LBB0_837:
	s_lshl_b32 s28, s71, 8
	v_add_u32_e32 v144, s28, v177
	v_ashrrev_i32_e32 v145, 31, v144
	s_lshl_b32 s26, s70, 8
	v_lshlrev_b64 v[2:3], 11, v[144:145]
	s_ashr_i32 s27, s26, 31
	v_lshl_add_u64 v[142:143], v[2:3], 0, s[26:27]
	v_or_b32_e32 v142, v142, v176
	s_cmp_lg_u32 s73, 0
	s_cselect_b64 s[24:25], -1, 0
	s_cmp_eq_u32 s73, 0
	v_lshl_add_u64 v[12:13], s[6:7], 0, v[142:143]
	s_nop 15
	s_nop 7
	s_nop 15
	s_nop 7
	s_nop 15
	s_nop 7
	s_nop 15
	s_nop 7
	s_cbranch_scc1 .LBB0_845
	global_load_dwordx4 v[146:149], v[12:13], off nt
	v_add_co_u32_e32 v2, vcc, 0x8000, v12
	v_mov_b32_e32 v151, 0
	s_nop 0
	v_addc_co_u32_e32 v3, vcc, 0, v13, vcc
	v_add_co_u32_e32 v4, vcc, 0x10000, v12
	v_mov_b32_e32 v150, 0
	s_nop 0
	v_addc_co_u32_e32 v5, vcc, 0, v13, vcc
	global_load_dwordx4 v[154:157], v[2:3], off nt
	global_load_dwordx4 v[6:9], v[4:5], off nt
	v_add_co_u32_e32 v188, vcc, 0x18000, v12
	v_mov_b32_e32 v152, 0
	s_nop 0
	v_addc_co_u32_e32 v189, vcc, 0, v13, vcc
	global_load_dwordx4 v[2:5], v[188:189], off nt
	s_or_b32 s26, s26, s53
	s_ashr_i32 s26, s26, 7
	s_ashr_i32 s27, s26, 31
	s_waitcnt vmcnt(0) lgkmcnt(0)
	v_cvt_f32_ubyte0_e32 v189, v147
	v_cvt_f32_ubyte1_e32 v201, v147
	v_max_f32_e32 v189, 0.5, v189
	v_max_f32_e32 v201, 0.5, v201
	v_mul_f32_e32 v189, 0x38808081, v189
	v_mul_f32_e32 v201, 0x38808081, v201
	v_cvt_f32_ubyte0_e32 v10, v146
	v_cvt_f32_ubyte1_e32 v153, v146
	v_cvt_f32_ubyte0_e32 v203, v148
	v_cvt_f32_ubyte1_e32 v204, v148
	v_mul_f32_e32 v189, v134, v189
	v_mul_f32_e32 v201, v135, v201
	v_cvt_f32_ubyte2_e32 v202, v147
	v_cvt_f32_ubyte3_e32 v147, v147
	v_max_f32_e32 v10, 0.5, v10
	v_max_f32_e32 v153, 0.5, v153
	v_max_f32_e32 v203, 0.5, v203
	v_max_f32_e32 v204, 0.5, v204
	v_med3_f32 v189, v189, s60, v200
	v_med3_f32 v201, v201, s60, v200
	v_cvt_f32_ubyte2_e32 v205, v148
	v_cvt_f32_ubyte3_e32 v148, v148
	v_max_f32_e32 v202, 0.5, v202
	v_max_f32_e32 v147, 0.5, v147
	v_mul_f32_e32 v10, 0x38808081, v10
	v_mul_f32_e32 v153, 0x38808081, v153
	v_mul_f32_e32 v203, 0x38808081, v203
	v_mul_f32_e32 v204, 0x38808081, v204
	v_cvt_pk_fp8_f32 v151, v189, v201
	v_max_f32_e32 v148, 0.5, v148
	v_mul_f32_e32 v202, 0x38808081, v202
	v_mul_f32_e32 v147, 0x38808081, v147
	v_mul_f32_e32 v10, v138, v10
	v_mul_f32_e32 v153, v139, v153
	v_mul_f32_e32 v203, v106, v203
	v_mul_f32_e32 v204, v107, v204
	v_cvt_f32_ubyte2_e32 v188, v146
	v_cvt_f32_ubyte3_e32 v146, v146
	v_mul_f32_e32 v148, 0x38808081, v148
	v_mul_f32_e32 v202, v136, v202
	v_mul_f32_e32 v147, v137, v147
	v_med3_f32 v10, v10, s60, v200
	v_med3_f32 v153, v153, s60, v200
	v_med3_f32 v203, v203, s60, v200
	v_med3_f32 v204, v204, s60, v200
	v_cvt_f32_ubyte0_e32 v206, v149
	v_cvt_f32_ubyte1_e32 v207, v149
	v_max_f32_e32 v188, 0.5, v188
	v_max_f32_e32 v146, 0.5, v146
	v_max_f32_e32 v205, 0.5, v205
	v_mul_f32_e32 v148, v109, v148
	v_med3_f32 v202, v202, s60, v200
	v_med3_f32 v147, v147, s60, v200
	v_cvt_pk_fp8_f32 v150, v10, v153
	v_cvt_pk_fp8_f32 v152, v203, v204
	v_mul_f32_e32 v188, 0x38808081, v188
	v_mul_f32_e32 v146, 0x38808081, v146
	v_mul_f32_e32 v205, 0x38808081, v205
	v_med3_f32 v10, v148, s60, v200
	v_cvt_pk_fp8_f32 v151, v202, v147 op_sel:[0,0,1]
	v_max_f32_e32 v147, 0.5, v206
	v_max_f32_e32 v148, 0.5, v207
	v_mul_f32_e32 v188, v140, v188
	v_mul_f32_e32 v146, v141, v146
	v_mul_f32_e32 v205, v108, v205
	v_mul_f32_e32 v147, 0x38808081, v147
	v_mul_f32_e32 v148, 0x38808081, v148
	v_med3_f32 v188, v188, s60, v200
	v_med3_f32 v146, v146, s60, v200
	v_med3_f32 v205, v205, s60, v200
	v_mul_f32_e32 v147, v102, v147
	v_mul_f32_e32 v148, v103, v148
	v_cvt_pk_fp8_f32 v150, v188, v146 op_sel:[0,0,1]
	v_cvt_pk_fp8_f32 v152, v205, v10 op_sel:[0,0,1]
	v_cvt_f32_ubyte2_e32 v10, v149
	v_cvt_f32_ubyte3_e32 v146, v149
	v_med3_f32 v147, v147, s60, v200
	v_med3_f32 v148, v148, s60, v200
	v_mov_b32_e32 v153, 0
	v_max_f32_e32 v10, 0.5, v10
	v_max_f32_e32 v146, 0.5, v146
	v_cvt_pk_fp8_f32 v153, v147, v148
	v_mul_f32_e32 v10, 0x38808081, v10
	v_mul_f32_e32 v146, 0x38808081, v146
	v_mul_f32_e32 v10, v104, v10
	v_mul_f32_e32 v146, v105, v146
	v_med3_f32 v10, v10, s60, v200
	v_med3_f32 v146, v146, s60, v200
	v_cvt_pk_fp8_f32 v153, v10, v146 op_sel:[0,0,1]
	v_lshrrev_b64 v[146:147], 4, v[144:145]
	v_and_b32_e32 v147, 0x1ffff, v147
	v_and_b32_e32 v146, -16, v146
	v_lshl_add_u64 v[146:147], v[146:147], 0, s[26:27]
	v_lshlrev_b64 v[146:147], 15, v[146:147]
	v_lshlrev_b32_e32 v10, 7, v144
	v_and_b32_e32 v10, 0x6780, v10
	v_lshl_add_u64 v[144:145], s[12:13], 0, v[146:147]
	v_lshl_add_u64 v[144:145], v[144:145], 0, v[10:11]
	v_lshl_add_u64 v[144:145], v[144:145], 0, v[178:179]
	global_store_dwordx4 v[144:145], v[150:153], off
	v_cvt_f32_ubyte0_e32 v10, v154
	v_cvt_f32_ubyte1_e32 v144, v154
	v_max_f32_e32 v10, 0.5, v10
	v_max_f32_e32 v144, 0.5, v144
	v_mul_f32_e32 v10, 0x38808081, v10
	v_mul_f32_e32 v144, 0x38808081, v144
	v_mul_f32_e32 v10, v130, v10
	v_mul_f32_e32 v144, v131, v144
	v_cvt_f32_ubyte2_e32 v145, v154
	v_cvt_f32_ubyte3_e32 v146, v154
	v_med3_f32 v10, v10, s60, v200
	v_med3_f32 v147, v144, s60, v200
	v_mov_b32_e32 v144, v11
	v_max_f32_e32 v145, 0.5, v145
	v_max_f32_e32 v146, 0.5, v146
	v_cvt_pk_fp8_f32 v144, v10, v147
	v_mul_f32_e32 v145, 0x38808081, v145
	v_mul_f32_e32 v146, 0x38808081, v146
	v_mul_f32_e32 v145, v132, v145
	v_mul_f32_e32 v10, v133, v146
	v_med3_f32 v145, v145, s60, v200
	v_med3_f32 v10, v10, s60, v200
	v_cvt_pk_fp8_f32 v144, v145, v10 op_sel:[0,0,1]
	v_cvt_f32_ubyte0_e32 v10, v155
	v_cvt_f32_ubyte1_e32 v145, v155
	v_max_f32_e32 v10, 0.5, v10
	v_max_f32_e32 v145, 0.5, v145
	v_mul_f32_e32 v10, 0x38808081, v10
	v_mul_f32_e32 v145, 0x38808081, v145
	v_mul_f32_e32 v10, v126, v10
	v_mul_f32_e32 v145, v127, v145
; __device__ __forceinline__ f32x4 u8x4_f32(unsigned w) { return (f32x4){(float)(w & 0xffu), (float)((w >> 8) & 0xffu), (float)((w >> 16) & 0xffu), (float)(w >> 24)}; }
; __device__ __forceinline__ unsigned pk4_fp8(float a, float b, float c, float d) { int w = 0; w = __builtin_amdgcn_cvt_pk_fp8_f32(clamp8(a), clamp8(b), w, false); w = __builtin_amdgcn_cvt_pk_fp8_f32(clamp8(c), clamp8(d), w, true); return (unsigned)w; }
; __host__ __device__ __forceinline__ size_t tiled_off(size_t r, int kb, int ktiles) { return (((r >> 8) * ktiles + (kb >> 7)) << 15) + ((r & 255) << 7) + (kb & 127); }
;     __device__ __forceinline__ void operator()(f32x4 (&acc)[2][2][4][2], const GUnit& u, int wr, int wc, int fr, int fq) const {
;     ...
; #pragma unroll
;         for (int ai = 0; ai < 2; ++ai) {
;             u32x4 qf[4];
; #pragma unroll
;             for (int m = 0; m < 4; ++m) qf[m] = __builtin_nontemporal_load((const u32x4*)(GZF + off0 + (size_t)(ai * 128 + m * 16) * D));
; #pragma unroll
;             for (int m = 0; m < 4; ++m) { u32x4 w;
; #pragma unroll
;                 for (int q = 0; q < 4; ++q) { const f32x4 f = u8x4_f32(qf[m][q]); const f32x4 a = acc[ai][q >> 1][m][q & 1]; f32x4 v;
; #pragma unroll
;                     for (int j = 0; j < 4; ++j) v[j] = a[j] * (fmaxf(f[j], 0.5f) * (W8_INV / 255.0f));
;                     w[q] = pk4_fp8(v[0], v[1], v[2], v[3]); }
;                 *(u32x4*)(M8 + tiled_off((size_t)(u.x0 * 256 + wr * 64 + fr + ai * 128 + m * 16), u.x1 * 256 + wc * 64 + 16 * fq, D / 128)) = w; }
;             asm volatile("" ::: "memory");
;         }
	v_cvt_f32_ubyte2_e32 v146, v155
	v_cvt_f32_ubyte3_e32 v147, v155
	v_med3_f32 v10, v10, s60, v200
	v_med3_f32 v148, v145, s60, v200
	v_mov_b32_e32 v145, v11
	v_max_f32_e32 v146, 0.5, v146
	v_max_f32_e32 v147, 0.5, v147
	v_cvt_pk_fp8_f32 v145, v10, v148
	v_mul_f32_e32 v146, 0x38808081, v146
	v_mul_f32_e32 v147, 0x38808081, v147
	v_mul_f32_e32 v146, v128, v146
	v_mul_f32_e32 v10, v129, v147
	v_med3_f32 v146, v146, s60, v200
	v_med3_f32 v10, v10, s60, v200
	v_cvt_pk_fp8_f32 v145, v146, v10 op_sel:[0,0,1]
	v_cvt_f32_ubyte0_e32 v10, v156
	v_cvt_f32_ubyte1_e32 v146, v156
	v_max_f32_e32 v10, 0.5, v10
	v_max_f32_e32 v146, 0.5, v146
	v_mul_f32_e32 v10, 0x38808081, v10
	v_mul_f32_e32 v146, 0x38808081, v146
	v_mul_f32_e32 v10, v98, v10
	v_mul_f32_e32 v146, v99, v146
	v_cvt_f32_ubyte2_e32 v147, v156
	v_cvt_f32_ubyte3_e32 v148, v156
	v_med3_f32 v10, v10, s60, v200
	v_med3_f32 v149, v146, s60, v200
	v_mov_b32_e32 v146, v11
	v_max_f32_e32 v147, 0.5, v147
	v_max_f32_e32 v148, 0.5, v148
	v_cvt_pk_fp8_f32 v146, v10, v149
	v_mul_f32_e32 v147, 0x38808081, v147
	v_mul_f32_e32 v148, 0x38808081, v148
	v_mul_f32_e32 v147, v100, v147
	v_mul_f32_e32 v10, v101, v148
	v_med3_f32 v147, v147, s60, v200
	v_med3_f32 v10, v10, s60, v200
	v_cvt_pk_fp8_f32 v146, v147, v10 op_sel:[0,0,1]
	v_cvt_f32_ubyte0_e32 v10, v157
	v_cvt_f32_ubyte1_e32 v147, v157
	v_max_f32_e32 v10, 0.5, v10
	v_max_f32_e32 v147, 0.5, v147
	v_mul_f32_e32 v10, 0x38808081, v10
	v_mul_f32_e32 v147, 0x38808081, v147
	v_mul_f32_e32 v10, v94, v10
	v_mul_f32_e32 v147, v95, v147
	v_cvt_f32_ubyte2_e32 v148, v157
	v_cvt_f32_ubyte3_e32 v149, v157
	v_med3_f32 v10, v10, s60, v200
	v_med3_f32 v150, v147, s60, v200
	v_mov_b32_e32 v147, v11
	v_max_f32_e32 v148, 0.5, v148
	v_max_f32_e32 v149, 0.5, v149
	v_cvt_pk_fp8_f32 v147, v10, v150
	v_mul_f32_e32 v148, 0x38808081, v148
	v_mul_f32_e32 v149, 0x38808081, v149
	v_mul_f32_e32 v148, v96, v148
	v_mul_f32_e32 v10, v97, v149
	v_med3_f32 v148, v148, s60, v200
	v_med3_f32 v10, v10, s60, v200
	v_cvt_pk_fp8_f32 v147, v148, v10 op_sel:[0,0,1]
	v_add_u32_e32 v148, s28, v191
	v_ashrrev_i32_e32 v149, 31, v148
	v_lshrrev_b64 v[150:151], 4, v[148:149]
	v_and_b32_e32 v151, 0x1ffff, v151
	v_and_b32_e32 v150, -16, v150
	v_lshl_add_u64 v[150:151], v[150:151], 0, s[26:27]
	v_lshlrev_b64 v[150:151], 15, v[150:151]
	v_lshlrev_b32_e32 v10, 7, v148
	v_and_b32_e32 v10, 0x7f80, v10
	v_lshl_add_u64 v[148:149], s[12:13], 0, v[150:151]
	v_lshl_add_u64 v[148:149], v[148:149], 0, v[10:11]
	v_lshl_add_u64 v[148:149], v[148:149], 0, v[178:179]
	global_store_dwordx4 v[148:149], v[144:147], off
	v_cvt_f32_ubyte0_e32 v10, v6
	v_max_f32_e32 v10, 0.5, v10
	v_cvt_f32_ubyte1_e32 v144, v6
	v_max_f32_e32 v144, 0.5, v144
	v_cvt_f32_ubyte2_e32 v145, v6
	v_cvt_f32_ubyte3_e32 v6, v6
	v_mul_f32_e32 v10, 0x38808081, v10
	v_mul_f32_e32 v144, 0x38808081, v144
	v_mul_f32_e32 v10, v122, v10
	v_mul_f32_e32 v144, v123, v144
	v_max_f32_e32 v6, 0.5, v6
	v_mul_f32_e32 v146, 0x38808081, v6
	v_med3_f32 v10, v10, s60, v200
	v_med3_f32 v144, v144, s60, v200
	v_mov_b32_e32 v6, v11
	v_max_f32_e32 v145, 0.5, v145
	v_cvt_pk_fp8_f32 v6, v10, v144
	v_mul_f32_e32 v145, 0x38808081, v145
	v_mul_f32_e32 v145, v124, v145
	v_mul_f32_e32 v10, v125, v146
	v_med3_f32 v144, v145, s60, v200
	v_med3_f32 v10, v10, s60, v200
	v_cvt_pk_fp8_f32 v6, v144, v10 op_sel:[0,0,1]
	v_cvt_f32_ubyte0_e32 v10, v7
	v_cvt_f32_ubyte1_e32 v144, v7
	v_max_f32_e32 v10, 0.5, v10
	v_max_f32_e32 v144, 0.5, v144
	v_cvt_f32_ubyte2_e32 v145, v7
	v_cvt_f32_ubyte3_e32 v7, v7
	v_mul_f32_e32 v10, 0x38808081, v10
	v_mul_f32_e32 v144, 0x38808081, v144
	v_mul_f32_e32 v10, v118, v10
	v_mul_f32_e32 v144, v119, v144
	v_max_f32_e32 v7, 0.5, v7
	v_mul_f32_e32 v146, 0x38808081, v7
	v_med3_f32 v10, v10, s60, v200
	v_med3_f32 v144, v144, s60, v200
	v_mov_b32_e32 v7, v11
	v_max_f32_e32 v145, 0.5, v145
	v_cvt_pk_fp8_f32 v7, v10, v144
	v_mul_f32_e32 v145, 0x38808081, v145
	v_mul_f32_e32 v145, v120, v145
	v_mul_f32_e32 v10, v121, v146
	v_med3_f32 v144, v145, s60, v200
	v_med3_f32 v10, v10, s60, v200
	v_cvt_pk_fp8_f32 v7, v144, v10 op_sel:[0,0,1]
	v_cvt_f32_ubyte0_e32 v10, v8
	v_cvt_f32_ubyte1_e32 v144, v8
	v_max_f32_e32 v10, 0.5, v10
	v_max_f32_e32 v144, 0.5, v144
	v_cvt_f32_ubyte2_e32 v145, v8
	v_cvt_f32_ubyte3_e32 v8, v8
	v_mul_f32_e32 v10, 0x38808081, v10
	v_mul_f32_e32 v144, 0x38808081, v144
	v_mul_f32_e32 v10, v90, v10
	v_mul_f32_e32 v144, v91, v144
	v_max_f32_e32 v8, 0.5, v8
	v_mul_f32_e32 v146, 0x38808081, v8
	v_med3_f32 v10, v10, s60, v200
	v_med3_f32 v144, v144, s60, v200
	v_mov_b32_e32 v8, v11
	v_max_f32_e32 v145, 0.5, v145
	v_cvt_pk_fp8_f32 v8, v10, v144
	v_mul_f32_e32 v145, 0x38808081, v145
	v_mul_f32_e32 v145, v92, v145
	v_mul_f32_e32 v10, v93, v146
	v_med3_f32 v144, v145, s60, v200
	v_med3_f32 v10, v10, s60, v200
	v_cvt_pk_fp8_f32 v8, v144, v10 op_sel:[0,0,1]
	v_cvt_f32_ubyte0_e32 v10, v9
	v_cvt_f32_ubyte1_e32 v144, v9
	v_max_f32_e32 v10, 0.5, v10
	v_max_f32_e32 v144, 0.5, v144
	v_cvt_f32_ubyte2_e32 v145, v9
	v_cvt_f32_ubyte3_e32 v9, v9
	v_mul_f32_e32 v10, 0x38808081, v10
	v_mul_f32_e32 v144, 0x38808081, v144
	v_mul_f32_e32 v10, v86, v10
	v_mul_f32_e32 v144, v87, v144
	v_max_f32_e32 v9, 0.5, v9
	v_mul_f32_e32 v146, 0x38808081, v9
	v_med3_f32 v10, v10, s60, v200
	v_med3_f32 v144, v144, s60, v200
	v_mov_b32_e32 v9, v11
	v_max_f32_e32 v145, 0.5, v145
	v_cvt_pk_fp8_f32 v9, v10, v144
	v_mul_f32_e32 v145, 0x38808081, v145
	v_mul_f32_e32 v145, v88, v145
	v_mul_f32_e32 v10, v89, v146
	v_med3_f32 v144, v145, s60, v200
	v_med3_f32 v10, v10, s60, v200
	v_cvt_pk_fp8_f32 v9, v144, v10 op_sel:[0,0,1]
	v_add_u32_e32 v144, s28, v192
	v_ashrrev_i32_e32 v145, 31, v144
	v_lshrrev_b64 v[146:147], 4, v[144:145]
; __device__ __forceinline__ f32x4 u8x4_f32(unsigned w) { return (f32x4){(float)(w & 0xffu), (float)((w >> 8) & 0xffu), (float)((w >> 16) & 0xffu), (float)(w >> 24)}; }
; __device__ __forceinline__ unsigned pk4_fp8(float a, float b, float c, float d) { int w = 0; w = __builtin_amdgcn_cvt_pk_fp8_f32(clamp8(a), clamp8(b), w, false); w = __builtin_amdgcn_cvt_pk_fp8_f32(clamp8(c), clamp8(d), w, true); return (unsigned)w; }
; __host__ __device__ __forceinline__ size_t tiled_off(size_t r, int kb, int ktiles) { return (((r >> 8) * ktiles + (kb >> 7)) << 15) + ((r & 255) << 7) + (kb & 127); }
;     __device__ __forceinline__ void operator()(f32x4 (&acc)[2][2][4][2], const GUnit& u, int wr, int wc, int fr, int fq) const {
;     ...
; #pragma unroll
;         for (int ai = 0; ai < 2; ++ai) {
;             u32x4 qf[4];
; #pragma unroll
;             for (int m = 0; m < 4; ++m) qf[m] = __builtin_nontemporal_load((const u32x4*)(GZF + off0 + (size_t)(ai * 128 + m * 16) * D));
; #pragma unroll
;             for (int m = 0; m < 4; ++m) { u32x4 w;
; #pragma unroll
;                 for (int q = 0; q < 4; ++q) { const f32x4 f = u8x4_f32(qf[m][q]); const f32x4 a = acc[ai][q >> 1][m][q & 1]; f32x4 v;
; #pragma unroll
;                     for (int j = 0; j < 4; ++j) v[j] = a[j] * (fmaxf(f[j], 0.5f) * (W8_INV / 255.0f));
;                     w[q] = pk4_fp8(v[0], v[1], v[2], v[3]); }
;                 *(u32x4*)(M8 + tiled_off((size_t)(u.x0 * 256 + wr * 64 + fr + ai * 128 + m * 16), u.x1 * 256 + wc * 64 + 16 * fq, D / 128)) = w; }
;             asm volatile("" ::: "memory");
;         }
	v_and_b32_e32 v147, 0x1ffff, v147
	v_and_b32_e32 v146, -16, v146
	v_lshl_add_u64 v[146:147], v[146:147], 0, s[26:27]
	v_lshlrev_b64 v[146:147], 15, v[146:147]
	v_lshlrev_b32_e32 v10, 7, v144
	v_and_b32_e32 v10, 0x7f80, v10
	v_lshl_add_u64 v[144:145], s[12:13], 0, v[146:147]
	v_lshl_add_u64 v[144:145], v[144:145], 0, v[10:11]
	v_lshl_add_u64 v[144:145], v[144:145], 0, v[178:179]
	global_store_dwordx4 v[144:145], v[6:9], off
	s_nop 1
	v_cvt_f32_ubyte0_e32 v6, v2
	v_cvt_f32_ubyte1_e32 v7, v2
	v_max_f32_e32 v6, 0.5, v6
	v_max_f32_e32 v7, 0.5, v7
	v_cvt_f32_ubyte2_e32 v8, v2
	v_cvt_f32_ubyte3_e32 v2, v2
	v_mul_f32_e32 v6, 0x38808081, v6
	v_mul_f32_e32 v7, 0x38808081, v7
	v_mul_f32_e32 v6, v114, v6
	v_mul_f32_e32 v7, v115, v7
	v_max_f32_e32 v2, 0.5, v2
	v_mul_f32_e32 v9, 0x38808081, v2
	v_med3_f32 v6, v6, s60, v200
	v_med3_f32 v7, v7, s60, v200
	v_mov_b32_e32 v2, v11
	v_max_f32_e32 v8, 0.5, v8
	v_cvt_pk_fp8_f32 v2, v6, v7
	v_mul_f32_e32 v8, 0x38808081, v8
	v_mul_f32_e32 v8, v116, v8
	v_mul_f32_e32 v6, v117, v9
	v_med3_f32 v7, v8, s60, v200
	v_med3_f32 v6, v6, s60, v200
	v_cvt_pk_fp8_f32 v2, v7, v6 op_sel:[0,0,1]
	v_cvt_f32_ubyte0_e32 v6, v3
	v_cvt_f32_ubyte1_e32 v7, v3
	v_max_f32_e32 v6, 0.5, v6
	v_max_f32_e32 v7, 0.5, v7
	v_cvt_f32_ubyte2_e32 v8, v3
	v_cvt_f32_ubyte3_e32 v3, v3
	v_mul_f32_e32 v6, 0x38808081, v6
	v_mul_f32_e32 v7, 0x38808081, v7
	v_mul_f32_e32 v6, v110, v6
	v_mul_f32_e32 v7, v111, v7
	v_max_f32_e32 v3, 0.5, v3
	v_mul_f32_e32 v9, 0x38808081, v3
	v_med3_f32 v6, v6, s60, v200
	v_med3_f32 v7, v7, s60, v200
	v_mov_b32_e32 v3, v11
	v_max_f32_e32 v8, 0.5, v8
	v_cvt_pk_fp8_f32 v3, v6, v7
	v_mul_f32_e32 v8, 0x38808081, v8
	v_mul_f32_e32 v8, v112, v8
	v_mul_f32_e32 v6, v113, v9
	v_med3_f32 v7, v8, s60, v200
	v_med3_f32 v6, v6, s60, v200
	v_cvt_pk_fp8_f32 v3, v7, v6 op_sel:[0,0,1]
	v_cvt_f32_ubyte0_e32 v6, v4
	v_cvt_f32_ubyte1_e32 v7, v4
	v_max_f32_e32 v6, 0.5, v6
	v_max_f32_e32 v7, 0.5, v7
	v_cvt_f32_ubyte2_e32 v8, v4
	v_cvt_f32_ubyte3_e32 v4, v4
	v_mul_f32_e32 v6, 0x38808081, v6
	v_mul_f32_e32 v7, 0x38808081, v7
	v_mul_f32_e32 v6, v82, v6
	v_mul_f32_e32 v7, v83, v7
	v_max_f32_e32 v4, 0.5, v4
	v_mul_f32_e32 v9, 0x38808081, v4
	v_med3_f32 v6, v6, s60, v200
	v_med3_f32 v7, v7, s60, v200
	v_mov_b32_e32 v4, v11
	v_max_f32_e32 v8, 0.5, v8
	v_cvt_pk_fp8_f32 v4, v6, v7
	v_mul_f32_e32 v8, 0x38808081, v8
	v_mul_f32_e32 v8, v84, v8
	v_mul_f32_e32 v6, v85, v9
	v_med3_f32 v7, v8, s60, v200
	v_med3_f32 v6, v6, s60, v200
	v_cvt_pk_fp8_f32 v4, v7, v6 op_sel:[0,0,1]
	v_cvt_f32_ubyte0_e32 v6, v5
	v_cvt_f32_ubyte1_e32 v7, v5
	v_max_f32_e32 v6, 0.5, v6
	v_max_f32_e32 v7, 0.5, v7
	v_cvt_f32_ubyte2_e32 v8, v5
	v_cvt_f32_ubyte3_e32 v5, v5
	v_mul_f32_e32 v6, 0x38808081, v6
	v_mul_f32_e32 v7, 0x38808081, v7
	v_mul_f32_e32 v6, v78, v6
	v_mul_f32_e32 v7, v79, v7
	v_max_f32_e32 v5, 0.5, v5
	v_mul_f32_e32 v9, 0x38808081, v5
	v_med3_f32 v6, v6, s60, v200
	v_med3_f32 v7, v7, s60, v200
	v_mov_b32_e32 v5, v11
	v_max_f32_e32 v8, 0.5, v8
	v_cvt_pk_fp8_f32 v5, v6, v7
	v_mul_f32_e32 v8, 0x38808081, v8
	v_mul_f32_e32 v8, v80, v8
	v_mul_f32_e32 v6, v81, v9
	v_med3_f32 v7, v8, s60, v200
	v_med3_f32 v6, v6, s60, v200
	v_cvt_pk_fp8_f32 v5, v7, v6 op_sel:[0,0,1]
	v_add_u32_e32 v6, s28, v193
	v_ashrrev_i32_e32 v7, 31, v6
	v_lshrrev_b64 v[8:9], 4, v[6:7]
	v_and_b32_e32 v9, 0x1ffff, v9
	v_and_b32_e32 v8, -16, v8
	v_lshl_add_u64 v[8:9], v[8:9], 0, s[26:27]
	v_lshlrev_b64 v[8:9], 15, v[8:9]
	v_lshlrev_b32_e32 v6, 7, v6
	v_and_b32_e32 v10, 0x7f80, v6
	v_lshl_add_u64 v[6:7], s[12:13], 0, v[8:9]
	v_lshl_add_u64 v[6:7], v[6:7], 0, v[10:11]
	v_lshl_add_u64 v[6:7], v[6:7], 0, v[178:179]
	global_store_dwordx4 v[6:7], v[2:5], off
	s_nop 1
	v_add_co_u32_e32 v2, vcc, s61, v12
	s_nop 1
	v_addc_co_u32_e32 v3, vcc, 0, v13, vcc
	global_load_dwordx4 v[144:147], v[2:3], off nt
	v_add_co_u32_e32 v2, vcc, s62, v12
	s_waitcnt vmcnt(0) lgkmcnt(0)
	v_cvt_f32_ubyte0_e32 v10, v144
	v_addc_co_u32_e32 v3, vcc, 0, v13, vcc
	global_load_dwordx4 v[148:151], v[2:3], off nt
	v_cvt_f32_ubyte1_e32 v152, v144
	v_max_f32_e32 v10, 0.5, v10
	v_max_f32_e32 v152, 0.5, v152
	v_cvt_f32_ubyte2_e32 v153, v144
	v_cvt_f32_ubyte3_e32 v144, v144
	v_mul_f32_e32 v10, 0x38808081, v10
	v_mul_f32_e32 v152, 0x38808081, v152
	v_mul_f32_e32 v10, v74, v10
	v_mul_f32_e32 v152, v75, v152
	v_max_f32_e32 v144, 0.5, v144
	v_mul_f32_e32 v154, 0x38808081, v144
	v_med3_f32 v10, v10, s60, v200
	v_med3_f32 v152, v152, s60, v200
	v_mov_b32_e32 v144, v11
	v_max_f32_e32 v153, 0.5, v153
	v_cvt_pk_fp8_f32 v144, v10, v152
	v_mul_f32_e32 v153, 0x38808081, v153
	v_add_co_u32_e32 v2, vcc, s63, v12
	v_mul_f32_e32 v153, v76, v153
	v_mul_f32_e32 v10, v77, v154
	v_addc_co_u32_e32 v3, vcc, 0, v13, vcc
	v_med3_f32 v152, v153, s60, v200
	v_med3_f32 v10, v10, s60, v200
	v_add_co_u32_e32 v4, vcc, s64, v12
	v_cvt_pk_fp8_f32 v144, v152, v10 op_sel:[0,0,1]
	v_cvt_f32_ubyte0_e32 v10, v145
	v_cvt_f32_ubyte1_e32 v152, v145
	v_addc_co_u32_e32 v5, vcc, 0, v13, vcc
	v_max_f32_e32 v10, 0.5, v10
	v_max_f32_e32 v152, 0.5, v152
	global_load_dwordx4 v[6:9], v[2:3], off nt
	s_nop 0
	global_load_dwordx4 v[2:5], v[4:5], off nt
	v_cvt_f32_ubyte2_e32 v153, v145
	v_cvt_f32_ubyte3_e32 v145, v145
	v_mul_f32_e32 v10, 0x38808081, v10
	v_mul_f32_e32 v152, 0x38808081, v152
	v_mul_f32_e32 v10, v70, v10
	v_mul_f32_e32 v152, v71, v152
	v_max_f32_e32 v145, 0.5, v145
	v_mul_f32_e32 v154, 0x38808081, v145
	v_med3_f32 v10, v10, s60, v200
	v_med3_f32 v152, v152, s60, v200
	v_mov_b32_e32 v145, v11
	v_max_f32_e32 v153, 0.5, v153
	v_cvt_pk_fp8_f32 v145, v10, v152
	v_mul_f32_e32 v153, 0x38808081, v153
	v_mul_f32_e32 v153, v72, v153
	v_mul_f32_e32 v10, v73, v154
	v_med3_f32 v152, v153, s60, v200
; __device__ __forceinline__ f32x4 u8x4_f32(unsigned w) { return (f32x4){(float)(w & 0xffu), (float)((w >> 8) & 0xffu), (float)((w >> 16) & 0xffu), (float)(w >> 24)}; }
; __device__ __forceinline__ unsigned pk4_fp8(float a, float b, float c, float d) { int w = 0; w = __builtin_amdgcn_cvt_pk_fp8_f32(clamp8(a), clamp8(b), w, false); w = __builtin_amdgcn_cvt_pk_fp8_f32(clamp8(c), clamp8(d), w, true); return (unsigned)w; }
; __host__ __device__ __forceinline__ size_t tiled_off(size_t r, int kb, int ktiles) { return (((r >> 8) * ktiles + (kb >> 7)) << 15) + ((r & 255) << 7) + (kb & 127); }
;     __device__ __forceinline__ void operator()(f32x4 (&acc)[2][2][4][2], const GUnit& u, int wr, int wc, int fr, int fq) const {
;     ...
; #pragma unroll
;         for (int ai = 0; ai < 2; ++ai) {
;             u32x4 qf[4];
; #pragma unroll
;             for (int m = 0; m < 4; ++m) qf[m] = __builtin_nontemporal_load((const u32x4*)(GZF + off0 + (size_t)(ai * 128 + m * 16) * D));
; #pragma unroll
;             for (int m = 0; m < 4; ++m) { u32x4 w;
; #pragma unroll
;                 for (int q = 0; q < 4; ++q) { const f32x4 f = u8x4_f32(qf[m][q]); const f32x4 a = acc[ai][q >> 1][m][q & 1]; f32x4 v;
; #pragma unroll
;                     for (int j = 0; j < 4; ++j) v[j] = a[j] * (fmaxf(f[j], 0.5f) * (W8_INV / 255.0f));
;                     w[q] = pk4_fp8(v[0], v[1], v[2], v[3]); }
;                 *(u32x4*)(M8 + tiled_off((size_t)(u.x0 * 256 + wr * 64 + fr + ai * 128 + m * 16), u.x1 * 256 + wc * 64 + 16 * fq, D / 128)) = w; }
;             asm volatile("" ::: "memory");
;         }
	v_med3_f32 v10, v10, s60, v200
	v_cvt_pk_fp8_f32 v145, v152, v10 op_sel:[0,0,1]
	v_cvt_f32_ubyte0_e32 v10, v146
	v_cvt_f32_ubyte1_e32 v152, v146
	v_max_f32_e32 v10, 0.5, v10
	v_max_f32_e32 v152, 0.5, v152
	v_cvt_f32_ubyte2_e32 v153, v146
	v_cvt_f32_ubyte3_e32 v146, v146
	v_mul_f32_e32 v10, 0x38808081, v10
	v_mul_f32_e32 v152, 0x38808081, v152
	v_mul_f32_e32 v10, v42, v10
	v_mul_f32_e32 v152, v43, v152
	v_max_f32_e32 v146, 0.5, v146
	v_mul_f32_e32 v154, 0x38808081, v146
	v_med3_f32 v10, v10, s60, v200
	v_med3_f32 v152, v152, s60, v200
	v_mov_b32_e32 v146, v11
	v_max_f32_e32 v153, 0.5, v153
	v_cvt_pk_fp8_f32 v146, v10, v152
	v_mul_f32_e32 v153, 0x38808081, v153
	v_mul_f32_e32 v153, v44, v153
	v_mul_f32_e32 v10, v45, v154
	v_med3_f32 v152, v153, s60, v200
	v_med3_f32 v10, v10, s60, v200
	v_cvt_pk_fp8_f32 v146, v152, v10 op_sel:[0,0,1]
	v_cvt_f32_ubyte0_e32 v10, v147
	v_cvt_f32_ubyte1_e32 v152, v147
	v_max_f32_e32 v10, 0.5, v10
	v_max_f32_e32 v152, 0.5, v152
	v_cvt_f32_ubyte2_e32 v153, v147
	v_cvt_f32_ubyte3_e32 v147, v147
	v_mul_f32_e32 v10, 0x38808081, v10
	v_mul_f32_e32 v152, 0x38808081, v152
	v_mul_f32_e32 v10, v38, v10
	v_mul_f32_e32 v152, v39, v152
	v_max_f32_e32 v147, 0.5, v147
	v_mul_f32_e32 v154, 0x38808081, v147
	v_med3_f32 v10, v10, s60, v200
	v_med3_f32 v152, v152, s60, v200
	v_mov_b32_e32 v147, v11
	v_max_f32_e32 v153, 0.5, v153
	v_cvt_pk_fp8_f32 v147, v10, v152
	v_mul_f32_e32 v153, 0x38808081, v153
	v_mul_f32_e32 v153, v40, v153
	v_mul_f32_e32 v10, v41, v154
	v_med3_f32 v152, v153, s60, v200
	v_med3_f32 v10, v10, s60, v200
	v_cvt_pk_fp8_f32 v147, v152, v10 op_sel:[0,0,1]
	v_add_u32_e32 v152, s28, v194
	v_ashrrev_i32_e32 v153, 31, v152
	v_lshrrev_b64 v[154:155], 4, v[152:153]
	v_and_b32_e32 v155, 0x1ffff, v155
	v_and_b32_e32 v154, -16, v154
	v_lshl_add_u64 v[154:155], v[154:155], 0, s[26:27]
	v_lshlrev_b64 v[154:155], 15, v[154:155]
	v_lshlrev_b32_e32 v10, 7, v152
	v_and_b32_e32 v10, 0x7f80, v10
	v_lshl_add_u64 v[152:153], s[12:13], 0, v[154:155]
	v_lshl_add_u64 v[152:153], v[152:153], 0, v[10:11]
	v_lshl_add_u64 v[152:153], v[152:153], 0, v[178:179]
	global_store_dwordx4 v[152:153], v[144:147], off
	s_waitcnt vmcnt(0) lgkmcnt(0)
	v_cvt_f32_ubyte0_e32 v10, v148
	v_max_f32_e32 v10, 0.5, v10
	v_cvt_f32_ubyte1_e32 v144, v148
	v_max_f32_e32 v144, 0.5, v144
	v_mul_f32_e32 v10, 0x38808081, v10
	v_mul_f32_e32 v144, 0x38808081, v144
	v_mul_f32_e32 v10, v66, v10
	v_mul_f32_e32 v144, v67, v144
	v_cvt_f32_ubyte2_e32 v145, v148
	v_cvt_f32_ubyte3_e32 v146, v148
	v_med3_f32 v10, v10, s60, v200
	v_med3_f32 v147, v144, s60, v200
	v_mov_b32_e32 v144, v11
	v_max_f32_e32 v145, 0.5, v145
	v_max_f32_e32 v146, 0.5, v146
	v_cvt_pk_fp8_f32 v144, v10, v147
	v_mul_f32_e32 v145, 0x38808081, v145
	v_mul_f32_e32 v146, 0x38808081, v146
	v_mul_f32_e32 v145, v68, v145
	v_mul_f32_e32 v10, v69, v146
	v_med3_f32 v145, v145, s60, v200
	v_med3_f32 v10, v10, s60, v200
	v_cvt_pk_fp8_f32 v144, v145, v10 op_sel:[0,0,1]
	v_cvt_f32_ubyte0_e32 v10, v149
	v_cvt_f32_ubyte1_e32 v145, v149
	v_max_f32_e32 v10, 0.5, v10
	v_max_f32_e32 v145, 0.5, v145
	v_mul_f32_e32 v10, 0x38808081, v10
	v_mul_f32_e32 v145, 0x38808081, v145
	v_mul_f32_e32 v10, v62, v10
	v_mul_f32_e32 v145, v63, v145
	v_cvt_f32_ubyte2_e32 v146, v149
	v_cvt_f32_ubyte3_e32 v147, v149
	v_med3_f32 v10, v10, s60, v200
	v_med3_f32 v148, v145, s60, v200
	v_mov_b32_e32 v145, v11
	v_max_f32_e32 v146, 0.5, v146
	v_max_f32_e32 v147, 0.5, v147
	v_cvt_pk_fp8_f32 v145, v10, v148
	v_mul_f32_e32 v146, 0x38808081, v146
	v_mul_f32_e32 v147, 0x38808081, v147
	v_mul_f32_e32 v146, v64, v146
	v_mul_f32_e32 v10, v65, v147
	v_med3_f32 v146, v146, s60, v200
	v_med3_f32 v10, v10, s60, v200
	v_cvt_pk_fp8_f32 v145, v146, v10 op_sel:[0,0,1]
	v_cvt_f32_ubyte0_e32 v10, v150
	v_cvt_f32_ubyte1_e32 v146, v150
	v_max_f32_e32 v10, 0.5, v10
	v_max_f32_e32 v146, 0.5, v146
	v_mul_f32_e32 v10, 0x38808081, v10
	v_mul_f32_e32 v146, 0x38808081, v146
	v_mul_f32_e32 v10, v34, v10
	v_mul_f32_e32 v146, v35, v146
	v_cvt_f32_ubyte2_e32 v147, v150
	v_cvt_f32_ubyte3_e32 v148, v150
	v_med3_f32 v10, v10, s60, v200
	v_med3_f32 v149, v146, s60, v200
	v_mov_b32_e32 v146, v11
	v_max_f32_e32 v147, 0.5, v147
	v_max_f32_e32 v148, 0.5, v148
	v_cvt_pk_fp8_f32 v146, v10, v149
	v_mul_f32_e32 v147, 0x38808081, v147
	v_mul_f32_e32 v148, 0x38808081, v148
	v_mul_f32_e32 v147, v36, v147
	v_mul_f32_e32 v10, v37, v148
	v_med3_f32 v147, v147, s60, v200
	v_med3_f32 v10, v10, s60, v200
	v_cvt_pk_fp8_f32 v146, v147, v10 op_sel:[0,0,1]
	v_cvt_f32_ubyte0_e32 v10, v151
	v_cvt_f32_ubyte1_e32 v147, v151
	v_max_f32_e32 v10, 0.5, v10
	v_max_f32_e32 v147, 0.5, v147
	v_mul_f32_e32 v10, 0x38808081, v10
	v_mul_f32_e32 v147, 0x38808081, v147
	v_mul_f32_e32 v10, v30, v10
	v_mul_f32_e32 v147, v31, v147
	v_cvt_f32_ubyte2_e32 v148, v151
	v_cvt_f32_ubyte3_e32 v149, v151
	v_med3_f32 v10, v10, s60, v200
	v_med3_f32 v150, v147, s60, v200
	v_mov_b32_e32 v147, v11
	v_max_f32_e32 v148, 0.5, v148
	v_max_f32_e32 v149, 0.5, v149
	v_cvt_pk_fp8_f32 v147, v10, v150
	v_mul_f32_e32 v148, 0x38808081, v148
	v_mul_f32_e32 v149, 0x38808081, v149
	v_mul_f32_e32 v148, v32, v148
	v_mul_f32_e32 v10, v33, v149
	v_med3_f32 v148, v148, s60, v200
	v_med3_f32 v10, v10, s60, v200
	v_cvt_pk_fp8_f32 v147, v148, v10 op_sel:[0,0,1]
	v_add_u32_e32 v148, s28, v195
	v_ashrrev_i32_e32 v149, 31, v148
	v_lshrrev_b64 v[150:151], 4, v[148:149]
	v_and_b32_e32 v151, 0x1ffff, v151
	v_and_b32_e32 v150, -16, v150
	v_lshl_add_u64 v[150:151], v[150:151], 0, s[26:27]
	v_lshlrev_b64 v[150:151], 15, v[150:151]
	v_lshlrev_b32_e32 v10, 7, v148
	v_and_b32_e32 v10, 0x7f80, v10
	v_lshl_add_u64 v[148:149], s[12:13], 0, v[150:151]
; __device__ __forceinline__ f32x4 u8x4_f32(unsigned w) { return (f32x4){(float)(w & 0xffu), (float)((w >> 8) & 0xffu), (float)((w >> 16) & 0xffu), (float)(w >> 24)}; }
; __device__ __forceinline__ unsigned pk4_fp8(float a, float b, float c, float d) { int w = 0; w = __builtin_amdgcn_cvt_pk_fp8_f32(clamp8(a), clamp8(b), w, false); w = __builtin_amdgcn_cvt_pk_fp8_f32(clamp8(c), clamp8(d), w, true); return (unsigned)w; }
; __host__ __device__ __forceinline__ size_t tiled_off(size_t r, int kb, int ktiles) { return (((r >> 8) * ktiles + (kb >> 7)) << 15) + ((r & 255) << 7) + (kb & 127); }
;     __device__ __forceinline__ void operator()(f32x4 (&acc)[2][2][4][2], const GUnit& u, int wr, int wc, int fr, int fq) const {
;     ...
; #pragma unroll
;         for (int ai = 0; ai < 2; ++ai) {
;             u32x4 qf[4];
; #pragma unroll
;             for (int m = 0; m < 4; ++m) qf[m] = __builtin_nontemporal_load((const u32x4*)(GZF + off0 + (size_t)(ai * 128 + m * 16) * D));
; #pragma unroll
;             for (int m = 0; m < 4; ++m) { u32x4 w;
; #pragma unroll
;                 for (int q = 0; q < 4; ++q) { const f32x4 f = u8x4_f32(qf[m][q]); const f32x4 a = acc[ai][q >> 1][m][q & 1]; f32x4 v;
; #pragma unroll
;                     for (int j = 0; j < 4; ++j) v[j] = a[j] * (fmaxf(f[j], 0.5f) * (W8_INV / 255.0f));
;                     w[q] = pk4_fp8(v[0], v[1], v[2], v[3]); }
;                 *(u32x4*)(M8 + tiled_off((size_t)(u.x0 * 256 + wr * 64 + fr + ai * 128 + m * 16), u.x1 * 256 + wc * 64 + 16 * fq, D / 128)) = w; }
;             asm volatile("" ::: "memory");
;         }
	v_lshl_add_u64 v[148:149], v[148:149], 0, v[10:11]
	v_lshl_add_u64 v[148:149], v[148:149], 0, v[178:179]
	global_store_dwordx4 v[148:149], v[144:147], off
	v_cvt_f32_ubyte0_e32 v10, v6
	v_max_f32_e32 v10, 0.5, v10
	v_cvt_f32_ubyte1_e32 v144, v6
	v_max_f32_e32 v144, 0.5, v144
	v_cvt_f32_ubyte2_e32 v145, v6
	v_cvt_f32_ubyte3_e32 v6, v6
	v_mul_f32_e32 v10, 0x38808081, v10
	v_mul_f32_e32 v144, 0x38808081, v144
	v_mul_f32_e32 v10, v58, v10
	v_mul_f32_e32 v144, v59, v144
	v_max_f32_e32 v6, 0.5, v6
	v_mul_f32_e32 v146, 0x38808081, v6
	v_med3_f32 v10, v10, s60, v200
	v_med3_f32 v144, v144, s60, v200
	v_mov_b32_e32 v6, v11
	v_max_f32_e32 v145, 0.5, v145
	v_cvt_pk_fp8_f32 v6, v10, v144
	v_mul_f32_e32 v145, 0x38808081, v145
	v_mul_f32_e32 v145, v60, v145
	v_mul_f32_e32 v10, v61, v146
	v_med3_f32 v144, v145, s60, v200
	v_med3_f32 v10, v10, s60, v200
	v_cvt_pk_fp8_f32 v6, v144, v10 op_sel:[0,0,1]
	v_cvt_f32_ubyte0_e32 v10, v7
	v_cvt_f32_ubyte1_e32 v144, v7
	v_max_f32_e32 v10, 0.5, v10
	v_max_f32_e32 v144, 0.5, v144
	v_cvt_f32_ubyte2_e32 v145, v7
	v_cvt_f32_ubyte3_e32 v7, v7
	v_mul_f32_e32 v10, 0x38808081, v10
	v_mul_f32_e32 v144, 0x38808081, v144
	v_mul_f32_e32 v10, v54, v10
	v_mul_f32_e32 v144, v55, v144
	v_max_f32_e32 v7, 0.5, v7
	v_mul_f32_e32 v146, 0x38808081, v7
	v_med3_f32 v10, v10, s60, v200
	v_med3_f32 v144, v144, s60, v200
	v_mov_b32_e32 v7, v11
	v_max_f32_e32 v145, 0.5, v145
	v_cvt_pk_fp8_f32 v7, v10, v144
	v_mul_f32_e32 v145, 0x38808081, v145
	v_mul_f32_e32 v145, v56, v145
	v_mul_f32_e32 v10, v57, v146
	v_med3_f32 v144, v145, s60, v200
	v_med3_f32 v10, v10, s60, v200
	v_cvt_pk_fp8_f32 v7, v144, v10 op_sel:[0,0,1]
	v_cvt_f32_ubyte0_e32 v10, v8
	v_cvt_f32_ubyte1_e32 v144, v8
	v_max_f32_e32 v10, 0.5, v10
	v_max_f32_e32 v144, 0.5, v144
	v_cvt_f32_ubyte2_e32 v145, v8
	v_cvt_f32_ubyte3_e32 v8, v8
	v_mul_f32_e32 v10, 0x38808081, v10
	v_mul_f32_e32 v144, 0x38808081, v144
	v_mul_f32_e32 v10, v26, v10
	v_mul_f32_e32 v144, v27, v144
	v_max_f32_e32 v8, 0.5, v8
	v_mul_f32_e32 v146, 0x38808081, v8
	v_med3_f32 v10, v10, s60, v200
	v_med3_f32 v144, v144, s60, v200
	v_mov_b32_e32 v8, v11
	v_max_f32_e32 v145, 0.5, v145
	v_cvt_pk_fp8_f32 v8, v10, v144
	v_mul_f32_e32 v145, 0x38808081, v145
	v_mul_f32_e32 v145, v28, v145
	v_mul_f32_e32 v10, v29, v146
	v_med3_f32 v144, v145, s60, v200
	v_med3_f32 v10, v10, s60, v200
	v_cvt_pk_fp8_f32 v8, v144, v10 op_sel:[0,0,1]
	v_cvt_f32_ubyte0_e32 v10, v9
	v_cvt_f32_ubyte1_e32 v144, v9
	v_max_f32_e32 v10, 0.5, v10
	v_max_f32_e32 v144, 0.5, v144
	v_cvt_f32_ubyte2_e32 v145, v9
	v_cvt_f32_ubyte3_e32 v9, v9
	v_mul_f32_e32 v10, 0x38808081, v10
	v_mul_f32_e32 v144, 0x38808081, v144
	v_mul_f32_e32 v10, v22, v10
	v_mul_f32_e32 v144, v23, v144
	v_max_f32_e32 v9, 0.5, v9
	v_mul_f32_e32 v146, 0x38808081, v9
	v_med3_f32 v10, v10, s60, v200
	v_med3_f32 v144, v144, s60, v200
	v_mov_b32_e32 v9, v11
	v_max_f32_e32 v145, 0.5, v145
	v_cvt_pk_fp8_f32 v9, v10, v144
	v_mul_f32_e32 v145, 0x38808081, v145
	v_mul_f32_e32 v145, v24, v145
	v_mul_f32_e32 v10, v25, v146
	v_med3_f32 v144, v145, s60, v200
	v_med3_f32 v10, v10, s60, v200
	v_cvt_pk_fp8_f32 v9, v144, v10 op_sel:[0,0,1]
	v_add_u32_e32 v144, s28, v196
	v_ashrrev_i32_e32 v145, 31, v144
	v_lshrrev_b64 v[146:147], 4, v[144:145]
	v_and_b32_e32 v147, 0x1ffff, v147
	v_and_b32_e32 v146, -16, v146
	v_lshl_add_u64 v[146:147], v[146:147], 0, s[26:27]
	v_lshlrev_b64 v[146:147], 15, v[146:147]
	v_lshlrev_b32_e32 v10, 7, v144
	v_and_b32_e32 v10, 0x7f80, v10
	v_lshl_add_u64 v[144:145], s[12:13], 0, v[146:147]
	v_lshl_add_u64 v[144:145], v[144:145], 0, v[10:11]
	v_lshl_add_u64 v[144:145], v[144:145], 0, v[178:179]
	global_store_dwordx4 v[144:145], v[6:9], off
	s_nop 1
	v_cvt_f32_ubyte0_e32 v6, v2
	v_cvt_f32_ubyte1_e32 v7, v2
	v_max_f32_e32 v6, 0.5, v6
	v_max_f32_e32 v7, 0.5, v7
	v_cvt_f32_ubyte2_e32 v8, v2
	v_cvt_f32_ubyte3_e32 v2, v2
	v_mul_f32_e32 v6, 0x38808081, v6
	v_mul_f32_e32 v7, 0x38808081, v7
	v_mul_f32_e32 v6, v50, v6
	v_mul_f32_e32 v7, v51, v7
	v_max_f32_e32 v2, 0.5, v2
	v_mul_f32_e32 v9, 0x38808081, v2
	v_med3_f32 v6, v6, s60, v200
	v_med3_f32 v7, v7, s60, v200
	v_mov_b32_e32 v2, v11
	v_max_f32_e32 v8, 0.5, v8
	v_cvt_pk_fp8_f32 v2, v6, v7
	v_mul_f32_e32 v8, 0x38808081, v8
	v_mul_f32_e32 v8, v52, v8
	v_mul_f32_e32 v6, v53, v9
	v_med3_f32 v7, v8, s60, v200
	v_med3_f32 v6, v6, s60, v200
	v_cvt_pk_fp8_f32 v2, v7, v6 op_sel:[0,0,1]
	v_cvt_f32_ubyte0_e32 v6, v3
	v_cvt_f32_ubyte1_e32 v7, v3
	v_max_f32_e32 v6, 0.5, v6
	v_max_f32_e32 v7, 0.5, v7
	v_cvt_f32_ubyte2_e32 v8, v3
	v_cvt_f32_ubyte3_e32 v3, v3
	v_mul_f32_e32 v6, 0x38808081, v6
	v_mul_f32_e32 v7, 0x38808081, v7
	v_mul_f32_e32 v6, v46, v6
	v_mul_f32_e32 v7, v47, v7
	v_max_f32_e32 v3, 0.5, v3
	v_mul_f32_e32 v9, 0x38808081, v3
	v_med3_f32 v6, v6, s60, v200
	v_med3_f32 v7, v7, s60, v200
	v_mov_b32_e32 v3, v11
	v_max_f32_e32 v8, 0.5, v8
	v_cvt_pk_fp8_f32 v3, v6, v7
	v_mul_f32_e32 v8, 0x38808081, v8
	v_mul_f32_e32 v8, v48, v8
	v_mul_f32_e32 v6, v49, v9
	v_med3_f32 v7, v8, s60, v200
	v_med3_f32 v6, v6, s60, v200
	v_cvt_pk_fp8_f32 v3, v7, v6 op_sel:[0,0,1]
	v_cvt_f32_ubyte0_e32 v6, v4
	v_cvt_f32_ubyte1_e32 v7, v4
	v_max_f32_e32 v6, 0.5, v6
	v_max_f32_e32 v7, 0.5, v7
	v_cvt_f32_ubyte2_e32 v8, v4
	v_cvt_f32_ubyte3_e32 v4, v4
	v_mul_f32_e32 v6, 0x38808081, v6
	v_mul_f32_e32 v7, 0x38808081, v7
	v_mul_f32_e32 v6, v18, v6
	v_mul_f32_e32 v7, v19, v7
	v_max_f32_e32 v4, 0.5, v4
	v_mul_f32_e32 v9, 0x38808081, v4
	v_med3_f32 v6, v6, s60, v200
	v_med3_f32 v7, v7, s60, v200
	v_mov_b32_e32 v4, v11
	v_max_f32_e32 v8, 0.5, v8
	v_cvt_pk_fp8_f32 v4, v6, v7
	v_mul_f32_e32 v8, 0x38808081, v8
	v_mul_f32_e32 v8, v20, v8
	v_mul_f32_e32 v6, v21, v9
	v_med3_f32 v7, v8, s60, v200
	v_med3_f32 v6, v6, s60, v200
	v_cvt_pk_fp8_f32 v4, v7, v6 op_sel:[0,0,1]
	v_cvt_f32_ubyte0_e32 v6, v5
	v_cvt_f32_ubyte1_e32 v7, v5
	v_max_f32_e32 v6, 0.5, v6
	v_max_f32_e32 v7, 0.5, v7
	v_cvt_f32_ubyte2_e32 v8, v5
	v_cvt_f32_ubyte3_e32 v5, v5
	v_mul_f32_e32 v6, 0x38808081, v6
	v_mul_f32_e32 v7, 0x38808081, v7
	v_mul_f32_e32 v6, v14, v6
	v_mul_f32_e32 v7, v15, v7
	v_max_f32_e32 v5, 0.5, v5
	v_mul_f32_e32 v9, 0x38808081, v5
	v_med3_f32 v6, v6, s60, v200
	v_med3_f32 v7, v7, s60, v200
	v_mov_b32_e32 v5, v11
	v_max_f32_e32 v8, 0.5, v8
	v_cvt_pk_fp8_f32 v5, v6, v7
	v_mul_f32_e32 v8, 0x38808081, v8
	v_mul_f32_e32 v8, v16, v8
	v_mul_f32_e32 v6, v17, v9
	v_med3_f32 v7, v8, s60, v200
	v_med3_f32 v6, v6, s60, v200
	v_cvt_pk_fp8_f32 v5, v7, v6 op_sel:[0,0,1]
	v_add_u32_e32 v6, s28, v197
	v_ashrrev_i32_e32 v7, 31, v6
	v_lshrrev_b64 v[8:9], 4, v[6:7]
	v_and_b32_e32 v9, 0x1ffff, v9
	v_and_b32_e32 v8, -16, v8
	v_lshl_add_u64 v[8:9], v[8:9], 0, s[26:27]
	v_lshlrev_b64 v[8:9], 15, v[8:9]
	v_lshlrev_b32_e32 v6, 7, v6
	v_and_b32_e32 v10, 0x7f80, v6
	v_lshl_add_u64 v[6:7], s[12:13], 0, v[8:9]
	v_lshl_add_u64 v[6:7], v[6:7], 0, v[10:11]
	v_lshl_add_u64 v[6:7], v[6:7], 0, v[178:179]
	global_store_dwordx4 v[6:7], v[2:5], off
	s_cbranch_execnz .LBB0_840
; __device__ __forceinline__ f32x4 u8x4_f32(unsigned w) { return (f32x4){(float)(w & 0xffu), (float)((w >> 8) & 0xffu), (float)((w >> 16) & 0xffu), (float)(w >> 24)}; }
;     __device__ __forceinline__ void operator()(f32x4 (&acc)[2][2][4][2], const GUnit& u, int wr, int wc, int fr, int fq) const {
;     ...
;         if (u.x2 == 0) {
; #pragma unroll
;             for (int ai = 0; ai < 2; ++ai) {
;                 u32x4 qs[4], qf[4];
; #pragma unroll
;                 for (int m = 0; m < 4; ++m) { const size_t off = off0 + (size_t)(ai * 128 + m * 16) * D; qs[m] = __builtin_nontemporal_load((const u32x4*)(GZS + off)); qf[m] = *(const u32x4*)(GZF + off); }
; #pragma unroll
;                 for (int m = 0; m < 4; ++m)
; #pragma unroll
;                     for (int q = 0; q < 4; ++q) { const f32x4 s = u8x4_f32(qs[m][q]), f = u8x4_f32(qf[m][q]); f32x4 r;
; #pragma unroll
;                         for (int j = 0; j < 4; ++j) r[j] = s[j] * S8_INV * __builtin_amdgcn_rcpf(fmaxf(f[j], 0.5f));
;                         acc[ai][q >> 1][m][q & 1] *= r; }
;                 asm volatile("" ::: "memory");
;             }
;             return;
.LBB0_839:
	global_load_dwordx4 v[202:205], v[12:13], off
	v_lshl_add_u64 v[188:189], s[14:15], 0, v[142:143]
	global_load_dwordx4 v[206:209], v[188:189], off nt
	v_add_co_u32_e32 v2, vcc, 0x8000, v188
	s_waitcnt vmcnt(0) lgkmcnt(0)
	v_cvt_f32_ubyte3_e32 v211, v206
	v_addc_co_u32_e32 v3, vcc, 0, v189, vcc
	v_add_co_u32_e32 v4, vcc, 0x8000, v12
	global_load_dwordx4 v[150:153], v[2:3], off nt
	s_nop 0
	v_addc_co_u32_e32 v5, vcc, 0, v13, vcc
	global_load_dwordx4 v[154:157], v[4:5], off
	v_add_co_u32_e32 v2, vcc, s49, v188
	v_cvt_f32_ubyte0_e32 v10, v202
	s_nop 0
	v_addc_co_u32_e32 v3, vcc, 0, v189, vcc
	v_add_co_u32_e32 v4, vcc, s49, v12
	global_load_dwordx4 v[142:145], v[2:3], off nt
	s_nop 0
	v_addc_co_u32_e32 v5, vcc, 0, v13, vcc
	global_load_dwordx4 v[146:149], v[4:5], off
	v_add_co_u32_e32 v2, vcc, s52, v188
	v_cvt_f32_ubyte1_e32 v201, v202
	s_nop 0
	v_addc_co_u32_e32 v3, vcc, 0, v189, vcc
	v_add_co_u32_e32 v6, vcc, s52, v12
	v_cvt_f32_ubyte2_e32 v210, v202
	s_nop 0
	v_addc_co_u32_e32 v7, vcc, 0, v13, vcc
	global_load_dwordx4 v[6:9], v[6:7], off
	v_cvt_f32_ubyte3_e32 v202, v202
	global_load_dwordx4 v[2:5], v[2:3], off nt
	v_cvt_f32_ubyte0_e32 v212, v203
	v_cvt_f32_ubyte1_e32 v213, v203
	v_cvt_f32_ubyte2_e32 v214, v203
	v_cvt_f32_ubyte3_e32 v215, v203
	v_max_f32_e32 v10, 0.5, v10
	v_max_f32_e32 v201, 0.5, v201
	v_max_f32_e32 v217, 0.5, v210
	v_max_f32_e32 v218, 0.5, v202
	v_cvt_f32_ubyte1_e32 v203, v206
	v_cvt_f32_ubyte0_e32 v202, v206
	v_cvt_f32_ubyte2_e32 v210, v206
	v_max_f32_e32 v219, 0.5, v212
	v_max_f32_e32 v220, 0.5, v213
	v_max_f32_e32 v221, 0.5, v214
	v_max_f32_e32 v224, 0.5, v215
	v_cvt_f32_ubyte1_e32 v213, v207
	v_cvt_f32_ubyte0_e32 v212, v207
	v_cvt_f32_ubyte3_e32 v215, v207
	v_cvt_f32_ubyte2_e32 v214, v207
	v_rcp_f32_e32 v206, v10
	v_rcp_f32_e32 v207, v201
	v_cvt_f32_ubyte0_e32 v216, v204
	v_max_f32_e32 v225, 0.5, v216
	v_rcp_f32_e32 v216, v217
	v_rcp_f32_e32 v217, v218
	v_rcp_f32_e32 v218, v219
	v_rcp_f32_e32 v219, v220
	v_cvt_f32_ubyte1_e32 v222, v204
	v_pk_mul_f32 v[202:203], v[202:203], s[18:19] op_sel_hi:[1,0]
	v_max_f32_e32 v10, 0.5, v222
	v_pk_mul_f32 v[202:203], v[202:203], v[206:207]
	v_cvt_f32_ubyte2_e32 v223, v204
	v_pk_mul_f32 v[210:211], v[210:211], s[18:19] op_sel_hi:[1,0]
	v_pk_mul_f32 v[212:213], v[212:213], s[18:19] op_sel_hi:[1,0]
	v_pk_mul_f32 v[138:139], v[138:139], v[202:203]
	v_rcp_f32_e32 v202, v225
	v_rcp_f32_e32 v203, v10
	v_cvt_f32_ubyte3_e32 v204, v204
	v_pk_mul_f32 v[206:207], v[210:211], v[216:217]
	v_pk_mul_f32 v[210:211], v[212:213], v[218:219]
	v_max_f32_e32 v10, 0.5, v223
	v_rcp_f32_e32 v220, v221
	v_rcp_f32_e32 v221, v224
	v_pk_mul_f32 v[140:141], v[140:141], v[206:207]
	v_pk_mul_f32 v[134:135], v[134:135], v[210:211]
	v_rcp_f32_e32 v206, v10
	v_max_f32_e32 v10, 0.5, v204
	v_cvt_f32_ubyte1_e32 v211, v208
	v_cvt_f32_ubyte0_e32 v210, v208
	v_rcp_f32_e32 v207, v10
	v_pk_mul_f32 v[210:211], v[210:211], s[18:19] op_sel_hi:[1,0]
	v_cvt_f32_ubyte0_e32 v10, v205
	v_pk_mul_f32 v[202:203], v[210:211], v[202:203]
	v_cvt_f32_ubyte1_e32 v201, v205
	v_max_f32_e32 v10, 0.5, v10
	v_pk_mul_f32 v[214:215], v[214:215], s[18:19] op_sel_hi:[1,0]
	v_pk_mul_f32 v[106:107], v[106:107], v[202:203]
	v_cvt_f32_ubyte2_e32 v204, v205
	v_rcp_f32_e32 v202, v10
	v_max_f32_e32 v10, 0.5, v201
	v_pk_mul_f32 v[212:213], v[214:215], v[220:221]
	v_cvt_f32_ubyte3_e32 v205, v205
	v_rcp_f32_e32 v203, v10
	v_max_f32_e32 v10, 0.5, v204
	v_pk_mul_f32 v[136:137], v[136:137], v[212:213]
	v_cvt_f32_ubyte3_e32 v213, v208
	v_cvt_f32_ubyte2_e32 v212, v208
	v_rcp_f32_e32 v204, v10
	v_max_f32_e32 v10, 0.5, v205
	v_pk_mul_f32 v[212:213], v[212:213], s[18:19] op_sel_hi:[1,0]
	v_rcp_f32_e32 v205, v10
	v_pk_mul_f32 v[206:207], v[212:213], v[206:207]
	v_cvt_f32_ubyte3_e32 v211, v209
	v_pk_mul_f32 v[108:109], v[108:109], v[206:207]
	v_cvt_f32_ubyte1_e32 v207, v209
	v_cvt_f32_ubyte0_e32 v206, v209
	v_cvt_f32_ubyte2_e32 v210, v209
	v_pk_mul_f32 v[208:209], v[210:211], s[18:19] op_sel_hi:[1,0]
	v_pk_mul_f32 v[206:207], v[206:207], s[18:19] op_sel_hi:[1,0]
	s_waitcnt vmcnt(0) lgkmcnt(0)
	v_cvt_f32_ubyte0_e32 v10, v154
	v_pk_mul_f32 v[202:203], v[206:207], v[202:203]
	v_pk_mul_f32 v[204:205], v[208:209], v[204:205]
	v_cvt_f32_ubyte1_e32 v201, v154
	v_max_f32_e32 v10, 0.5, v10
	v_pk_mul_f32 v[104:105], v[104:105], v[204:205]
	v_pk_mul_f32 v[102:103], v[102:103], v[202:203]
	v_cvt_f32_ubyte2_e32 v204, v154
	v_rcp_f32_e32 v202, v10
	v_max_f32_e32 v10, 0.5, v201
	v_cvt_f32_ubyte3_e32 v154, v154
	v_rcp_f32_e32 v203, v10
	v_max_f32_e32 v10, 0.5, v204
	v_rcp_f32_e32 v204, v10
	v_max_f32_e32 v10, 0.5, v154
	v_rcp_f32_e32 v205, v10
	v_cvt_f32_ubyte1_e32 v207, v150
	v_cvt_f32_ubyte0_e32 v206, v150
	v_cvt_f32_ubyte0_e32 v10, v155
	v_cvt_f32_ubyte3_e32 v209, v150
	v_cvt_f32_ubyte2_e32 v208, v150
	v_pk_mul_f32 v[206:207], v[206:207], s[18:19] op_sel_hi:[1,0]
	v_cvt_f32_ubyte1_e32 v150, v155
	v_max_f32_e32 v10, 0.5, v10
	v_pk_mul_f32 v[202:203], v[206:207], v[202:203]
	v_cvt_f32_ubyte2_e32 v201, v155
	v_rcp_f32_e32 v154, v10
	v_max_f32_e32 v10, 0.5, v150
	v_pk_mul_f32 v[130:131], v[130:131], v[202:203]
	v_cvt_f32_ubyte3_e32 v203, v155
	v_rcp_f32_e32 v155, v10
	v_max_f32_e32 v10, 0.5, v201
	v_rcp_f32_e32 v202, v10
	v_max_f32_e32 v10, 0.5, v203
	v_rcp_f32_e32 v203, v10
	v_pk_mul_f32 v[208:209], v[208:209], s[18:19] op_sel_hi:[1,0]
	v_cvt_f32_ubyte3_e32 v207, v151
	v_pk_mul_f32 v[204:205], v[208:209], v[204:205]
	v_cvt_f32_ubyte2_e32 v206, v151
	v_pk_mul_f32 v[132:133], v[132:133], v[204:205]
	v_cvt_f32_ubyte1_e32 v205, v151
	v_cvt_f32_ubyte0_e32 v204, v151
	v_pk_mul_f32 v[150:151], v[206:207], s[18:19] op_sel_hi:[1,0]
	v_pk_mul_f32 v[204:205], v[204:205], s[18:19] op_sel_hi:[1,0]
; __device__ __forceinline__ f32x4 u8x4_f32(unsigned w) { return (f32x4){(float)(w & 0xffu), (float)((w >> 8) & 0xffu), (float)((w >> 16) & 0xffu), (float)(w >> 24)}; }
;     __device__ __forceinline__ void operator()(f32x4 (&acc)[2][2][4][2], const GUnit& u, int wr, int wc, int fr, int fq) const {
;     ...
;         if (u.x2 == 0) {
; #pragma unroll
;             for (int ai = 0; ai < 2; ++ai) {
;                 u32x4 qs[4], qf[4];
; #pragma unroll
;                 for (int m = 0; m < 4; ++m) { const size_t off = off0 + (size_t)(ai * 128 + m * 16) * D; qs[m] = __builtin_nontemporal_load((const u32x4*)(GZS + off)); qf[m] = *(const u32x4*)(GZF + off); }
; #pragma unroll
;                 for (int m = 0; m < 4; ++m)
; #pragma unroll
;                     for (int q = 0; q < 4; ++q) { const f32x4 s = u8x4_f32(qs[m][q]), f = u8x4_f32(qf[m][q]); f32x4 r;
; #pragma unroll
;                         for (int j = 0; j < 4; ++j) r[j] = s[j] * S8_INV * __builtin_amdgcn_rcpf(fmaxf(f[j], 0.5f));
;                         acc[ai][q >> 1][m][q & 1] *= r; }
;                 asm volatile("" ::: "memory");
;             }
;             return;
	v_pk_mul_f32 v[150:151], v[150:151], v[202:203]
	v_cvt_f32_ubyte0_e32 v10, v156
	v_pk_mul_f32 v[154:155], v[204:205], v[154:155]
	v_pk_mul_f32 v[128:129], v[128:129], v[150:151]
	v_cvt_f32_ubyte1_e32 v151, v156
	v_max_f32_e32 v10, 0.5, v10
	v_pk_mul_f32 v[126:127], v[126:127], v[154:155]
	v_cvt_f32_ubyte2_e32 v154, v156
	v_rcp_f32_e32 v150, v10
	v_max_f32_e32 v10, 0.5, v151
	v_cvt_f32_ubyte3_e32 v155, v156
	v_rcp_f32_e32 v151, v10
	v_max_f32_e32 v10, 0.5, v154
	v_rcp_f32_e32 v154, v10
	v_max_f32_e32 v10, 0.5, v155
	v_rcp_f32_e32 v155, v10
	v_cvt_f32_ubyte1_e32 v203, v152
	v_cvt_f32_ubyte0_e32 v202, v152
	v_pk_mul_f32 v[202:203], v[202:203], s[18:19] op_sel_hi:[1,0]
	v_cvt_f32_ubyte3_e32 v205, v152
	v_cvt_f32_ubyte2_e32 v204, v152
	v_pk_mul_f32 v[150:151], v[202:203], v[150:151]
	v_cvt_f32_ubyte0_e32 v10, v157
	v_pk_mul_f32 v[204:205], v[204:205], s[18:19] op_sel_hi:[1,0]
	v_pk_mul_f32 v[98:99], v[98:99], v[150:151]
	v_cvt_f32_ubyte1_e32 v151, v157
	v_max_f32_e32 v10, 0.5, v10
	v_pk_mul_f32 v[154:155], v[204:205], v[154:155]
	v_cvt_f32_ubyte2_e32 v152, v157
	v_rcp_f32_e32 v150, v10
	v_max_f32_e32 v10, 0.5, v151
	v_pk_mul_f32 v[100:101], v[100:101], v[154:155]
	v_cvt_f32_ubyte3_e32 v155, v157
	v_rcp_f32_e32 v151, v10
	v_max_f32_e32 v10, 0.5, v152
	v_rcp_f32_e32 v154, v10
	v_max_f32_e32 v10, 0.5, v155
	v_rcp_f32_e32 v155, v10
	v_cvt_f32_ubyte1_e32 v157, v153
	v_cvt_f32_ubyte0_e32 v156, v153
	v_pk_mul_f32 v[156:157], v[156:157], s[18:19] op_sel_hi:[1,0]
	v_cvt_f32_ubyte3_e32 v203, v153
	v_cvt_f32_ubyte2_e32 v202, v153
	v_pk_mul_f32 v[150:151], v[156:157], v[150:151]
	v_cvt_f32_ubyte0_e32 v10, v146
	v_pk_mul_f32 v[152:153], v[202:203], s[18:19] op_sel_hi:[1,0]
	v_pk_mul_f32 v[94:95], v[94:95], v[150:151]
	v_cvt_f32_ubyte1_e32 v151, v146
	v_max_f32_e32 v10, 0.5, v10
	v_pk_mul_f32 v[152:153], v[152:153], v[154:155]
	v_rcp_f32_e32 v150, v10
	v_max_f32_e32 v10, 0.5, v151
	v_pk_mul_f32 v[96:97], v[96:97], v[152:153]
	v_cvt_f32_ubyte2_e32 v152, v146
	v_rcp_f32_e32 v151, v10
	v_cvt_f32_ubyte3_e32 v146, v146
	v_max_f32_e32 v10, 0.5, v152
	v_rcp_f32_e32 v152, v10
	v_max_f32_e32 v10, 0.5, v146
	v_cvt_f32_ubyte1_e32 v155, v142
	v_cvt_f32_ubyte0_e32 v154, v142
	v_rcp_f32_e32 v153, v10
	v_pk_mul_f32 v[154:155], v[154:155], s[18:19] op_sel_hi:[1,0]
	v_cvt_f32_ubyte0_e32 v10, v147
	v_cvt_f32_ubyte3_e32 v157, v142
	v_cvt_f32_ubyte2_e32 v156, v142
	v_pk_mul_f32 v[150:151], v[154:155], v[150:151]
	v_cvt_f32_ubyte1_e32 v142, v147
	v_max_f32_e32 v10, 0.5, v10
	v_pk_mul_f32 v[122:123], v[122:123], v[150:151]
	v_cvt_f32_ubyte2_e32 v150, v147
	v_rcp_f32_e32 v146, v10
	v_max_f32_e32 v10, 0.5, v142
	v_cvt_f32_ubyte3_e32 v151, v147
	v_rcp_f32_e32 v147, v10
	v_max_f32_e32 v10, 0.5, v150
	v_rcp_f32_e32 v150, v10
	v_max_f32_e32 v10, 0.5, v151
	v_rcp_f32_e32 v151, v10
	v_pk_mul_f32 v[156:157], v[156:157], s[18:19] op_sel_hi:[1,0]
	v_cvt_f32_ubyte3_e32 v155, v143
	v_pk_mul_f32 v[152:153], v[156:157], v[152:153]
	v_cvt_f32_ubyte2_e32 v154, v143
	v_pk_mul_f32 v[124:125], v[124:125], v[152:153]
	v_cvt_f32_ubyte1_e32 v153, v143
	v_cvt_f32_ubyte0_e32 v152, v143
	v_pk_mul_f32 v[142:143], v[154:155], s[18:19] op_sel_hi:[1,0]
	v_cvt_f32_ubyte0_e32 v10, v148
	v_pk_mul_f32 v[142:143], v[142:143], v[150:151]
	v_max_f32_e32 v10, 0.5, v10
	v_pk_mul_f32 v[120:121], v[120:121], v[142:143]
	v_cvt_f32_ubyte1_e32 v143, v148
	v_pk_mul_f32 v[152:153], v[152:153], s[18:19] op_sel_hi:[1,0]
	v_rcp_f32_e32 v142, v10
	v_max_f32_e32 v10, 0.5, v143
	v_pk_mul_f32 v[146:147], v[152:153], v[146:147]
	v_rcp_f32_e32 v143, v10
	v_pk_mul_f32 v[118:119], v[118:119], v[146:147]
	v_cvt_f32_ubyte2_e32 v146, v148
	v_cvt_f32_ubyte3_e32 v147, v148
	v_max_f32_e32 v10, 0.5, v146
	v_cvt_f32_ubyte1_e32 v151, v144
	v_cvt_f32_ubyte0_e32 v150, v144
	v_rcp_f32_e32 v146, v10
	v_max_f32_e32 v10, 0.5, v147
	v_pk_mul_f32 v[150:151], v[150:151], s[18:19] op_sel_hi:[1,0]
	v_rcp_f32_e32 v147, v10
	v_pk_mul_f32 v[142:143], v[150:151], v[142:143]
	v_cvt_f32_ubyte0_e32 v10, v149
	v_pk_mul_f32 v[90:91], v[90:91], v[142:143]
	v_cvt_f32_ubyte1_e32 v143, v149
	v_max_f32_e32 v10, 0.5, v10
	v_cvt_f32_ubyte3_e32 v153, v144
	v_cvt_f32_ubyte2_e32 v152, v144
	v_rcp_f32_e32 v142, v10
	v_max_f32_e32 v10, 0.5, v143
	v_pk_mul_f32 v[152:153], v[152:153], s[18:19] op_sel_hi:[1,0]
	v_rcp_f32_e32 v143, v10
	v_pk_mul_f32 v[146:147], v[152:153], v[146:147]
	v_cvt_f32_ubyte2_e32 v144, v149
	v_pk_mul_f32 v[92:93], v[92:93], v[146:147]
	v_cvt_f32_ubyte3_e32 v147, v149
	v_max_f32_e32 v10, 0.5, v144
	v_cvt_f32_ubyte1_e32 v149, v145
	v_cvt_f32_ubyte0_e32 v148, v145
	v_rcp_f32_e32 v146, v10
	v_max_f32_e32 v10, 0.5, v147
	v_pk_mul_f32 v[148:149], v[148:149], s[18:19] op_sel_hi:[1,0]
	v_rcp_f32_e32 v147, v10
	v_pk_mul_f32 v[142:143], v[148:149], v[142:143]
	v_cvt_f32_ubyte0_e32 v10, v6
	v_pk_mul_f32 v[86:87], v[86:87], v[142:143]
	v_cvt_f32_ubyte1_e32 v143, v6
	v_max_f32_e32 v10, 0.5, v10
	v_cvt_f32_ubyte3_e32 v151, v145
	v_cvt_f32_ubyte2_e32 v150, v145
	v_rcp_f32_e32 v142, v10
	v_max_f32_e32 v10, 0.5, v143
	v_pk_mul_f32 v[144:145], v[150:151], s[18:19] op_sel_hi:[1,0]
	v_rcp_f32_e32 v143, v10
	v_pk_mul_f32 v[144:145], v[144:145], v[146:147]
	v_cvt_f32_ubyte1_e32 v147, v2
	v_pk_mul_f32 v[88:89], v[88:89], v[144:145]
	v_cvt_f32_ubyte2_e32 v144, v6
	v_cvt_f32_ubyte0_e32 v146, v2
	v_cvt_f32_ubyte3_e32 v6, v6
	v_max_f32_e32 v10, 0.5, v144
	v_cvt_f32_ubyte3_e32 v149, v2
	v_cvt_f32_ubyte2_e32 v148, v2
	v_pk_mul_f32 v[146:147], v[146:147], s[18:19] op_sel_hi:[1,0]
	v_cvt_f32_ubyte0_e32 v2, v7
	v_rcp_f32_e32 v144, v10
	v_max_f32_e32 v6, 0.5, v6
	v_pk_mul_f32 v[142:143], v[146:147], v[142:143]
	v_cvt_f32_ubyte1_e32 v10, v7
	v_max_f32_e32 v2, 0.5, v2
	v_rcp_f32_e32 v145, v6
; __device__ __forceinline__ f32x4 u8x4_f32(unsigned w) { return (f32x4){(float)(w & 0xffu), (float)((w >> 8) & 0xffu), (float)((w >> 16) & 0xffu), (float)(w >> 24)}; }
;     __device__ __forceinline__ void operator()(f32x4 (&acc)[2][2][4][2], const GUnit& u, int wr, int wc, int fr, int fq) const {
;     ...
;         if (u.x2 == 0) {
; #pragma unroll
;             for (int ai = 0; ai < 2; ++ai) {
;                 u32x4 qs[4], qf[4];
; #pragma unroll
;                 for (int m = 0; m < 4; ++m) { const size_t off = off0 + (size_t)(ai * 128 + m * 16) * D; qs[m] = __builtin_nontemporal_load((const u32x4*)(GZS + off)); qf[m] = *(const u32x4*)(GZF + off); }
; #pragma unroll
;                 for (int m = 0; m < 4; ++m)
; #pragma unroll
;                     for (int q = 0; q < 4; ++q) { const f32x4 s = u8x4_f32(qs[m][q]), f = u8x4_f32(qf[m][q]); f32x4 r;
; #pragma unroll
;                         for (int j = 0; j < 4; ++j) r[j] = s[j] * S8_INV * __builtin_amdgcn_rcpf(fmaxf(f[j], 0.5f));
;                         acc[ai][q >> 1][m][q & 1] *= r; }
;                 asm volatile("" ::: "memory");
;             }
;             return;
	v_pk_mul_f32 v[114:115], v[114:115], v[142:143]
	v_cvt_f32_ubyte2_e32 v142, v7
	v_rcp_f32_e32 v6, v2
	v_max_f32_e32 v2, 0.5, v10
	v_cvt_f32_ubyte3_e32 v143, v7
	v_rcp_f32_e32 v7, v2
	v_max_f32_e32 v2, 0.5, v142
	v_rcp_f32_e32 v142, v2
	v_max_f32_e32 v2, 0.5, v143
	v_rcp_f32_e32 v143, v2
	v_pk_mul_f32 v[148:149], v[148:149], s[18:19] op_sel_hi:[1,0]
	v_cvt_f32_ubyte3_e32 v147, v3
	v_pk_mul_f32 v[144:145], v[148:149], v[144:145]
	v_cvt_f32_ubyte2_e32 v146, v3
	v_pk_mul_f32 v[116:117], v[116:117], v[144:145]
	v_cvt_f32_ubyte1_e32 v145, v3
	v_cvt_f32_ubyte0_e32 v144, v3
	v_pk_mul_f32 v[2:3], v[146:147], s[18:19] op_sel_hi:[1,0]
	v_pk_mul_f32 v[144:145], v[144:145], s[18:19] op_sel_hi:[1,0]
	v_pk_mul_f32 v[2:3], v[2:3], v[142:143]
	v_pk_mul_f32 v[6:7], v[144:145], v[6:7]
	v_pk_mul_f32 v[112:113], v[112:113], v[2:3]
	v_add_co_u32_e32 v2, vcc, s61, v12
	v_pk_mul_f32 v[110:111], v[110:111], v[6:7]
	s_nop 0
	v_addc_co_u32_e32 v3, vcc, 0, v13, vcc
	global_load_dwordx4 v[202:205], v[2:3], off
	v_add_co_u32_e32 v6, vcc, s61, v188
	v_cvt_f32_ubyte0_e32 v2, v8
	s_nop 0
	v_addc_co_u32_e32 v7, vcc, 0, v189, vcc
	global_load_dwordx4 v[206:209], v[6:7], off nt
	v_cvt_f32_ubyte1_e32 v3, v8
	v_max_f32_e32 v2, 0.5, v2
	v_max_f32_e32 v3, 0.5, v3
	v_rcp_f32_e32 v2, v2
	v_rcp_f32_e32 v3, v3
	v_cvt_f32_ubyte2_e32 v10, v8
	v_cvt_f32_ubyte3_e32 v8, v8
	v_cvt_f32_ubyte1_e32 v143, v4
	v_cvt_f32_ubyte0_e32 v142, v4
	v_max_f32_e32 v6, 0.5, v10
	v_max_f32_e32 v7, 0.5, v8
	v_pk_mul_f32 v[142:143], v[142:143], s[18:19] op_sel_hi:[1,0]
	v_rcp_f32_e32 v6, v6
	v_rcp_f32_e32 v7, v7
	v_pk_mul_f32 v[2:3], v[142:143], v[2:3]
	v_cvt_f32_ubyte3_e32 v145, v4
	v_pk_mul_f32 v[82:83], v[82:83], v[2:3]
	v_cvt_f32_ubyte0_e32 v2, v9
	v_cvt_f32_ubyte1_e32 v3, v9
	v_cvt_f32_ubyte2_e32 v144, v4
	v_max_f32_e32 v2, 0.5, v2
	v_max_f32_e32 v3, 0.5, v3
	v_pk_mul_f32 v[144:145], v[144:145], s[18:19] op_sel_hi:[1,0]
	v_rcp_f32_e32 v2, v2
	v_rcp_f32_e32 v3, v3
	v_pk_mul_f32 v[6:7], v[144:145], v[6:7]
	v_cvt_f32_ubyte2_e32 v4, v9
	v_pk_mul_f32 v[84:85], v[84:85], v[6:7]
	v_cvt_f32_ubyte3_e32 v7, v9
	v_cvt_f32_ubyte1_e32 v9, v5
	v_cvt_f32_ubyte0_e32 v8, v5
	v_pk_mul_f32 v[8:9], v[8:9], s[18:19] op_sel_hi:[1,0]
	v_max_f32_e32 v4, 0.5, v4
	v_pk_mul_f32 v[2:3], v[8:9], v[2:3]
	v_rcp_f32_e32 v6, v4
	v_pk_mul_f32 v[78:79], v[78:79], v[2:3]
	v_add_co_u32_e32 v2, vcc, s62, v188
	v_max_f32_e32 v4, 0.5, v7
	s_nop 0
	v_addc_co_u32_e32 v3, vcc, 0, v189, vcc
	global_load_dwordx4 v[150:153], v[2:3], off nt
	v_add_co_u32_e32 v2, vcc, s62, v12
	v_cvt_f32_ubyte3_e32 v143, v5
	s_nop 0
	v_addc_co_u32_e32 v3, vcc, 0, v13, vcc
	global_load_dwordx4 v[154:157], v[2:3], off
	v_add_co_u32_e32 v2, vcc, s63, v188
	v_cvt_f32_ubyte2_e32 v142, v5
	s_nop 0
	v_addc_co_u32_e32 v3, vcc, 0, v189, vcc
	v_rcp_f32_e32 v7, v4
	v_pk_mul_f32 v[4:5], v[142:143], s[18:19] op_sel_hi:[1,0]
	global_load_dwordx4 v[142:145], v[2:3], off nt
	v_add_co_u32_e32 v2, vcc, s63, v12
	v_pk_mul_f32 v[4:5], v[4:5], v[6:7]
	s_nop 0
	v_addc_co_u32_e32 v3, vcc, 0, v13, vcc
	global_load_dwordx4 v[146:149], v[2:3], off
	v_add_co_u32_e32 v2, vcc, s64, v188
	v_pk_mul_f32 v[80:81], v[80:81], v[4:5]
	s_nop 0
	v_addc_co_u32_e32 v3, vcc, 0, v189, vcc
	v_add_co_u32_e32 v6, vcc, s64, v12
	global_load_dwordx4 v[2:5], v[2:3], off nt
	s_nop 0
	v_addc_co_u32_e32 v7, vcc, 0, v13, vcc
	global_load_dwordx4 v[6:9], v[6:7], off
	s_waitcnt vmcnt(0) lgkmcnt(0)
	v_cvt_f32_ubyte0_e32 v10, v202
	v_cvt_f32_ubyte1_e32 v13, v202
	v_max_f32_e32 v10, 0.5, v10
	v_cvt_f32_ubyte2_e32 v188, v202
	v_rcp_f32_e32 v12, v10
	v_max_f32_e32 v10, 0.5, v13
	v_cvt_f32_ubyte3_e32 v189, v202
	v_rcp_f32_e32 v13, v10
	v_max_f32_e32 v10, 0.5, v188
	v_rcp_f32_e32 v188, v10
	v_max_f32_e32 v10, 0.5, v189
	v_rcp_f32_e32 v189, v10
	v_cvt_f32_ubyte1_e32 v211, v206
	v_cvt_f32_ubyte0_e32 v210, v206
	v_cvt_f32_ubyte3_e32 v213, v206
	v_cvt_f32_ubyte2_e32 v212, v206
	v_pk_mul_f32 v[210:211], v[210:211], s[18:19] op_sel_hi:[1,0]
	v_pk_mul_f32 v[212:213], v[212:213], s[18:19] op_sel_hi:[1,0]
	v_pk_mul_f32 v[12:13], v[210:211], v[12:13]
	v_cvt_f32_ubyte0_e32 v10, v203
	v_pk_mul_f32 v[188:189], v[212:213], v[188:189]
	v_pk_mul_f32 v[74:75], v[74:75], v[12:13]
	v_cvt_f32_ubyte1_e32 v13, v203
	v_max_f32_e32 v10, 0.5, v10
	v_pk_mul_f32 v[76:77], v[76:77], v[188:189]
	v_cvt_f32_ubyte2_e32 v188, v203
	v_rcp_f32_e32 v12, v10
	v_max_f32_e32 v10, 0.5, v13
	v_cvt_f32_ubyte3_e32 v189, v203
	v_rcp_f32_e32 v13, v10
	v_max_f32_e32 v10, 0.5, v188
	v_rcp_f32_e32 v188, v10
	v_max_f32_e32 v10, 0.5, v189
	v_rcp_f32_e32 v189, v10
	v_cvt_f32_ubyte1_e32 v203, v207
	v_cvt_f32_ubyte0_e32 v202, v207
	v_cvt_f32_ubyte3_e32 v211, v207
	v_cvt_f32_ubyte2_e32 v210, v207
	v_pk_mul_f32 v[202:203], v[202:203], s[18:19] op_sel_hi:[1,0]
	v_pk_mul_f32 v[206:207], v[210:211], s[18:19] op_sel_hi:[1,0]
	v_pk_mul_f32 v[12:13], v[202:203], v[12:13]
	v_cvt_f32_ubyte0_e32 v10, v204
	v_pk_mul_f32 v[188:189], v[206:207], v[188:189]
	v_pk_mul_f32 v[70:71], v[70:71], v[12:13]
	v_cvt_f32_ubyte1_e32 v13, v204
	v_max_f32_e32 v10, 0.5, v10
	v_pk_mul_f32 v[72:73], v[72:73], v[188:189]
	v_cvt_f32_ubyte2_e32 v188, v204
	v_rcp_f32_e32 v12, v10
	v_max_f32_e32 v10, 0.5, v13
	v_cvt_f32_ubyte3_e32 v189, v204
	v_rcp_f32_e32 v13, v10
	v_max_f32_e32 v10, 0.5, v188
	v_rcp_f32_e32 v188, v10
	v_max_f32_e32 v10, 0.5, v189
	v_rcp_f32_e32 v189, v10
	v_cvt_f32_ubyte1_e32 v203, v208
	v_cvt_f32_ubyte0_e32 v202, v208
	v_pk_mul_f32 v[202:203], v[202:203], s[18:19] op_sel_hi:[1,0]
	v_cvt_f32_ubyte3_e32 v207, v208
	v_cvt_f32_ubyte2_e32 v206, v208
	v_pk_mul_f32 v[12:13], v[202:203], v[12:13]
	v_cvt_f32_ubyte0_e32 v10, v205
	v_pk_mul_f32 v[206:207], v[206:207], s[18:19] op_sel_hi:[1,0]
; __device__ __forceinline__ f32x4 u8x4_f32(unsigned w) { return (f32x4){(float)(w & 0xffu), (float)((w >> 8) & 0xffu), (float)((w >> 16) & 0xffu), (float)(w >> 24)}; }
;     __device__ __forceinline__ void operator()(f32x4 (&acc)[2][2][4][2], const GUnit& u, int wr, int wc, int fr, int fq) const {
;     ...
;         if (u.x2 == 0) {
; #pragma unroll
;             for (int ai = 0; ai < 2; ++ai) {
;                 u32x4 qs[4], qf[4];
; #pragma unroll
;                 for (int m = 0; m < 4; ++m) { const size_t off = off0 + (size_t)(ai * 128 + m * 16) * D; qs[m] = __builtin_nontemporal_load((const u32x4*)(GZS + off)); qf[m] = *(const u32x4*)(GZF + off); }
; #pragma unroll
;                 for (int m = 0; m < 4; ++m)
; #pragma unroll
;                     for (int q = 0; q < 4; ++q) { const f32x4 s = u8x4_f32(qs[m][q]), f = u8x4_f32(qf[m][q]); f32x4 r;
; #pragma unroll
;                         for (int j = 0; j < 4; ++j) r[j] = s[j] * S8_INV * __builtin_amdgcn_rcpf(fmaxf(f[j], 0.5f));
;                         acc[ai][q >> 1][m][q & 1] *= r; }
;                 asm volatile("" ::: "memory");
;             }
;             return;
	v_pk_mul_f32 v[42:43], v[42:43], v[12:13]
	v_cvt_f32_ubyte1_e32 v13, v205
	v_max_f32_e32 v10, 0.5, v10
	v_pk_mul_f32 v[188:189], v[206:207], v[188:189]
	v_rcp_f32_e32 v12, v10
	v_max_f32_e32 v10, 0.5, v13
	v_pk_mul_f32 v[44:45], v[44:45], v[188:189]
	v_cvt_f32_ubyte2_e32 v188, v205
	v_rcp_f32_e32 v13, v10
	v_cvt_f32_ubyte3_e32 v189, v205
	v_max_f32_e32 v10, 0.5, v188
	v_rcp_f32_e32 v188, v10
	v_max_f32_e32 v10, 0.5, v189
	v_cvt_f32_ubyte1_e32 v203, v209
	v_cvt_f32_ubyte0_e32 v202, v209
	v_rcp_f32_e32 v189, v10
	v_pk_mul_f32 v[202:203], v[202:203], s[18:19] op_sel_hi:[1,0]
	v_cvt_f32_ubyte0_e32 v10, v154
	v_pk_mul_f32 v[12:13], v[202:203], v[12:13]
	v_cvt_f32_ubyte3_e32 v205, v209
	v_cvt_f32_ubyte2_e32 v204, v209
	v_pk_mul_f32 v[38:39], v[38:39], v[12:13]
	v_cvt_f32_ubyte1_e32 v13, v154
	v_max_f32_e32 v10, 0.5, v10
	v_pk_mul_f32 v[204:205], v[204:205], s[18:19] op_sel_hi:[1,0]
	v_rcp_f32_e32 v12, v10
	v_max_f32_e32 v10, 0.5, v13
	v_pk_mul_f32 v[188:189], v[204:205], v[188:189]
	v_rcp_f32_e32 v13, v10
	v_pk_mul_f32 v[40:41], v[40:41], v[188:189]
	v_cvt_f32_ubyte2_e32 v188, v154
	v_cvt_f32_ubyte3_e32 v154, v154
	v_max_f32_e32 v10, 0.5, v188
	v_cvt_f32_ubyte1_e32 v203, v150
	v_cvt_f32_ubyte0_e32 v202, v150
	v_rcp_f32_e32 v188, v10
	v_max_f32_e32 v10, 0.5, v154
	v_pk_mul_f32 v[202:203], v[202:203], s[18:19] op_sel_hi:[1,0]
	v_rcp_f32_e32 v189, v10
	v_pk_mul_f32 v[12:13], v[202:203], v[12:13]
	v_cvt_f32_ubyte0_e32 v10, v155
	v_pk_mul_f32 v[66:67], v[66:67], v[12:13]
	v_cvt_f32_ubyte1_e32 v13, v155
	v_max_f32_e32 v10, 0.5, v10
	v_cvt_f32_ubyte3_e32 v205, v150
	v_cvt_f32_ubyte2_e32 v204, v150
	v_cvt_f32_ubyte2_e32 v150, v155
	v_rcp_f32_e32 v12, v10
	v_max_f32_e32 v10, 0.5, v13
	v_cvt_f32_ubyte3_e32 v155, v155
	v_rcp_f32_e32 v13, v10
	v_max_f32_e32 v10, 0.5, v150
	v_pk_mul_f32 v[204:205], v[204:205], s[18:19] op_sel_hi:[1,0]
	v_rcp_f32_e32 v154, v10
	v_max_f32_e32 v10, 0.5, v155
	v_pk_mul_f32 v[188:189], v[204:205], v[188:189]
	v_rcp_f32_e32 v155, v10
	v_pk_mul_f32 v[68:69], v[68:69], v[188:189]
	v_cvt_f32_ubyte1_e32 v189, v151
	v_cvt_f32_ubyte0_e32 v188, v151
	v_cvt_f32_ubyte3_e32 v203, v151
	v_cvt_f32_ubyte2_e32 v202, v151
	v_pk_mul_f32 v[188:189], v[188:189], s[18:19] op_sel_hi:[1,0]
	v_pk_mul_f32 v[150:151], v[202:203], s[18:19] op_sel_hi:[1,0]
	v_pk_mul_f32 v[12:13], v[188:189], v[12:13]
	v_cvt_f32_ubyte0_e32 v10, v156
	v_pk_mul_f32 v[150:151], v[150:151], v[154:155]
	v_pk_mul_f32 v[62:63], v[62:63], v[12:13]
	v_cvt_f32_ubyte1_e32 v13, v156
	v_max_f32_e32 v10, 0.5, v10
	v_pk_mul_f32 v[64:65], v[64:65], v[150:151]
	v_cvt_f32_ubyte2_e32 v150, v156
	v_rcp_f32_e32 v12, v10
	v_max_f32_e32 v10, 0.5, v13
	v_cvt_f32_ubyte3_e32 v151, v156
	v_rcp_f32_e32 v13, v10
	v_max_f32_e32 v10, 0.5, v150
	v_rcp_f32_e32 v150, v10
	v_max_f32_e32 v10, 0.5, v151
	v_rcp_f32_e32 v151, v10
	v_cvt_f32_ubyte1_e32 v155, v152
	v_cvt_f32_ubyte0_e32 v154, v152
	v_pk_mul_f32 v[154:155], v[154:155], s[18:19] op_sel_hi:[1,0]
	v_cvt_f32_ubyte3_e32 v189, v152
	v_cvt_f32_ubyte2_e32 v188, v152
	v_pk_mul_f32 v[12:13], v[154:155], v[12:13]
	v_cvt_f32_ubyte0_e32 v10, v157
	v_pk_mul_f32 v[188:189], v[188:189], s[18:19] op_sel_hi:[1,0]
	v_pk_mul_f32 v[34:35], v[34:35], v[12:13]
	v_cvt_f32_ubyte1_e32 v13, v157
	v_max_f32_e32 v10, 0.5, v10
	v_pk_mul_f32 v[150:151], v[188:189], v[150:151]
	v_rcp_f32_e32 v12, v10
	v_max_f32_e32 v10, 0.5, v13
	v_pk_mul_f32 v[36:37], v[36:37], v[150:151]
	v_cvt_f32_ubyte2_e32 v150, v157
	v_rcp_f32_e32 v13, v10
	v_cvt_f32_ubyte3_e32 v151, v157
	v_max_f32_e32 v10, 0.5, v150
	v_rcp_f32_e32 v150, v10
	v_max_f32_e32 v10, 0.5, v151
	v_cvt_f32_ubyte1_e32 v155, v153
	v_cvt_f32_ubyte0_e32 v154, v153
	v_rcp_f32_e32 v151, v10
	v_pk_mul_f32 v[154:155], v[154:155], s[18:19] op_sel_hi:[1,0]
	v_cvt_f32_ubyte0_e32 v10, v146
	v_pk_mul_f32 v[12:13], v[154:155], v[12:13]
	v_cvt_f32_ubyte3_e32 v157, v153
	v_cvt_f32_ubyte2_e32 v156, v153
	v_pk_mul_f32 v[30:31], v[30:31], v[12:13]
	v_cvt_f32_ubyte1_e32 v13, v146
	v_max_f32_e32 v10, 0.5, v10
	v_pk_mul_f32 v[152:153], v[156:157], s[18:19] op_sel_hi:[1,0]
	v_rcp_f32_e32 v12, v10
	v_max_f32_e32 v10, 0.5, v13
	v_pk_mul_f32 v[150:151], v[152:153], v[150:151]
	v_rcp_f32_e32 v13, v10
	v_pk_mul_f32 v[32:33], v[32:33], v[150:151]
	v_cvt_f32_ubyte2_e32 v150, v146
	v_cvt_f32_ubyte3_e32 v146, v146
	v_max_f32_e32 v10, 0.5, v150
	v_cvt_f32_ubyte1_e32 v153, v142
	v_cvt_f32_ubyte0_e32 v152, v142
	v_rcp_f32_e32 v150, v10
	v_max_f32_e32 v10, 0.5, v146
	v_pk_mul_f32 v[152:153], v[152:153], s[18:19] op_sel_hi:[1,0]
	v_rcp_f32_e32 v151, v10
	v_pk_mul_f32 v[12:13], v[152:153], v[12:13]
	v_cvt_f32_ubyte0_e32 v10, v147
	v_pk_mul_f32 v[58:59], v[58:59], v[12:13]
	v_cvt_f32_ubyte1_e32 v13, v147
	v_max_f32_e32 v10, 0.5, v10
	v_cvt_f32_ubyte3_e32 v155, v142
	v_cvt_f32_ubyte2_e32 v154, v142
	v_cvt_f32_ubyte2_e32 v142, v147
	v_rcp_f32_e32 v12, v10
	v_max_f32_e32 v10, 0.5, v13
	v_pk_mul_f32 v[154:155], v[154:155], s[18:19] op_sel_hi:[1,0]
	v_cvt_f32_ubyte3_e32 v147, v147
	v_rcp_f32_e32 v13, v10
	v_max_f32_e32 v10, 0.5, v142
	v_pk_mul_f32 v[150:151], v[154:155], v[150:151]
; __device__ __forceinline__ f32x4 u8x4_f32(unsigned w) { return (f32x4){(float)(w & 0xffu), (float)((w >> 8) & 0xffu), (float)((w >> 16) & 0xffu), (float)(w >> 24)}; }
;     __device__ __forceinline__ void operator()(f32x4 (&acc)[2][2][4][2], const GUnit& u, int wr, int wc, int fr, int fq) const {
;     ...
;         if (u.x2 == 0) {
; #pragma unroll
;             for (int ai = 0; ai < 2; ++ai) {
;                 u32x4 qs[4], qf[4];
; #pragma unroll
;                 for (int m = 0; m < 4; ++m) { const size_t off = off0 + (size_t)(ai * 128 + m * 16) * D; qs[m] = __builtin_nontemporal_load((const u32x4*)(GZS + off)); qf[m] = *(const u32x4*)(GZF + off); }
; #pragma unroll
;                 for (int m = 0; m < 4; ++m)
; #pragma unroll
;                     for (int q = 0; q < 4; ++q) { const f32x4 s = u8x4_f32(qs[m][q]), f = u8x4_f32(qf[m][q]); f32x4 r;
; #pragma unroll
;                         for (int j = 0; j < 4; ++j) r[j] = s[j] * S8_INV * __builtin_amdgcn_rcpf(fmaxf(f[j], 0.5f));
;                         acc[ai][q >> 1][m][q & 1] *= r; }
;                 asm volatile("" ::: "memory");
;             }
;             return;
	v_rcp_f32_e32 v146, v10
	v_max_f32_e32 v10, 0.5, v147
	v_pk_mul_f32 v[60:61], v[60:61], v[150:151]
	v_rcp_f32_e32 v147, v10
	v_cvt_f32_ubyte1_e32 v151, v143
	v_cvt_f32_ubyte0_e32 v150, v143
	v_pk_mul_f32 v[150:151], v[150:151], s[18:19] op_sel_hi:[1,0]
	v_cvt_f32_ubyte3_e32 v153, v143
	v_cvt_f32_ubyte2_e32 v152, v143
	v_pk_mul_f32 v[12:13], v[150:151], v[12:13]
	v_cvt_f32_ubyte0_e32 v10, v148
	v_pk_mul_f32 v[142:143], v[152:153], s[18:19] op_sel_hi:[1,0]
	v_pk_mul_f32 v[54:55], v[54:55], v[12:13]
	v_cvt_f32_ubyte1_e32 v13, v148
	v_max_f32_e32 v10, 0.5, v10
	v_pk_mul_f32 v[142:143], v[142:143], v[146:147]
	v_rcp_f32_e32 v12, v10
	v_max_f32_e32 v10, 0.5, v13
	v_pk_mul_f32 v[56:57], v[56:57], v[142:143]
	v_cvt_f32_ubyte2_e32 v142, v148
	v_rcp_f32_e32 v13, v10
	v_cvt_f32_ubyte3_e32 v143, v148
	v_max_f32_e32 v10, 0.5, v142
	v_rcp_f32_e32 v142, v10
	v_max_f32_e32 v10, 0.5, v143
	v_cvt_f32_ubyte1_e32 v147, v144
	v_cvt_f32_ubyte0_e32 v146, v144
	v_rcp_f32_e32 v143, v10
	v_pk_mul_f32 v[146:147], v[146:147], s[18:19] op_sel_hi:[1,0]
	v_cvt_f32_ubyte0_e32 v10, v149
	v_pk_mul_f32 v[12:13], v[146:147], v[12:13]
	v_cvt_f32_ubyte3_e32 v151, v144
	v_cvt_f32_ubyte2_e32 v150, v144
	v_pk_mul_f32 v[26:27], v[26:27], v[12:13]
	v_cvt_f32_ubyte1_e32 v13, v149
	v_max_f32_e32 v10, 0.5, v10
	v_pk_mul_f32 v[150:151], v[150:151], s[18:19] op_sel_hi:[1,0]
	v_rcp_f32_e32 v12, v10
	v_max_f32_e32 v10, 0.5, v13
	v_pk_mul_f32 v[142:143], v[150:151], v[142:143]
	v_rcp_f32_e32 v13, v10
	v_pk_mul_f32 v[28:29], v[28:29], v[142:143]
	v_cvt_f32_ubyte2_e32 v142, v149
	v_cvt_f32_ubyte3_e32 v143, v149
	v_max_f32_e32 v10, 0.5, v142
	v_cvt_f32_ubyte1_e32 v147, v145
	v_cvt_f32_ubyte0_e32 v146, v145
	v_rcp_f32_e32 v142, v10
	v_max_f32_e32 v10, 0.5, v143
	v_pk_mul_f32 v[146:147], v[146:147], s[18:19] op_sel_hi:[1,0]
	v_rcp_f32_e32 v143, v10
	v_pk_mul_f32 v[12:13], v[146:147], v[12:13]
	v_cvt_f32_ubyte0_e32 v10, v6
	v_pk_mul_f32 v[22:23], v[22:23], v[12:13]
	v_cvt_f32_ubyte1_e32 v13, v6
	v_max_f32_e32 v10, 0.5, v10
	v_cvt_f32_ubyte3_e32 v149, v145
	v_cvt_f32_ubyte2_e32 v148, v145
	v_rcp_f32_e32 v12, v10
	v_max_f32_e32 v10, 0.5, v13
	v_pk_mul_f32 v[144:145], v[148:149], s[18:19] op_sel_hi:[1,0]
	v_rcp_f32_e32 v13, v10
	v_pk_mul_f32 v[142:143], v[144:145], v[142:143]
	v_cvt_f32_ubyte1_e32 v145, v2
	v_pk_mul_f32 v[24:25], v[24:25], v[142:143]
	v_cvt_f32_ubyte2_e32 v142, v6
	v_cvt_f32_ubyte0_e32 v144, v2
	v_cvt_f32_ubyte3_e32 v6, v6
	v_max_f32_e32 v10, 0.5, v142
	v_cvt_f32_ubyte3_e32 v147, v2
	v_cvt_f32_ubyte2_e32 v146, v2
	v_pk_mul_f32 v[144:145], v[144:145], s[18:19] op_sel_hi:[1,0]
	v_cvt_f32_ubyte0_e32 v2, v7
	v_rcp_f32_e32 v142, v10
	v_max_f32_e32 v6, 0.5, v6
	v_pk_mul_f32 v[12:13], v[144:145], v[12:13]
	v_cvt_f32_ubyte1_e32 v10, v7
	v_max_f32_e32 v2, 0.5, v2
	v_rcp_f32_e32 v143, v6
	v_pk_mul_f32 v[50:51], v[50:51], v[12:13]
	v_cvt_f32_ubyte2_e32 v12, v7
	v_rcp_f32_e32 v6, v2
	v_max_f32_e32 v2, 0.5, v10
	v_cvt_f32_ubyte3_e32 v13, v7
	v_rcp_f32_e32 v7, v2
	v_max_f32_e32 v2, 0.5, v12
	v_rcp_f32_e32 v12, v2
	v_max_f32_e32 v2, 0.5, v13
	v_pk_mul_f32 v[146:147], v[146:147], s[18:19] op_sel_hi:[1,0]
	v_rcp_f32_e32 v13, v2
	v_pk_mul_f32 v[142:143], v[146:147], v[142:143]
	v_cvt_f32_ubyte3_e32 v145, v3
	v_pk_mul_f32 v[52:53], v[52:53], v[142:143]
	v_cvt_f32_ubyte1_e32 v143, v3
	v_cvt_f32_ubyte0_e32 v142, v3
	v_cvt_f32_ubyte2_e32 v144, v3
	v_pk_mul_f32 v[2:3], v[144:145], s[18:19] op_sel_hi:[1,0]
	v_pk_mul_f32 v[142:143], v[142:143], s[18:19] op_sel_hi:[1,0]
	v_pk_mul_f32 v[2:3], v[2:3], v[12:13]
	v_pk_mul_f32 v[6:7], v[142:143], v[6:7]
	v_pk_mul_f32 v[48:49], v[48:49], v[2:3]
	v_pk_mul_f32 v[46:47], v[46:47], v[6:7]
	v_cvt_f32_ubyte0_e32 v2, v8
	v_cvt_f32_ubyte1_e32 v3, v8
	v_cvt_f32_ubyte2_e32 v6, v8
	v_cvt_f32_ubyte3_e32 v7, v8
	v_max_f32_e32 v2, 0.5, v2
	v_max_f32_e32 v3, 0.5, v3
	v_max_f32_e32 v6, 0.5, v6
	v_max_f32_e32 v7, 0.5, v7
	v_rcp_f32_e32 v2, v2
	v_rcp_f32_e32 v3, v3
	v_rcp_f32_e32 v6, v6
	v_rcp_f32_e32 v7, v7
	v_cvt_f32_ubyte1_e32 v13, v4
	v_cvt_f32_ubyte0_e32 v12, v4
	v_cvt_f32_ubyte3_e32 v143, v4
	v_cvt_f32_ubyte2_e32 v142, v4
	v_pk_mul_f32 v[142:143], v[142:143], s[18:19] op_sel_hi:[1,0]
	v_pk_mul_f32 v[12:13], v[12:13], s[18:19] op_sel_hi:[1,0]
	v_pk_mul_f32 v[6:7], v[142:143], v[6:7]
	v_pk_mul_f32 v[2:3], v[12:13], v[2:3]
	v_cvt_f32_ubyte2_e32 v4, v9
	v_pk_mul_f32 v[20:21], v[20:21], v[6:7]
	v_pk_mul_f32 v[18:19], v[18:19], v[2:3]
	v_cvt_f32_ubyte0_e32 v2, v9
	v_cvt_f32_ubyte1_e32 v3, v9
	v_cvt_f32_ubyte3_e32 v7, v9
	v_max_f32_e32 v4, 0.5, v4
	v_max_f32_e32 v2, 0.5, v2
	v_max_f32_e32 v3, 0.5, v3
	v_rcp_f32_e32 v6, v4
	v_max_f32_e32 v4, 0.5, v7
	v_rcp_f32_e32 v2, v2
	v_rcp_f32_e32 v3, v3
	v_rcp_f32_e32 v7, v4
	v_cvt_f32_ubyte1_e32 v9, v5
	v_cvt_f32_ubyte0_e32 v8, v5
	v_cvt_f32_ubyte3_e32 v13, v5
	v_cvt_f32_ubyte2_e32 v12, v5
	v_pk_mul_f32 v[4:5], v[12:13], s[18:19] op_sel_hi:[1,0]
	v_pk_mul_f32 v[8:9], v[8:9], s[18:19] op_sel_hi:[1,0]
	v_pk_mul_f32 v[4:5], v[4:5], v[6:7]
	v_pk_mul_f32 v[2:3], v[8:9], v[2:3]
	v_pk_mul_f32 v[16:17], v[16:17], v[4:5]
	v_pk_mul_f32 v[14:15], v[14:15], v[2:3]

; #define PG8_STAGE(bufoff, gbase, voff) do { _Pragma("unroll") for (int _i = 0; _i < 2; ++_i) \
;         __builtin_amdgcn_global_load_lds((const unsigned*)((const char*)(gbase) + (voff)[_i]), (PG8_LAS unsigned*)(lds + (bufoff) + ldsw + _i * 8192), 16, 0, 0); } while (0)
; #define PG8_WAIT_V(n) asm volatile("s_waitcnt vmcnt(" #n ")" ::: "memory")
; #define PG8_WAIT_L(n) asm volatile("s_waitcnt lgkmcnt(" #n ")" ::: "memory")
; template <class Epi, class Sched, bool ALIGN_EPI = true, bool F8 = false>
; __device__ __forceinline__ void gemm_phase(PG8_LAS unsigned char* lds, const Sched& S, const Epi& E) {
;     ...
;         for (int t = 0; t < nt; t += 2) {
;             const bool last = (t == nt - 2);
;             if constexpr (Sched::GATHER) { if (last && has_next) S.a_off(nxt, Rs, Cs, voffAn); }
;             const char* a1 = cA + (size_t)(t + 1) * kstep;
;             const char* a2 = last ? nA : cA + (size_t)(t + 2) * kstep; const char* b2 = last ? nB : cB + (size_t)(t + 2) * kstepB;
;             const char* a3 = a2 + kstep; const char* b3 = b2 + kstepB;
;             unsigned vA2[2][2];
; #pragma unroll
;             for (int h = 0; h < 2; ++h)
; #pragma unroll
;                 for (int i = 0; i < 2; ++i) { if constexpr (Sched::GATHER) vA2[h][i] = (last && has_next) ? voffAn[h][i] : voffA[h][i]; else vA2[h][i] = voffA[h][i]; }
;             PG8_LDB(B0, 0, 0); PG8_LDB(B1, 0, 1); PG8_SCHED; PG8_LDA(At, 0, 0); PG8_STAGE(PG8_SA(1, 1), a1, voffA[1]);
;             PG8_WAIT_V(8); PG8_WAIT_L(0); PG8_BAR; PG8_MMA(0, 0, At, B0); PG8_MMA(0, 1, At, B1); PG8_BAR; PG8_SCHED;
;             PG8_LDA(At, 0, 1); PG8_STAGE(PG8_SB(0, 0), b2, voffB[0]); PG8_STAGE(PG8_SB(0, 1), b2, voffB[1]); PG8_STAGE(PG8_SA(0, 0), a2, vA2[0]);
;             PG8_WAIT_V(8); PG8_WAIT_L(0); PG8_BAR; PG8_MMA(1, 0, At, B0); PG8_MMA(1, 1, At, B1); PG8_BAR; PG8_SCHED;
;             PG8_LDB(B0, 1, 0); PG8_LDB(B1, 1, 1); PG8_SCHED; PG8_LDA(At, 1, 0); PG8_STAGE(PG8_SA(0, 1), a2, vA2[1]);
;             PG8_WAIT_V(8); PG8_WAIT_L(0); PG8_BAR; PG8_MMA(0, 0, At, B0); PG8_MMA(0, 1, At, B1); PG8_BAR; PG8_SCHED;
;             PG8_LDA(At, 1, 1); PG8_STAGE(PG8_SB(1, 0), b3, voffB[0]); PG8_STAGE(PG8_SB(1, 1), b3, voffB[1]); PG8_STAGE(PG8_SA(1, 0), a3, vA2[0]);
;             PG8_WAIT_V(8); PG8_WAIT_L(0); PG8_BAR; PG8_MMA(1, 0, At, B0); PG8_MMA(1, 1, At, B1); PG8_BAR; PG8_SCHED;
.LBB0_911:
	ds_read_b128 v[18:21], v191
	ds_read_b128 v[22:25], v191 offset:1024
	ds_read_b128 v[26:29], v191 offset:2048
	ds_read_b128 v[30:33], v191 offset:3072
	ds_read_b128 v[2:5], v192
	ds_read_b128 v[6:9], v192 offset:1024
	ds_read_b128 v[10:13], v192 offset:2048
	ds_read_b128 v[14:17], v192 offset:3072
	s_add_u32 s30, s28, 0x8000
	s_addc_u32 s31, s29, 0
	s_cmp_eq_u32 s65, 12
	s_cselect_b32 s42, s22, s30
	s_cselect_b32 s43, s23, s31
	s_cselect_b32 s40, s24, s19
	s_cselect_b32 s41, s25, s21
	s_add_u32 s30, s42, 0x8000
	s_addc_u32 s31, s43, 0
	s_add_i32 m0, s27, 0xc000
	ds_read_b128 v[196:199], v193
	ds_read_b128 v[200:203], v193 offset:1024
	ds_read_b128 v[204:207], v193 offset:2048
	ds_read_b128 v[208:211], v193 offset:3072
	ds_read_b128 v[212:215], v193 offset:4096
	ds_read_b128 v[216:219], v193 offset:5120
	ds_read_b128 v[220:223], v193 offset:6144
	ds_read_b128 v[224:227], v193 offset:7168
	global_load_lds_dwordx4 v182, s[28:29]
	s_add_i32 m0, s27, 0xe000
	s_nop 0
	global_load_lds_dwordx4 v180, s[28:29]
	s_waitcnt vmcnt(8)
	s_waitcnt lgkmcnt(0)
	s_setprio 1
	s_waitcnt lgkmcnt(0)
	v_mfma_scale_f32_16x16x128_f8f6f4 v[158:161], v[18:25], v[196:203], v[158:161], v194, v194 op_sel_hi:[0,0,0]
	v_mfma_scale_f32_16x16x128_f8f6f4 v[154:157], v[26:33], v[196:203], v[154:157], v194, v194 op_sel_hi:[0,0,0]
	v_mfma_scale_f32_16x16x128_f8f6f4 v[150:153], v[18:25], v[204:211], v[150:153], v194, v194 op_sel_hi:[0,0,0]
	v_mfma_scale_f32_16x16x128_f8f6f4 v[146:149], v[26:33], v[204:211], v[146:149], v194, v194 op_sel_hi:[0,0,0]
	v_mfma_scale_f32_16x16x128_f8f6f4 v[130:133], v[18:25], v[212:219], v[130:133], v194, v194 op_sel_hi:[0,0,0]
	v_mfma_scale_f32_16x16x128_f8f6f4 v[122:125], v[26:33], v[212:219], v[122:125], v194, v194 op_sel_hi:[0,0,0]
	v_mfma_scale_f32_16x16x128_f8f6f4 v[114:117], v[18:25], v[220:227], v[114:117], v194, v194 op_sel_hi:[0,0,0]
	v_mfma_scale_f32_16x16x128_f8f6f4 v[106:109], v[26:33], v[220:227], v[106:109], v194, v194 op_sel_hi:[0,0,0]
	s_nop 3
	s_setprio 0
	s_setprio 1
	v_mfma_scale_f32_16x16x128_f8f6f4 v[142:145], v[2:9], v[196:203], v[142:145], v194, v194 op_sel_hi:[0,0,0]
	v_mfma_scale_f32_16x16x128_f8f6f4 v[138:141], v[10:17], v[196:203], v[138:141], v194, v194 op_sel_hi:[0,0,0]
	v_mfma_scale_f32_16x16x128_f8f6f4 v[134:137], v[2:9], v[204:211], v[134:137], v194, v194 op_sel_hi:[0,0,0]
	v_mfma_scale_f32_16x16x128_f8f6f4 v[126:129], v[10:17], v[204:211], v[126:129], v194, v194 op_sel_hi:[0,0,0]
	v_mfma_scale_f32_16x16x128_f8f6f4 v[118:121], v[2:9], v[212:219], v[118:121], v194, v194 op_sel_hi:[0,0,0]
	v_mfma_scale_f32_16x16x128_f8f6f4 v[110:113], v[10:17], v[212:219], v[110:113], v194, v194 op_sel_hi:[0,0,0]
	v_mfma_scale_f32_16x16x128_f8f6f4 v[102:105], v[2:9], v[220:227], v[102:105], v194, v194 op_sel_hi:[0,0,0]
	v_mfma_scale_f32_16x16x128_f8f6f4 v[98:101], v[10:17], v[220:227], v[98:101], v194, v194 op_sel_hi:[0,0,0]
	s_nop 3
	s_setprio 0
	s_barrier
	s_add_i32 s66, s60, s48
	s_mov_b32 m0, s66
	ds_read_b128 v[196:199], v193 offset:16384
	ds_read_b128 v[200:203], v193 offset:17408
	ds_read_b128 v[204:207], v193 offset:18432
	ds_read_b128 v[208:211], v193 offset:19456
	ds_read_b128 v[212:215], v193 offset:20480
	ds_read_b128 v[216:219], v193 offset:21504
	ds_read_b128 v[220:223], v193 offset:22528
	ds_read_b128 v[224:227], v193 offset:23552
	global_load_lds_dwordx4 v162, s[40:41]
	s_add_i32 m0, s66, 0x2000
	s_add_i32 s66, s61, s48
	global_load_lds_dwordx4 v164, s[40:41]
	s_add_u32 s98, s40, s6
	s_addc_u32 s99, s41, s7
	s_mov_b32 m0, s66
	s_nop 0
	global_load_lds_dwordx4 v162, s[98:99]
	s_add_u32 s100, s40, s6
	s_addc_u32 s101, s41, s7
	s_add_i32 m0, s66, 0x2000
	s_nop 0
	global_load_lds_dwordx4 v164, s[100:101]
	s_mov_b32 m0, s27
	s_nop 0
	global_load_lds_dwordx4 v166, s[42:43]
	s_mov_b32 m0, s49
	s_nop 0
	global_load_lds_dwordx4 v168, s[42:43]
	s_waitcnt vmcnt(8)
	s_waitcnt lgkmcnt(0)
	s_setprio 1
	s_waitcnt lgkmcnt(0)
	v_mfma_scale_f32_16x16x128_f8f6f4 v[94:97], v[18:25], v[196:203], v[94:97], v194, v194 op_sel_hi:[0,0,0]
	v_mfma_scale_f32_16x16x128_f8f6f4 v[90:93], v[26:33], v[196:203], v[90:93], v194, v194 op_sel_hi:[0,0,0]
	v_mfma_scale_f32_16x16x128_f8f6f4 v[82:85], v[18:25], v[204:211], v[82:85], v194, v194 op_sel_hi:[0,0,0]
	v_mfma_scale_f32_16x16x128_f8f6f4 v[74:77], v[26:33], v[204:211], v[74:77], v194, v194 op_sel_hi:[0,0,0]
	v_mfma_scale_f32_16x16x128_f8f6f4 v[66:69], v[18:25], v[212:219], v[66:69], v194, v194 op_sel_hi:[0,0,0]
	v_mfma_scale_f32_16x16x128_f8f6f4 v[58:61], v[26:33], v[212:219], v[58:61], v194, v194 op_sel_hi:[0,0,0]
	v_mfma_scale_f32_16x16x128_f8f6f4 v[50:53], v[18:25], v[220:227], v[50:53], v194, v194 op_sel_hi:[0,0,0]
	v_mfma_scale_f32_16x16x128_f8f6f4 v[42:45], v[26:33], v[220:227], v[42:45], v194, v194 op_sel_hi:[0,0,0]
	s_nop 3
	s_setprio 0
	s_setprio 1
	v_mfma_scale_f32_16x16x128_f8f6f4 v[86:89], v[2:9], v[196:203], v[86:89], v194, v194 op_sel_hi:[0,0,0]
	v_mfma_scale_f32_16x16x128_f8f6f4 v[78:81], v[10:17], v[196:203], v[78:81], v194, v194 op_sel_hi:[0,0,0]
	v_mfma_scale_f32_16x16x128_f8f6f4 v[70:73], v[2:9], v[204:211], v[70:73], v194, v194 op_sel_hi:[0,0,0]
	v_mfma_scale_f32_16x16x128_f8f6f4 v[62:65], v[10:17], v[204:211], v[62:65], v194, v194 op_sel_hi:[0,0,0]
	v_mfma_scale_f32_16x16x128_f8f6f4 v[54:57], v[2:9], v[212:219], v[54:57], v194, v194 op_sel_hi:[0,0,0]
	v_mfma_scale_f32_16x16x128_f8f6f4 v[46:49], v[10:17], v[212:219], v[46:49], v194, v194 op_sel_hi:[0,0,0]
	v_mfma_scale_f32_16x16x128_f8f6f4 v[38:41], v[2:9], v[220:227], v[38:41], v194, v194 op_sel_hi:[0,0,0]
	v_mfma_scale_f32_16x16x128_f8f6f4 v[34:37], v[10:17], v[220:227], v[34:37], v194, v194 op_sel_hi:[0,0,0]
	s_nop 3
	s_setprio 0
	s_barrier
; #define PG8_STAGE(bufoff, gbase, voff) do { _Pragma("unroll") for (int _i = 0; _i < 2; ++_i) \
;         __builtin_amdgcn_global_load_lds((const unsigned*)((const char*)(gbase) + (voff)[_i]), (PG8_LAS unsigned*)(lds + (bufoff) + ldsw + _i * 8192), 16, 0, 0); } while (0)
; #define PG8_WAIT_V(n) asm volatile("s_waitcnt vmcnt(" #n ")" ::: "memory")
; #define PG8_WAIT_L(n) asm volatile("s_waitcnt lgkmcnt(" #n ")" ::: "memory")
; template <class Epi, class Sched, bool ALIGN_EPI = true, bool F8 = false>
; __device__ __forceinline__ void gemm_phase(PG8_LAS unsigned char* lds, const Sched& S, const Epi& E) {
;     ...
;         for (int t = 0; t < nt; t += 2) {
;             const bool last = (t == nt - 2);
;             if constexpr (Sched::GATHER) { if (last && has_next) S.a_off(nxt, Rs, Cs, voffAn); }
;             const char* a1 = cA + (size_t)(t + 1) * kstep;
;             const char* a2 = last ? nA : cA + (size_t)(t + 2) * kstep; const char* b2 = last ? nB : cB + (size_t)(t + 2) * kstepB;
;             const char* a3 = a2 + kstep; const char* b3 = b2 + kstepB;
;             unsigned vA2[2][2];
; #pragma unroll
;             for (int h = 0; h < 2; ++h)
; #pragma unroll
;                 for (int i = 0; i < 2; ++i) { if constexpr (Sched::GATHER) vA2[h][i] = (last && has_next) ? voffAn[h][i] : voffA[h][i]; else vA2[h][i] = voffA[h][i]; }
;             PG8_LDB(B0, 0, 0); PG8_LDB(B1, 0, 1); PG8_SCHED; PG8_LDA(At, 0, 0); PG8_STAGE(PG8_SA(1, 1), a1, voffA[1]);
;             PG8_WAIT_V(8); PG8_WAIT_L(0); PG8_BAR; PG8_MMA(0, 0, At, B0); PG8_MMA(0, 1, At, B1); PG8_BAR; PG8_SCHED;
;             PG8_LDA(At, 0, 1); PG8_STAGE(PG8_SB(0, 0), b2, voffB[0]); PG8_STAGE(PG8_SB(0, 1), b2, voffB[1]); PG8_STAGE(PG8_SA(0, 0), a2, vA2[0]);
;             PG8_WAIT_V(8); PG8_WAIT_L(0); PG8_BAR; PG8_MMA(1, 0, At, B0); PG8_MMA(1, 1, At, B1); PG8_BAR; PG8_SCHED;
;             PG8_LDB(B0, 1, 0); PG8_LDB(B1, 1, 1); PG8_SCHED; PG8_LDA(At, 1, 0); PG8_STAGE(PG8_SA(0, 1), a2, vA2[1]);
;             PG8_WAIT_V(8); PG8_WAIT_L(0); PG8_BAR; PG8_MMA(0, 0, At, B0); PG8_MMA(0, 1, At, B1); PG8_BAR; PG8_SCHED;
;             PG8_LDA(At, 1, 1); PG8_STAGE(PG8_SB(1, 0), b3, voffB[0]); PG8_STAGE(PG8_SB(1, 1), b3, voffB[1]); PG8_STAGE(PG8_SA(1, 0), a3, vA2[0]);
;             PG8_WAIT_V(8); PG8_WAIT_L(0); PG8_BAR; PG8_MMA(1, 0, At, B0); PG8_MMA(1, 1, At, B1); PG8_BAR; PG8_SCHED;
	s_add_i32 s66, 0, 0x18000
	s_add_i32 s67, 0, 0x1c000
	v_add_u32_e32 v14, s66, v189
	v_add_u32_e32 v30, s67, v189
	ds_read_b128 v[2:5], v14
	ds_read_b128 v[6:9], v14 offset:1024
	ds_read_b128 v[10:13], v14 offset:2048
	ds_read_b128 v[14:17], v14 offset:3072
	ds_read_b128 v[18:21], v30
	ds_read_b128 v[22:25], v30 offset:1024
	ds_read_b128 v[26:29], v30 offset:2048
	ds_read_b128 v[30:33], v30 offset:3072
	s_mov_b32 m0, s50
	ds_read_b128 v[196:199], v193 offset:32768
	ds_read_b128 v[200:203], v193 offset:33792
	ds_read_b128 v[204:207], v193 offset:34816
	ds_read_b128 v[208:211], v193 offset:35840
	ds_read_b128 v[212:215], v193 offset:36864
	ds_read_b128 v[216:219], v193 offset:37888
	ds_read_b128 v[220:223], v193 offset:38912
	ds_read_b128 v[224:227], v193 offset:39936
	global_load_lds_dwordx4 v172, s[42:43]
	s_mov_b32 m0, s51
	s_nop 0
	global_load_lds_dwordx4 v174, s[42:43]
	s_waitcnt vmcnt(8)
	s_waitcnt lgkmcnt(0)
	s_setprio 1
	s_waitcnt lgkmcnt(0)
	v_mfma_scale_f32_16x16x128_f8f6f4 v[158:161], v[2:9], v[196:203], v[158:161], v194, v194 op_sel_hi:[0,0,0]
	v_mfma_scale_f32_16x16x128_f8f6f4 v[154:157], v[10:17], v[196:203], v[154:157], v194, v194 op_sel_hi:[0,0,0]
	v_mfma_scale_f32_16x16x128_f8f6f4 v[150:153], v[2:9], v[204:211], v[150:153], v194, v194 op_sel_hi:[0,0,0]
	v_mfma_scale_f32_16x16x128_f8f6f4 v[146:149], v[10:17], v[204:211], v[146:149], v194, v194 op_sel_hi:[0,0,0]
	v_mfma_scale_f32_16x16x128_f8f6f4 v[130:133], v[2:9], v[212:219], v[130:133], v194, v194 op_sel_hi:[0,0,0]
	v_mfma_scale_f32_16x16x128_f8f6f4 v[122:125], v[10:17], v[212:219], v[122:125], v194, v194 op_sel_hi:[0,0,0]
	v_mfma_scale_f32_16x16x128_f8f6f4 v[114:117], v[2:9], v[220:227], v[114:117], v194, v194 op_sel_hi:[0,0,0]
	v_mfma_scale_f32_16x16x128_f8f6f4 v[106:109], v[10:17], v[220:227], v[106:109], v194, v194 op_sel_hi:[0,0,0]
	s_nop 3
	s_setprio 0
	s_setprio 1
	v_mfma_scale_f32_16x16x128_f8f6f4 v[142:145], v[18:25], v[196:203], v[142:145], v194, v194 op_sel_hi:[0,0,0]
	v_mfma_scale_f32_16x16x128_f8f6f4 v[138:141], v[26:33], v[196:203], v[138:141], v194, v194 op_sel_hi:[0,0,0]
	v_mfma_scale_f32_16x16x128_f8f6f4 v[134:137], v[18:25], v[204:211], v[134:137], v194, v194 op_sel_hi:[0,0,0]
	v_mfma_scale_f32_16x16x128_f8f6f4 v[126:129], v[26:33], v[204:211], v[126:129], v194, v194 op_sel_hi:[0,0,0]
	v_mfma_scale_f32_16x16x128_f8f6f4 v[118:121], v[18:25], v[212:219], v[118:121], v194, v194 op_sel_hi:[0,0,0]
	v_mfma_scale_f32_16x16x128_f8f6f4 v[110:113], v[26:33], v[212:219], v[110:113], v194, v194 op_sel_hi:[0,0,0]
	v_mfma_scale_f32_16x16x128_f8f6f4 v[102:105], v[18:25], v[220:227], v[102:105], v194, v194 op_sel_hi:[0,0,0]
	v_mfma_scale_f32_16x16x128_f8f6f4 v[98:101], v[26:33], v[220:227], v[98:101], v194, v194 op_sel_hi:[0,0,0]
	s_nop 3
	s_setprio 0
	s_barrier
	s_add_u32 s40, s40, 0x8000
	s_addc_u32 s41, s41, 0
	s_add_i32 s42, s66, s48
	s_mov_b32 m0, s42
	ds_read_b128 v[196:199], v193 offset:49152
	ds_read_b128 v[200:203], v193 offset:50176
	ds_read_b128 v[204:207], v193 offset:51200
	ds_read_b128 v[208:211], v193 offset:52224
	ds_read_b128 v[212:215], v193 offset:53248
	ds_read_b128 v[216:219], v193 offset:54272
	ds_read_b128 v[220:223], v193 offset:55296
	ds_read_b128 v[224:227], v193 offset:56320
	global_load_lds_dwordx4 v162, s[40:41]
	s_add_i32 m0, s42, 0x2000
	s_add_i32 s42, s67, s48
	global_load_lds_dwordx4 v164, s[40:41]
	s_mov_b32 m0, s42
	s_nop 0
	global_load_lds_dwordx4 v176, s[40:41]
	s_add_i32 m0, s42, 0x2000
	s_nop 0
	global_load_lds_dwordx4 v178, s[40:41]
	s_mov_b32 m0, s53
	s_nop 0
	global_load_lds_dwordx4 v166, s[30:31]
	s_mov_b32 m0, s58
	s_nop 0
	global_load_lds_dwordx4 v168, s[30:31]
	s_waitcnt vmcnt(8)
	s_waitcnt lgkmcnt(0)
	s_setprio 1
	s_waitcnt lgkmcnt(0)
	v_mfma_scale_f32_16x16x128_f8f6f4 v[94:97], v[2:9], v[196:203], v[94:97], v194, v194 op_sel_hi:[0,0,0]
	v_mfma_scale_f32_16x16x128_f8f6f4 v[90:93], v[10:17], v[196:203], v[90:93], v194, v194 op_sel_hi:[0,0,0]
	v_mfma_scale_f32_16x16x128_f8f6f4 v[82:85], v[2:9], v[204:211], v[82:85], v194, v194 op_sel_hi:[0,0,0]
	v_mfma_scale_f32_16x16x128_f8f6f4 v[74:77], v[10:17], v[204:211], v[74:77], v194, v194 op_sel_hi:[0,0,0]
	v_mfma_scale_f32_16x16x128_f8f6f4 v[66:69], v[2:9], v[212:219], v[66:69], v194, v194 op_sel_hi:[0,0,0]
	v_mfma_scale_f32_16x16x128_f8f6f4 v[58:61], v[10:17], v[212:219], v[58:61], v194, v194 op_sel_hi:[0,0,0]
	v_mfma_scale_f32_16x16x128_f8f6f4 v[50:53], v[2:9], v[220:227], v[50:53], v194, v194 op_sel_hi:[0,0,0]
	v_mfma_scale_f32_16x16x128_f8f6f4 v[42:45], v[10:17], v[220:227], v[42:45], v194, v194 op_sel_hi:[0,0,0]
	s_nop 3
	s_setprio 0
	s_setprio 1
	v_mfma_scale_f32_16x16x128_f8f6f4 v[86:89], v[18:25], v[196:203], v[86:89], v194, v194 op_sel_hi:[0,0,0]
	v_mfma_scale_f32_16x16x128_f8f6f4 v[78:81], v[26:33], v[196:203], v[78:81], v194, v194 op_sel_hi:[0,0,0]
	v_mfma_scale_f32_16x16x128_f8f6f4 v[70:73], v[18:25], v[204:211], v[70:73], v194, v194 op_sel_hi:[0,0,0]
	v_mfma_scale_f32_16x16x128_f8f6f4 v[62:65], v[26:33], v[204:211], v[62:65], v194, v194 op_sel_hi:[0,0,0]
	v_mfma_scale_f32_16x16x128_f8f6f4 v[54:57], v[18:25], v[212:219], v[54:57], v194, v194 op_sel_hi:[0,0,0]
	v_mfma_scale_f32_16x16x128_f8f6f4 v[46:49], v[26:33], v[212:219], v[46:49], v194, v194 op_sel_hi:[0,0,0]
	v_mfma_scale_f32_16x16x128_f8f6f4 v[38:41], v[18:25], v[220:227], v[38:41], v194, v194 op_sel_hi:[0,0,0]
	v_mfma_scale_f32_16x16x128_f8f6f4 v[34:37], v[26:33], v[220:227], v[34:37], v194, v194 op_sel_hi:[0,0,0]
	s_nop 3
	s_setprio 0
	s_barrier
	s_add_i32 s65, s65, 2
	s_add_u32 s19, s19, 0x10000
	s_addc_u32 s21, s21, 0
	s_add_u32 s28, s28, 0x10000
	s_addc_u32 s29, s29, 0
	s_cmp_gt_u32 s65, 13
	s_cbranch_scc0 .LBB0_911
	s_branch .Lfx_26630
; #define PG8_STAGE(bufoff, gbase, voff) do { _Pragma("unroll") for (int _i = 0; _i < 2; ++_i) \
;         __builtin_amdgcn_global_load_lds((const unsigned*)((const char*)(gbase) + (voff)[_i]), (PG8_LAS unsigned*)(lds + (bufoff) + ldsw + _i * 8192), 16, 0, 0); } while (0)
; #define PG8_WAIT_V(n) asm volatile("s_waitcnt vmcnt(" #n ")" ::: "memory")
; #define PG8_WAIT_L(n) asm volatile("s_waitcnt lgkmcnt(" #n ")" ::: "memory")
; template <class Epi, class Sched, bool ALIGN_EPI = true, bool F8 = false>
; __device__ __forceinline__ void gemm_phase(PG8_LAS unsigned char* lds, const Sched& S, const Epi& E) {
;     ...
;         for (int t = 0; t < nt; t += 2) {
;             const bool last = (t == nt - 2);
;             if constexpr (Sched::GATHER) { if (last && has_next) S.a_off(nxt, Rs, Cs, voffAn); }
;             const char* a1 = cA + (size_t)(t + 1) * kstep;
;             const char* a2 = last ? nA : cA + (size_t)(t + 2) * kstep; const char* b2 = last ? nB : cB + (size_t)(t + 2) * kstepB;
;             const char* a3 = a2 + kstep; const char* b3 = b2 + kstepB;
;             unsigned vA2[2][2];
; #pragma unroll
;             for (int h = 0; h < 2; ++h)
; #pragma unroll
;                 for (int i = 0; i < 2; ++i) { if constexpr (Sched::GATHER) vA2[h][i] = (last && has_next) ? voffAn[h][i] : voffA[h][i]; else vA2[h][i] = voffA[h][i]; }
;             PG8_LDB(B0, 0, 0); PG8_LDB(B1, 0, 1); PG8_SCHED; PG8_LDA(At, 0, 0); PG8_STAGE(PG8_SA(1, 1), a1, voffA[1]);
;             PG8_WAIT_V(8); PG8_WAIT_L(0); PG8_BAR; PG8_MMA(0, 0, At, B0); PG8_MMA(0, 1, At, B1); PG8_BAR; PG8_SCHED;
;             PG8_LDA(At, 0, 1); PG8_STAGE(PG8_SB(0, 0), b2, voffB[0]); PG8_STAGE(PG8_SB(0, 1), b2, voffB[1]); PG8_STAGE(PG8_SA(0, 0), a2, vA2[0]);
;             PG8_WAIT_V(8); PG8_WAIT_L(0); PG8_BAR; PG8_MMA(1, 0, At, B0); PG8_MMA(1, 1, At, B1); PG8_BAR; PG8_SCHED;
;             PG8_LDB(B0, 1, 0); PG8_LDB(B1, 1, 1); PG8_SCHED; PG8_LDA(At, 1, 0); PG8_STAGE(PG8_SA(0, 1), a2, vA2[1]);
;             PG8_WAIT_V(8); PG8_WAIT_L(0); PG8_BAR; PG8_MMA(0, 0, At, B0); PG8_MMA(0, 1, At, B1); PG8_BAR; PG8_SCHED;
;             PG8_LDA(At, 1, 1); PG8_STAGE(PG8_SB(1, 0), b3, voffB[0]); PG8_STAGE(PG8_SB(1, 1), b3, voffB[1]); PG8_STAGE(PG8_SA(1, 0), a3, vA2[0]);
;             PG8_WAIT_V(8); PG8_WAIT_L(0); PG8_BAR; PG8_MMA(1, 0, At, B0); PG8_MMA(1, 1, At, B1); PG8_BAR; PG8_SCHED;
.Lh1e_26630:
.Lh1_911:
	ds_read_b128 v[18:21], v191
	ds_read_b128 v[22:25], v191 offset:1024
	ds_read_b128 v[26:29], v191 offset:2048
	ds_read_b128 v[30:33], v191 offset:3072
	ds_read_b128 v[2:5], v192
	ds_read_b128 v[6:9], v192 offset:1024
	ds_read_b128 v[10:13], v192 offset:2048
	ds_read_b128 v[14:17], v192 offset:3072
	s_add_u32 s30, s28, 0x8000
	s_addc_u32 s31, s29, 0
	s_cmp_eq_u32 s65, 12
	s_cselect_b32 s42, s22, s30
	s_cselect_b32 s43, s23, s31
	s_cselect_b32 s40, s24, s19
	s_cselect_b32 s41, s25, s21
	s_add_u32 s30, s42, 0x8000
	s_addc_u32 s31, s43, 0
	s_add_i32 m0, s27, 0xc000
	ds_read_b128 v[196:199], v193
	ds_read_b128 v[200:203], v193 offset:1024
	ds_read_b128 v[204:207], v193 offset:2048
	ds_read_b128 v[208:211], v193 offset:3072
	ds_read_b128 v[212:215], v193 offset:4096
	ds_read_b128 v[216:219], v193 offset:5120
	ds_read_b128 v[220:223], v193 offset:6144
	ds_read_b128 v[224:227], v193 offset:7168
	global_load_lds_dwordx4 v182, s[28:29]
	s_add_i32 m0, s27, 0xe000
	s_nop 0
	global_load_lds_dwordx4 v180, s[28:29]
	s_waitcnt vmcnt(8)
	s_waitcnt lgkmcnt(0)
	s_barrier
	s_setprio 2
	s_waitcnt lgkmcnt(0)
	v_mfma_scale_f32_16x16x128_f8f6f4 v[158:161], v[18:25], v[196:203], v[158:161], v194, v194 op_sel_hi:[0,0,0]
	v_mfma_scale_f32_16x16x128_f8f6f4 v[154:157], v[26:33], v[196:203], v[154:157], v194, v194 op_sel_hi:[0,0,0]
	v_mfma_scale_f32_16x16x128_f8f6f4 v[150:153], v[18:25], v[204:211], v[150:153], v194, v194 op_sel_hi:[0,0,0]
	v_mfma_scale_f32_16x16x128_f8f6f4 v[146:149], v[26:33], v[204:211], v[146:149], v194, v194 op_sel_hi:[0,0,0]
	v_mfma_scale_f32_16x16x128_f8f6f4 v[130:133], v[18:25], v[212:219], v[130:133], v194, v194 op_sel_hi:[0,0,0]
	v_mfma_scale_f32_16x16x128_f8f6f4 v[122:125], v[26:33], v[212:219], v[122:125], v194, v194 op_sel_hi:[0,0,0]
	v_mfma_scale_f32_16x16x128_f8f6f4 v[114:117], v[18:25], v[220:227], v[114:117], v194, v194 op_sel_hi:[0,0,0]
	v_mfma_scale_f32_16x16x128_f8f6f4 v[106:109], v[26:33], v[220:227], v[106:109], v194, v194 op_sel_hi:[0,0,0]
	s_nop 3
	s_setprio 0
	s_setprio 2
	v_mfma_scale_f32_16x16x128_f8f6f4 v[142:145], v[2:9], v[196:203], v[142:145], v194, v194 op_sel_hi:[0,0,0]
	v_mfma_scale_f32_16x16x128_f8f6f4 v[138:141], v[10:17], v[196:203], v[138:141], v194, v194 op_sel_hi:[0,0,0]
	v_mfma_scale_f32_16x16x128_f8f6f4 v[134:137], v[2:9], v[204:211], v[134:137], v194, v194 op_sel_hi:[0,0,0]
	v_mfma_scale_f32_16x16x128_f8f6f4 v[126:129], v[10:17], v[204:211], v[126:129], v194, v194 op_sel_hi:[0,0,0]
	v_mfma_scale_f32_16x16x128_f8f6f4 v[118:121], v[2:9], v[212:219], v[118:121], v194, v194 op_sel_hi:[0,0,0]
	v_mfma_scale_f32_16x16x128_f8f6f4 v[110:113], v[10:17], v[212:219], v[110:113], v194, v194 op_sel_hi:[0,0,0]
	v_mfma_scale_f32_16x16x128_f8f6f4 v[102:105], v[2:9], v[220:227], v[102:105], v194, v194 op_sel_hi:[0,0,0]
	v_mfma_scale_f32_16x16x128_f8f6f4 v[98:101], v[10:17], v[220:227], v[98:101], v194, v194 op_sel_hi:[0,0,0]
	s_nop 3
	s_setprio 0
	s_add_i32 s66, s60, s48
	s_mov_b32 m0, s66
	ds_read_b128 v[196:199], v193 offset:16384
	ds_read_b128 v[200:203], v193 offset:17408
	ds_read_b128 v[204:207], v193 offset:18432
	ds_read_b128 v[208:211], v193 offset:19456
	ds_read_b128 v[212:215], v193 offset:20480
	ds_read_b128 v[216:219], v193 offset:21504
	ds_read_b128 v[220:223], v193 offset:22528
	ds_read_b128 v[224:227], v193 offset:23552
	global_load_lds_dwordx4 v162, s[40:41]
	s_add_i32 m0, s66, 0x2000
	s_add_i32 s66, s61, s48
	global_load_lds_dwordx4 v164, s[40:41]
	s_add_u32 s98, s40, s6
	s_addc_u32 s99, s41, s7
	s_mov_b32 m0, s66
	s_nop 0
	global_load_lds_dwordx4 v162, s[98:99]
	s_add_u32 s100, s40, s6
	s_addc_u32 s101, s41, s7
	s_add_i32 m0, s66, 0x2000
	s_nop 0
	global_load_lds_dwordx4 v164, s[100:101]
	s_mov_b32 m0, s27
	s_nop 0
	global_load_lds_dwordx4 v166, s[42:43]
	s_mov_b32 m0, s49
	s_nop 0
	global_load_lds_dwordx4 v168, s[42:43]
	s_waitcnt vmcnt(8)
	s_waitcnt lgkmcnt(0)
	s_barrier
	s_setprio 2
	s_waitcnt lgkmcnt(0)
	v_mfma_scale_f32_16x16x128_f8f6f4 v[94:97], v[18:25], v[196:203], v[94:97], v194, v194 op_sel_hi:[0,0,0]
	v_mfma_scale_f32_16x16x128_f8f6f4 v[90:93], v[26:33], v[196:203], v[90:93], v194, v194 op_sel_hi:[0,0,0]
	v_mfma_scale_f32_16x16x128_f8f6f4 v[82:85], v[18:25], v[204:211], v[82:85], v194, v194 op_sel_hi:[0,0,0]
	v_mfma_scale_f32_16x16x128_f8f6f4 v[74:77], v[26:33], v[204:211], v[74:77], v194, v194 op_sel_hi:[0,0,0]
	v_mfma_scale_f32_16x16x128_f8f6f4 v[66:69], v[18:25], v[212:219], v[66:69], v194, v194 op_sel_hi:[0,0,0]
	v_mfma_scale_f32_16x16x128_f8f6f4 v[58:61], v[26:33], v[212:219], v[58:61], v194, v194 op_sel_hi:[0,0,0]
	v_mfma_scale_f32_16x16x128_f8f6f4 v[50:53], v[18:25], v[220:227], v[50:53], v194, v194 op_sel_hi:[0,0,0]
	v_mfma_scale_f32_16x16x128_f8f6f4 v[42:45], v[26:33], v[220:227], v[42:45], v194, v194 op_sel_hi:[0,0,0]
	s_nop 3
	s_setprio 0
	s_setprio 2
	v_mfma_scale_f32_16x16x128_f8f6f4 v[86:89], v[2:9], v[196:203], v[86:89], v194, v194 op_sel_hi:[0,0,0]
	v_mfma_scale_f32_16x16x128_f8f6f4 v[78:81], v[10:17], v[196:203], v[78:81], v194, v194 op_sel_hi:[0,0,0]
	v_mfma_scale_f32_16x16x128_f8f6f4 v[70:73], v[2:9], v[204:211], v[70:73], v194, v194 op_sel_hi:[0,0,0]
	v_mfma_scale_f32_16x16x128_f8f6f4 v[62:65], v[10:17], v[204:211], v[62:65], v194, v194 op_sel_hi:[0,0,0]
	v_mfma_scale_f32_16x16x128_f8f6f4 v[54:57], v[2:9], v[212:219], v[54:57], v194, v194 op_sel_hi:[0,0,0]
	v_mfma_scale_f32_16x16x128_f8f6f4 v[46:49], v[10:17], v[212:219], v[46:49], v194, v194 op_sel_hi:[0,0,0]
	v_mfma_scale_f32_16x16x128_f8f6f4 v[38:41], v[2:9], v[220:227], v[38:41], v194, v194 op_sel_hi:[0,0,0]
	v_mfma_scale_f32_16x16x128_f8f6f4 v[34:37], v[10:17], v[220:227], v[34:37], v194, v194 op_sel_hi:[0,0,0]
	s_nop 3
	s_setprio 0
	s_add_i32 s66, 0, 0x18000
	s_add_i32 s67, 0, 0x1c000
	v_add_u32_e32 v14, s66, v189
	v_add_u32_e32 v30, s67, v189
	ds_read_b128 v[2:5], v14
	ds_read_b128 v[6:9], v14 offset:1024
	ds_read_b128 v[10:13], v14 offset:2048
	ds_read_b128 v[14:17], v14 offset:3072
	ds_read_b128 v[18:21], v30
	ds_read_b128 v[22:25], v30 offset:1024
	ds_read_b128 v[26:29], v30 offset:2048
	ds_read_b128 v[30:33], v30 offset:3072
	s_mov_b32 m0, s50
	ds_read_b128 v[196:199], v193 offset:32768
	ds_read_b128 v[200:203], v193 offset:33792
	ds_read_b128 v[204:207], v193 offset:34816
	ds_read_b128 v[208:211], v193 offset:35840
	ds_read_b128 v[212:215], v193 offset:36864
	ds_read_b128 v[216:219], v193 offset:37888
	ds_read_b128 v[220:223], v193 offset:38912
	ds_read_b128 v[224:227], v193 offset:39936
	global_load_lds_dwordx4 v172, s[42:43]
	s_mov_b32 m0, s51
	s_nop 0
	global_load_lds_dwordx4 v174, s[42:43]
	s_waitcnt vmcnt(8)
	s_waitcnt lgkmcnt(0)
	s_barrier
; #define PG8_STAGE(bufoff, gbase, voff) do { _Pragma("unroll") for (int _i = 0; _i < 2; ++_i) \
;         __builtin_amdgcn_global_load_lds((const unsigned*)((const char*)(gbase) + (voff)[_i]), (PG8_LAS unsigned*)(lds + (bufoff) + ldsw + _i * 8192), 16, 0, 0); } while (0)
; #define PG8_WAIT_V(n) asm volatile("s_waitcnt vmcnt(" #n ")" ::: "memory")
; #define PG8_WAIT_L(n) asm volatile("s_waitcnt lgkmcnt(" #n ")" ::: "memory")
; template <class Epi, class Sched, bool ALIGN_EPI = true, bool F8 = false>
; __device__ __forceinline__ void gemm_phase(PG8_LAS unsigned char* lds, const Sched& S, const Epi& E) {
;     ...
;         for (int t = 0; t < nt; t += 2) {
;             const bool last = (t == nt - 2);
;             if constexpr (Sched::GATHER) { if (last && has_next) S.a_off(nxt, Rs, Cs, voffAn); }
;             const char* a1 = cA + (size_t)(t + 1) * kstep;
;             const char* a2 = last ? nA : cA + (size_t)(t + 2) * kstep; const char* b2 = last ? nB : cB + (size_t)(t + 2) * kstepB;
;             const char* a3 = a2 + kstep; const char* b3 = b2 + kstepB;
;             unsigned vA2[2][2];
; #pragma unroll
;             for (int h = 0; h < 2; ++h)
; #pragma unroll
;                 for (int i = 0; i < 2; ++i) { if constexpr (Sched::GATHER) vA2[h][i] = (last && has_next) ? voffAn[h][i] : voffA[h][i]; else vA2[h][i] = voffA[h][i]; }
;             PG8_LDB(B0, 0, 0); PG8_LDB(B1, 0, 1); PG8_SCHED; PG8_LDA(At, 0, 0); PG8_STAGE(PG8_SA(1, 1), a1, voffA[1]);
;             PG8_WAIT_V(8); PG8_WAIT_L(0); PG8_BAR; PG8_MMA(0, 0, At, B0); PG8_MMA(0, 1, At, B1); PG8_BAR; PG8_SCHED;
;             PG8_LDA(At, 0, 1); PG8_STAGE(PG8_SB(0, 0), b2, voffB[0]); PG8_STAGE(PG8_SB(0, 1), b2, voffB[1]); PG8_STAGE(PG8_SA(0, 0), a2, vA2[0]);
;             PG8_WAIT_V(8); PG8_WAIT_L(0); PG8_BAR; PG8_MMA(1, 0, At, B0); PG8_MMA(1, 1, At, B1); PG8_BAR; PG8_SCHED;
;             PG8_LDB(B0, 1, 0); PG8_LDB(B1, 1, 1); PG8_SCHED; PG8_LDA(At, 1, 0); PG8_STAGE(PG8_SA(0, 1), a2, vA2[1]);
;             PG8_WAIT_V(8); PG8_WAIT_L(0); PG8_BAR; PG8_MMA(0, 0, At, B0); PG8_MMA(0, 1, At, B1); PG8_BAR; PG8_SCHED;
;             PG8_LDA(At, 1, 1); PG8_STAGE(PG8_SB(1, 0), b3, voffB[0]); PG8_STAGE(PG8_SB(1, 1), b3, voffB[1]); PG8_STAGE(PG8_SA(1, 0), a3, vA2[0]);
;             PG8_WAIT_V(8); PG8_WAIT_L(0); PG8_BAR; PG8_MMA(1, 0, At, B0); PG8_MMA(1, 1, At, B1); PG8_BAR; PG8_SCHED;
	s_setprio 2
	s_waitcnt lgkmcnt(0)
	v_mfma_scale_f32_16x16x128_f8f6f4 v[158:161], v[2:9], v[196:203], v[158:161], v194, v194 op_sel_hi:[0,0,0]
	v_mfma_scale_f32_16x16x128_f8f6f4 v[154:157], v[10:17], v[196:203], v[154:157], v194, v194 op_sel_hi:[0,0,0]
	v_mfma_scale_f32_16x16x128_f8f6f4 v[150:153], v[2:9], v[204:211], v[150:153], v194, v194 op_sel_hi:[0,0,0]
	v_mfma_scale_f32_16x16x128_f8f6f4 v[146:149], v[10:17], v[204:211], v[146:149], v194, v194 op_sel_hi:[0,0,0]
	v_mfma_scale_f32_16x16x128_f8f6f4 v[130:133], v[2:9], v[212:219], v[130:133], v194, v194 op_sel_hi:[0,0,0]
	v_mfma_scale_f32_16x16x128_f8f6f4 v[122:125], v[10:17], v[212:219], v[122:125], v194, v194 op_sel_hi:[0,0,0]
	v_mfma_scale_f32_16x16x128_f8f6f4 v[114:117], v[2:9], v[220:227], v[114:117], v194, v194 op_sel_hi:[0,0,0]
	v_mfma_scale_f32_16x16x128_f8f6f4 v[106:109], v[10:17], v[220:227], v[106:109], v194, v194 op_sel_hi:[0,0,0]
	s_nop 3
	s_setprio 0
	s_setprio 2
	v_mfma_scale_f32_16x16x128_f8f6f4 v[142:145], v[18:25], v[196:203], v[142:145], v194, v194 op_sel_hi:[0,0,0]
	v_mfma_scale_f32_16x16x128_f8f6f4 v[138:141], v[26:33], v[196:203], v[138:141], v194, v194 op_sel_hi:[0,0,0]
	v_mfma_scale_f32_16x16x128_f8f6f4 v[134:137], v[18:25], v[204:211], v[134:137], v194, v194 op_sel_hi:[0,0,0]
	v_mfma_scale_f32_16x16x128_f8f6f4 v[126:129], v[26:33], v[204:211], v[126:129], v194, v194 op_sel_hi:[0,0,0]
	v_mfma_scale_f32_16x16x128_f8f6f4 v[118:121], v[18:25], v[212:219], v[118:121], v194, v194 op_sel_hi:[0,0,0]
	v_mfma_scale_f32_16x16x128_f8f6f4 v[110:113], v[26:33], v[212:219], v[110:113], v194, v194 op_sel_hi:[0,0,0]
	v_mfma_scale_f32_16x16x128_f8f6f4 v[102:105], v[18:25], v[220:227], v[102:105], v194, v194 op_sel_hi:[0,0,0]
	v_mfma_scale_f32_16x16x128_f8f6f4 v[98:101], v[26:33], v[220:227], v[98:101], v194, v194 op_sel_hi:[0,0,0]
	s_nop 3
	s_setprio 0
	s_add_u32 s40, s40, 0x8000
	s_addc_u32 s41, s41, 0
	s_add_i32 s42, s66, s48
	s_mov_b32 m0, s42
	ds_read_b128 v[196:199], v193 offset:49152
	ds_read_b128 v[200:203], v193 offset:50176
	ds_read_b128 v[204:207], v193 offset:51200
	ds_read_b128 v[208:211], v193 offset:52224
	ds_read_b128 v[212:215], v193 offset:53248
	ds_read_b128 v[216:219], v193 offset:54272
	ds_read_b128 v[220:223], v193 offset:55296
	ds_read_b128 v[224:227], v193 offset:56320
	global_load_lds_dwordx4 v162, s[40:41]
	s_add_i32 m0, s42, 0x2000
	s_add_i32 s42, s67, s48
	global_load_lds_dwordx4 v164, s[40:41]
	s_mov_b32 m0, s42
	s_nop 0
	global_load_lds_dwordx4 v176, s[40:41]
	s_add_i32 m0, s42, 0x2000
	s_nop 0
	global_load_lds_dwordx4 v178, s[40:41]
	s_mov_b32 m0, s53
	s_nop 0
	global_load_lds_dwordx4 v166, s[30:31]
	s_mov_b32 m0, s58
	s_nop 0
	global_load_lds_dwordx4 v168, s[30:31]
	s_waitcnt vmcnt(8)
	s_waitcnt lgkmcnt(0)
	s_barrier
	s_setprio 2
	s_waitcnt lgkmcnt(0)
	v_mfma_scale_f32_16x16x128_f8f6f4 v[94:97], v[2:9], v[196:203], v[94:97], v194, v194 op_sel_hi:[0,0,0]
	v_mfma_scale_f32_16x16x128_f8f6f4 v[90:93], v[10:17], v[196:203], v[90:93], v194, v194 op_sel_hi:[0,0,0]
	v_mfma_scale_f32_16x16x128_f8f6f4 v[82:85], v[2:9], v[204:211], v[82:85], v194, v194 op_sel_hi:[0,0,0]
	v_mfma_scale_f32_16x16x128_f8f6f4 v[74:77], v[10:17], v[204:211], v[74:77], v194, v194 op_sel_hi:[0,0,0]
	v_mfma_scale_f32_16x16x128_f8f6f4 v[66:69], v[2:9], v[212:219], v[66:69], v194, v194 op_sel_hi:[0,0,0]
	v_mfma_scale_f32_16x16x128_f8f6f4 v[58:61], v[10:17], v[212:219], v[58:61], v194, v194 op_sel_hi:[0,0,0]
	v_mfma_scale_f32_16x16x128_f8f6f4 v[50:53], v[2:9], v[220:227], v[50:53], v194, v194 op_sel_hi:[0,0,0]
	v_mfma_scale_f32_16x16x128_f8f6f4 v[42:45], v[10:17], v[220:227], v[42:45], v194, v194 op_sel_hi:[0,0,0]
	s_nop 3
	s_setprio 0
	s_setprio 2
	v_mfma_scale_f32_16x16x128_f8f6f4 v[86:89], v[18:25], v[196:203], v[86:89], v194, v194 op_sel_hi:[0,0,0]
	v_mfma_scale_f32_16x16x128_f8f6f4 v[78:81], v[26:33], v[196:203], v[78:81], v194, v194 op_sel_hi:[0,0,0]
	v_mfma_scale_f32_16x16x128_f8f6f4 v[70:73], v[18:25], v[204:211], v[70:73], v194, v194 op_sel_hi:[0,0,0]
	v_mfma_scale_f32_16x16x128_f8f6f4 v[62:65], v[26:33], v[204:211], v[62:65], v194, v194 op_sel_hi:[0,0,0]
	v_mfma_scale_f32_16x16x128_f8f6f4 v[54:57], v[18:25], v[212:219], v[54:57], v194, v194 op_sel_hi:[0,0,0]
	v_mfma_scale_f32_16x16x128_f8f6f4 v[46:49], v[26:33], v[212:219], v[46:49], v194, v194 op_sel_hi:[0,0,0]
	v_mfma_scale_f32_16x16x128_f8f6f4 v[38:41], v[18:25], v[220:227], v[38:41], v194, v194 op_sel_hi:[0,0,0]
	v_mfma_scale_f32_16x16x128_f8f6f4 v[34:37], v[26:33], v[220:227], v[34:37], v194, v194 op_sel_hi:[0,0,0]
	s_nop 3
	s_setprio 0
	s_add_i32 s65, s65, 2
	s_add_u32 s19, s19, 0x10000
	s_addc_u32 s21, s21, 0
	s_add_u32 s28, s28, 0x10000
	s_addc_u32 s29, s29, 0
	s_cmp_gt_u32 s65, 13
	s_cbranch_scc0 .Lh1_911

; __device__ __forceinline__ unsigned pk4_fp8(float a, float b, float c, float d) { int w = 0; w = __builtin_amdgcn_cvt_pk_fp8_f32(clamp8(a), clamp8(b), w, false); w = __builtin_amdgcn_cvt_pk_fp8_f32(clamp8(c), clamp8(d), w, true); return (unsigned)w; }
;     __device__ __forceinline__ void operator()(AccRef acc, const GUnit& u, int wr, int wc, int fr, int fq) const {
;         const int pm = u.x0, pn = u.x1; const float* gate = modv + (size_t)(pm >> 5) * 12288 + 2 * D;
;         const int col0 = pn * 256 + wc * 64 + 16 * fq;
;         f32x4 gv[4];
; #pragma unroll
;         for (int q = 0; q < 4; ++q) gv[q] = *(const f32x4*)(gate + col0 + 4 * q) * (W8_INV * MG8_SCALE);
; #pragma unroll
;         for (int ai = 0; ai < 2; ++ai)
; #pragma unroll
;             for (int m = 0; m < 4; ++m) { u32x4 w;
; #pragma unroll
;                 for (int q = 0; q < 4; ++q) { const f32x4 v = acc[ai][q >> 1][m][q & 1] * gv[q]; w[q] = pk4_fp8(v[0], v[1], v[2], v[3]); }
;                 *(u32x4*)(MG + (size_t)(pm * 256 + ai * 128 + wr * 64 + m * 16 + fr) * D + col0) = w; }
;     }
.LBB0_914:
	s_ashr_i32 s19, s26, 5
	s_mul_hi_i32 s21, s19, 0xc000
	s_mul_i32 s19, s19, 0xc000
	s_add_u32 s28, s36, s19
	v_lshl_or_b32 v2, s64, 8, v190
	s_addc_u32 s29, s37, s21
	v_ashrrev_i32_e32 v3, 31, v2
	v_lshl_add_u64 v[4:5], v[2:3], 2, s[28:29]
	v_add_co_u32_e32 v6, vcc, s62, v4
	s_nop 15
	s_nop 7
	s_nop 15
	s_nop 7
	s_nop 15
	s_nop 7
	s_nop 15
	s_nop 7
	s_nop 1
	v_addc_co_u32_e32 v7, vcc, 0, v5, vcc
	global_load_dwordx4 v[6:9], v[6:7], off
	v_lshl_add_u64 v[4:5], v[4:5], 0, s[14:15]
	global_load_dwordx4 v[10:13], v[4:5], off offset:16
	global_load_dwordx4 v[22:25], v[4:5], off offset:32
	global_load_dwordx4 v[26:29], v[4:5], off offset:48
	v_lshl_add_u32 v4, s26, 8, v188
	v_ashrrev_i32_e32 v5, 31, v4
	v_mov_b32_e32 v30, 0
	v_lshlrev_b64 v[14:15], 11, v[4:5]
	v_lshl_add_u64 v[14:15], s[10:11], 0, v[14:15]
	v_lshl_add_u64 v[200:201], v[14:15], 0, v[2:3]
	v_mov_b32_e32 v199, 0
	v_mov_b32_e32 v196, 0
	v_mov_b32_e32 v197, 0
	v_mov_b32_e32 v198, 0
	v_mov_b32_e32 v31, 0
	v_mov_b32_e32 v32, 0
	v_mov_b32_e32 v33, 0
	s_andn2_b64 vcc, exec, s[0:1]
	s_mov_b64 s[0:1], -1
	s_waitcnt vmcnt(0) lgkmcnt(0)
	v_pk_mul_f32 v[16:17], v[10:11], s[16:17] op_sel_hi:[1,0]
	v_pk_mul_f32 v[20:21], v[6:7], s[16:17] op_sel_hi:[1,0]
	v_pk_mul_f32 v[10:11], v[24:25], s[16:17] op_sel_hi:[1,0]
	v_pk_mul_f32 v[24:25], v[158:159], v[20:21]
	v_pk_mul_f32 v[18:19], v[8:9], s[16:17] op_sel_hi:[1,0]
	v_med3_f32 v5, v24, s63, v195
	v_med3_f32 v24, v25, s63, v195
	v_cvt_pk_fp8_f32 v30, v5, v24
	v_pk_mul_f32 v[14:15], v[12:13], s[16:17] op_sel_hi:[1,0]
	v_pk_mul_f32 v[12:13], v[22:23], s[16:17] op_sel_hi:[1,0]
	v_pk_mul_f32 v[22:23], v[160:161], v[18:19]
	v_pk_mul_f32 v[8:9], v[26:27], s[16:17] op_sel_hi:[1,0]
	v_med3_f32 v22, v22, s63, v195
	v_med3_f32 v23, v23, s63, v195
	v_cvt_pk_fp8_f32 v30, v22, v23 op_sel:[0,0,1]
	v_pk_mul_f32 v[22:23], v[126:127], v[8:9]
	v_pk_mul_f32 v[6:7], v[28:29], s[16:17] op_sel_hi:[1,0]
	v_pk_mul_f32 v[28:29], v[154:155], v[16:17]
	v_pk_mul_f32 v[144:145], v[144:145], v[10:11]
	v_pk_mul_f32 v[142:143], v[142:143], v[12:13]
	v_pk_mul_f32 v[150:151], v[150:151], v[20:21]
	v_pk_mul_f32 v[146:147], v[146:147], v[16:17]
	v_pk_mul_f32 v[134:135], v[134:135], v[12:13]
	v_med3_f32 v5, v22, s63, v195
	v_med3_f32 v22, v23, s63, v195
	v_med3_f32 v25, v28, s63, v195
	v_med3_f32 v28, v29, s63, v195
	v_med3_f32 v29, v142, s63, v195
	v_med3_f32 v142, v143, s63, v195
	v_med3_f32 v143, v144, s63, v195
	v_med3_f32 v144, v145, s63, v195
	v_med3_f32 v145, v150, s63, v195
	v_med3_f32 v150, v151, s63, v195
	v_med3_f32 v146, v146, s63, v195
	v_med3_f32 v147, v147, s63, v195
	v_med3_f32 v134, v134, s63, v195
	v_med3_f32 v135, v135, s63, v195
	v_cvt_pk_fp8_f32 v199, v5, v22
	v_cvt_pk_fp8_f32 v196, v145, v150
	v_cvt_pk_fp8_f32 v197, v146, v147
	v_cvt_pk_fp8_f32 v198, v134, v135
	v_pk_mul_f32 v[22:23], v[128:129], v[6:7]
	v_pk_mul_f32 v[152:153], v[152:153], v[18:19]
	v_pk_mul_f32 v[148:149], v[148:149], v[14:15]
	v_pk_mul_f32 v[136:137], v[136:137], v[10:11]
	v_med3_f32 v5, v22, s63, v195
	v_med3_f32 v22, v23, s63, v195
	v_med3_f32 v151, v152, s63, v195
	v_med3_f32 v152, v153, s63, v195
	v_med3_f32 v148, v148, s63, v195
	v_med3_f32 v149, v149, s63, v195
	v_med3_f32 v136, v136, s63, v195
	v_med3_f32 v137, v137, s63, v195
	v_cvt_pk_fp8_f32 v199, v5, v22 op_sel:[0,0,1]
	v_or_b32_e32 v22, 16, v4
	v_cvt_pk_fp8_f32 v196, v151, v152 op_sel:[0,0,1]
	v_cvt_pk_fp8_f32 v197, v148, v149 op_sel:[0,0,1]
	v_cvt_pk_fp8_f32 v198, v136, v137 op_sel:[0,0,1]
	v_ashrrev_i32_e32 v23, 31, v22
	v_lshlrev_b64 v[22:23], 11, v[22:23]
	v_lshl_add_u64 v[22:23], s[10:11], 0, v[22:23]
	v_lshl_add_u64 v[22:23], v[22:23], 0, v[2:3]
	global_store_dwordx4 v[22:23], v[196:199], off
	v_pk_mul_f32 v[22:23], v[130:131], v[20:21]
	v_cvt_pk_fp8_f32 v31, v25, v28
	v_med3_f32 v5, v22, s63, v195
	v_med3_f32 v23, v23, s63, v195
	v_mov_b32_e32 v22, 0
	v_cvt_pk_fp8_f32 v22, v5, v23
	v_pk_mul_f32 v[24:25], v[132:133], v[18:19]
	v_pk_mul_f32 v[26:27], v[156:157], v[14:15]
	v_med3_f32 v5, v24, s63, v195
	v_med3_f32 v23, v25, s63, v195
	v_pk_mul_f32 v[24:25], v[122:123], v[16:17]
	v_cvt_pk_fp8_f32 v22, v5, v23 op_sel:[0,0,1]
	v_med3_f32 v5, v24, s63, v195
	v_med3_f32 v24, v25, s63, v195
	v_mov_b32_e32 v23, 0
	v_cvt_pk_fp8_f32 v23, v5, v24
	v_pk_mul_f32 v[24:25], v[124:125], v[14:15]
	v_med3_f32 v26, v26, s63, v195
	v_med3_f32 v5, v24, s63, v195
	v_med3_f32 v24, v25, s63, v195
	v_cvt_pk_fp8_f32 v23, v5, v24 op_sel:[0,0,1]
	v_pk_mul_f32 v[24:25], v[118:119], v[12:13]
	v_med3_f32 v27, v27, s63, v195
	v_med3_f32 v5, v24, s63, v195
	v_med3_f32 v25, v25, s63, v195
	v_mov_b32_e32 v24, 0
	v_cvt_pk_fp8_f32 v24, v5, v25
	v_cvt_pk_fp8_f32 v31, v26, v27 op_sel:[0,0,1]
	v_pk_mul_f32 v[26:27], v[120:121], v[10:11]
	v_cvt_pk_fp8_f32 v32, v29, v142
	v_med3_f32 v5, v26, s63, v195
	v_med3_f32 v25, v27, s63, v195
	v_pk_mul_f32 v[26:27], v[110:111], v[8:9]
	v_cvt_pk_fp8_f32 v24, v5, v25 op_sel:[0,0,1]
	v_med3_f32 v5, v26, s63, v195
	v_med3_f32 v26, v27, s63, v195
	v_mov_b32_e32 v25, 0
	v_cvt_pk_fp8_f32 v25, v5, v26
	v_pk_mul_f32 v[26:27], v[112:113], v[6:7]
	v_pk_mul_f32 v[28:29], v[88:89], v[10:11]
	v_med3_f32 v5, v26, s63, v195
	v_med3_f32 v26, v27, s63, v195
	v_cvt_pk_fp8_f32 v25, v5, v26 op_sel:[0,0,1]
	v_or_b32_e32 v26, 32, v4
	v_ashrrev_i32_e32 v27, 31, v26
	v_lshlrev_b64 v[26:27], 11, v[26:27]
	v_lshl_add_u64 v[26:27], s[10:11], 0, v[26:27]
	v_lshl_add_u64 v[26:27], v[26:27], 0, v[2:3]
	global_store_dwordx4 v[26:27], v[22:25], off
	v_pk_mul_f32 v[26:27], v[104:105], v[10:11]
	v_pk_mul_f32 v[138:139], v[138:139], v[8:9]
	v_pk_mul_f32 v[22:23], v[114:115], v[20:21]
	v_pk_mul_f32 v[24:25], v[116:117], v[18:19]
	v_med3_f32 v5, v22, s63, v195
; __device__ __forceinline__ unsigned pk4_fp8(float a, float b, float c, float d) { int w = 0; w = __builtin_amdgcn_cvt_pk_fp8_f32(clamp8(a), clamp8(b), w, false); w = __builtin_amdgcn_cvt_pk_fp8_f32(clamp8(c), clamp8(d), w, true); return (unsigned)w; }
;     __device__ __forceinline__ void operator()(AccRef acc, const GUnit& u, int wr, int wc, int fr, int fq) const {
;     ...
;         for (int ai = 0; ai < 2; ++ai)
; #pragma unroll
;             for (int m = 0; m < 4; ++m) { u32x4 w;
; #pragma unroll
;                 for (int q = 0; q < 4; ++q) { const f32x4 v = acc[ai][q >> 1][m][q & 1] * gv[q]; w[q] = pk4_fp8(v[0], v[1], v[2], v[3]); }
;                 *(u32x4*)(MG + (size_t)(pm * 256 + ai * 128 + wr * 64 + m * 16 + fr) * D + col0) = w; }
	v_med3_f32 v23, v23, s63, v195
	v_mov_b32_e32 v22, 0
	v_cvt_pk_fp8_f32 v22, v5, v23
	v_med3_f32 v5, v24, s63, v195
	v_med3_f32 v23, v25, s63, v195
	v_pk_mul_f32 v[24:25], v[106:107], v[16:17]
	v_cvt_pk_fp8_f32 v22, v5, v23 op_sel:[0,0,1]
	v_med3_f32 v5, v24, s63, v195
	v_med3_f32 v24, v25, s63, v195
	v_mov_b32_e32 v23, 0
	v_cvt_pk_fp8_f32 v23, v5, v24
	v_pk_mul_f32 v[24:25], v[108:109], v[14:15]
	v_med3_f32 v138, v138, s63, v195
	v_med3_f32 v5, v24, s63, v195
	v_med3_f32 v24, v25, s63, v195
	v_cvt_pk_fp8_f32 v23, v5, v24 op_sel:[0,0,1]
	v_pk_mul_f32 v[24:25], v[102:103], v[12:13]
	v_med3_f32 v139, v139, s63, v195
	v_med3_f32 v5, v24, s63, v195
	v_med3_f32 v25, v25, s63, v195
	v_mov_b32_e32 v24, 0
	v_cvt_pk_fp8_f32 v24, v5, v25
	v_med3_f32 v5, v26, s63, v195
	v_med3_f32 v25, v27, s63, v195
	v_pk_mul_f32 v[26:27], v[98:99], v[8:9]
	v_cvt_pk_fp8_f32 v24, v5, v25 op_sel:[0,0,1]
	v_med3_f32 v5, v26, s63, v195
	v_med3_f32 v26, v27, s63, v195
	v_mov_b32_e32 v25, 0
	v_cvt_pk_fp8_f32 v25, v5, v26
	v_pk_mul_f32 v[26:27], v[100:101], v[6:7]
	v_cvt_pk_fp8_f32 v33, v138, v139
	v_med3_f32 v5, v26, s63, v195
	v_med3_f32 v26, v27, s63, v195
	v_cvt_pk_fp8_f32 v25, v5, v26 op_sel:[0,0,1]
	v_or_b32_e32 v26, 48, v4
	v_ashrrev_i32_e32 v27, 31, v26
	v_lshlrev_b64 v[26:27], 11, v[26:27]
	v_lshl_add_u64 v[26:27], s[10:11], 0, v[26:27]
	v_lshl_add_u64 v[26:27], v[26:27], 0, v[2:3]
	global_store_dwordx4 v[26:27], v[22:25], off
	v_add_u32_e32 v26, 0x80, v4
	v_pk_mul_f32 v[140:141], v[140:141], v[6:7]
	v_pk_mul_f32 v[22:23], v[94:95], v[20:21]
	v_pk_mul_f32 v[24:25], v[96:97], v[18:19]
	v_med3_f32 v5, v22, s63, v195
	v_med3_f32 v23, v23, s63, v195
	v_mov_b32_e32 v22, 0
	v_cvt_pk_fp8_f32 v22, v5, v23
	v_med3_f32 v5, v24, s63, v195
	v_med3_f32 v23, v25, s63, v195
	v_pk_mul_f32 v[24:25], v[90:91], v[16:17]
	v_cvt_pk_fp8_f32 v22, v5, v23 op_sel:[0,0,1]
	v_med3_f32 v5, v24, s63, v195
	v_med3_f32 v24, v25, s63, v195
	v_mov_b32_e32 v23, 0
	v_cvt_pk_fp8_f32 v23, v5, v24
	v_pk_mul_f32 v[24:25], v[92:93], v[14:15]
	v_med3_f32 v140, v140, s63, v195
	v_med3_f32 v5, v24, s63, v195
	v_med3_f32 v24, v25, s63, v195
	v_cvt_pk_fp8_f32 v23, v5, v24 op_sel:[0,0,1]
	v_pk_mul_f32 v[24:25], v[86:87], v[12:13]
	v_med3_f32 v141, v141, s63, v195
	v_med3_f32 v5, v24, s63, v195
	v_med3_f32 v25, v25, s63, v195
	v_mov_b32_e32 v24, 0
	v_cvt_pk_fp8_f32 v24, v5, v25
	v_med3_f32 v5, v28, s63, v195
	v_med3_f32 v25, v29, s63, v195
	v_pk_mul_f32 v[28:29], v[78:79], v[8:9]
	v_cvt_pk_fp8_f32 v24, v5, v25 op_sel:[0,0,1]
	v_med3_f32 v5, v28, s63, v195
	v_med3_f32 v27, v29, s63, v195
	v_mov_b32_e32 v25, 0
	v_cvt_pk_fp8_f32 v25, v5, v27
	v_pk_mul_f32 v[28:29], v[80:81], v[6:7]
	v_cvt_pk_fp8_f32 v32, v143, v144 op_sel:[0,0,1]
	v_med3_f32 v5, v28, s63, v195
	v_med3_f32 v27, v29, s63, v195
	v_cvt_pk_fp8_f32 v25, v5, v27 op_sel:[0,0,1]
	v_ashrrev_i32_e32 v27, 31, v26
	v_lshlrev_b64 v[26:27], 11, v[26:27]
	v_lshl_add_u64 v[26:27], s[10:11], 0, v[26:27]
	v_lshl_add_u64 v[26:27], v[26:27], 0, v[2:3]
	global_store_dwordx4 v[26:27], v[22:25], off
	v_pk_mul_f32 v[26:27], v[72:73], v[10:11]
	v_cvt_pk_fp8_f32 v33, v140, v141 op_sel:[0,0,1]
	v_pk_mul_f32 v[22:23], v[82:83], v[20:21]
	v_pk_mul_f32 v[24:25], v[84:85], v[18:19]
	v_med3_f32 v5, v22, s63, v195
	v_med3_f32 v23, v23, s63, v195
	v_mov_b32_e32 v22, 0
	v_cvt_pk_fp8_f32 v22, v5, v23
	v_med3_f32 v5, v24, s63, v195
	v_med3_f32 v23, v25, s63, v195
	v_pk_mul_f32 v[24:25], v[74:75], v[16:17]
	v_cvt_pk_fp8_f32 v22, v5, v23 op_sel:[0,0,1]
	v_med3_f32 v5, v24, s63, v195
	v_med3_f32 v24, v25, s63, v195
	v_mov_b32_e32 v23, 0
	v_cvt_pk_fp8_f32 v23, v5, v24
	v_pk_mul_f32 v[24:25], v[76:77], v[14:15]
	global_store_dwordx4 v[200:201], v[30:33], off
	v_med3_f32 v5, v24, s63, v195
	v_med3_f32 v24, v25, s63, v195
	v_cvt_pk_fp8_f32 v23, v5, v24 op_sel:[0,0,1]
	v_pk_mul_f32 v[24:25], v[70:71], v[12:13]
; __device__ __forceinline__ unsigned pk4_fp8(float a, float b, float c, float d) { int w = 0; w = __builtin_amdgcn_cvt_pk_fp8_f32(clamp8(a), clamp8(b), w, false); w = __builtin_amdgcn_cvt_pk_fp8_f32(clamp8(c), clamp8(d), w, true); return (unsigned)w; }
;     __device__ __forceinline__ void operator()(AccRef acc, const GUnit& u, int wr, int wc, int fr, int fq) const {
;     ...
;         for (int ai = 0; ai < 2; ++ai)
; #pragma unroll
;             for (int m = 0; m < 4; ++m) { u32x4 w;
; #pragma unroll
;                 for (int q = 0; q < 4; ++q) { const f32x4 v = acc[ai][q >> 1][m][q & 1] * gv[q]; w[q] = pk4_fp8(v[0], v[1], v[2], v[3]); }
;                 *(u32x4*)(MG + (size_t)(pm * 256 + ai * 128 + wr * 64 + m * 16 + fr) * D + col0) = w; }
	s_nop 0
	v_med3_f32 v5, v24, s63, v195
	v_med3_f32 v25, v25, s63, v195
	v_mov_b32_e32 v24, 0
	v_cvt_pk_fp8_f32 v24, v5, v25
	v_med3_f32 v5, v26, s63, v195
	v_med3_f32 v25, v27, s63, v195
	v_pk_mul_f32 v[26:27], v[62:63], v[8:9]
	v_cvt_pk_fp8_f32 v24, v5, v25 op_sel:[0,0,1]
	v_med3_f32 v5, v26, s63, v195
	v_med3_f32 v26, v27, s63, v195
	v_mov_b32_e32 v25, 0
	v_cvt_pk_fp8_f32 v25, v5, v26
	v_pk_mul_f32 v[26:27], v[64:65], v[6:7]
	s_nop 0
	v_med3_f32 v5, v26, s63, v195
	v_med3_f32 v26, v27, s63, v195
	v_cvt_pk_fp8_f32 v25, v5, v26 op_sel:[0,0,1]
	v_add_u32_e32 v26, 0x90, v4
	v_ashrrev_i32_e32 v27, 31, v26
	v_lshlrev_b64 v[26:27], 11, v[26:27]
	v_lshl_add_u64 v[26:27], s[10:11], 0, v[26:27]
	v_lshl_add_u64 v[26:27], v[26:27], 0, v[2:3]
	global_store_dwordx4 v[26:27], v[22:25], off
	v_pk_mul_f32 v[26:27], v[56:57], v[10:11]
	v_pk_mul_f32 v[10:11], v[40:41], v[10:11]
	v_pk_mul_f32 v[22:23], v[66:67], v[20:21]
	v_pk_mul_f32 v[24:25], v[68:69], v[18:19]
	v_med3_f32 v5, v22, s63, v195
	v_med3_f32 v23, v23, s63, v195
	v_mov_b32_e32 v22, 0
	v_cvt_pk_fp8_f32 v22, v5, v23
	v_med3_f32 v5, v24, s63, v195
	v_med3_f32 v23, v25, s63, v195
	v_pk_mul_f32 v[24:25], v[58:59], v[16:17]
	v_cvt_pk_fp8_f32 v22, v5, v23 op_sel:[0,0,1]
	v_med3_f32 v5, v24, s63, v195
	v_med3_f32 v24, v25, s63, v195
	v_mov_b32_e32 v23, 0
	v_cvt_pk_fp8_f32 v23, v5, v24
	v_pk_mul_f32 v[24:25], v[60:61], v[14:15]
	v_pk_mul_f32 v[20:21], v[50:51], v[20:21]
	v_med3_f32 v5, v24, s63, v195
	v_med3_f32 v24, v25, s63, v195
	v_cvt_pk_fp8_f32 v23, v5, v24 op_sel:[0,0,1]
	v_pk_mul_f32 v[24:25], v[54:55], v[12:13]
	v_med3_f32 v21, v21, s63, v195
	v_med3_f32 v5, v24, s63, v195
	v_med3_f32 v25, v25, s63, v195
	v_mov_b32_e32 v24, 0
	v_cvt_pk_fp8_f32 v24, v5, v25
	v_med3_f32 v5, v26, s63, v195
	v_med3_f32 v25, v27, s63, v195
	v_pk_mul_f32 v[26:27], v[46:47], v[8:9]
	v_cvt_pk_fp8_f32 v24, v5, v25 op_sel:[0,0,1]
	v_med3_f32 v5, v26, s63, v195
	v_med3_f32 v26, v27, s63, v195
	v_mov_b32_e32 v25, 0
	v_cvt_pk_fp8_f32 v25, v5, v26
	v_pk_mul_f32 v[26:27], v[48:49], v[6:7]
	v_pk_mul_f32 v[18:19], v[52:53], v[18:19]
	v_med3_f32 v5, v26, s63, v195
	v_med3_f32 v26, v27, s63, v195
	v_cvt_pk_fp8_f32 v25, v5, v26 op_sel:[0,0,1]
	v_med3_f32 v5, v20, s63, v195
	v_mov_b32_e32 v20, 0
	v_cvt_pk_fp8_f32 v20, v5, v21
	v_med3_f32 v5, v18, s63, v195
	v_med3_f32 v18, v19, s63, v195
	v_pk_mul_f32 v[16:17], v[42:43], v[16:17]
	v_add_u32_e32 v26, 0xa0, v4
	v_cvt_pk_fp8_f32 v20, v5, v18 op_sel:[0,0,1]
	v_med3_f32 v5, v16, s63, v195
	v_med3_f32 v16, v17, s63, v195
	v_mov_b32_e32 v21, 0
	v_ashrrev_i32_e32 v27, 31, v26
	v_cvt_pk_fp8_f32 v21, v5, v16
	v_lshlrev_b64 v[26:27], 11, v[26:27]
	v_lshl_add_u64 v[26:27], s[10:11], 0, v[26:27]
	v_pk_mul_f32 v[14:15], v[44:45], v[14:15]
	v_lshl_add_u64 v[26:27], v[26:27], 0, v[2:3]
	v_med3_f32 v5, v14, s63, v195
	v_med3_f32 v14, v15, s63, v195
	v_pk_mul_f32 v[12:13], v[38:39], v[12:13]
	global_store_dwordx4 v[26:27], v[22:25], off
	v_cvt_pk_fp8_f32 v21, v5, v14 op_sel:[0,0,1]
	v_med3_f32 v5, v12, s63, v195
	v_med3_f32 v12, v13, s63, v195
	v_mov_b32_e32 v22, 0
	v_cvt_pk_fp8_f32 v22, v5, v12
	v_med3_f32 v5, v10, s63, v195
	v_med3_f32 v10, v11, s63, v195
	v_pk_mul_f32 v[8:9], v[34:35], v[8:9]
	v_cvt_pk_fp8_f32 v22, v5, v10 op_sel:[0,0,1]
	v_med3_f32 v5, v8, s63, v195
	v_med3_f32 v8, v9, s63, v195
	v_mov_b32_e32 v23, 0
	v_cvt_pk_fp8_f32 v23, v5, v8
	v_pk_mul_f32 v[6:7], v[36:37], v[6:7]
	v_add_u32_e32 v4, 0xb0, v4
	v_med3_f32 v5, v6, s63, v195
	v_med3_f32 v6, v7, s63, v195
	v_cvt_pk_fp8_f32 v23, v5, v6 op_sel:[0,0,1]
	v_ashrrev_i32_e32 v5, 31, v4
	v_lshlrev_b64 v[4:5], 11, v[4:5]
	v_lshl_add_u64 v[4:5], s[10:11], 0, v[4:5]
	v_lshl_add_u64 v[2:3], v[4:5], 0, v[2:3]
	global_store_dwordx4 v[2:3], v[20:23], off
	s_cbranch_vccnz .LBB0_903
	s_andn2_b64 vcc, exec, s[8:9]
	s_cbranch_vccnz .LBB0_902
	s_branch .LBB0_902

; template <class Epi, class Sched, bool ALIGN_EPI = true, bool F8 = false>
; __device__ __forceinline__ void gemm_phase(PG8_LAS unsigned char* lds, const Sched& S, const Epi& E) {
;     ...
;             if constexpr (Sched::GATHER) { if (last && has_next) S.a_off(nxt, Rs, Cs, voffAn); }
;             const char* a1 = cA + (size_t)(t + 1) * kstep;
;             const char* a2 = last ? nA : cA + (size_t)(t + 2) * kstep; const char* b2 = last ? nB : cB + (size_t)(t + 2) * kstepB;
;             const char* a3 = a2 + kstep; const char* b3 = b2 + kstepB;
;             unsigned vA2[2][2];
; #pragma unroll
;             for (int h = 0; h < 2; ++h)
; #pragma unroll
;                 for (int i = 0; i < 2; ++i) { if constexpr (Sched::GATHER) vA2[h][i] = (last && has_next) ? voffAn[h][i] : voffA[h][i]; else vA2[h][i] = voffA[h][i]; }
;     __device__ __forceinline__ void a_off(const GUnit& u, const int (&R)[2], const int (&C)[2], unsigned (&v)[2][2]) const {
;         const int* rl = rowlist + (size_t)u.x0 * ECAP; const int base = u.x1 * 256, cm = u.x3 - 1;
; #pragma unroll
;         for (int h = 0; h < 2; ++h)
; #pragma unroll
;             for (int i = 0; i < 2; ++i) { int p = base + h * 128 + R[i]; p = p < cm ? p : cm; const unsigned ent = (unsigned)rl[p]; v[h][i] = (ent >> SHIFT) * (unsigned)PA + (unsigned)C[i] * 2u; } }
.Lh1e_31412:
.Lh1_1058:
	s_cmpk_eq_i32 s30, 0x700
	s_cselect_b64 s[40:41], -1, 0
	s_and_b64 s[28:29], s[26:27], s[40:41]
	s_andn2_b64 vcc, exec, s[28:29]
	v_mov_b64_e32 v[198:199], v[174:175]
	v_mov_b64_e32 v[200:201], v[176:177]
	v_mov_b32_e32 v202, v172
	v_mov_b32_e32 v170, v216
	s_cbranch_vccnz .Lh1_1060
	flat_load_dword v2, v[186:187]
	flat_load_dword v3, v[188:189]
	flat_load_dword v4, v[190:191]
	flat_load_dword v5, v[192:193]
	v_mov_b32_e32 v199, v171
	s_waitcnt vmcnt(0) lgkmcnt(0)
	v_lshlrev_b32_e32 v2, 10, v2
	v_lshlrev_b32_e32 v3, 10, v3
	v_lshlrev_b32_e32 v4, 10, v4
	v_lshlrev_b32_e32 v5, 10, v5
	v_and_or_b32 v218, v2, s1, v208
	v_and_or_b32 v217, v3, s1, v208
	v_and_or_b32 v170, v4, s1, v208
	v_and_or_b32 v198, v5, s1, v208
	v_mov_b64_e32 v[200:201], v[170:171]
	v_mov_b32_e32 v219, v198
	v_mov_b32_e32 v220, v170
	v_mov_b32_e32 v202, v217
	v_mov_b32_e32 v170, v218

; __device__ __forceinline__ float fsigmoid(float x) { return __builtin_amdgcn_rcpf(1.0f + __builtin_amdgcn_exp2f(-1.44269504f * x)); }
; __device__ __forceinline__ unsigned pk4_fp8(float a, float b, float c, float d) { int w = 0; w = __builtin_amdgcn_cvt_pk_fp8_f32(clamp8(a), clamp8(b), w, false); w = __builtin_amdgcn_cvt_pk_fp8_f32(clamp8(c), clamp8(d), w, true); return (unsigned)w; }
;     __device__ __forceinline__ void operator()(AccRef acc, const GUnit& u, int wr, int wc, int fr, int fq) const {
;         const int e = u.x0, rt = u.x1, ct = u.x2, cnt = u.x3; const int p0 = rt * 256 + wr * 64 + fr;
;         const int odd = fq & 1;
;         unsigned char* blk = HID + ((size_t)((__builtin_amdgcn_readfirstlane(pre[e]) + rt) * (DE / 128) + ct) << 15) + (wr * 64 + fr) * 128 + wc * 32 + 16 * (fq >> 1);
; #pragma unroll
;         for (int ai = 0; ai < 2; ++ai)
; #pragma unroll
;             for (int mp = 0; mp < 4; mp += 2) {
;                 f32x4 v0, v1, w0, w1;
; #pragma unroll
;                 for (int j = 0; j < 4; ++j) { const float a0 = acc[ai][0][mp][0][j] * W8_INV, a1 = acc[ai][0][mp][1][j] * W8_INV; v0[j] = a0 * fsigmoid(a0) * (acc[ai][1][mp][0][j] * W8_INV); v1[j] = a1 * fsigmoid(a1) * (acc[ai][1][mp][1][j] * W8_INV); }
; #pragma unroll
;                 for (int j = 0; j < 4; ++j) { const float a0 = acc[ai][0][mp + 1][0][j] * W8_INV, a1 = acc[ai][0][mp + 1][1][j] * W8_INV; w0[j] = a0 * fsigmoid(a0) * (acc[ai][1][mp + 1][0][j] * W8_INV); w1[j] = a1 * fsigmoid(a1) * (acc[ai][1][mp + 1][1][j] * W8_INV); }
;                 const unsigned lo0 = pk4_fp8(v0[0], v0[1], v0[2], v0[3]), hi0 = pk4_fp8(v1[0], v1[1], v1[2], v1[3]), lo1 = pk4_fp8(w0[0], w0[1], w0[2], w0[3]), hi1 = pk4_fp8(w1[0], w1[1], w1[2], w1[3]);
;                 const auto sl = __builtin_amdgcn_permlane16_swap(lo0, lo1, false, false), sh = __builtin_amdgcn_permlane16_swap(hi0, hi1, false, false);
;                 const int p = p0 + ai * 128 + (mp + odd) * 16;
;                 if (p < cnt) *(u32x4*)(blk + (ai * 128 + (mp + odd) * 16) * 128) = (u32x4){sl[0], sh[0], sl[1], sh[1]}; }
;     }
.LBB0_1064:
	s_lshl_b32 s21, s0, 2
	s_add_i32 s21, s21, 0
	s_add_i32 s21, s21, 0x24100
	v_mov_b32_e32 v2, s21
	s_nop 15
	s_nop 7
	s_nop 15
	s_nop 7
	s_nop 15
	s_nop 7
	s_nop 15
	s_nop 7
	ds_read_b32 v2, v2
	v_mul_f32_e32 v4, 0x3c800000, v138
	v_mul_f32_e32 v5, 0xbfb8aa3b, v4
	v_exp_f32_e32 v5, v5
	v_mul_f32_e32 v9, 0x3c800000, v139
	s_waitcnt lgkmcnt(0)
	v_readfirstlane_b32 s21, v2
	v_mul_f32_e32 v2, 0x3c800000, v142
	v_mul_f32_e32 v3, 0xbfb8aa3b, v2
	v_exp_f32_e32 v3, v3
	v_add_f32_e32 v5, 1.0, v5
	v_rcp_f32_e32 v5, v5
	v_mul_f32_e32 v11, 0xbfb8aa3b, v9
	v_add_f32_e32 v3, 1.0, v3
	v_rcp_f32_e32 v3, v3
	v_exp_f32_e32 v11, v11
	v_mul_f32_e32 v12, 0x3c800000, v140
	v_mul_f32_e32 v13, 0xbfb8aa3b, v12
	v_mul_f32_e32 v2, v2, v3
	v_mul_f32_e32 v3, 0x3c800000, v110
	v_mul_f32_e32 v2, v3, v2
	v_mul_f32_e32 v3, v4, v5
	v_mul_f32_e32 v5, 0x3c800000, v143
	v_mul_f32_e32 v8, 0xbfb8aa3b, v5
	v_exp_f32_e32 v8, v8
	v_mul_f32_e32 v4, 0x3c800000, v106
	v_mul_f32_e32 v3, v4, v3
	v_add_f32_e32 v4, 1.0, v11
	v_add_f32_e32 v8, 1.0, v8
	v_rcp_f32_e32 v8, v8
	v_rcp_f32_e32 v4, v4
	v_exp_f32_e32 v13, v13
	v_mul_f32_e32 v14, 0x3c800000, v141
	v_mul_f32_e32 v5, v5, v8
	v_mul_f32_e32 v8, 0x3c800000, v111
	v_mul_f32_e32 v5, v8, v5
	v_mul_f32_e32 v4, v9, v4
	v_mul_f32_e32 v8, 0x3c800000, v107
	v_mul_f32_e32 v9, 0x3c800000, v144
	v_mul_f32_e32 v11, 0xbfb8aa3b, v9
	v_mul_f32_e32 v4, v8, v4
	v_add_f32_e32 v8, 1.0, v13
	v_exp_f32_e32 v11, v11
	v_rcp_f32_e32 v8, v8
	v_mul_f32_e32 v15, 0xbfb8aa3b, v14
	v_exp_f32_e32 v15, v15
	v_add_f32_e32 v11, 1.0, v11
	v_mul_f32_e32 v8, v12, v8
	v_mul_f32_e32 v12, 0x3c800000, v145
	v_rcp_f32_e32 v11, v11
	v_mul_f32_e32 v13, 0xbfb8aa3b, v12
	v_exp_f32_e32 v13, v13
	v_mul_f32_e32 v16, 0x3c800000, v130
	v_mul_f32_e32 v9, v9, v11
	v_mul_f32_e32 v11, 0x3c800000, v112
	v_mul_f32_e32 v9, v11, v9
	v_mul_f32_e32 v11, 0x3c800000, v108
	v_add_f32_e32 v13, 1.0, v13
	v_rcp_f32_e32 v13, v13
	v_mul_f32_e32 v8, v11, v8
	v_add_f32_e32 v11, 1.0, v15
	v_rcp_f32_e32 v11, v11
	v_mul_f32_e32 v17, 0xbfb8aa3b, v16
	v_exp_f32_e32 v17, v17
	v_mul_f32_e32 v12, v12, v13
	v_mul_f32_e32 v13, 0x3c800000, v113
	v_mul_f32_e32 v12, v13, v12
	v_mul_f32_e32 v11, v14, v11
	v_mul_f32_e32 v13, 0x3c800000, v109
	v_mul_f32_e32 v14, 0x3c800000, v134
	v_mul_f32_e32 v15, 0xbfb8aa3b, v14
	v_mul_f32_e32 v11, v13, v11
	v_add_f32_e32 v13, 1.0, v17
	v_exp_f32_e32 v15, v15
	v_rcp_f32_e32 v13, v13
	v_mul_f32_e32 v18, 0x3c800000, v131
	v_mul_f32_e32 v19, 0xbfb8aa3b, v18
	v_add_f32_e32 v15, 1.0, v15
	v_mul_f32_e32 v13, v16, v13
	v_mul_f32_e32 v16, 0x3c800000, v135
	v_rcp_f32_e32 v15, v15
	v_mul_f32_e32 v17, 0xbfb8aa3b, v16
	v_exp_f32_e32 v17, v17
	v_exp_f32_e32 v19, v19
	v_mul_f32_e32 v14, v14, v15
	v_mul_f32_e32 v15, 0x3c800000, v102
	v_mul_f32_e32 v14, v15, v14
	v_mul_f32_e32 v15, 0x3c800000, v98
	v_add_f32_e32 v17, 1.0, v17
	v_rcp_f32_e32 v17, v17
	v_mul_f32_e32 v13, v15, v13
	v_add_f32_e32 v15, 1.0, v19
	v_mul_f32_e32 v20, 0x3c800000, v132
	v_rcp_f32_e32 v15, v15
	v_mul_f32_e32 v21, 0xbfb8aa3b, v20
	v_exp_f32_e32 v21, v21
	v_mul_f32_e32 v16, v16, v17
	v_mul_f32_e32 v17, 0x3c800000, v103
	v_mul_f32_e32 v16, v17, v16
	v_mul_f32_e32 v15, v18, v15
	v_mul_f32_e32 v17, 0x3c800000, v99
	v_mul_f32_e32 v18, 0x3c800000, v136
	v_mul_f32_e32 v19, 0xbfb8aa3b, v18
	v_mul_f32_e32 v15, v17, v15
	v_add_f32_e32 v17, 1.0, v21
	v_exp_f32_e32 v19, v19
	v_rcp_f32_e32 v17, v17
	v_mul_f32_e32 v22, 0x3c800000, v133
	v_mul_f32_e32 v23, 0xbfb8aa3b, v22
	v_add_f32_e32 v19, 1.0, v19
	v_mul_f32_e32 v17, v20, v17
	v_mul_f32_e32 v20, 0x3c800000, v137
	v_rcp_f32_e32 v19, v19
	v_mul_f32_e32 v21, 0xbfb8aa3b, v20
	v_exp_f32_e32 v21, v21
	v_exp_f32_e32 v23, v23
	v_mul_f32_e32 v18, v18, v19
	v_mul_f32_e32 v19, 0x3c800000, v104
	v_mul_f32_e32 v18, v19, v18
	v_mul_f32_e32 v19, 0x3c800000, v100
	v_add_f32_e32 v21, 1.0, v21
	v_rcp_f32_e32 v21, v21
	v_mul_f32_e32 v17, v19, v17
	v_add_f32_e32 v19, 1.0, v23
	v_rcp_f32_e32 v19, v19
	v_mul_f32_e32 v20, v20, v21
	v_mul_f32_e32 v21, 0x3c800000, v105
	v_mul_f32_e32 v20, v21, v20
	v_mul_f32_e32 v19, v22, v19
	v_mul_f32_e32 v21, 0x3c800000, v101
	v_mul_f32_e32 v19, v21, v19
	v_med3_f32 v21, v2, s63, v215
	v_med3_f32 v5, v5, s63, v215
	v_mov_b32_e32 v2, v171
	v_cvt_pk_fp8_f32 v2, v21, v5
	v_med3_f32 v5, v9, s63, v215
	v_med3_f32 v9, v12, s63, v215
	v_med3_f32 v12, v3, s63, v215
	v_med3_f32 v4, v4, s63, v215
	v_mov_b32_e32 v3, v171
	v_cvt_pk_fp8_f32 v3, v12, v4
	v_cvt_pk_fp8_f32 v2, v5, v9 op_sel:[0,0,1]
	v_med3_f32 v4, v8, s63, v215
	v_med3_f32 v5, v11, s63, v215
	v_cvt_pk_fp8_f32 v3, v4, v5 op_sel:[0,0,1]
	v_med3_f32 v5, v14, s63, v215
	v_med3_f32 v8, v16, s63, v215
	v_mov_b32_e32 v4, v171
	v_cvt_pk_fp8_f32 v4, v5, v8
	v_med3_f32 v11, v13, s63, v215
	v_med3_f32 v12, v15, s63, v215
	v_mov_b32_e32 v5, v171
	v_cvt_pk_fp8_f32 v5, v11, v12
	s_add_i32 s21, s21, s50
	v_med3_f32 v8, v18, s63, v215
	v_med3_f32 v9, v20, s63, v215
	s_lshl_b32 s21, s21, 3
	v_cvt_pk_fp8_f32 v4, v8, v9 op_sel:[0,0,1]
	v_med3_f32 v8, v17, s63, v215
	v_med3_f32 v9, v19, s63, v215
	s_add_i32 s28, s21, s49
	v_cvt_pk_fp8_f32 v5, v8, v9 op_sel:[0,0,1]
	s_ashr_i32 s29, s28, 31
	s_lshl_b64 s[28:29], s[28:29], 15
	v_lshl_add_u32 v10, s50, 8, v209
	v_lshl_add_u64 v[6:7], v[178:179], 0, s[28:29]
	v_or_b32_e32 v8, v10, v173
	v_permlane16_swap_b32_e32 v2, v4
	v_permlane16_swap_b32_e32 v3, v5
	v_cmp_gt_i32_e32 vcc, s51, v8
	v_lshl_add_u64 v[8:9], v[6:7], 0, v[180:181]
	s_and_saveexec_b64 s[28:29], vcc
	s_cbranch_execz .LBB0_1066
	global_store_dwordx4 v[8:9], v[2:5], off
; __device__ __forceinline__ float fsigmoid(float x) { return __builtin_amdgcn_rcpf(1.0f + __builtin_amdgcn_exp2f(-1.44269504f * x)); }
; __device__ __forceinline__ unsigned pk4_fp8(float a, float b, float c, float d) { int w = 0; w = __builtin_amdgcn_cvt_pk_fp8_f32(clamp8(a), clamp8(b), w, false); w = __builtin_amdgcn_cvt_pk_fp8_f32(clamp8(c), clamp8(d), w, true); return (unsigned)w; }
;     __device__ __forceinline__ void operator()(AccRef acc, const GUnit& u, int wr, int wc, int fr, int fq) const {
;         const int e = u.x0, rt = u.x1, ct = u.x2, cnt = u.x3; const int p0 = rt * 256 + wr * 64 + fr;
;         const int odd = fq & 1;
;         unsigned char* blk = HID + ((size_t)((__builtin_amdgcn_readfirstlane(pre[e]) + rt) * (DE / 128) + ct) << 15) + (wr * 64 + fr) * 128 + wc * 32 + 16 * (fq >> 1);
; #pragma unroll
;         for (int ai = 0; ai < 2; ++ai)
; #pragma unroll
;             for (int mp = 0; mp < 4; mp += 2) {
;                 f32x4 v0, v1, w0, w1;
; #pragma unroll
;                 for (int j = 0; j < 4; ++j) { const float a0 = acc[ai][0][mp][0][j] * W8_INV, a1 = acc[ai][0][mp][1][j] * W8_INV; v0[j] = a0 * fsigmoid(a0) * (acc[ai][1][mp][0][j] * W8_INV); v1[j] = a1 * fsigmoid(a1) * (acc[ai][1][mp][1][j] * W8_INV); }
; #pragma unroll
;                 for (int j = 0; j < 4; ++j) { const float a0 = acc[ai][0][mp + 1][0][j] * W8_INV, a1 = acc[ai][0][mp + 1][1][j] * W8_INV; w0[j] = a0 * fsigmoid(a0) * (acc[ai][1][mp + 1][0][j] * W8_INV); w1[j] = a1 * fsigmoid(a1) * (acc[ai][1][mp + 1][1][j] * W8_INV); }
;                 const unsigned lo0 = pk4_fp8(v0[0], v0[1], v0[2], v0[3]), hi0 = pk4_fp8(v1[0], v1[1], v1[2], v1[3]), lo1 = pk4_fp8(w0[0], w0[1], w0[2], w0[3]), hi1 = pk4_fp8(w1[0], w1[1], w1[2], w1[3]);
;                 const auto sl = __builtin_amdgcn_permlane16_swap(lo0, lo1, false, false), sh = __builtin_amdgcn_permlane16_swap(hi0, hi1, false, false);
;                 const int p = p0 + ai * 128 + (mp + odd) * 16;
;                 if (p < cnt) *(u32x4*)(blk + (ai * 128 + (mp + odd) * 16) * 128) = (u32x4){sl[0], sh[0], sl[1], sh[1]}; }
;     }
.LBB0_1066:
	s_or_b64 exec, exec, s[28:29]
	s_nop 0
	v_mul_f32_e32 v2, 0x3c800000, v126
	v_mul_f32_e32 v3, 0x3c800000, v122
	v_mul_f32_e32 v4, 0xbfb8aa3b, v2
	v_mul_f32_e32 v5, 0xbfb8aa3b, v3
	v_exp_f32_e32 v4, v4
	v_exp_f32_e32 v5, v5
	v_mul_f32_e32 v11, 0x3c800000, v94
	v_mul_f32_e32 v12, 0x3c800000, v123
	v_add_f32_e32 v4, 1.0, v4
	v_add_f32_e32 v5, 1.0, v5
	v_rcp_f32_e32 v4, v4
	v_rcp_f32_e32 v5, v5
	v_mul_f32_e32 v13, 0xbfb8aa3b, v12
	v_exp_f32_e32 v13, v13
	v_mul_f32_e32 v2, v2, v4
	v_mul_f32_e32 v3, v3, v5
	v_mul_f32_e32 v5, 0x3c800000, v127
	v_mul_f32_e32 v2, v11, v2
	v_mul_f32_e32 v11, 0xbfb8aa3b, v5
	v_exp_f32_e32 v11, v11
	v_mul_f32_e32 v4, 0x3c800000, v90
	v_mul_f32_e32 v3, v4, v3
	v_add_f32_e32 v4, 1.0, v13
	v_add_f32_e32 v11, 1.0, v11
	v_rcp_f32_e32 v11, v11
	v_mul_f32_e32 v14, 0x3c800000, v124
	v_rcp_f32_e32 v4, v4
	v_mul_f32_e32 v15, 0xbfb8aa3b, v14
	v_exp_f32_e32 v15, v15
	v_mul_f32_e32 v5, v5, v11
	v_mul_f32_e32 v11, 0x3c800000, v95
	v_mul_f32_e32 v5, v11, v5
	v_mul_f32_e32 v4, v12, v4
	v_mul_f32_e32 v11, 0x3c800000, v91
	v_mul_f32_e32 v12, 0x3c800000, v128
	v_mul_f32_e32 v13, 0xbfb8aa3b, v12
	v_mul_f32_e32 v4, v11, v4
	v_add_f32_e32 v11, 1.0, v15
	v_exp_f32_e32 v13, v13
	v_rcp_f32_e32 v11, v11
	v_mul_f32_e32 v16, 0x3c800000, v125
	v_mul_f32_e32 v17, 0xbfb8aa3b, v16
	v_add_f32_e32 v13, 1.0, v13
	v_mul_f32_e32 v11, v14, v11
	v_mul_f32_e32 v14, 0x3c800000, v129
	v_rcp_f32_e32 v13, v13
	v_mul_f32_e32 v15, 0xbfb8aa3b, v14
	v_exp_f32_e32 v15, v15
	v_exp_f32_e32 v17, v17
	v_mul_f32_e32 v12, v12, v13
	v_mul_f32_e32 v13, 0x3c800000, v96
	v_mul_f32_e32 v12, v13, v12
	v_mul_f32_e32 v13, 0x3c800000, v92
	v_add_f32_e32 v15, 1.0, v15
	v_rcp_f32_e32 v15, v15
	v_mul_f32_e32 v11, v13, v11
	v_add_f32_e32 v13, 1.0, v17
	v_mul_f32_e32 v18, 0x3c800000, v114
	v_rcp_f32_e32 v13, v13
	v_mul_f32_e32 v19, 0xbfb8aa3b, v18
	v_exp_f32_e32 v19, v19
	v_mul_f32_e32 v14, v14, v15
	v_mul_f32_e32 v15, 0x3c800000, v97
	v_mul_f32_e32 v14, v15, v14
	v_mul_f32_e32 v13, v16, v13
	v_mul_f32_e32 v15, 0x3c800000, v93
	v_mul_f32_e32 v16, 0x3c800000, v118
	v_mul_f32_e32 v17, 0xbfb8aa3b, v16
	v_mul_f32_e32 v13, v15, v13
	v_add_f32_e32 v15, 1.0, v19
	v_exp_f32_e32 v17, v17
	v_rcp_f32_e32 v15, v15
	v_mul_f32_e32 v20, 0x3c800000, v115
	v_mul_f32_e32 v21, 0xbfb8aa3b, v20
	v_add_f32_e32 v17, 1.0, v17
	v_mul_f32_e32 v15, v18, v15
	v_mul_f32_e32 v18, 0x3c800000, v119
	v_rcp_f32_e32 v17, v17
	v_mul_f32_e32 v19, 0xbfb8aa3b, v18
	v_exp_f32_e32 v19, v19
	v_exp_f32_e32 v21, v21
	v_mul_f32_e32 v16, v16, v17
	v_mul_f32_e32 v17, 0x3c800000, v86
	v_mul_f32_e32 v16, v17, v16
	v_mul_f32_e32 v17, 0x3c800000, v82
	v_add_f32_e32 v19, 1.0, v19
	v_rcp_f32_e32 v19, v19
	v_mul_f32_e32 v15, v17, v15
	v_add_f32_e32 v17, 1.0, v21
	v_mul_f32_e32 v22, 0x3c800000, v116
	v_rcp_f32_e32 v17, v17
	v_mul_f32_e32 v23, 0xbfb8aa3b, v22
	v_exp_f32_e32 v23, v23
	v_mul_f32_e32 v18, v18, v19
	v_mul_f32_e32 v19, 0x3c800000, v87
	v_mul_f32_e32 v18, v19, v18
	v_mul_f32_e32 v17, v20, v17
	v_mul_f32_e32 v19, 0x3c800000, v83
	v_mul_f32_e32 v20, 0x3c800000, v120
	v_mul_f32_e32 v21, 0xbfb8aa3b, v20
	v_mul_f32_e32 v17, v19, v17
	v_add_f32_e32 v19, 1.0, v23
	v_exp_f32_e32 v21, v21
	v_rcp_f32_e32 v19, v19
	v_mul_f32_e32 v24, 0x3c800000, v117
	v_mul_f32_e32 v25, 0xbfb8aa3b, v24
	v_add_f32_e32 v21, 1.0, v21
	v_mul_f32_e32 v19, v22, v19
	v_mul_f32_e32 v22, 0x3c800000, v121
	v_rcp_f32_e32 v21, v21
	v_mul_f32_e32 v23, 0xbfb8aa3b, v22
	v_exp_f32_e32 v23, v23
	v_exp_f32_e32 v25, v25
	v_mul_f32_e32 v20, v20, v21
	v_mul_f32_e32 v21, 0x3c800000, v88
	v_mul_f32_e32 v20, v21, v20
	v_mul_f32_e32 v21, 0x3c800000, v84
	v_add_f32_e32 v23, 1.0, v23
	v_rcp_f32_e32 v23, v23
	v_mul_f32_e32 v19, v21, v19
	v_add_f32_e32 v21, 1.0, v25
	v_rcp_f32_e32 v21, v21
	v_mul_f32_e32 v22, v22, v23
	v_mul_f32_e32 v23, 0x3c800000, v89
	v_mul_f32_e32 v22, v23, v22
	v_mul_f32_e32 v21, v24, v21
	v_mul_f32_e32 v23, 0x3c800000, v85
	v_mul_f32_e32 v21, v23, v21
	v_med3_f32 v23, v2, s63, v215
	v_med3_f32 v5, v5, s63, v215
	v_mov_b32_e32 v2, v171
	v_cvt_pk_fp8_f32 v2, v23, v5
	v_med3_f32 v5, v12, s63, v215
	v_med3_f32 v12, v14, s63, v215
	v_med3_f32 v14, v3, s63, v215
	v_med3_f32 v4, v4, s63, v215
	v_mov_b32_e32 v3, v171
	v_cvt_pk_fp8_f32 v3, v14, v4
	v_cvt_pk_fp8_f32 v2, v5, v12 op_sel:[0,0,1]
	v_med3_f32 v4, v11, s63, v215
	v_med3_f32 v5, v13, s63, v215
	v_cvt_pk_fp8_f32 v3, v4, v5 op_sel:[0,0,1]
	v_med3_f32 v5, v16, s63, v215
	v_med3_f32 v11, v18, s63, v215
	v_mov_b32_e32 v4, v171
	v_cvt_pk_fp8_f32 v4, v5, v11
	v_med3_f32 v13, v15, s63, v215
	v_med3_f32 v14, v17, s63, v215
	v_mov_b32_e32 v5, v171
	v_cvt_pk_fp8_f32 v5, v13, v14
	v_med3_f32 v11, v20, s63, v215
	v_med3_f32 v12, v22, s63, v215
	v_cvt_pk_fp8_f32 v4, v11, v12 op_sel:[0,0,1]
	v_med3_f32 v11, v19, s63, v215
	v_med3_f32 v12, v21, s63, v215
	v_cvt_pk_fp8_f32 v5, v11, v12 op_sel:[0,0,1]
	v_or_b32_e32 v11, v10, v211
	v_permlane16_swap_b32_e32 v2, v4
	v_permlane16_swap_b32_e32 v3, v5
	v_cmp_gt_i32_e32 vcc, s51, v11
	s_and_saveexec_b64 s[28:29], vcc
	s_cbranch_execz .LBB0_1068
	v_lshl_add_u64 v[12:13], v[6:7], 0, v[182:183]
	global_store_dwordx4 v[12:13], v[2:5], off
; __device__ __forceinline__ float fsigmoid(float x) { return __builtin_amdgcn_rcpf(1.0f + __builtin_amdgcn_exp2f(-1.44269504f * x)); }
; __device__ __forceinline__ unsigned pk4_fp8(float a, float b, float c, float d) { int w = 0; w = __builtin_amdgcn_cvt_pk_fp8_f32(clamp8(a), clamp8(b), w, false); w = __builtin_amdgcn_cvt_pk_fp8_f32(clamp8(c), clamp8(d), w, true); return (unsigned)w; }
;     __device__ __forceinline__ void operator()(AccRef acc, const GUnit& u, int wr, int wc, int fr, int fq) const {
;     ...
; #pragma unroll
;         for (int ai = 0; ai < 2; ++ai)
; #pragma unroll
;             for (int mp = 0; mp < 4; mp += 2) {
;                 f32x4 v0, v1, w0, w1;
; #pragma unroll
;                 for (int j = 0; j < 4; ++j) { const float a0 = acc[ai][0][mp][0][j] * W8_INV, a1 = acc[ai][0][mp][1][j] * W8_INV; v0[j] = a0 * fsigmoid(a0) * (acc[ai][1][mp][0][j] * W8_INV); v1[j] = a1 * fsigmoid(a1) * (acc[ai][1][mp][1][j] * W8_INV); }
; #pragma unroll
;                 for (int j = 0; j < 4; ++j) { const float a0 = acc[ai][0][mp + 1][0][j] * W8_INV, a1 = acc[ai][0][mp + 1][1][j] * W8_INV; w0[j] = a0 * fsigmoid(a0) * (acc[ai][1][mp + 1][0][j] * W8_INV); w1[j] = a1 * fsigmoid(a1) * (acc[ai][1][mp + 1][1][j] * W8_INV); }
;                 const unsigned lo0 = pk4_fp8(v0[0], v0[1], v0[2], v0[3]), hi0 = pk4_fp8(v1[0], v1[1], v1[2], v1[3]), lo1 = pk4_fp8(w0[0], w0[1], w0[2], w0[3]), hi1 = pk4_fp8(w1[0], w1[1], w1[2], w1[3]);
;                 const auto sl = __builtin_amdgcn_permlane16_swap(lo0, lo1, false, false), sh = __builtin_amdgcn_permlane16_swap(hi0, hi1, false, false);
;                 const int p = p0 + ai * 128 + (mp + odd) * 16;
;                 if (p < cnt) *(u32x4*)(blk + (ai * 128 + (mp + odd) * 16) * 128) = (u32x4){sl[0], sh[0], sl[1], sh[1]}; }
.LBB0_1068:
	s_or_b64 exec, exec, s[28:29]
	s_nop 0
	v_mul_f32_e32 v2, 0x3c800000, v78
	v_mul_f32_e32 v3, 0xbfb8aa3b, v2
	v_mul_f32_e32 v4, 0x3c800000, v74
	v_exp_f32_e32 v3, v3
	v_mul_f32_e32 v5, 0xbfb8aa3b, v4
	v_exp_f32_e32 v5, v5
	v_mul_f32_e32 v12, 0x3c800000, v75
	v_add_f32_e32 v3, 1.0, v3
	v_rcp_f32_e32 v3, v3
	v_add_f32_e32 v5, 1.0, v5
	v_rcp_f32_e32 v5, v5
	v_mul_f32_e32 v13, 0xbfb8aa3b, v12
	v_mul_f32_e32 v2, v2, v3
	v_mul_f32_e32 v3, 0x3c800000, v46
	v_mul_f32_e32 v2, v3, v2
	v_mul_f32_e32 v3, v4, v5
	v_mul_f32_e32 v5, 0x3c800000, v79
	v_mul_f32_e32 v11, 0xbfb8aa3b, v5
	v_exp_f32_e32 v11, v11
	v_exp_f32_e32 v13, v13
	v_mul_f32_e32 v4, 0x3c800000, v42
	v_mul_f32_e32 v3, v4, v3
	v_add_f32_e32 v11, 1.0, v11
	v_rcp_f32_e32 v11, v11
	v_add_f32_e32 v4, 1.0, v13
	v_mul_f32_e32 v14, 0x3c800000, v76
	v_rcp_f32_e32 v4, v4
	v_mul_f32_e32 v15, 0xbfb8aa3b, v14
	v_exp_f32_e32 v15, v15
	v_mul_f32_e32 v5, v5, v11
	v_mul_f32_e32 v11, 0x3c800000, v47
	v_mul_f32_e32 v5, v11, v5
	v_mul_f32_e32 v4, v12, v4
	v_mul_f32_e32 v11, 0x3c800000, v43
	v_mul_f32_e32 v12, 0x3c800000, v80
	v_mul_f32_e32 v13, 0xbfb8aa3b, v12
	v_mul_f32_e32 v4, v11, v4
	v_add_f32_e32 v11, 1.0, v15
	v_exp_f32_e32 v13, v13
	v_rcp_f32_e32 v11, v11
	v_mul_f32_e32 v16, 0x3c800000, v77
	v_mul_f32_e32 v17, 0xbfb8aa3b, v16
	v_add_f32_e32 v13, 1.0, v13
	v_mul_f32_e32 v11, v14, v11
	v_mul_f32_e32 v14, 0x3c800000, v81
	v_rcp_f32_e32 v13, v13
	v_mul_f32_e32 v15, 0xbfb8aa3b, v14
	v_exp_f32_e32 v15, v15
	v_exp_f32_e32 v17, v17
	v_mul_f32_e32 v12, v12, v13
	v_mul_f32_e32 v13, 0x3c800000, v48
	v_mul_f32_e32 v12, v13, v12
	v_mul_f32_e32 v13, 0x3c800000, v44
	v_add_f32_e32 v15, 1.0, v15
	v_rcp_f32_e32 v15, v15
	v_mul_f32_e32 v11, v13, v11
	v_add_f32_e32 v13, 1.0, v17
	v_mul_f32_e32 v18, 0x3c800000, v66
	v_rcp_f32_e32 v13, v13
	v_mul_f32_e32 v19, 0xbfb8aa3b, v18
	v_exp_f32_e32 v19, v19
	v_mul_f32_e32 v14, v14, v15
	v_mul_f32_e32 v15, 0x3c800000, v49
	v_mul_f32_e32 v14, v15, v14
	v_mul_f32_e32 v13, v16, v13
	v_mul_f32_e32 v15, 0x3c800000, v45
	v_mul_f32_e32 v16, 0x3c800000, v70
	v_mul_f32_e32 v17, 0xbfb8aa3b, v16
	v_mul_f32_e32 v13, v15, v13
	v_add_f32_e32 v15, 1.0, v19
	v_exp_f32_e32 v17, v17
	v_rcp_f32_e32 v15, v15
	v_mul_f32_e32 v20, 0x3c800000, v67
	v_mul_f32_e32 v21, 0xbfb8aa3b, v20
	v_add_f32_e32 v17, 1.0, v17
	v_mul_f32_e32 v15, v18, v15
	v_mul_f32_e32 v18, 0x3c800000, v71
	v_rcp_f32_e32 v17, v17
	v_mul_f32_e32 v19, 0xbfb8aa3b, v18
	v_exp_f32_e32 v19, v19
	v_exp_f32_e32 v21, v21
	v_mul_f32_e32 v16, v16, v17
	v_mul_f32_e32 v17, 0x3c800000, v38
	v_mul_f32_e32 v16, v17, v16
	v_mul_f32_e32 v17, 0x3c800000, v34
	v_add_f32_e32 v19, 1.0, v19
	v_rcp_f32_e32 v19, v19
	v_mul_f32_e32 v15, v17, v15
	v_add_f32_e32 v17, 1.0, v21
	v_mul_f32_e32 v22, 0x3c800000, v68
	v_rcp_f32_e32 v17, v17
	v_mul_f32_e32 v23, 0xbfb8aa3b, v22
	v_exp_f32_e32 v23, v23
	v_mul_f32_e32 v18, v18, v19
	v_mul_f32_e32 v19, 0x3c800000, v39
	v_mul_f32_e32 v18, v19, v18
	v_mul_f32_e32 v17, v20, v17
	v_mul_f32_e32 v19, 0x3c800000, v35
	v_mul_f32_e32 v20, 0x3c800000, v72
	v_mul_f32_e32 v21, 0xbfb8aa3b, v20
	v_mul_f32_e32 v17, v19, v17
	v_add_f32_e32 v19, 1.0, v23
	v_exp_f32_e32 v21, v21
	v_rcp_f32_e32 v19, v19
	v_mul_f32_e32 v24, 0x3c800000, v69
	v_mul_f32_e32 v25, 0xbfb8aa3b, v24
	v_add_f32_e32 v21, 1.0, v21
	v_mul_f32_e32 v19, v22, v19
	v_mul_f32_e32 v22, 0x3c800000, v73
	v_rcp_f32_e32 v21, v21
	v_mul_f32_e32 v23, 0xbfb8aa3b, v22
	v_exp_f32_e32 v23, v23
	v_exp_f32_e32 v25, v25
	v_mul_f32_e32 v20, v20, v21
	v_mul_f32_e32 v21, 0x3c800000, v40
	v_mul_f32_e32 v20, v21, v20
	v_mul_f32_e32 v21, 0x3c800000, v36
	v_add_f32_e32 v23, 1.0, v23
	v_rcp_f32_e32 v23, v23
	v_mul_f32_e32 v19, v21, v19
	v_add_f32_e32 v21, 1.0, v25
	v_rcp_f32_e32 v21, v21
	v_mul_f32_e32 v22, v22, v23
	v_mul_f32_e32 v23, 0x3c800000, v41
	v_mul_f32_e32 v22, v23, v22
	v_mul_f32_e32 v21, v24, v21
	v_mul_f32_e32 v23, 0x3c800000, v37
	v_mul_f32_e32 v21, v23, v21
	v_med3_f32 v23, v2, s63, v215
	v_med3_f32 v5, v5, s63, v215
	v_mov_b32_e32 v2, v171
	v_cvt_pk_fp8_f32 v2, v23, v5
	v_med3_f32 v5, v12, s63, v215
	v_med3_f32 v12, v14, s63, v215
	v_med3_f32 v14, v3, s63, v215
	v_med3_f32 v4, v4, s63, v215
	v_mov_b32_e32 v3, v171
	v_cvt_pk_fp8_f32 v3, v14, v4
	v_cvt_pk_fp8_f32 v2, v5, v12 op_sel:[0,0,1]
	v_med3_f32 v4, v11, s63, v215
	v_med3_f32 v5, v13, s63, v215
	v_cvt_pk_fp8_f32 v3, v4, v5 op_sel:[0,0,1]
	v_med3_f32 v5, v16, s63, v215
	v_med3_f32 v11, v18, s63, v215
	v_mov_b32_e32 v4, v171
	v_cvt_pk_fp8_f32 v4, v5, v11
	v_med3_f32 v13, v15, s63, v215
	v_med3_f32 v14, v17, s63, v215
	v_mov_b32_e32 v5, v171
	v_cvt_pk_fp8_f32 v5, v13, v14
	v_med3_f32 v11, v20, s63, v215
	v_med3_f32 v12, v22, s63, v215
	v_cvt_pk_fp8_f32 v4, v11, v12 op_sel:[0,0,1]
	v_med3_f32 v11, v19, s63, v215
	v_med3_f32 v12, v21, s63, v215
	v_cvt_pk_fp8_f32 v5, v11, v12 op_sel:[0,0,1]
	v_add_u32_e32 v10, 0x80, v10
	v_or_b32_e32 v11, v10, v173
	v_permlane16_swap_b32_e32 v2, v4
	v_permlane16_swap_b32_e32 v3, v5
	v_cmp_gt_i32_e32 vcc, s51, v11
	s_and_saveexec_b64 s[28:29], vcc
	s_cbranch_execz .LBB0_1070
	v_add_co_u32_e32 v8, vcc, 0x4000, v8
	s_nop 1
	v_addc_co_u32_e32 v9, vcc, 0, v9, vcc
	global_store_dwordx4 v[8:9], v[2:5], off
; __device__ __forceinline__ float fsigmoid(float x) { return __builtin_amdgcn_rcpf(1.0f + __builtin_amdgcn_exp2f(-1.44269504f * x)); }
; __device__ __forceinline__ unsigned pk4_fp8(float a, float b, float c, float d) { int w = 0; w = __builtin_amdgcn_cvt_pk_fp8_f32(clamp8(a), clamp8(b), w, false); w = __builtin_amdgcn_cvt_pk_fp8_f32(clamp8(c), clamp8(d), w, true); return (unsigned)w; }
;     __device__ __forceinline__ void operator()(AccRef acc, const GUnit& u, int wr, int wc, int fr, int fq) const {
;     ...
; #pragma unroll
;         for (int ai = 0; ai < 2; ++ai)
; #pragma unroll
;             for (int mp = 0; mp < 4; mp += 2) {
;                 f32x4 v0, v1, w0, w1;
; #pragma unroll
;                 for (int j = 0; j < 4; ++j) { const float a0 = acc[ai][0][mp][0][j] * W8_INV, a1 = acc[ai][0][mp][1][j] * W8_INV; v0[j] = a0 * fsigmoid(a0) * (acc[ai][1][mp][0][j] * W8_INV); v1[j] = a1 * fsigmoid(a1) * (acc[ai][1][mp][1][j] * W8_INV); }
; #pragma unroll
;                 for (int j = 0; j < 4; ++j) { const float a0 = acc[ai][0][mp + 1][0][j] * W8_INV, a1 = acc[ai][0][mp + 1][1][j] * W8_INV; w0[j] = a0 * fsigmoid(a0) * (acc[ai][1][mp + 1][0][j] * W8_INV); w1[j] = a1 * fsigmoid(a1) * (acc[ai][1][mp + 1][1][j] * W8_INV); }
;                 const unsigned lo0 = pk4_fp8(v0[0], v0[1], v0[2], v0[3]), hi0 = pk4_fp8(v1[0], v1[1], v1[2], v1[3]), lo1 = pk4_fp8(w0[0], w0[1], w0[2], w0[3]), hi1 = pk4_fp8(w1[0], w1[1], w1[2], w1[3]);
;                 const auto sl = __builtin_amdgcn_permlane16_swap(lo0, lo1, false, false), sh = __builtin_amdgcn_permlane16_swap(hi0, hi1, false, false);
;                 const int p = p0 + ai * 128 + (mp + odd) * 16;
;                 if (p < cnt) *(u32x4*)(blk + (ai * 128 + (mp + odd) * 16) * 128) = (u32x4){sl[0], sh[0], sl[1], sh[1]}; }
.LBB0_1070:
	s_or_b64 exec, exec, s[28:29]
	s_nop 0
	v_mul_f32_e32 v2, 0x3c800000, v62
	v_mul_f32_e32 v3, 0x3c800000, v58
	v_mul_f32_e32 v4, 0xbfb8aa3b, v2
	v_mul_f32_e32 v5, 0xbfb8aa3b, v3
	v_exp_f32_e32 v4, v4
	v_exp_f32_e32 v5, v5
	v_mul_f32_e32 v8, 0x3c800000, v146
	v_mul_f32_e32 v9, 0x3c800000, v59
	v_add_f32_e32 v4, 1.0, v4
	v_add_f32_e32 v5, 1.0, v5
	v_rcp_f32_e32 v4, v4
	v_rcp_f32_e32 v5, v5
	v_mul_f32_e32 v11, 0xbfb8aa3b, v9
	v_exp_f32_e32 v11, v11
	v_mul_f32_e32 v2, v2, v4
	v_mul_f32_e32 v3, v3, v5
	v_mul_f32_e32 v5, 0x3c800000, v63
	v_mul_f32_e32 v2, v8, v2
	v_mul_f32_e32 v8, 0xbfb8aa3b, v5
	v_exp_f32_e32 v8, v8
	v_mul_f32_e32 v4, 0x3c800000, v150
	v_mul_f32_e32 v3, v4, v3
	v_add_f32_e32 v4, 1.0, v11
	v_add_f32_e32 v8, 1.0, v8
	v_rcp_f32_e32 v8, v8
	v_mul_f32_e32 v12, 0x3c800000, v60
	v_rcp_f32_e32 v4, v4
	v_mul_f32_e32 v13, 0xbfb8aa3b, v12
	v_exp_f32_e32 v13, v13
	v_mul_f32_e32 v5, v5, v8
	v_mul_f32_e32 v8, 0x3c800000, v147
	v_mul_f32_e32 v5, v8, v5
	v_mul_f32_e32 v4, v9, v4
	v_mul_f32_e32 v8, 0x3c800000, v151
	v_mul_f32_e32 v9, 0x3c800000, v64
	v_mul_f32_e32 v11, 0xbfb8aa3b, v9
	v_mul_f32_e32 v4, v8, v4
	v_add_f32_e32 v8, 1.0, v13
	v_exp_f32_e32 v11, v11
	v_rcp_f32_e32 v8, v8
	v_mul_f32_e32 v14, 0x3c800000, v61
	v_mul_f32_e32 v15, 0xbfb8aa3b, v14
	v_add_f32_e32 v11, 1.0, v11
	v_mul_f32_e32 v8, v12, v8
	v_mul_f32_e32 v12, 0x3c800000, v65
	v_rcp_f32_e32 v11, v11
	v_mul_f32_e32 v13, 0xbfb8aa3b, v12
	v_exp_f32_e32 v13, v13
	v_exp_f32_e32 v15, v15
	v_mul_f32_e32 v9, v9, v11
	v_mul_f32_e32 v11, 0x3c800000, v148
	v_mul_f32_e32 v9, v11, v9
	v_mul_f32_e32 v11, 0x3c800000, v152
	v_add_f32_e32 v13, 1.0, v13
	v_rcp_f32_e32 v13, v13
	v_mul_f32_e32 v8, v11, v8
	v_add_f32_e32 v11, 1.0, v15
	v_mul_f32_e32 v16, 0x3c800000, v50
	v_rcp_f32_e32 v11, v11
	v_mul_f32_e32 v17, 0xbfb8aa3b, v16
	v_exp_f32_e32 v17, v17
	v_mul_f32_e32 v12, v12, v13
	v_mul_f32_e32 v13, 0x3c800000, v149
	v_mul_f32_e32 v12, v13, v12
	v_mul_f32_e32 v11, v14, v11
	v_mul_f32_e32 v13, 0x3c800000, v153
	v_mul_f32_e32 v14, 0x3c800000, v54
	v_mul_f32_e32 v15, 0xbfb8aa3b, v14
	v_mul_f32_e32 v11, v13, v11
	v_add_f32_e32 v13, 1.0, v17
	v_exp_f32_e32 v15, v15
	v_rcp_f32_e32 v13, v13
	v_mul_f32_e32 v18, 0x3c800000, v51
	v_mul_f32_e32 v19, 0xbfb8aa3b, v18
	v_add_f32_e32 v15, 1.0, v15
	v_mul_f32_e32 v13, v16, v13
	v_mul_f32_e32 v16, 0x3c800000, v55
	v_rcp_f32_e32 v15, v15
	v_mul_f32_e32 v17, 0xbfb8aa3b, v16
	v_exp_f32_e32 v17, v17
	v_exp_f32_e32 v19, v19
	v_mul_f32_e32 v14, v14, v15
	v_mul_f32_e32 v15, 0x3c800000, v154
	v_mul_f32_e32 v14, v15, v14
	v_mul_f32_e32 v15, 0x3c800000, v158
	v_add_f32_e32 v17, 1.0, v17
	v_rcp_f32_e32 v17, v17
	v_mul_f32_e32 v13, v15, v13
	v_add_f32_e32 v15, 1.0, v19
	v_mul_f32_e32 v20, 0x3c800000, v52
	v_rcp_f32_e32 v15, v15
	v_mul_f32_e32 v21, 0xbfb8aa3b, v20
	v_exp_f32_e32 v21, v21
	v_mul_f32_e32 v16, v16, v17
	v_mul_f32_e32 v17, 0x3c800000, v155
	v_mul_f32_e32 v16, v17, v16
	v_mul_f32_e32 v15, v18, v15
	v_mul_f32_e32 v17, 0x3c800000, v159
	v_mul_f32_e32 v18, 0x3c800000, v56
	v_mul_f32_e32 v19, 0xbfb8aa3b, v18
	v_mul_f32_e32 v15, v17, v15
	v_add_f32_e32 v17, 1.0, v21
	v_exp_f32_e32 v19, v19
	v_rcp_f32_e32 v17, v17
	v_mul_f32_e32 v22, 0x3c800000, v53
	v_mul_f32_e32 v23, 0xbfb8aa3b, v22
	v_add_f32_e32 v19, 1.0, v19
	v_mul_f32_e32 v17, v20, v17
	v_mul_f32_e32 v20, 0x3c800000, v57
	v_rcp_f32_e32 v19, v19
	v_mul_f32_e32 v21, 0xbfb8aa3b, v20
	v_exp_f32_e32 v21, v21
	v_exp_f32_e32 v23, v23
	v_mul_f32_e32 v18, v18, v19
	v_mul_f32_e32 v19, 0x3c800000, v156
	v_mul_f32_e32 v18, v19, v18
	v_mul_f32_e32 v19, 0x3c800000, v160
	v_add_f32_e32 v21, 1.0, v21
	v_rcp_f32_e32 v21, v21
	v_mul_f32_e32 v17, v19, v17
	v_add_f32_e32 v19, 1.0, v23
	v_rcp_f32_e32 v19, v19
	v_mul_f32_e32 v20, v20, v21
	v_mul_f32_e32 v21, 0x3c800000, v157
	v_mul_f32_e32 v20, v21, v20
	v_mul_f32_e32 v19, v22, v19
	v_mul_f32_e32 v21, 0x3c800000, v161
	v_mul_f32_e32 v19, v21, v19
	v_med3_f32 v21, v2, s63, v215
	v_med3_f32 v5, v5, s63, v215
	v_mov_b32_e32 v2, v171
	v_cvt_pk_fp8_f32 v2, v21, v5
	v_med3_f32 v5, v9, s63, v215
	v_med3_f32 v9, v12, s63, v215
	v_med3_f32 v12, v3, s63, v215
	v_med3_f32 v4, v4, s63, v215
	v_mov_b32_e32 v3, v171
	v_cvt_pk_fp8_f32 v3, v12, v4
	v_cvt_pk_fp8_f32 v2, v5, v9 op_sel:[0,0,1]
	v_med3_f32 v4, v8, s63, v215
	v_med3_f32 v5, v11, s63, v215
	v_cvt_pk_fp8_f32 v3, v4, v5 op_sel:[0,0,1]
	v_med3_f32 v5, v14, s63, v215
	v_med3_f32 v8, v16, s63, v215
	v_mov_b32_e32 v4, v171
	v_cvt_pk_fp8_f32 v4, v5, v8
	v_med3_f32 v11, v13, s63, v215
	v_med3_f32 v12, v15, s63, v215
	v_mov_b32_e32 v5, v171
	v_cvt_pk_fp8_f32 v5, v11, v12
	v_med3_f32 v8, v18, s63, v215
	v_med3_f32 v9, v20, s63, v215
	v_cvt_pk_fp8_f32 v4, v8, v9 op_sel:[0,0,1]
	v_med3_f32 v8, v17, s63, v215
	v_med3_f32 v9, v19, s63, v215
	v_cvt_pk_fp8_f32 v5, v8, v9 op_sel:[0,0,1]
	v_or_b32_e32 v8, v10, v211
	v_permlane16_swap_b32_e32 v2, v4
	v_permlane16_swap_b32_e32 v3, v5
	v_cmp_gt_i32_e32 vcc, s51, v8
	s_and_saveexec_b64 s[28:29], vcc
	s_cbranch_execz .LBB0_1072
	v_lshl_add_u64 v[6:7], v[6:7], 0, v[184:185]
	global_store_dwordx4 v[6:7], v[2:5], off
	s_or_b64 exec, exec, s[28:29]
	s_andn2_b64 vcc, exec, s[26:27]
	s_cbranch_vccnz .LBB0_1052
	s_branch .LBB0_1073

; #define PG8_STAGE(bufoff, gbase, voff) do { _Pragma("unroll") for (int _i = 0; _i < 2; ++_i) \
;         __builtin_amdgcn_global_load_lds((const unsigned*)((const char*)(gbase) + (voff)[_i]), (PG8_LAS unsigned*)(lds + (bufoff) + ldsw + _i * 8192), 16, 0, 0); } while (0)
; #define PG8_WAIT_V(n) asm volatile("s_waitcnt vmcnt(" #n ")" ::: "memory")
; #define PG8_WAIT_L(n) asm volatile("s_waitcnt lgkmcnt(" #n ")" ::: "memory")
; template <class Epi, class Sched, bool ALIGN_EPI = true, bool F8 = false>
; __device__ __forceinline__ void gemm_phase(PG8_LAS unsigned char* lds, const Sched& S, const Epi& E) {
;     ...
;         for (int t = 0; t < nt; t += 2) {
;             const bool last = (t == nt - 2);
;             if constexpr (Sched::GATHER) { if (last && has_next) S.a_off(nxt, Rs, Cs, voffAn); }
;             const char* a1 = cA + (size_t)(t + 1) * kstep;
;             const char* a2 = last ? nA : cA + (size_t)(t + 2) * kstep; const char* b2 = last ? nB : cB + (size_t)(t + 2) * kstepB;
;             const char* a3 = a2 + kstep; const char* b3 = b2 + kstepB;
;             unsigned vA2[2][2];
; #pragma unroll
;             for (int h = 0; h < 2; ++h)
; #pragma unroll
;                 for (int i = 0; i < 2; ++i) { if constexpr (Sched::GATHER) vA2[h][i] = (last && has_next) ? voffAn[h][i] : voffA[h][i]; else vA2[h][i] = voffA[h][i]; }
;             PG8_LDB(B0, 0, 0); PG8_LDB(B1, 0, 1); PG8_SCHED; PG8_LDA(At, 0, 0); PG8_STAGE(PG8_SA(1, 1), a1, voffA[1]);
;             PG8_WAIT_V(8); PG8_WAIT_L(0); PG8_BAR; PG8_MMA(0, 0, At, B0); PG8_MMA(0, 1, At, B1); PG8_BAR; PG8_SCHED;
;             PG8_LDA(At, 0, 1); PG8_STAGE(PG8_SB(0, 0), b2, voffB[0]); PG8_STAGE(PG8_SB(0, 1), b2, voffB[1]); PG8_STAGE(PG8_SA(0, 0), a2, vA2[0]);
;             PG8_WAIT_V(8); PG8_WAIT_L(0); PG8_BAR; PG8_MMA(1, 0, At, B0); PG8_MMA(1, 1, At, B1); PG8_BAR; PG8_SCHED;
;             PG8_LDB(B0, 1, 0); PG8_LDB(B1, 1, 1); PG8_SCHED; PG8_LDA(At, 1, 0); PG8_STAGE(PG8_SA(0, 1), a2, vA2[1]);
;             PG8_WAIT_V(8); PG8_WAIT_L(0); PG8_BAR; PG8_MMA(0, 0, At, B0); PG8_MMA(0, 1, At, B1); PG8_BAR; PG8_SCHED;
;             PG8_LDA(At, 1, 1); PG8_STAGE(PG8_SB(1, 0), b3, voffB[0]); PG8_STAGE(PG8_SB(1, 1), b3, voffB[1]); PG8_STAGE(PG8_SA(1, 0), a3, vA2[0]);
;             PG8_WAIT_V(8); PG8_WAIT_L(0); PG8_BAR; PG8_MMA(1, 0, At, B0); PG8_MMA(1, 1, At, B1); PG8_BAR; PG8_SCHED;
.LBB0_1138:
	ds_read_b128 v[18:21], v189
	ds_read_b128 v[22:25], v189 offset:1024
	ds_read_b128 v[26:29], v189 offset:2048
	ds_read_b128 v[30:33], v189 offset:3072
	ds_read_b128 v[2:5], v190
	ds_read_b128 v[6:9], v190 offset:1024
	ds_read_b128 v[10:13], v190 offset:2048
	ds_read_b128 v[14:17], v190 offset:3072
	s_add_u32 s26, s24, 0x8000
	s_addc_u32 s27, s25, 0
	s_cmp_eq_u32 s68, 4
	s_cselect_b32 s30, s16, s26
	s_cselect_b32 s31, s17, s27
	s_cselect_b32 s28, s18, s23
	s_cselect_b32 s29, s19, s67
	s_add_u32 s26, s30, 0x8000
	s_addc_u32 s27, s31, 0
	s_add_i32 m0, s44, 0xc000
	ds_read_b128 v[194:197], v191
	ds_read_b128 v[198:201], v191 offset:1024
	ds_read_b128 v[202:205], v191 offset:2048
	ds_read_b128 v[206:209], v191 offset:3072
	ds_read_b128 v[210:213], v191 offset:4096
	ds_read_b128 v[214:217], v191 offset:5120
	ds_read_b128 v[218:221], v191 offset:6144
	ds_read_b128 v[222:225], v191 offset:7168
	global_load_lds_dwordx4 v184, s[24:25]
	s_add_i32 m0, s44, 0xe000
	s_nop 0
	global_load_lds_dwordx4 v182, s[24:25]
	s_waitcnt vmcnt(8)
	s_waitcnt lgkmcnt(0)
	s_setprio 1
	s_waitcnt lgkmcnt(0)
	v_mfma_scale_f32_16x16x128_f8f6f4 v[158:161], v[18:25], v[194:201], v[158:161], v192, v192 op_sel_hi:[0,0,0]
	v_mfma_scale_f32_16x16x128_f8f6f4 v[154:157], v[26:33], v[194:201], v[154:157], v192, v192 op_sel_hi:[0,0,0]
	v_mfma_scale_f32_16x16x128_f8f6f4 v[142:145], v[18:25], v[202:209], v[142:145], v192, v192 op_sel_hi:[0,0,0]
	v_mfma_scale_f32_16x16x128_f8f6f4 v[138:141], v[26:33], v[202:209], v[138:141], v192, v192 op_sel_hi:[0,0,0]
	v_mfma_scale_f32_16x16x128_f8f6f4 v[126:129], v[18:25], v[210:217], v[126:129], v192, v192 op_sel_hi:[0,0,0]
	v_mfma_scale_f32_16x16x128_f8f6f4 v[122:125], v[26:33], v[210:217], v[122:125], v192, v192 op_sel_hi:[0,0,0]
	v_mfma_scale_f32_16x16x128_f8f6f4 v[110:113], v[18:25], v[218:225], v[110:113], v192, v192 op_sel_hi:[0,0,0]
	v_mfma_scale_f32_16x16x128_f8f6f4 v[106:109], v[26:33], v[218:225], v[106:109], v192, v192 op_sel_hi:[0,0,0]
	s_nop 3
	s_setprio 0
	s_setprio 1
	v_mfma_scale_f32_16x16x128_f8f6f4 v[150:153], v[2:9], v[194:201], v[150:153], v192, v192 op_sel_hi:[0,0,0]
	v_mfma_scale_f32_16x16x128_f8f6f4 v[146:149], v[10:17], v[194:201], v[146:149], v192, v192 op_sel_hi:[0,0,0]
	v_mfma_scale_f32_16x16x128_f8f6f4 v[134:137], v[2:9], v[202:209], v[134:137], v192, v192 op_sel_hi:[0,0,0]
	v_mfma_scale_f32_16x16x128_f8f6f4 v[130:133], v[10:17], v[202:209], v[130:133], v192, v192 op_sel_hi:[0,0,0]
	v_mfma_scale_f32_16x16x128_f8f6f4 v[118:121], v[2:9], v[210:217], v[118:121], v192, v192 op_sel_hi:[0,0,0]
	v_mfma_scale_f32_16x16x128_f8f6f4 v[114:117], v[10:17], v[210:217], v[114:117], v192, v192 op_sel_hi:[0,0,0]
	v_mfma_scale_f32_16x16x128_f8f6f4 v[102:105], v[2:9], v[218:225], v[102:105], v192, v192 op_sel_hi:[0,0,0]
	v_mfma_scale_f32_16x16x128_f8f6f4 v[98:101], v[10:17], v[218:225], v[98:101], v192, v192 op_sel_hi:[0,0,0]
	s_nop 3
	s_setprio 0
	s_barrier
	s_add_i32 s69, s53, s43
	s_mov_b32 m0, s69
	ds_read_b128 v[194:197], v191 offset:16384
	ds_read_b128 v[198:201], v191 offset:17408
	ds_read_b128 v[202:205], v191 offset:18432
	ds_read_b128 v[206:209], v191 offset:19456
	ds_read_b128 v[210:213], v191 offset:20480
	ds_read_b128 v[214:217], v191 offset:21504
	ds_read_b128 v[218:221], v191 offset:22528
	ds_read_b128 v[222:225], v191 offset:23552
	global_load_lds_dwordx4 v164, s[28:29]
	s_add_i32 m0, s69, 0x2000
	s_add_i32 s69, s58, s43
	global_load_lds_dwordx4 v166, s[28:29]
	s_add_u32 s98, s28, s4
	s_addc_u32 s99, s29, s5
	s_mov_b32 m0, s69
	s_nop 0
	global_load_lds_dwordx4 v164, s[98:99]
	s_add_u32 s100, s28, s4
	s_addc_u32 s101, s29, s5
	s_add_i32 m0, s69, 0x2000
	s_nop 0
	global_load_lds_dwordx4 v166, s[100:101]
	s_mov_b32 m0, s44
	s_nop 0
	global_load_lds_dwordx4 v168, s[30:31]
	s_mov_b32 m0, s45
	s_nop 0
	global_load_lds_dwordx4 v170, s[30:31]
	s_waitcnt vmcnt(8)
	s_waitcnt lgkmcnt(0)
	s_setprio 1
	s_waitcnt lgkmcnt(0)
	v_mfma_scale_f32_16x16x128_f8f6f4 v[94:97], v[18:25], v[194:201], v[94:97], v192, v192 op_sel_hi:[0,0,0]
	v_mfma_scale_f32_16x16x128_f8f6f4 v[90:93], v[26:33], v[194:201], v[90:93], v192, v192 op_sel_hi:[0,0,0]
	v_mfma_scale_f32_16x16x128_f8f6f4 v[78:81], v[18:25], v[202:209], v[78:81], v192, v192 op_sel_hi:[0,0,0]
	v_mfma_scale_f32_16x16x128_f8f6f4 v[74:77], v[26:33], v[202:209], v[74:77], v192, v192 op_sel_hi:[0,0,0]
	v_mfma_scale_f32_16x16x128_f8f6f4 v[62:65], v[18:25], v[210:217], v[62:65], v192, v192 op_sel_hi:[0,0,0]
	v_mfma_scale_f32_16x16x128_f8f6f4 v[58:61], v[26:33], v[210:217], v[58:61], v192, v192 op_sel_hi:[0,0,0]
	v_mfma_scale_f32_16x16x128_f8f6f4 v[46:49], v[18:25], v[218:225], v[46:49], v192, v192 op_sel_hi:[0,0,0]
	v_mfma_scale_f32_16x16x128_f8f6f4 v[42:45], v[26:33], v[218:225], v[42:45], v192, v192 op_sel_hi:[0,0,0]
	s_nop 3
	s_setprio 0
	s_setprio 1
	v_mfma_scale_f32_16x16x128_f8f6f4 v[86:89], v[2:9], v[194:201], v[86:89], v192, v192 op_sel_hi:[0,0,0]
	v_mfma_scale_f32_16x16x128_f8f6f4 v[82:85], v[10:17], v[194:201], v[82:85], v192, v192 op_sel_hi:[0,0,0]
	v_mfma_scale_f32_16x16x128_f8f6f4 v[70:73], v[2:9], v[202:209], v[70:73], v192, v192 op_sel_hi:[0,0,0]
	v_mfma_scale_f32_16x16x128_f8f6f4 v[66:69], v[10:17], v[202:209], v[66:69], v192, v192 op_sel_hi:[0,0,0]
	v_mfma_scale_f32_16x16x128_f8f6f4 v[54:57], v[2:9], v[210:217], v[54:57], v192, v192 op_sel_hi:[0,0,0]
	v_mfma_scale_f32_16x16x128_f8f6f4 v[50:53], v[10:17], v[210:217], v[50:53], v192, v192 op_sel_hi:[0,0,0]
	v_mfma_scale_f32_16x16x128_f8f6f4 v[38:41], v[2:9], v[218:225], v[38:41], v192, v192 op_sel_hi:[0,0,0]
	v_mfma_scale_f32_16x16x128_f8f6f4 v[34:37], v[10:17], v[218:225], v[34:37], v192, v192 op_sel_hi:[0,0,0]
	s_nop 3
	s_setprio 0
	s_barrier
; #define PG8_STAGE(bufoff, gbase, voff) do { _Pragma("unroll") for (int _i = 0; _i < 2; ++_i) \
;         __builtin_amdgcn_global_load_lds((const unsigned*)((const char*)(gbase) + (voff)[_i]), (PG8_LAS unsigned*)(lds + (bufoff) + ldsw + _i * 8192), 16, 0, 0); } while (0)
; #define PG8_WAIT_V(n) asm volatile("s_waitcnt vmcnt(" #n ")" ::: "memory")
; #define PG8_WAIT_L(n) asm volatile("s_waitcnt lgkmcnt(" #n ")" ::: "memory")
; template <class Epi, class Sched, bool ALIGN_EPI = true, bool F8 = false>
; __device__ __forceinline__ void gemm_phase(PG8_LAS unsigned char* lds, const Sched& S, const Epi& E) {
;     ...
;         for (int t = 0; t < nt; t += 2) {
;             const bool last = (t == nt - 2);
;             if constexpr (Sched::GATHER) { if (last && has_next) S.a_off(nxt, Rs, Cs, voffAn); }
;             const char* a1 = cA + (size_t)(t + 1) * kstep;
;             const char* a2 = last ? nA : cA + (size_t)(t + 2) * kstep; const char* b2 = last ? nB : cB + (size_t)(t + 2) * kstepB;
;             const char* a3 = a2 + kstep; const char* b3 = b2 + kstepB;
;             unsigned vA2[2][2];
; #pragma unroll
;             for (int h = 0; h < 2; ++h)
; #pragma unroll
;                 for (int i = 0; i < 2; ++i) { if constexpr (Sched::GATHER) vA2[h][i] = (last && has_next) ? voffAn[h][i] : voffA[h][i]; else vA2[h][i] = voffA[h][i]; }
;             PG8_LDB(B0, 0, 0); PG8_LDB(B1, 0, 1); PG8_SCHED; PG8_LDA(At, 0, 0); PG8_STAGE(PG8_SA(1, 1), a1, voffA[1]);
;             PG8_WAIT_V(8); PG8_WAIT_L(0); PG8_BAR; PG8_MMA(0, 0, At, B0); PG8_MMA(0, 1, At, B1); PG8_BAR; PG8_SCHED;
;             PG8_LDA(At, 0, 1); PG8_STAGE(PG8_SB(0, 0), b2, voffB[0]); PG8_STAGE(PG8_SB(0, 1), b2, voffB[1]); PG8_STAGE(PG8_SA(0, 0), a2, vA2[0]);
;             PG8_WAIT_V(8); PG8_WAIT_L(0); PG8_BAR; PG8_MMA(1, 0, At, B0); PG8_MMA(1, 1, At, B1); PG8_BAR; PG8_SCHED;
;             PG8_LDB(B0, 1, 0); PG8_LDB(B1, 1, 1); PG8_SCHED; PG8_LDA(At, 1, 0); PG8_STAGE(PG8_SA(0, 1), a2, vA2[1]);
;             PG8_WAIT_V(8); PG8_WAIT_L(0); PG8_BAR; PG8_MMA(0, 0, At, B0); PG8_MMA(0, 1, At, B1); PG8_BAR; PG8_SCHED;
;             PG8_LDA(At, 1, 1); PG8_STAGE(PG8_SB(1, 0), b3, voffB[0]); PG8_STAGE(PG8_SB(1, 1), b3, voffB[1]); PG8_STAGE(PG8_SA(1, 0), a3, vA2[0]);
;             PG8_WAIT_V(8); PG8_WAIT_L(0); PG8_BAR; PG8_MMA(1, 0, At, B0); PG8_MMA(1, 1, At, B1); PG8_BAR; PG8_SCHED;
	s_add_i32 s69, 0, 0x18000
	s_add_i32 s70, 0, 0x1c000
	v_add_u32_e32 v14, s69, v187
	v_add_u32_e32 v30, s70, v187
	ds_read_b128 v[2:5], v14
	ds_read_b128 v[6:9], v14 offset:1024
	ds_read_b128 v[10:13], v14 offset:2048
	ds_read_b128 v[14:17], v14 offset:3072
	ds_read_b128 v[18:21], v30
	ds_read_b128 v[22:25], v30 offset:1024
	ds_read_b128 v[26:29], v30 offset:2048
	ds_read_b128 v[30:33], v30 offset:3072
	s_mov_b32 m0, s46
	ds_read_b128 v[194:197], v191 offset:32768
	ds_read_b128 v[198:201], v191 offset:33792
	ds_read_b128 v[202:205], v191 offset:34816
	ds_read_b128 v[206:209], v191 offset:35840
	ds_read_b128 v[210:213], v191 offset:36864
	ds_read_b128 v[214:217], v191 offset:37888
	ds_read_b128 v[218:221], v191 offset:38912
	ds_read_b128 v[222:225], v191 offset:39936
	global_load_lds_dwordx4 v172, s[30:31]
	s_mov_b32 m0, s47
	s_nop 0
	global_load_lds_dwordx4 v174, s[30:31]
	s_waitcnt vmcnt(8)
	s_waitcnt lgkmcnt(0)
	s_setprio 1
	s_waitcnt lgkmcnt(0)
	v_mfma_scale_f32_16x16x128_f8f6f4 v[158:161], v[2:9], v[194:201], v[158:161], v192, v192 op_sel_hi:[0,0,0]
	v_mfma_scale_f32_16x16x128_f8f6f4 v[154:157], v[10:17], v[194:201], v[154:157], v192, v192 op_sel_hi:[0,0,0]
	v_mfma_scale_f32_16x16x128_f8f6f4 v[142:145], v[2:9], v[202:209], v[142:145], v192, v192 op_sel_hi:[0,0,0]
	v_mfma_scale_f32_16x16x128_f8f6f4 v[138:141], v[10:17], v[202:209], v[138:141], v192, v192 op_sel_hi:[0,0,0]
	v_mfma_scale_f32_16x16x128_f8f6f4 v[126:129], v[2:9], v[210:217], v[126:129], v192, v192 op_sel_hi:[0,0,0]
	v_mfma_scale_f32_16x16x128_f8f6f4 v[122:125], v[10:17], v[210:217], v[122:125], v192, v192 op_sel_hi:[0,0,0]
	v_mfma_scale_f32_16x16x128_f8f6f4 v[110:113], v[2:9], v[218:225], v[110:113], v192, v192 op_sel_hi:[0,0,0]
	v_mfma_scale_f32_16x16x128_f8f6f4 v[106:109], v[10:17], v[218:225], v[106:109], v192, v192 op_sel_hi:[0,0,0]
	s_nop 3
	s_setprio 0
	s_setprio 1
	v_mfma_scale_f32_16x16x128_f8f6f4 v[150:153], v[18:25], v[194:201], v[150:153], v192, v192 op_sel_hi:[0,0,0]
	v_mfma_scale_f32_16x16x128_f8f6f4 v[146:149], v[26:33], v[194:201], v[146:149], v192, v192 op_sel_hi:[0,0,0]
	v_mfma_scale_f32_16x16x128_f8f6f4 v[134:137], v[18:25], v[202:209], v[134:137], v192, v192 op_sel_hi:[0,0,0]
	v_mfma_scale_f32_16x16x128_f8f6f4 v[130:133], v[26:33], v[202:209], v[130:133], v192, v192 op_sel_hi:[0,0,0]
	v_mfma_scale_f32_16x16x128_f8f6f4 v[118:121], v[18:25], v[210:217], v[118:121], v192, v192 op_sel_hi:[0,0,0]
	v_mfma_scale_f32_16x16x128_f8f6f4 v[114:117], v[26:33], v[210:217], v[114:117], v192, v192 op_sel_hi:[0,0,0]
	v_mfma_scale_f32_16x16x128_f8f6f4 v[102:105], v[18:25], v[218:225], v[102:105], v192, v192 op_sel_hi:[0,0,0]
	v_mfma_scale_f32_16x16x128_f8f6f4 v[98:101], v[26:33], v[218:225], v[98:101], v192, v192 op_sel_hi:[0,0,0]
	s_nop 3
	s_setprio 0
	s_barrier
	s_add_u32 s28, s28, 0x8000
	s_addc_u32 s29, s29, 0
	s_add_i32 s30, s69, s43
	s_mov_b32 m0, s30
	ds_read_b128 v[194:197], v191 offset:49152
	ds_read_b128 v[198:201], v191 offset:50176
	ds_read_b128 v[202:205], v191 offset:51200
	ds_read_b128 v[206:209], v191 offset:52224
	ds_read_b128 v[210:213], v191 offset:53248
	ds_read_b128 v[214:217], v191 offset:54272
	ds_read_b128 v[218:221], v191 offset:55296
	ds_read_b128 v[222:225], v191 offset:56320
	global_load_lds_dwordx4 v164, s[28:29]
	s_add_i32 m0, s30, 0x2000
	s_add_i32 s30, s70, s43
	global_load_lds_dwordx4 v166, s[28:29]
	s_mov_b32 m0, s30
	s_nop 0
	global_load_lds_dwordx4 v178, s[28:29]
	s_add_i32 m0, s30, 0x2000
	s_nop 0
	global_load_lds_dwordx4 v180, s[28:29]
	s_mov_b32 m0, s51
	s_nop 0
	global_load_lds_dwordx4 v168, s[26:27]
	s_mov_b32 m0, s52
	s_nop 0
	global_load_lds_dwordx4 v170, s[26:27]
	s_waitcnt vmcnt(8)
	s_waitcnt lgkmcnt(0)
	s_setprio 1
	s_waitcnt lgkmcnt(0)
	v_mfma_scale_f32_16x16x128_f8f6f4 v[94:97], v[2:9], v[194:201], v[94:97], v192, v192 op_sel_hi:[0,0,0]
	v_mfma_scale_f32_16x16x128_f8f6f4 v[90:93], v[10:17], v[194:201], v[90:93], v192, v192 op_sel_hi:[0,0,0]
	v_mfma_scale_f32_16x16x128_f8f6f4 v[78:81], v[2:9], v[202:209], v[78:81], v192, v192 op_sel_hi:[0,0,0]
	v_mfma_scale_f32_16x16x128_f8f6f4 v[74:77], v[10:17], v[202:209], v[74:77], v192, v192 op_sel_hi:[0,0,0]
	v_mfma_scale_f32_16x16x128_f8f6f4 v[62:65], v[2:9], v[210:217], v[62:65], v192, v192 op_sel_hi:[0,0,0]
	v_mfma_scale_f32_16x16x128_f8f6f4 v[58:61], v[10:17], v[210:217], v[58:61], v192, v192 op_sel_hi:[0,0,0]
	v_mfma_scale_f32_16x16x128_f8f6f4 v[46:49], v[2:9], v[218:225], v[46:49], v192, v192 op_sel_hi:[0,0,0]
	v_mfma_scale_f32_16x16x128_f8f6f4 v[42:45], v[10:17], v[218:225], v[42:45], v192, v192 op_sel_hi:[0,0,0]
	s_nop 3
	s_setprio 0
	s_setprio 1
	v_mfma_scale_f32_16x16x128_f8f6f4 v[86:89], v[18:25], v[194:201], v[86:89], v192, v192 op_sel_hi:[0,0,0]
	v_mfma_scale_f32_16x16x128_f8f6f4 v[82:85], v[26:33], v[194:201], v[82:85], v192, v192 op_sel_hi:[0,0,0]
	v_mfma_scale_f32_16x16x128_f8f6f4 v[70:73], v[18:25], v[202:209], v[70:73], v192, v192 op_sel_hi:[0,0,0]
	v_mfma_scale_f32_16x16x128_f8f6f4 v[66:69], v[26:33], v[202:209], v[66:69], v192, v192 op_sel_hi:[0,0,0]
	v_mfma_scale_f32_16x16x128_f8f6f4 v[54:57], v[18:25], v[210:217], v[54:57], v192, v192 op_sel_hi:[0,0,0]
	v_mfma_scale_f32_16x16x128_f8f6f4 v[50:53], v[26:33], v[210:217], v[50:53], v192, v192 op_sel_hi:[0,0,0]
	v_mfma_scale_f32_16x16x128_f8f6f4 v[38:41], v[18:25], v[218:225], v[38:41], v192, v192 op_sel_hi:[0,0,0]
	v_mfma_scale_f32_16x16x128_f8f6f4 v[34:37], v[26:33], v[218:225], v[34:37], v192, v192 op_sel_hi:[0,0,0]
	s_nop 3
	s_setprio 0
	s_barrier
	s_add_i32 s68, s68, 2
	s_add_u32 s23, s23, 0x10000
	s_addc_u32 s67, s67, 0
	s_add_u32 s24, s24, 0x10000
	s_addc_u32 s25, s25, 0
	s_cmp_gt_u32 s68, 5
	s_cbranch_scc0 .LBB0_1138
	s_branch .Lfx_33571
; #define PG8_STAGE(bufoff, gbase, voff) do { _Pragma("unroll") for (int _i = 0; _i < 2; ++_i) \
;         __builtin_amdgcn_global_load_lds((const unsigned*)((const char*)(gbase) + (voff)[_i]), (PG8_LAS unsigned*)(lds + (bufoff) + ldsw + _i * 8192), 16, 0, 0); } while (0)
; #define PG8_WAIT_V(n) asm volatile("s_waitcnt vmcnt(" #n ")" ::: "memory")
; #define PG8_WAIT_L(n) asm volatile("s_waitcnt lgkmcnt(" #n ")" ::: "memory")
; template <class Epi, class Sched, bool ALIGN_EPI = true, bool F8 = false>
; __device__ __forceinline__ void gemm_phase(PG8_LAS unsigned char* lds, const Sched& S, const Epi& E) {
;     ...
;         for (int t = 0; t < nt; t += 2) {
;             const bool last = (t == nt - 2);
;             if constexpr (Sched::GATHER) { if (last && has_next) S.a_off(nxt, Rs, Cs, voffAn); }
;             const char* a1 = cA + (size_t)(t + 1) * kstep;
;             const char* a2 = last ? nA : cA + (size_t)(t + 2) * kstep; const char* b2 = last ? nB : cB + (size_t)(t + 2) * kstepB;
;             const char* a3 = a2 + kstep; const char* b3 = b2 + kstepB;
;             unsigned vA2[2][2];
; #pragma unroll
;             for (int h = 0; h < 2; ++h)
; #pragma unroll
;                 for (int i = 0; i < 2; ++i) { if constexpr (Sched::GATHER) vA2[h][i] = (last && has_next) ? voffAn[h][i] : voffA[h][i]; else vA2[h][i] = voffA[h][i]; }
;             PG8_LDB(B0, 0, 0); PG8_LDB(B1, 0, 1); PG8_SCHED; PG8_LDA(At, 0, 0); PG8_STAGE(PG8_SA(1, 1), a1, voffA[1]);
;             PG8_WAIT_V(8); PG8_WAIT_L(0); PG8_BAR; PG8_MMA(0, 0, At, B0); PG8_MMA(0, 1, At, B1); PG8_BAR; PG8_SCHED;
;             PG8_LDA(At, 0, 1); PG8_STAGE(PG8_SB(0, 0), b2, voffB[0]); PG8_STAGE(PG8_SB(0, 1), b2, voffB[1]); PG8_STAGE(PG8_SA(0, 0), a2, vA2[0]);
;             PG8_WAIT_V(8); PG8_WAIT_L(0); PG8_BAR; PG8_MMA(1, 0, At, B0); PG8_MMA(1, 1, At, B1); PG8_BAR; PG8_SCHED;
;             PG8_LDB(B0, 1, 0); PG8_LDB(B1, 1, 1); PG8_SCHED; PG8_LDA(At, 1, 0); PG8_STAGE(PG8_SA(0, 1), a2, vA2[1]);
;             PG8_WAIT_V(8); PG8_WAIT_L(0); PG8_BAR; PG8_MMA(0, 0, At, B0); PG8_MMA(0, 1, At, B1); PG8_BAR; PG8_SCHED;
;             PG8_LDA(At, 1, 1); PG8_STAGE(PG8_SB(1, 0), b3, voffB[0]); PG8_STAGE(PG8_SB(1, 1), b3, voffB[1]); PG8_STAGE(PG8_SA(1, 0), a3, vA2[0]);
;             PG8_WAIT_V(8); PG8_WAIT_L(0); PG8_BAR; PG8_MMA(1, 0, At, B0); PG8_MMA(1, 1, At, B1); PG8_BAR; PG8_SCHED;
.Lh1e_33571:
.Lh1_1138:
	ds_read_b128 v[18:21], v189
	ds_read_b128 v[22:25], v189 offset:1024
	ds_read_b128 v[26:29], v189 offset:2048
	ds_read_b128 v[30:33], v189 offset:3072
	ds_read_b128 v[2:5], v190
	ds_read_b128 v[6:9], v190 offset:1024
	ds_read_b128 v[10:13], v190 offset:2048
	ds_read_b128 v[14:17], v190 offset:3072
	s_add_u32 s26, s24, 0x8000
	s_addc_u32 s27, s25, 0
	s_cmp_eq_u32 s68, 4
	s_cselect_b32 s30, s16, s26
	s_cselect_b32 s31, s17, s27
	s_cselect_b32 s28, s18, s23
	s_cselect_b32 s29, s19, s67
	s_add_u32 s26, s30, 0x8000
	s_addc_u32 s27, s31, 0
	s_add_i32 m0, s44, 0xc000
	ds_read_b128 v[194:197], v191
	ds_read_b128 v[198:201], v191 offset:1024
	ds_read_b128 v[202:205], v191 offset:2048
	ds_read_b128 v[206:209], v191 offset:3072
	ds_read_b128 v[210:213], v191 offset:4096
	ds_read_b128 v[214:217], v191 offset:5120
	ds_read_b128 v[218:221], v191 offset:6144
	ds_read_b128 v[222:225], v191 offset:7168
	global_load_lds_dwordx4 v184, s[24:25]
	s_add_i32 m0, s44, 0xe000
	s_nop 0
	global_load_lds_dwordx4 v182, s[24:25]
	s_waitcnt vmcnt(8)
	s_waitcnt lgkmcnt(0)
	s_barrier
	s_setprio 2
	s_waitcnt lgkmcnt(0)
	v_mfma_scale_f32_16x16x128_f8f6f4 v[158:161], v[18:25], v[194:201], v[158:161], v192, v192 op_sel_hi:[0,0,0]
	v_mfma_scale_f32_16x16x128_f8f6f4 v[154:157], v[26:33], v[194:201], v[154:157], v192, v192 op_sel_hi:[0,0,0]
	v_mfma_scale_f32_16x16x128_f8f6f4 v[142:145], v[18:25], v[202:209], v[142:145], v192, v192 op_sel_hi:[0,0,0]
	v_mfma_scale_f32_16x16x128_f8f6f4 v[138:141], v[26:33], v[202:209], v[138:141], v192, v192 op_sel_hi:[0,0,0]
	v_mfma_scale_f32_16x16x128_f8f6f4 v[126:129], v[18:25], v[210:217], v[126:129], v192, v192 op_sel_hi:[0,0,0]
	v_mfma_scale_f32_16x16x128_f8f6f4 v[122:125], v[26:33], v[210:217], v[122:125], v192, v192 op_sel_hi:[0,0,0]
	v_mfma_scale_f32_16x16x128_f8f6f4 v[110:113], v[18:25], v[218:225], v[110:113], v192, v192 op_sel_hi:[0,0,0]
	v_mfma_scale_f32_16x16x128_f8f6f4 v[106:109], v[26:33], v[218:225], v[106:109], v192, v192 op_sel_hi:[0,0,0]
	s_nop 3
	s_setprio 0
	s_setprio 2
	v_mfma_scale_f32_16x16x128_f8f6f4 v[150:153], v[2:9], v[194:201], v[150:153], v192, v192 op_sel_hi:[0,0,0]
	v_mfma_scale_f32_16x16x128_f8f6f4 v[146:149], v[10:17], v[194:201], v[146:149], v192, v192 op_sel_hi:[0,0,0]
	v_mfma_scale_f32_16x16x128_f8f6f4 v[134:137], v[2:9], v[202:209], v[134:137], v192, v192 op_sel_hi:[0,0,0]
	v_mfma_scale_f32_16x16x128_f8f6f4 v[130:133], v[10:17], v[202:209], v[130:133], v192, v192 op_sel_hi:[0,0,0]
	v_mfma_scale_f32_16x16x128_f8f6f4 v[118:121], v[2:9], v[210:217], v[118:121], v192, v192 op_sel_hi:[0,0,0]
	v_mfma_scale_f32_16x16x128_f8f6f4 v[114:117], v[10:17], v[210:217], v[114:117], v192, v192 op_sel_hi:[0,0,0]
	v_mfma_scale_f32_16x16x128_f8f6f4 v[102:105], v[2:9], v[218:225], v[102:105], v192, v192 op_sel_hi:[0,0,0]
	v_mfma_scale_f32_16x16x128_f8f6f4 v[98:101], v[10:17], v[218:225], v[98:101], v192, v192 op_sel_hi:[0,0,0]
	s_nop 3
	s_setprio 0
	s_add_i32 s69, s53, s43
	s_mov_b32 m0, s69
	ds_read_b128 v[194:197], v191 offset:16384
	ds_read_b128 v[198:201], v191 offset:17408
	ds_read_b128 v[202:205], v191 offset:18432
	ds_read_b128 v[206:209], v191 offset:19456
	ds_read_b128 v[210:213], v191 offset:20480
	ds_read_b128 v[214:217], v191 offset:21504
	ds_read_b128 v[218:221], v191 offset:22528
	ds_read_b128 v[222:225], v191 offset:23552
	global_load_lds_dwordx4 v164, s[28:29]
	s_add_i32 m0, s69, 0x2000
	s_add_i32 s69, s58, s43
	global_load_lds_dwordx4 v166, s[28:29]
	s_add_u32 s98, s28, s4
	s_addc_u32 s99, s29, s5
	s_mov_b32 m0, s69
	s_nop 0
	global_load_lds_dwordx4 v164, s[98:99]
	s_add_u32 s100, s28, s4
	s_addc_u32 s101, s29, s5
	s_add_i32 m0, s69, 0x2000
	s_nop 0
	global_load_lds_dwordx4 v166, s[100:101]
	s_mov_b32 m0, s44
	s_nop 0
	global_load_lds_dwordx4 v168, s[30:31]
	s_mov_b32 m0, s45
	s_nop 0
	global_load_lds_dwordx4 v170, s[30:31]
	s_waitcnt vmcnt(8)
	s_waitcnt lgkmcnt(0)
	s_barrier
	s_setprio 2
	s_waitcnt lgkmcnt(0)
	v_mfma_scale_f32_16x16x128_f8f6f4 v[94:97], v[18:25], v[194:201], v[94:97], v192, v192 op_sel_hi:[0,0,0]
	v_mfma_scale_f32_16x16x128_f8f6f4 v[90:93], v[26:33], v[194:201], v[90:93], v192, v192 op_sel_hi:[0,0,0]
	v_mfma_scale_f32_16x16x128_f8f6f4 v[78:81], v[18:25], v[202:209], v[78:81], v192, v192 op_sel_hi:[0,0,0]
	v_mfma_scale_f32_16x16x128_f8f6f4 v[74:77], v[26:33], v[202:209], v[74:77], v192, v192 op_sel_hi:[0,0,0]
	v_mfma_scale_f32_16x16x128_f8f6f4 v[62:65], v[18:25], v[210:217], v[62:65], v192, v192 op_sel_hi:[0,0,0]
	v_mfma_scale_f32_16x16x128_f8f6f4 v[58:61], v[26:33], v[210:217], v[58:61], v192, v192 op_sel_hi:[0,0,0]
	v_mfma_scale_f32_16x16x128_f8f6f4 v[46:49], v[18:25], v[218:225], v[46:49], v192, v192 op_sel_hi:[0,0,0]
	v_mfma_scale_f32_16x16x128_f8f6f4 v[42:45], v[26:33], v[218:225], v[42:45], v192, v192 op_sel_hi:[0,0,0]
	s_nop 3
	s_setprio 0
	s_setprio 2
	v_mfma_scale_f32_16x16x128_f8f6f4 v[86:89], v[2:9], v[194:201], v[86:89], v192, v192 op_sel_hi:[0,0,0]
	v_mfma_scale_f32_16x16x128_f8f6f4 v[82:85], v[10:17], v[194:201], v[82:85], v192, v192 op_sel_hi:[0,0,0]
	v_mfma_scale_f32_16x16x128_f8f6f4 v[70:73], v[2:9], v[202:209], v[70:73], v192, v192 op_sel_hi:[0,0,0]
	v_mfma_scale_f32_16x16x128_f8f6f4 v[66:69], v[10:17], v[202:209], v[66:69], v192, v192 op_sel_hi:[0,0,0]
	v_mfma_scale_f32_16x16x128_f8f6f4 v[54:57], v[2:9], v[210:217], v[54:57], v192, v192 op_sel_hi:[0,0,0]
	v_mfma_scale_f32_16x16x128_f8f6f4 v[50:53], v[10:17], v[210:217], v[50:53], v192, v192 op_sel_hi:[0,0,0]
	v_mfma_scale_f32_16x16x128_f8f6f4 v[38:41], v[2:9], v[218:225], v[38:41], v192, v192 op_sel_hi:[0,0,0]
	v_mfma_scale_f32_16x16x128_f8f6f4 v[34:37], v[10:17], v[218:225], v[34:37], v192, v192 op_sel_hi:[0,0,0]
	s_nop 3
	s_setprio 0
	s_add_i32 s69, 0, 0x18000
	s_add_i32 s70, 0, 0x1c000
	v_add_u32_e32 v14, s69, v187
	v_add_u32_e32 v30, s70, v187
	ds_read_b128 v[2:5], v14
	ds_read_b128 v[6:9], v14 offset:1024
	ds_read_b128 v[10:13], v14 offset:2048
	ds_read_b128 v[14:17], v14 offset:3072
	ds_read_b128 v[18:21], v30
	ds_read_b128 v[22:25], v30 offset:1024
	ds_read_b128 v[26:29], v30 offset:2048
	ds_read_b128 v[30:33], v30 offset:3072
	s_mov_b32 m0, s46
	ds_read_b128 v[194:197], v191 offset:32768
	ds_read_b128 v[198:201], v191 offset:33792
	ds_read_b128 v[202:205], v191 offset:34816
	ds_read_b128 v[206:209], v191 offset:35840
	ds_read_b128 v[210:213], v191 offset:36864
	ds_read_b128 v[214:217], v191 offset:37888
	ds_read_b128 v[218:221], v191 offset:38912
	ds_read_b128 v[222:225], v191 offset:39936
	global_load_lds_dwordx4 v172, s[30:31]
	s_mov_b32 m0, s47
	s_nop 0
	global_load_lds_dwordx4 v174, s[30:31]
	s_waitcnt vmcnt(8)
	s_waitcnt lgkmcnt(0)
	s_barrier
; #define PG8_STAGE(bufoff, gbase, voff) do { _Pragma("unroll") for (int _i = 0; _i < 2; ++_i) \
;         __builtin_amdgcn_global_load_lds((const unsigned*)((const char*)(gbase) + (voff)[_i]), (PG8_LAS unsigned*)(lds + (bufoff) + ldsw + _i * 8192), 16, 0, 0); } while (0)
; #define PG8_WAIT_V(n) asm volatile("s_waitcnt vmcnt(" #n ")" ::: "memory")
; #define PG8_WAIT_L(n) asm volatile("s_waitcnt lgkmcnt(" #n ")" ::: "memory")
; template <class Epi, class Sched, bool ALIGN_EPI = true, bool F8 = false>
; __device__ __forceinline__ void gemm_phase(PG8_LAS unsigned char* lds, const Sched& S, const Epi& E) {
;     ...
;         for (int t = 0; t < nt; t += 2) {
;             const bool last = (t == nt - 2);
;             if constexpr (Sched::GATHER) { if (last && has_next) S.a_off(nxt, Rs, Cs, voffAn); }
;             const char* a1 = cA + (size_t)(t + 1) * kstep;
;             const char* a2 = last ? nA : cA + (size_t)(t + 2) * kstep; const char* b2 = last ? nB : cB + (size_t)(t + 2) * kstepB;
;             const char* a3 = a2 + kstep; const char* b3 = b2 + kstepB;
;             unsigned vA2[2][2];
; #pragma unroll
;             for (int h = 0; h < 2; ++h)
; #pragma unroll
;                 for (int i = 0; i < 2; ++i) { if constexpr (Sched::GATHER) vA2[h][i] = (last && has_next) ? voffAn[h][i] : voffA[h][i]; else vA2[h][i] = voffA[h][i]; }
;             PG8_LDB(B0, 0, 0); PG8_LDB(B1, 0, 1); PG8_SCHED; PG8_LDA(At, 0, 0); PG8_STAGE(PG8_SA(1, 1), a1, voffA[1]);
;             PG8_WAIT_V(8); PG8_WAIT_L(0); PG8_BAR; PG8_MMA(0, 0, At, B0); PG8_MMA(0, 1, At, B1); PG8_BAR; PG8_SCHED;
;             PG8_LDA(At, 0, 1); PG8_STAGE(PG8_SB(0, 0), b2, voffB[0]); PG8_STAGE(PG8_SB(0, 1), b2, voffB[1]); PG8_STAGE(PG8_SA(0, 0), a2, vA2[0]);
;             PG8_WAIT_V(8); PG8_WAIT_L(0); PG8_BAR; PG8_MMA(1, 0, At, B0); PG8_MMA(1, 1, At, B1); PG8_BAR; PG8_SCHED;
;             PG8_LDB(B0, 1, 0); PG8_LDB(B1, 1, 1); PG8_SCHED; PG8_LDA(At, 1, 0); PG8_STAGE(PG8_SA(0, 1), a2, vA2[1]);
;             PG8_WAIT_V(8); PG8_WAIT_L(0); PG8_BAR; PG8_MMA(0, 0, At, B0); PG8_MMA(0, 1, At, B1); PG8_BAR; PG8_SCHED;
;             PG8_LDA(At, 1, 1); PG8_STAGE(PG8_SB(1, 0), b3, voffB[0]); PG8_STAGE(PG8_SB(1, 1), b3, voffB[1]); PG8_STAGE(PG8_SA(1, 0), a3, vA2[0]);
;             PG8_WAIT_V(8); PG8_WAIT_L(0); PG8_BAR; PG8_MMA(1, 0, At, B0); PG8_MMA(1, 1, At, B1); PG8_BAR; PG8_SCHED;
	s_setprio 2
	s_waitcnt lgkmcnt(0)
	v_mfma_scale_f32_16x16x128_f8f6f4 v[158:161], v[2:9], v[194:201], v[158:161], v192, v192 op_sel_hi:[0,0,0]
	v_mfma_scale_f32_16x16x128_f8f6f4 v[154:157], v[10:17], v[194:201], v[154:157], v192, v192 op_sel_hi:[0,0,0]
	v_mfma_scale_f32_16x16x128_f8f6f4 v[142:145], v[2:9], v[202:209], v[142:145], v192, v192 op_sel_hi:[0,0,0]
	v_mfma_scale_f32_16x16x128_f8f6f4 v[138:141], v[10:17], v[202:209], v[138:141], v192, v192 op_sel_hi:[0,0,0]
	v_mfma_scale_f32_16x16x128_f8f6f4 v[126:129], v[2:9], v[210:217], v[126:129], v192, v192 op_sel_hi:[0,0,0]
	v_mfma_scale_f32_16x16x128_f8f6f4 v[122:125], v[10:17], v[210:217], v[122:125], v192, v192 op_sel_hi:[0,0,0]
	v_mfma_scale_f32_16x16x128_f8f6f4 v[110:113], v[2:9], v[218:225], v[110:113], v192, v192 op_sel_hi:[0,0,0]
	v_mfma_scale_f32_16x16x128_f8f6f4 v[106:109], v[10:17], v[218:225], v[106:109], v192, v192 op_sel_hi:[0,0,0]
	s_nop 3
	s_setprio 0
	s_setprio 2
	v_mfma_scale_f32_16x16x128_f8f6f4 v[150:153], v[18:25], v[194:201], v[150:153], v192, v192 op_sel_hi:[0,0,0]
	v_mfma_scale_f32_16x16x128_f8f6f4 v[146:149], v[26:33], v[194:201], v[146:149], v192, v192 op_sel_hi:[0,0,0]
	v_mfma_scale_f32_16x16x128_f8f6f4 v[134:137], v[18:25], v[202:209], v[134:137], v192, v192 op_sel_hi:[0,0,0]
	v_mfma_scale_f32_16x16x128_f8f6f4 v[130:133], v[26:33], v[202:209], v[130:133], v192, v192 op_sel_hi:[0,0,0]
	v_mfma_scale_f32_16x16x128_f8f6f4 v[118:121], v[18:25], v[210:217], v[118:121], v192, v192 op_sel_hi:[0,0,0]
	v_mfma_scale_f32_16x16x128_f8f6f4 v[114:117], v[26:33], v[210:217], v[114:117], v192, v192 op_sel_hi:[0,0,0]
	v_mfma_scale_f32_16x16x128_f8f6f4 v[102:105], v[18:25], v[218:225], v[102:105], v192, v192 op_sel_hi:[0,0,0]
	v_mfma_scale_f32_16x16x128_f8f6f4 v[98:101], v[26:33], v[218:225], v[98:101], v192, v192 op_sel_hi:[0,0,0]
	s_nop 3
	s_setprio 0
	s_add_u32 s28, s28, 0x8000
	s_addc_u32 s29, s29, 0
	s_add_i32 s30, s69, s43
	s_mov_b32 m0, s30
	ds_read_b128 v[194:197], v191 offset:49152
	ds_read_b128 v[198:201], v191 offset:50176
	ds_read_b128 v[202:205], v191 offset:51200
	ds_read_b128 v[206:209], v191 offset:52224
	ds_read_b128 v[210:213], v191 offset:53248
	ds_read_b128 v[214:217], v191 offset:54272
	ds_read_b128 v[218:221], v191 offset:55296
	ds_read_b128 v[222:225], v191 offset:56320
	global_load_lds_dwordx4 v164, s[28:29]
	s_add_i32 m0, s30, 0x2000
	s_add_i32 s30, s70, s43
	global_load_lds_dwordx4 v166, s[28:29]
	s_mov_b32 m0, s30
	s_nop 0
	global_load_lds_dwordx4 v178, s[28:29]
	s_add_i32 m0, s30, 0x2000
	s_nop 0
	global_load_lds_dwordx4 v180, s[28:29]
	s_mov_b32 m0, s51
	s_nop 0
	global_load_lds_dwordx4 v168, s[26:27]
	s_mov_b32 m0, s52
	s_nop 0
	global_load_lds_dwordx4 v170, s[26:27]
	s_waitcnt vmcnt(8)
	s_waitcnt lgkmcnt(0)
	s_barrier
	s_setprio 2
	s_waitcnt lgkmcnt(0)
	v_mfma_scale_f32_16x16x128_f8f6f4 v[94:97], v[2:9], v[194:201], v[94:97], v192, v192 op_sel_hi:[0,0,0]
	v_mfma_scale_f32_16x16x128_f8f6f4 v[90:93], v[10:17], v[194:201], v[90:93], v192, v192 op_sel_hi:[0,0,0]
	v_mfma_scale_f32_16x16x128_f8f6f4 v[78:81], v[2:9], v[202:209], v[78:81], v192, v192 op_sel_hi:[0,0,0]
	v_mfma_scale_f32_16x16x128_f8f6f4 v[74:77], v[10:17], v[202:209], v[74:77], v192, v192 op_sel_hi:[0,0,0]
	v_mfma_scale_f32_16x16x128_f8f6f4 v[62:65], v[2:9], v[210:217], v[62:65], v192, v192 op_sel_hi:[0,0,0]
	v_mfma_scale_f32_16x16x128_f8f6f4 v[58:61], v[10:17], v[210:217], v[58:61], v192, v192 op_sel_hi:[0,0,0]
	v_mfma_scale_f32_16x16x128_f8f6f4 v[46:49], v[2:9], v[218:225], v[46:49], v192, v192 op_sel_hi:[0,0,0]
	v_mfma_scale_f32_16x16x128_f8f6f4 v[42:45], v[10:17], v[218:225], v[42:45], v192, v192 op_sel_hi:[0,0,0]
	s_nop 3
	s_setprio 0
	s_setprio 2
	v_mfma_scale_f32_16x16x128_f8f6f4 v[86:89], v[18:25], v[194:201], v[86:89], v192, v192 op_sel_hi:[0,0,0]
	v_mfma_scale_f32_16x16x128_f8f6f4 v[82:85], v[26:33], v[194:201], v[82:85], v192, v192 op_sel_hi:[0,0,0]
	v_mfma_scale_f32_16x16x128_f8f6f4 v[70:73], v[18:25], v[202:209], v[70:73], v192, v192 op_sel_hi:[0,0,0]
	v_mfma_scale_f32_16x16x128_f8f6f4 v[66:69], v[26:33], v[202:209], v[66:69], v192, v192 op_sel_hi:[0,0,0]
	v_mfma_scale_f32_16x16x128_f8f6f4 v[54:57], v[18:25], v[210:217], v[54:57], v192, v192 op_sel_hi:[0,0,0]
	v_mfma_scale_f32_16x16x128_f8f6f4 v[50:53], v[26:33], v[210:217], v[50:53], v192, v192 op_sel_hi:[0,0,0]
	v_mfma_scale_f32_16x16x128_f8f6f4 v[38:41], v[18:25], v[218:225], v[38:41], v192, v192 op_sel_hi:[0,0,0]
	v_mfma_scale_f32_16x16x128_f8f6f4 v[34:37], v[26:33], v[218:225], v[34:37], v192, v192 op_sel_hi:[0,0,0]
	s_nop 3
	s_setprio 0
	s_add_i32 s68, s68, 2
	s_add_u32 s23, s23, 0x10000
	s_addc_u32 s67, s67, 0
	s_add_u32 s24, s24, 0x10000
	s_addc_u32 s25, s25, 0
	s_cmp_gt_u32 s68, 5
	s_cbranch_scc0 .Lh1_1138

; __device__ __forceinline__ unsigned pk4_fp8(float a, float b, float c, float d) { int w = 0; w = __builtin_amdgcn_cvt_pk_fp8_f32(clamp8(a), clamp8(b), w, false); w = __builtin_amdgcn_cvt_pk_fp8_f32(clamp8(c), clamp8(d), w, true); return (unsigned)w; }
; template <class Epi, class Sched, bool ALIGN_EPI = true, bool F8 = false>
; __device__ __forceinline__ void gemm_phase(PG8_LAS unsigned char* lds, const Sched& S, const Epi& E) {
;     ...
;         if constexpr (F8) {
; #pragma unroll
;             for (int a = 0; a < 2; ++a)
; #pragma unroll
;                 for (int b = 0; b < 2; ++b)
;                     asm volatile("s_nop 15\n\ts_nop 7" : "+v"(acc[a][b][0][0]), "+v"(acc[a][b][0][1]), "+v"(acc[a][b][1][0]), "+v"(acc[a][b][1][1]), "+v"(acc[a][b][2][0]), "+v"(acc[a][b][2][1]), "+v"(acc[a][b][3][0]), "+v"(acc[a][b][3][1]));
;     __device__ __forceinline__ void operator()(AccRef acc, const GUnit& u, int wr, int wc, int fr, int fq) const {
;         const int e = u.x0, rt = u.x1, ct = u.x2, cnt = u.x3; const int* rl = rowlist + (size_t)e * ECAP; const int p0 = rt * 256 + wr * 64 + fr;
;         unsigned ent[2][4];
; #pragma unroll
;         for (int ai = 0; ai < 2; ++ai)
; #pragma unroll
;             for (int m = 0; m < 4; ++m) { int p = p0 + ai * 128 + m * 16; p = p < cnt ? p : cnt - 1; ent[ai][m] = (unsigned)rl[p]; }
; #pragma unroll
;         for (int ai = 0; ai < 2; ++ai)
; #pragma unroll
;             for (int m = 0; m < 4; ++m) { const int p = p0 + ai * 128 + m * 16;
;                 if (p < cnt) { u32x4 w;
; #pragma unroll
;                     for (int q = 0; q < 4; ++q) { const f32x4 v = acc[ai][q >> 1][m][q & 1] * (W8_INV * Y8_SCALE); w[q] = pk4_fp8(v[0], v[1], v[2], v[3]); }
;                     *(u32x4*)(Y + (size_t)ent[ai][m] * D + ct * 256 + wc * 64 + 16 * fq) = w; } }
.LBB0_1141:
	s_ashr_i32 s23, s22, 31
	s_lshl_b64 s[22:23], s[22:23], 17
	s_add_u32 s26, s49, s22
	v_lshl_add_u32 v16, s66, 8, v186
	s_addc_u32 s27, s50, s23
	s_add_i32 s22, s48, -1
	v_or_b32_e32 v15, 16, v16
	v_min_i32_e32 v2, s22, v15
	v_ashrrev_i32_e32 v3, 31, v2
	v_or_b32_e32 v13, 32, v16
	v_lshl_add_u64 v[18:19], v[2:3], 2, s[26:27]
	v_min_i32_e32 v2, s22, v13
	v_ashrrev_i32_e32 v3, 31, v2
	v_or_b32_e32 v11, 48, v16
	v_lshl_add_u64 v[20:21], v[2:3], 2, s[26:27]
	v_min_i32_e32 v2, s22, v11
	v_ashrrev_i32_e32 v3, 31, v2
	v_add_u32_e32 v9, 0x80, v16
	v_lshl_add_u64 v[22:23], v[2:3], 2, s[26:27]
	v_min_i32_e32 v2, s22, v9
	v_ashrrev_i32_e32 v3, 31, v2
	v_add_u32_e32 v7, 0x90, v16
	v_lshl_add_u64 v[24:25], v[2:3], 2, s[26:27]
	v_min_i32_e32 v2, s22, v7
	v_ashrrev_i32_e32 v3, 31, v2
	v_add_u32_e32 v5, 0xa0, v16
	v_lshl_add_u64 v[26:27], v[2:3], 2, s[26:27]
	v_min_i32_e32 v2, s22, v5
	v_ashrrev_i32_e32 v3, 31, v2
	v_lshl_add_u64 v[28:29], v[2:3], 2, s[26:27]
	v_add_u32_e32 v3, 0xb0, v16
	v_min_i32_e32 v30, s22, v3
	v_ashrrev_i32_e32 v31, 31, v30
	s_nop 15
	s_nop 7
	s_nop 15
	s_nop 7
	s_nop 15
	s_nop 7
	s_nop 15
	s_nop 7
	v_lshl_add_u64 v[30:31], v[30:31], 2, s[26:27]
	global_load_dword v14, v[18:19], off
	global_load_dword v12, v[20:21], off
	global_load_dword v10, v[22:23], off
	global_load_dword v8, v[24:25], off
	global_load_dword v6, v[26:27], off
	global_load_dword v4, v[28:29], off
	global_load_dword v2, v[30:31], off
	s_lshl_b32 s22, s65, 8
	s_ashr_i32 s23, s22, 31
	v_cmp_gt_i32_e32 vcc, s48, v16
	s_and_saveexec_b64 s[24:25], vcc
	s_cbranch_execz .LBB0_1150
	v_ashrrev_i32_e32 v17, 31, v16
	v_lshl_add_u64 v[16:17], v[16:17], 2, s[26:27]
	global_load_dword v176, v[16:17], off
	v_pk_mul_f32 v[16:17], v[158:159], s[14:15] op_sel_hi:[1,0]
	s_nop 0
	v_med3_f32 v18, v16, s59, v193
	v_med3_f32 v17, v17, s59, v193
	v_mov_b32_e32 v16, v177
	v_cvt_pk_fp8_f32 v16, v18, v17
	v_pk_mul_f32 v[18:19], v[160:161], s[14:15] op_sel_hi:[1,0]
	s_nop 0
	v_med3_f32 v17, v18, s59, v193
	v_med3_f32 v18, v19, s59, v193
	v_cvt_pk_fp8_f32 v16, v17, v18 op_sel:[0,0,1]
	v_pk_mul_f32 v[18:19], v[154:155], s[14:15] op_sel_hi:[1,0]
	v_mov_b32_e32 v17, v177
	v_med3_f32 v18, v18, s59, v193
	v_med3_f32 v19, v19, s59, v193
	v_cvt_pk_fp8_f32 v17, v18, v19
	v_pk_mul_f32 v[18:19], v[156:157], s[14:15] op_sel_hi:[1,0]
	s_nop 0
	v_med3_f32 v18, v18, s59, v193
	v_med3_f32 v19, v19, s59, v193
	v_cvt_pk_fp8_f32 v17, v18, v19 op_sel:[0,0,1]
	v_pk_mul_f32 v[18:19], v[150:151], s[14:15] op_sel_hi:[1,0]
	s_nop 0
	v_med3_f32 v20, v18, s59, v193
	v_med3_f32 v19, v19, s59, v193
	v_mov_b32_e32 v18, v177
	v_cvt_pk_fp8_f32 v18, v20, v19
	v_pk_mul_f32 v[20:21], v[152:153], s[14:15] op_sel_hi:[1,0]
	s_nop 0
	v_med3_f32 v19, v20, s59, v193
	v_med3_f32 v20, v21, s59, v193
	v_cvt_pk_fp8_f32 v18, v19, v20 op_sel:[0,0,1]
	v_pk_mul_f32 v[20:21], v[146:147], s[14:15] op_sel_hi:[1,0]
	v_mov_b32_e32 v19, v177
	v_med3_f32 v20, v20, s59, v193
	v_med3_f32 v21, v21, s59, v193
	v_cvt_pk_fp8_f32 v19, v20, v21
	v_pk_mul_f32 v[20:21], v[148:149], s[14:15] op_sel_hi:[1,0]
	s_nop 0
	v_med3_f32 v20, v20, s59, v193
	v_med3_f32 v21, v21, s59, v193
	v_cvt_pk_fp8_f32 v19, v20, v21 op_sel:[0,0,1]
	s_waitcnt vmcnt(0) lgkmcnt(0)
	v_lshlrev_b64 v[20:21], 11, v[176:177]
	v_lshl_add_u64 v[20:21], s[10:11], 0, v[20:21]
	v_lshl_add_u64 v[20:21], v[20:21], 0, s[22:23]
	v_lshl_add_u64 v[20:21], v[20:21], 0, s[6:7]
	v_lshl_add_u64 v[20:21], v[20:21], 0, v[162:163]
	global_store_dwordx4 v[20:21], v[16:19], off
	s_or_b64 exec, exec, s[24:25]
	v_cmp_gt_i32_e32 vcc, s48, v15
	s_and_saveexec_b64 s[24:25], vcc
	s_cbranch_execnz .LBB0_1151

; __device__ __forceinline__ unsigned pk4_fp8(float a, float b, float c, float d) { int w = 0; w = __builtin_amdgcn_cvt_pk_fp8_f32(clamp8(a), clamp8(b), w, false); w = __builtin_amdgcn_cvt_pk_fp8_f32(clamp8(c), clamp8(d), w, true); return (unsigned)w; }
;     __device__ __forceinline__ void operator()(AccRef acc, const GUnit& u, int wr, int wc, int fr, int fq) const {
;     ...
;         for (int ai = 0; ai < 2; ++ai)
; #pragma unroll
;             for (int m = 0; m < 4; ++m) { const int p = p0 + ai * 128 + m * 16;
;                 if (p < cnt) { u32x4 w;
; #pragma unroll
;                     for (int q = 0; q < 4; ++q) { const f32x4 v = acc[ai][q >> 1][m][q & 1] * (W8_INV * Y8_SCALE); w[q] = pk4_fp8(v[0], v[1], v[2], v[3]); }
;                     *(u32x4*)(Y + (size_t)ent[ai][m] * D + ct * 256 + wc * 64 + 16 * fq) = w; } }
.LBB0_1144:
	s_waitcnt vmcnt(0) lgkmcnt(0)
	v_pk_mul_f32 v[14:15], v[126:127], s[14:15] op_sel_hi:[1,0]
	v_pk_mul_f32 v[16:17], v[128:129], s[14:15] op_sel_hi:[1,0]
	v_med3_f32 v13, v14, s59, v193
	v_med3_f32 v15, v15, s59, v193
	v_mov_b32_e32 v14, v177
	v_cvt_pk_fp8_f32 v14, v13, v15
	v_med3_f32 v13, v16, s59, v193
	v_med3_f32 v15, v17, s59, v193
	v_pk_mul_f32 v[16:17], v[122:123], s[14:15] op_sel_hi:[1,0]
	v_cvt_pk_fp8_f32 v14, v13, v15 op_sel:[0,0,1]
	v_med3_f32 v13, v16, s59, v193
	v_med3_f32 v16, v17, s59, v193
	v_mov_b32_e32 v15, v177
	v_cvt_pk_fp8_f32 v15, v13, v16
	v_pk_mul_f32 v[16:17], v[124:125], s[14:15] op_sel_hi:[1,0]
	v_pk_mul_f32 v[18:19], v[120:121], s[14:15] op_sel_hi:[1,0]
	v_med3_f32 v13, v16, s59, v193
	v_med3_f32 v16, v17, s59, v193
	v_cvt_pk_fp8_f32 v15, v13, v16 op_sel:[0,0,1]
	v_pk_mul_f32 v[16:17], v[118:119], s[14:15] op_sel_hi:[1,0]
	s_nop 0
	v_med3_f32 v13, v16, s59, v193
	v_med3_f32 v17, v17, s59, v193
	v_mov_b32_e32 v16, v177
	v_cvt_pk_fp8_f32 v16, v13, v17
	v_med3_f32 v13, v18, s59, v193
	v_med3_f32 v17, v19, s59, v193
	v_pk_mul_f32 v[18:19], v[114:115], s[14:15] op_sel_hi:[1,0]
	v_cvt_pk_fp8_f32 v16, v13, v17 op_sel:[0,0,1]
	v_med3_f32 v13, v18, s59, v193
	v_med3_f32 v18, v19, s59, v193
	v_mov_b32_e32 v17, v177
	v_cvt_pk_fp8_f32 v17, v13, v18
	v_pk_mul_f32 v[18:19], v[116:117], s[14:15] op_sel_hi:[1,0]
	s_nop 0
	v_med3_f32 v13, v18, s59, v193
	v_med3_f32 v18, v19, s59, v193
	v_cvt_pk_fp8_f32 v17, v13, v18 op_sel:[0,0,1]
	v_mov_b32_e32 v13, v177
	v_lshlrev_b64 v[12:13], 11, v[12:13]
	v_lshl_add_u64 v[12:13], s[10:11], 0, v[12:13]
	v_lshl_add_u64 v[12:13], v[12:13], 0, s[22:23]
	v_lshl_add_u64 v[12:13], v[12:13], 0, s[6:7]
	v_lshl_add_u64 v[12:13], v[12:13], 0, v[162:163]
	global_store_dwordx4 v[12:13], v[14:17], off
	s_or_b64 exec, exec, s[24:25]
	v_cmp_gt_i32_e32 vcc, s48, v11
	s_and_saveexec_b64 s[24:25], vcc
	s_cbranch_execnz .LBB0_1153

; __device__ __forceinline__ unsigned pk4_fp8(float a, float b, float c, float d) { int w = 0; w = __builtin_amdgcn_cvt_pk_fp8_f32(clamp8(a), clamp8(b), w, false); w = __builtin_amdgcn_cvt_pk_fp8_f32(clamp8(c), clamp8(d), w, true); return (unsigned)w; }
;     __device__ __forceinline__ void operator()(AccRef acc, const GUnit& u, int wr, int wc, int fr, int fq) const {
;     ...
;         for (int ai = 0; ai < 2; ++ai)
; #pragma unroll
;             for (int m = 0; m < 4; ++m) { const int p = p0 + ai * 128 + m * 16;
;                 if (p < cnt) { u32x4 w;
; #pragma unroll
;                     for (int q = 0; q < 4; ++q) { const f32x4 v = acc[ai][q >> 1][m][q & 1] * (W8_INV * Y8_SCALE); w[q] = pk4_fp8(v[0], v[1], v[2], v[3]); }
;                     *(u32x4*)(Y + (size_t)ent[ai][m] * D + ct * 256 + wc * 64 + 16 * fq) = w; } }
.LBB0_1146:
	s_waitcnt vmcnt(0) lgkmcnt(0)
	v_pk_mul_f32 v[10:11], v[94:95], s[14:15] op_sel_hi:[1,0]
	v_pk_mul_f32 v[12:13], v[96:97], s[14:15] op_sel_hi:[1,0]
	v_med3_f32 v9, v10, s59, v193
	v_med3_f32 v11, v11, s59, v193
	v_mov_b32_e32 v10, v177
	v_cvt_pk_fp8_f32 v10, v9, v11
	v_med3_f32 v9, v12, s59, v193
	v_med3_f32 v11, v13, s59, v193
	v_pk_mul_f32 v[12:13], v[90:91], s[14:15] op_sel_hi:[1,0]
	v_cvt_pk_fp8_f32 v10, v9, v11 op_sel:[0,0,1]
	v_med3_f32 v9, v12, s59, v193
	v_med3_f32 v12, v13, s59, v193
	v_mov_b32_e32 v11, v177
	v_cvt_pk_fp8_f32 v11, v9, v12
	v_pk_mul_f32 v[12:13], v[92:93], s[14:15] op_sel_hi:[1,0]
	v_pk_mul_f32 v[14:15], v[88:89], s[14:15] op_sel_hi:[1,0]
	v_med3_f32 v9, v12, s59, v193
	v_med3_f32 v12, v13, s59, v193
	v_cvt_pk_fp8_f32 v11, v9, v12 op_sel:[0,0,1]
	v_pk_mul_f32 v[12:13], v[86:87], s[14:15] op_sel_hi:[1,0]
	s_nop 0
	v_med3_f32 v9, v12, s59, v193
	v_med3_f32 v13, v13, s59, v193
	v_mov_b32_e32 v12, v177
	v_cvt_pk_fp8_f32 v12, v9, v13
	v_med3_f32 v9, v14, s59, v193
	v_med3_f32 v13, v15, s59, v193
	v_pk_mul_f32 v[14:15], v[82:83], s[14:15] op_sel_hi:[1,0]
	v_cvt_pk_fp8_f32 v12, v9, v13 op_sel:[0,0,1]
	v_med3_f32 v9, v14, s59, v193
	v_med3_f32 v14, v15, s59, v193
	v_mov_b32_e32 v13, v177
	v_cvt_pk_fp8_f32 v13, v9, v14
	v_pk_mul_f32 v[14:15], v[84:85], s[14:15] op_sel_hi:[1,0]
	s_nop 0
	v_med3_f32 v9, v14, s59, v193
	v_med3_f32 v14, v15, s59, v193
	v_cvt_pk_fp8_f32 v13, v9, v14 op_sel:[0,0,1]
	v_mov_b32_e32 v9, v177
	v_lshlrev_b64 v[8:9], 11, v[8:9]
	v_lshl_add_u64 v[8:9], s[10:11], 0, v[8:9]
	v_lshl_add_u64 v[8:9], v[8:9], 0, s[22:23]
	v_lshl_add_u64 v[8:9], v[8:9], 0, s[6:7]
	v_lshl_add_u64 v[8:9], v[8:9], 0, v[162:163]
	global_store_dwordx4 v[8:9], v[10:13], off
	s_or_b64 exec, exec, s[24:25]
	v_cmp_gt_i32_e32 vcc, s48, v7
	s_and_saveexec_b64 s[24:25], vcc
	s_cbranch_execnz .LBB0_1155

; __device__ __forceinline__ unsigned pk4_fp8(float a, float b, float c, float d) { int w = 0; w = __builtin_amdgcn_cvt_pk_fp8_f32(clamp8(a), clamp8(b), w, false); w = __builtin_amdgcn_cvt_pk_fp8_f32(clamp8(c), clamp8(d), w, true); return (unsigned)w; }
;     __device__ __forceinline__ void operator()(AccRef acc, const GUnit& u, int wr, int wc, int fr, int fq) const {
;     ...
;         for (int ai = 0; ai < 2; ++ai)
; #pragma unroll
;             for (int m = 0; m < 4; ++m) { const int p = p0 + ai * 128 + m * 16;
;                 if (p < cnt) { u32x4 w;
; #pragma unroll
;                     for (int q = 0; q < 4; ++q) { const f32x4 v = acc[ai][q >> 1][m][q & 1] * (W8_INV * Y8_SCALE); w[q] = pk4_fp8(v[0], v[1], v[2], v[3]); }
;                     *(u32x4*)(Y + (size_t)ent[ai][m] * D + ct * 256 + wc * 64 + 16 * fq) = w; } }
.LBB0_1148:
	s_waitcnt vmcnt(0) lgkmcnt(0)
	v_pk_mul_f32 v[6:7], v[62:63], s[14:15] op_sel_hi:[1,0]
	v_pk_mul_f32 v[8:9], v[64:65], s[14:15] op_sel_hi:[1,0]
	v_med3_f32 v5, v6, s59, v193
	v_med3_f32 v7, v7, s59, v193
	v_mov_b32_e32 v6, v177
	v_cvt_pk_fp8_f32 v6, v5, v7
	v_med3_f32 v5, v8, s59, v193
	v_med3_f32 v7, v9, s59, v193
	v_pk_mul_f32 v[8:9], v[58:59], s[14:15] op_sel_hi:[1,0]
	v_cvt_pk_fp8_f32 v6, v5, v7 op_sel:[0,0,1]
	v_med3_f32 v5, v8, s59, v193
	v_med3_f32 v8, v9, s59, v193
	v_mov_b32_e32 v7, v177
	v_cvt_pk_fp8_f32 v7, v5, v8
	v_pk_mul_f32 v[8:9], v[60:61], s[14:15] op_sel_hi:[1,0]
	v_pk_mul_f32 v[10:11], v[56:57], s[14:15] op_sel_hi:[1,0]
	v_med3_f32 v5, v8, s59, v193
	v_med3_f32 v8, v9, s59, v193
	v_cvt_pk_fp8_f32 v7, v5, v8 op_sel:[0,0,1]
	v_pk_mul_f32 v[8:9], v[54:55], s[14:15] op_sel_hi:[1,0]
	s_nop 0
	v_med3_f32 v5, v8, s59, v193
	v_med3_f32 v9, v9, s59, v193
	v_mov_b32_e32 v8, v177
	v_cvt_pk_fp8_f32 v8, v5, v9
	v_med3_f32 v5, v10, s59, v193
	v_med3_f32 v9, v11, s59, v193
	v_pk_mul_f32 v[10:11], v[50:51], s[14:15] op_sel_hi:[1,0]
	v_cvt_pk_fp8_f32 v8, v5, v9 op_sel:[0,0,1]
	v_med3_f32 v5, v10, s59, v193
	v_med3_f32 v10, v11, s59, v193
	v_mov_b32_e32 v9, v177
	v_cvt_pk_fp8_f32 v9, v5, v10
	v_pk_mul_f32 v[10:11], v[52:53], s[14:15] op_sel_hi:[1,0]
	s_nop 0
	v_med3_f32 v5, v10, s59, v193
	v_med3_f32 v10, v11, s59, v193
	v_cvt_pk_fp8_f32 v9, v5, v10 op_sel:[0,0,1]
	v_mov_b32_e32 v5, v177
	v_lshlrev_b64 v[4:5], 11, v[4:5]
	v_lshl_add_u64 v[4:5], s[10:11], 0, v[4:5]
	v_lshl_add_u64 v[4:5], v[4:5], 0, s[22:23]
	v_lshl_add_u64 v[4:5], v[4:5], 0, s[6:7]
	v_lshl_add_u64 v[4:5], v[4:5], 0, v[162:163]
	global_store_dwordx4 v[4:5], v[6:9], off
	s_or_b64 exec, exec, s[24:25]
	v_cmp_gt_i32_e32 vcc, s48, v3
	s_and_saveexec_b64 s[24:25], vcc
	s_cbranch_execnz .LBB0_1157

; __device__ __forceinline__ unsigned pk4_fp8(float a, float b, float c, float d) { int w = 0; w = __builtin_amdgcn_cvt_pk_fp8_f32(clamp8(a), clamp8(b), w, false); w = __builtin_amdgcn_cvt_pk_fp8_f32(clamp8(c), clamp8(d), w, true); return (unsigned)w; }
;     __device__ __forceinline__ void operator()(AccRef acc, const GUnit& u, int wr, int wc, int fr, int fq) const {
;     ...
;         for (int ai = 0; ai < 2; ++ai)
; #pragma unroll
;             for (int m = 0; m < 4; ++m) { const int p = p0 + ai * 128 + m * 16;
;                 if (p < cnt) { u32x4 w;
; #pragma unroll
;                     for (int q = 0; q < 4; ++q) { const f32x4 v = acc[ai][q >> 1][m][q & 1] * (W8_INV * Y8_SCALE); w[q] = pk4_fp8(v[0], v[1], v[2], v[3]); }
;                     *(u32x4*)(Y + (size_t)ent[ai][m] * D + ct * 256 + wc * 64 + 16 * fq) = w; } }
.LBB0_1151:
	v_pk_mul_f32 v[16:17], v[142:143], s[14:15] op_sel_hi:[1,0]
	v_pk_mul_f32 v[18:19], v[144:145], s[14:15] op_sel_hi:[1,0]
	v_med3_f32 v15, v16, s59, v193
	v_med3_f32 v17, v17, s59, v193
	v_mov_b32_e32 v16, v177
	v_cvt_pk_fp8_f32 v16, v15, v17
	v_med3_f32 v15, v18, s59, v193
	v_med3_f32 v17, v19, s59, v193
	v_pk_mul_f32 v[18:19], v[138:139], s[14:15] op_sel_hi:[1,0]
	v_cvt_pk_fp8_f32 v16, v15, v17 op_sel:[0,0,1]
	v_med3_f32 v15, v18, s59, v193
	v_med3_f32 v18, v19, s59, v193
	v_mov_b32_e32 v17, v177
	v_cvt_pk_fp8_f32 v17, v15, v18
	v_pk_mul_f32 v[18:19], v[140:141], s[14:15] op_sel_hi:[1,0]
	v_pk_mul_f32 v[20:21], v[136:137], s[14:15] op_sel_hi:[1,0]
	v_med3_f32 v15, v18, s59, v193
	v_med3_f32 v18, v19, s59, v193
	v_cvt_pk_fp8_f32 v17, v15, v18 op_sel:[0,0,1]
	v_pk_mul_f32 v[18:19], v[134:135], s[14:15] op_sel_hi:[1,0]
	s_nop 0
	v_med3_f32 v15, v18, s59, v193
	v_med3_f32 v19, v19, s59, v193
	v_mov_b32_e32 v18, v177
	v_cvt_pk_fp8_f32 v18, v15, v19
	v_med3_f32 v15, v20, s59, v193
	v_med3_f32 v19, v21, s59, v193
	v_pk_mul_f32 v[20:21], v[130:131], s[14:15] op_sel_hi:[1,0]
	v_cvt_pk_fp8_f32 v18, v15, v19 op_sel:[0,0,1]
	v_med3_f32 v15, v20, s59, v193
	v_med3_f32 v20, v21, s59, v193
	v_mov_b32_e32 v19, v177
	v_cvt_pk_fp8_f32 v19, v15, v20
	v_pk_mul_f32 v[20:21], v[132:133], s[14:15] op_sel_hi:[1,0]
	s_nop 0
	v_med3_f32 v15, v20, s59, v193
	v_med3_f32 v20, v21, s59, v193
	v_cvt_pk_fp8_f32 v19, v15, v20 op_sel:[0,0,1]
	v_mov_b32_e32 v15, v177
	s_waitcnt vmcnt(0) lgkmcnt(0)
	v_lshlrev_b64 v[14:15], 11, v[14:15]
	v_lshl_add_u64 v[14:15], s[10:11], 0, v[14:15]
	v_lshl_add_u64 v[14:15], v[14:15], 0, s[22:23]
	v_lshl_add_u64 v[14:15], v[14:15], 0, s[6:7]
	v_lshl_add_u64 v[14:15], v[14:15], 0, v[162:163]
	global_store_dwordx4 v[14:15], v[16:19], off
	s_or_b64 exec, exec, s[24:25]
	v_cmp_gt_i32_e32 vcc, s48, v13
	s_and_saveexec_b64 s[24:25], vcc
	s_cbranch_execnz .LBB0_1144

; __device__ __forceinline__ unsigned pk4_fp8(float a, float b, float c, float d) { int w = 0; w = __builtin_amdgcn_cvt_pk_fp8_f32(clamp8(a), clamp8(b), w, false); w = __builtin_amdgcn_cvt_pk_fp8_f32(clamp8(c), clamp8(d), w, true); return (unsigned)w; }
;     __device__ __forceinline__ void operator()(AccRef acc, const GUnit& u, int wr, int wc, int fr, int fq) const {
;     ...
;         for (int ai = 0; ai < 2; ++ai)
; #pragma unroll
;             for (int m = 0; m < 4; ++m) { const int p = p0 + ai * 128 + m * 16;
;                 if (p < cnt) { u32x4 w;
; #pragma unroll
;                     for (int q = 0; q < 4; ++q) { const f32x4 v = acc[ai][q >> 1][m][q & 1] * (W8_INV * Y8_SCALE); w[q] = pk4_fp8(v[0], v[1], v[2], v[3]); }
;                     *(u32x4*)(Y + (size_t)ent[ai][m] * D + ct * 256 + wc * 64 + 16 * fq) = w; } }
.LBB0_1153:
	s_waitcnt vmcnt(0) lgkmcnt(0)
	v_pk_mul_f32 v[12:13], v[110:111], s[14:15] op_sel_hi:[1,0]
	v_pk_mul_f32 v[14:15], v[112:113], s[14:15] op_sel_hi:[1,0]
	v_med3_f32 v11, v12, s59, v193
	v_med3_f32 v13, v13, s59, v193
	v_mov_b32_e32 v12, v177
	v_cvt_pk_fp8_f32 v12, v11, v13
	v_med3_f32 v11, v14, s59, v193
	v_med3_f32 v13, v15, s59, v193
	v_pk_mul_f32 v[14:15], v[106:107], s[14:15] op_sel_hi:[1,0]
	v_cvt_pk_fp8_f32 v12, v11, v13 op_sel:[0,0,1]
	v_med3_f32 v11, v14, s59, v193
	v_med3_f32 v14, v15, s59, v193
	v_mov_b32_e32 v13, v177
	v_cvt_pk_fp8_f32 v13, v11, v14
	v_pk_mul_f32 v[14:15], v[108:109], s[14:15] op_sel_hi:[1,0]
	v_pk_mul_f32 v[16:17], v[104:105], s[14:15] op_sel_hi:[1,0]
	v_med3_f32 v11, v14, s59, v193
	v_med3_f32 v14, v15, s59, v193
	v_cvt_pk_fp8_f32 v13, v11, v14 op_sel:[0,0,1]
	v_pk_mul_f32 v[14:15], v[102:103], s[14:15] op_sel_hi:[1,0]
	s_nop 0
	v_med3_f32 v11, v14, s59, v193
	v_med3_f32 v15, v15, s59, v193
	v_mov_b32_e32 v14, v177
	v_cvt_pk_fp8_f32 v14, v11, v15
	v_med3_f32 v11, v16, s59, v193
	v_med3_f32 v15, v17, s59, v193
	v_pk_mul_f32 v[16:17], v[98:99], s[14:15] op_sel_hi:[1,0]
	v_cvt_pk_fp8_f32 v14, v11, v15 op_sel:[0,0,1]
	v_med3_f32 v11, v16, s59, v193
	v_med3_f32 v16, v17, s59, v193
	v_mov_b32_e32 v15, v177
	v_cvt_pk_fp8_f32 v15, v11, v16
	v_pk_mul_f32 v[16:17], v[100:101], s[14:15] op_sel_hi:[1,0]
	s_nop 0
	v_med3_f32 v11, v16, s59, v193
	v_med3_f32 v16, v17, s59, v193
	v_cvt_pk_fp8_f32 v15, v11, v16 op_sel:[0,0,1]
	v_mov_b32_e32 v11, v177
	v_lshlrev_b64 v[10:11], 11, v[10:11]
	v_lshl_add_u64 v[10:11], s[10:11], 0, v[10:11]
	v_lshl_add_u64 v[10:11], v[10:11], 0, s[22:23]
	v_lshl_add_u64 v[10:11], v[10:11], 0, s[6:7]
	v_lshl_add_u64 v[10:11], v[10:11], 0, v[162:163]
	global_store_dwordx4 v[10:11], v[12:15], off
	s_or_b64 exec, exec, s[24:25]
	v_cmp_gt_i32_e32 vcc, s48, v9
	s_and_saveexec_b64 s[24:25], vcc
	s_cbranch_execnz .LBB0_1146

; __device__ __forceinline__ unsigned pk4_fp8(float a, float b, float c, float d) { int w = 0; w = __builtin_amdgcn_cvt_pk_fp8_f32(clamp8(a), clamp8(b), w, false); w = __builtin_amdgcn_cvt_pk_fp8_f32(clamp8(c), clamp8(d), w, true); return (unsigned)w; }
;     __device__ __forceinline__ void operator()(AccRef acc, const GUnit& u, int wr, int wc, int fr, int fq) const {
;     ...
;         for (int ai = 0; ai < 2; ++ai)
; #pragma unroll
;             for (int m = 0; m < 4; ++m) { const int p = p0 + ai * 128 + m * 16;
;                 if (p < cnt) { u32x4 w;
; #pragma unroll
;                     for (int q = 0; q < 4; ++q) { const f32x4 v = acc[ai][q >> 1][m][q & 1] * (W8_INV * Y8_SCALE); w[q] = pk4_fp8(v[0], v[1], v[2], v[3]); }
;                     *(u32x4*)(Y + (size_t)ent[ai][m] * D + ct * 256 + wc * 64 + 16 * fq) = w; } }
.LBB0_1155:
	s_waitcnt vmcnt(0) lgkmcnt(0)
	v_pk_mul_f32 v[8:9], v[78:79], s[14:15] op_sel_hi:[1,0]
	v_pk_mul_f32 v[10:11], v[80:81], s[14:15] op_sel_hi:[1,0]
	v_med3_f32 v7, v8, s59, v193
	v_med3_f32 v9, v9, s59, v193
	v_mov_b32_e32 v8, v177
	v_cvt_pk_fp8_f32 v8, v7, v9
	v_med3_f32 v7, v10, s59, v193
	v_med3_f32 v9, v11, s59, v193
	v_pk_mul_f32 v[10:11], v[74:75], s[14:15] op_sel_hi:[1,0]
	v_cvt_pk_fp8_f32 v8, v7, v9 op_sel:[0,0,1]
	v_med3_f32 v7, v10, s59, v193
	v_med3_f32 v10, v11, s59, v193
	v_mov_b32_e32 v9, v177
	v_cvt_pk_fp8_f32 v9, v7, v10
	v_pk_mul_f32 v[10:11], v[76:77], s[14:15] op_sel_hi:[1,0]
	v_pk_mul_f32 v[12:13], v[72:73], s[14:15] op_sel_hi:[1,0]
	v_med3_f32 v7, v10, s59, v193
	v_med3_f32 v10, v11, s59, v193
	v_cvt_pk_fp8_f32 v9, v7, v10 op_sel:[0,0,1]
	v_pk_mul_f32 v[10:11], v[70:71], s[14:15] op_sel_hi:[1,0]
	s_nop 0
	v_med3_f32 v7, v10, s59, v193
	v_med3_f32 v11, v11, s59, v193
	v_mov_b32_e32 v10, v177
	v_cvt_pk_fp8_f32 v10, v7, v11
	v_med3_f32 v7, v12, s59, v193
	v_med3_f32 v11, v13, s59, v193
	v_pk_mul_f32 v[12:13], v[66:67], s[14:15] op_sel_hi:[1,0]
	v_cvt_pk_fp8_f32 v10, v7, v11 op_sel:[0,0,1]
	v_med3_f32 v7, v12, s59, v193
	v_med3_f32 v12, v13, s59, v193
	v_mov_b32_e32 v11, v177
	v_cvt_pk_fp8_f32 v11, v7, v12
	v_pk_mul_f32 v[12:13], v[68:69], s[14:15] op_sel_hi:[1,0]
	s_nop 0
	v_med3_f32 v7, v12, s59, v193
	v_med3_f32 v12, v13, s59, v193
	v_cvt_pk_fp8_f32 v11, v7, v12 op_sel:[0,0,1]
	v_mov_b32_e32 v7, v177
	v_lshlrev_b64 v[6:7], 11, v[6:7]
	v_lshl_add_u64 v[6:7], s[10:11], 0, v[6:7]
	v_lshl_add_u64 v[6:7], v[6:7], 0, s[22:23]
	v_lshl_add_u64 v[6:7], v[6:7], 0, s[6:7]
	v_lshl_add_u64 v[6:7], v[6:7], 0, v[162:163]
	global_store_dwordx4 v[6:7], v[8:11], off
	s_or_b64 exec, exec, s[24:25]
	v_cmp_gt_i32_e32 vcc, s48, v5
	s_and_saveexec_b64 s[24:25], vcc
	s_cbranch_execnz .LBB0_1148

; __device__ __forceinline__ unsigned pk4_fp8(float a, float b, float c, float d) { int w = 0; w = __builtin_amdgcn_cvt_pk_fp8_f32(clamp8(a), clamp8(b), w, false); w = __builtin_amdgcn_cvt_pk_fp8_f32(clamp8(c), clamp8(d), w, true); return (unsigned)w; }
;     __device__ __forceinline__ void operator()(AccRef acc, const GUnit& u, int wr, int wc, int fr, int fq) const {
;     ...
;         for (int ai = 0; ai < 2; ++ai)
; #pragma unroll
;             for (int m = 0; m < 4; ++m) { const int p = p0 + ai * 128 + m * 16;
;                 if (p < cnt) { u32x4 w;
; #pragma unroll
;                     for (int q = 0; q < 4; ++q) { const f32x4 v = acc[ai][q >> 1][m][q & 1] * (W8_INV * Y8_SCALE); w[q] = pk4_fp8(v[0], v[1], v[2], v[3]); }
;                     *(u32x4*)(Y + (size_t)ent[ai][m] * D + ct * 256 + wc * 64 + 16 * fq) = w; } }
.LBB0_1157:
	s_waitcnt vmcnt(0) lgkmcnt(0)
	v_pk_mul_f32 v[4:5], v[46:47], s[14:15] op_sel_hi:[1,0]
	v_pk_mul_f32 v[6:7], v[48:49], s[14:15] op_sel_hi:[1,0]
	v_med3_f32 v3, v4, s59, v193
	v_med3_f32 v5, v5, s59, v193
	v_mov_b32_e32 v4, v177
	v_cvt_pk_fp8_f32 v4, v3, v5
	v_med3_f32 v3, v6, s59, v193
	v_med3_f32 v5, v7, s59, v193
	v_pk_mul_f32 v[6:7], v[42:43], s[14:15] op_sel_hi:[1,0]
	v_cvt_pk_fp8_f32 v4, v3, v5 op_sel:[0,0,1]
	v_med3_f32 v3, v6, s59, v193
	v_med3_f32 v6, v7, s59, v193
	v_mov_b32_e32 v5, v177
	v_cvt_pk_fp8_f32 v5, v3, v6
	v_pk_mul_f32 v[6:7], v[44:45], s[14:15] op_sel_hi:[1,0]
	v_pk_mul_f32 v[8:9], v[40:41], s[14:15] op_sel_hi:[1,0]
	v_med3_f32 v3, v6, s59, v193
	v_med3_f32 v6, v7, s59, v193
	v_cvt_pk_fp8_f32 v5, v3, v6 op_sel:[0,0,1]
	v_pk_mul_f32 v[6:7], v[38:39], s[14:15] op_sel_hi:[1,0]
	s_nop 0
	v_med3_f32 v3, v6, s59, v193
	v_med3_f32 v7, v7, s59, v193
	v_mov_b32_e32 v6, v177
	v_cvt_pk_fp8_f32 v6, v3, v7
	v_med3_f32 v3, v8, s59, v193
	v_med3_f32 v7, v9, s59, v193
	v_pk_mul_f32 v[8:9], v[34:35], s[14:15] op_sel_hi:[1,0]
	v_cvt_pk_fp8_f32 v6, v3, v7 op_sel:[0,0,1]
	v_med3_f32 v3, v8, s59, v193
	v_med3_f32 v8, v9, s59, v193
	v_mov_b32_e32 v7, v177
	v_cvt_pk_fp8_f32 v7, v3, v8
	v_pk_mul_f32 v[8:9], v[36:37], s[14:15] op_sel_hi:[1,0]
	s_nop 0
	v_med3_f32 v3, v8, s59, v193
	v_med3_f32 v8, v9, s59, v193
	v_cvt_pk_fp8_f32 v7, v3, v8 op_sel:[0,0,1]
	v_mov_b32_e32 v3, v177
	v_lshlrev_b64 v[2:3], 11, v[2:3]
	v_lshl_add_u64 v[2:3], s[10:11], 0, v[2:3]
	v_lshl_add_u64 v[2:3], v[2:3], 0, s[22:23]
	v_lshl_add_u64 v[2:3], v[2:3], 0, s[6:7]
	v_lshl_add_u64 v[2:3], v[2:3], 0, v[162:163]
	global_store_dwordx4 v[2:3], v[4:7], off
	s_or_b64 exec, exec, s[24:25]
	s_andn2_b64 vcc, exec, s[20:21]
	s_mov_b64 s[20:21], -1
	s_cbranch_vccnz .LBB0_1132

; __global__ void __launch_bounds__(NWAVES * 64, 2) fwd_kernel(Args a) {
;     extern __shared__ __attribute__((aligned(16))) unsigned char lds_raw[];
	.amdhsa_kernel _Z10fwd_kernel4Args
		.amdhsa_group_segment_fixed_size 0
		.amdhsa_private_segment_fixed_size 0
		.amdhsa_kernarg_size 528
		.amdhsa_user_sgpr_count 2
		.amdhsa_user_sgpr_dispatch_ptr 0
		.amdhsa_user_sgpr_queue_ptr 0
		.amdhsa_user_sgpr_kernarg_segment_ptr 1
		.amdhsa_user_sgpr_dispatch_id 0
		.amdhsa_user_sgpr_kernarg_preload_length 0
		.amdhsa_user_sgpr_kernarg_preload_offset 0
		.amdhsa_user_sgpr_private_segment_size 0
		.amdhsa_uses_dynamic_stack 0
		.amdhsa_enable_private_segment 0
		.amdhsa_system_sgpr_workgroup_id_x 1
		.amdhsa_system_sgpr_workgroup_id_y 0
		.amdhsa_system_sgpr_workgroup_id_z 0
		.amdhsa_system_sgpr_workgroup_info 0
		.amdhsa_system_vgpr_workitem_id 0
		.amdhsa_next_free_vgpr 256
		.amdhsa_next_free_sgpr 102
		.amdhsa_accum_offset 256
		.amdhsa_reserve_vcc 1
		.amdhsa_float_round_mode_32 0
		.amdhsa_float_round_mode_16_64 0
		.amdhsa_float_denorm_mode_32 3
		.amdhsa_float_denorm_mode_16_64 3
		.amdhsa_dx10_clamp 1
		.amdhsa_ieee_mode 1
		.amdhsa_fp16_overflow 0
		.amdhsa_tg_split 0
		.amdhsa_exception_fp_ieee_invalid_op 0
		.amdhsa_exception_fp_denorm_src 0
		.amdhsa_exception_fp_ieee_div_zero 0
		.amdhsa_exception_fp_ieee_overflow 0
		.amdhsa_exception_fp_ieee_underflow 0
		.amdhsa_exception_fp_ieee_inexact 0
		.amdhsa_exception_int_div_zero 0
	.end_amdhsa_kernel

; __global__ void __launch_bounds__(NWAVES * 64, 2) fwd_kernel(Args a) {
;     extern __shared__ __attribute__((aligned(16))) unsigned char lds_raw[];
amdhsa.kernels:
  - .agpr_count:     0
    .args:
      - .offset:         0
        .size:           272
        .value_kind:     by_value
      - .offset:         272
        .size:           4
        .value_kind:     hidden_block_count_x
      - .offset:         276
        .size:           4
        .value_kind:     hidden_block_count_y
      - .offset:         280
        .size:           4
        .value_kind:     hidden_block_count_z
      - .offset:         284
        .size:           2
        .value_kind:     hidden_group_size_x
      - .offset:         286
        .size:           2
        .value_kind:     hidden_group_size_y
      - .offset:         288
        .size:           2
        .value_kind:     hidden_group_size_z
      - .offset:         290
        .size:           2
        .value_kind:     hidden_remainder_x
      - .offset:         292
        .size:           2
        .value_kind:     hidden_remainder_y
      - .offset:         294
        .size:           2
        .value_kind:     hidden_remainder_z
      - .offset:         312
        .size:           8
        .value_kind:     hidden_global_offset_x
      - .offset:         320
        .size:           8
        .value_kind:     hidden_global_offset_y
      - .offset:         328
        .size:           8
        .value_kind:     hidden_global_offset_z
      - .offset:         336
        .size:           2
        .value_kind:     hidden_grid_dims
      - .offset:         392
        .size:           4
        .value_kind:     hidden_dynamic_lds_size
    .group_segment_fixed_size: 0
    .kernarg_segment_align: 8
    .kernarg_segment_size: 528
    .language:       OpenCL C
    .language_version:
      - 2
      - 0
    .max_flat_workgroup_size: 512
    .name:           _Z10fwd_kernel4Args
    .private_segment_fixed_size: 0
    .sgpr_count:     108
    .sgpr_spill_count: 0
    .symbol:         _Z10fwd_kernel4Args.kd
    .uniform_work_group_size: 1
    .uses_dynamic_stack: false
    .vgpr_count:     256
    .vgpr_spill_count: 0
    .wavefront_size: 64
